# v010 + expert-id load merged (no dependent 2nd round trip) + accumulator clears as v_mov_b64 + trailing-half restore barrier moved to K-loop entry
# speedup vs baseline: 1.0048x; 1.0040x over previous
;     __device__ __forceinline__ size_t boff(const Unit& u) const { return (size_t)__builtin_amdgcn_readfirstlane(panel_e[u.pm]) * estride; }
; #define PG8_STAGE_A(bufoff, h, ptr, nsel) do { if constexpr (Sched::GATHER) { if (nsel) PG8_STAGE_X(bufoff, ptr, vAn[h], PG8_A_AUX); else PG8_STAGE_X(bufoff, ptr, vAc[h], PG8_A_AUX); } \
;         else PG8_STAGE_X(bufoff, (ptr) + (h) * hstep, voffA, PG8_A_AUX); } while (0)
; #define PG8_BAR __builtin_amdgcn_s_barrier()
; template <class Epi, class Sched, bool ALIGN_EPI = false, bool SP2 = false>
; __device__ __forceinline__ void gemm_phase(PG8_LAS unsigned char* lds, const Gemm g, const Sched& S, const Epi& E) {
;     ...
;     const int tid = tid_, wid = __builtin_amdgcn_readfirstlane(tid >> 6), lane = tid & 63, wr = wid >> 2, wc = wid & 3, fr = lane & 15, fq = lane >> 4;
;     const int K = g.K, nt = K / BK;
;     unsigned voffA[2], voffB[2];
; #pragma unroll
;     for (int i = 0; i < 2; ++i) { int R, C; stage_rc(tid * 16 + i * 8192, R, C); const int Rb = Epi::PERM ? ((R & ~31) + perm32(R & 31)) : R;
;         voffA[i] = (unsigned)(R * K + C) * 2u; voffB[i] = (unsigned)(Rb * K + C) * 2u; }
;     unsigned vAc[2][2] = {{0u, 0u}, {0u, 0u}}, vAn[2][2] = {{0u, 0u}, {0u, 0u}};
;     ...
;     const size_t kstep = (size_t)(BK * 2);
;     const size_t hstep = (size_t)HALF * K * 2;
;     const size_t tstep = 2 * hstep;
;     const unsigned ldsw = (unsigned)wid * 1024u;
;     const int aoff = lds_byte(wr * 64 + fr, fq * 8), boff = lds_byte(wc * 32 + fr, fq * 8);
;     ...
;     Unit cur, nxt; int ui = 0;
;     if (!S.next(0, cur)) return;
;     f32x4 acc[2][2][4][2];
; #pragma unroll
;     for (int a = 0; a < 2; ++a)
; #pragma unroll
;         for (int b = 0; b < 2; ++b)
; #pragma unroll
;             for (int m = 0; m < 4; ++m)
; #pragma unroll
;                 for (int n = 0; n < 2; ++n) acc[a][b][m][n] = (f32x4){0.f, 0.f, 0.f, 0.f};
;     bf16x8 At[4][2], B0[2][2], B1[2][2];
;     const char* cA = Sched::GATHER ? (const char*)g.A : (const char*)g.A + (size_t)cur.pm * tstep; PG8_SETA(vAc, cur); const char* cB = (const char*)g.Bt + S.boff(cur) + (size_t)cur.pn * tstep;
;     S.a_ready(cur);
;     if constexpr (SP2) {
;         PG8_STAGE(PG8_SB(0, 0), cB, voffB); PG8_STAGE(PG8_SB(0, 1), cB + hstep, voffB); PG8_STAGE_A(PG8_SA(0, 0), 0, cA, false); PG8_STAGE_A(PG8_SA(0, 1), 1, cA, false);
;         if (wr == 1) PG8_BAR;
.LBB13_228:
	s_andn2_b64 vcc, exec, s[4:5]
	s_cbranch_vccnz .LBB13_409
	v_ashrrev_i32_e32 v10, 31, v12
	v_lshrrev_b32_e32 v10, 26, v10
	v_add_u32_e32 v10, v12, v10
	v_ashrrev_i32_e32 v13, 6, v10
	v_bfe_i32 v10, v12, 27, 1
	v_lshlrev_b32_e32 v7, 4, v12
	v_lshrrev_b32_e32 v10, 22, v10
	v_add_u32_e32 v10, v7, v10
	v_and_b32_e32 v10, 0xfffffc00, v10
	v_mov_b64_e32 v[2:3], s[0:1]
	v_readlane_b32 s0, v249, 1
	v_sub_u32_e32 v10, v7, v10
	v_readlane_b32 s1, v249, 2
	v_lshrrev_b32_e32 v11, 4, v10
	s_load_dwordx2 s[0:1], s[0:1], 0xe8
	v_bitop3_b32 v10, v11, v10, 32 bitop3:0x6c
	v_ashrrev_i32_e32 v14, 31, v10
	v_lshrrev_b32_e32 v14, 26, v14
	v_add_u32_e32 v15, v10, v14
	v_lshlrev_b32_e32 v11, 3, v13
	v_ashrrev_i32_e32 v14, 6, v15
	v_and_b32_e32 v15, 0xc0, v15
	s_waitcnt lgkmcnt(0)
	v_lshl_add_u64 v[2:3], s[0:1], 0, v[2:3]
	s_mov_b64 s[0:1], 0x20700000
	s_mul_i32 s76, s68, 0x580000
	v_and_b32_e32 v11, -16, v11
	v_sub_u32_e32 v10, v10, v15
	v_lshl_add_u64 v[8:9], v[2:3], 0, s[0:1]
	v_lshl_add_u64 v[4:5], s[76:77], 1, v[2:3]
	s_mov_b64 s[0:1], 0x1000000
	v_add_u32_e32 v11, v14, v11
	v_ashrrev_i16_sdwa v10, v238, sext(v10) dst_sel:DWORD dst_unused:UNUSED_PAD src0_sel:DWORD src1_sel:BYTE_0
	v_lshl_add_u64 v[4:5], v[4:5], 0, s[0:1]
	v_lshlrev_b32_e32 v16, 5, v13
	v_bfe_i32 v15, v10, 0, 16
	v_lshlrev_b32_e32 v10, 1, v11
	v_lshrrev_b32_e32 v17, 2, v11
	v_and_b32_e32 v18, 3, v14
	s_mov_b32 s0, 0x1fffe0
	v_and_b32_e32 v16, 32, v16
	v_and_b32_e32 v10, 24, v10
	v_and_b32_e32 v17, 4, v17
	v_and_or_b32 v18, v11, s0, v18
	v_or3_b32 v10, v18, v17, v10
	v_add_lshl_u32 v16, v16, v15, 1
	v_add_u32_e32 v7, 0x2000, v7
	v_lshl_add_u32 v142, v10, 11, v16
	v_ashrrev_i32_e32 v10, 31, v7
	v_lshrrev_b32_e32 v10, 22, v10
	v_add_u32_e32 v10, v7, v10
	v_lshl_add_u32 v140, v11, 11, v16
	v_ashrrev_i32_e32 v16, 10, v10
	v_mul_i32_i24_e32 v10, 0x400, v16
	v_sub_u32_e32 v7, v7, v10
	v_lshrrev_b32_e32 v10, 4, v7
	v_bitop3_b32 v7, v10, v7, 32 bitop3:0x6c
	v_ashrrev_i32_e32 v11, 31, v7
	v_lshrrev_b32_e32 v11, 26, v11
	v_add_u32_e32 v11, v7, v11
	v_lshlrev_b32_e32 v10, 3, v16
	v_ashrrev_i32_e32 v17, 6, v11
	v_and_b32_e32 v11, 0xc0, v11
	v_and_b32_e32 v10, -16, v10
	v_sub_u32_e32 v7, v7, v11
	v_add_u32_e32 v10, v17, v10
	v_lshlrev_b32_e32 v18, 5, v16
	v_ashrrev_i16_sdwa v7, v238, sext(v7) dst_sel:DWORD dst_unused:UNUSED_PAD src0_sel:DWORD src1_sel:BYTE_0
	v_add_u32_e64 v1, 0, s3
	s_ashr_i32 s6, s2, 6
	v_and_b32_e32 v20, 32, v18
	v_bfe_i32 v18, v7, 0, 16
	v_lshlrev_b32_e32 v7, 1, v10
	v_lshrrev_b32_e32 v11, 2, v10
	v_and_b32_e32 v21, 3, v17
	v_add_u32_e32 v6, 0x10000, v1
	v_and_b32_e32 v7, 24, v7
	v_and_b32_e32 v11, 4, v11
	v_and_or_b32 v21, v10, s0, v21
	s_lshl_b32 s40, s6, 10
	s_ashr_i32 s11, s10, 31
	v_or3_b32 v7, v21, v11, v7
	v_add_lshl_u32 v11, v20, v18, 1
	s_lshl_b64 s[12:13], s[10:11], 19
	v_add_u32_e32 v20, s40, v6
	v_add_u32_e32 v19, 0x14000, v1
	v_lshl_add_u32 v144, v10, 11, v11
	v_lshl_add_u32 v146, v7, 11, v11
	v_lshl_add_u64 v[10:11], v[4:5], 0, s[12:13]
	v_mov_b32_e32 v143, v98
	v_readfirstlane_b32 s5, v20
	v_add_u32_e32 v20, 0x2000, v20
	v_readfirstlane_b32 s35, v4
	v_readfirstlane_b32 s36, v5
	v_readfirstlane_b32 s39, v19
	v_lshl_add_u64 v[4:5], v[10:11], 0, v[142:143]
	s_mov_b32 m0, s5
	v_mov_b32_e32 v147, v98
	v_readfirstlane_b32 s5, v20
	s_mov_b64 s[14:15], 0x40000
	v_add_u32_e32 v19, s40, v19
	v_readfirstlane_b32 s37, v6
	s_ashr_i32 s9, s8, 31
	v_readfirstlane_b32 s24, v10
	v_readfirstlane_b32 s25, v11
	global_load_lds_dwordx4 v[4:5], off
	v_lshl_add_u64 v[6:7], v[10:11], 0, v[146:147]
	s_mov_b32 m0, s5
	v_lshl_add_u64 v[10:11], v[10:11], 0, s[14:15]
	v_readfirstlane_b32 s5, v19
	v_add_u32_e32 v19, 0x2000, v19
	v_readfirstlane_b32 s3, v1
	s_lshl_b64 s[0:1], s[8:9], 19
	global_load_lds_dwordx4 v[6:7], off
	v_lshl_add_u64 v[20:21], v[10:11], 0, v[142:143]
	s_mov_b32 m0, s5
	v_readfirstlane_b32 s5, v19
	v_add_u32_e32 v1, s40, v1
	global_load_lds_dwordx4 v[20:21], off
	v_lshl_add_u64 v[10:11], v[10:11], 0, v[146:147]
	s_mov_b32 m0, s5
	v_lshl_add_u64 v[20:21], v[8:9], 0, s[0:1]
	v_mov_b32_e32 v141, v98
	v_readfirstlane_b32 s0, v1
	v_add_u32_e32 v19, 0x2000, v1
	v_readfirstlane_b32 s31, v8
	v_readfirstlane_b32 s34, v9
	global_load_lds_dwordx4 v[10:11], off
	v_lshl_add_u64 v[8:9], v[20:21], 0, v[140:141]
	s_mov_b32 m0, s0
	v_mov_b32_e32 v145, v98
	v_readfirstlane_b32 s0, v19
	v_add_u32_e32 v19, 0x4000, v1
	v_readfirstlane_b32 s12, v20
	v_readfirstlane_b32 s13, v21
	global_load_lds_dwordx4 v[8:9], off
	v_lshl_add_u64 v[10:11], v[20:21], 0, v[144:145]
	s_mov_b32 m0, s0
	v_lshl_add_u64 v[20:21], v[20:21], 0, s[14:15]
	v_readfirstlane_b32 s0, v19
	v_add_u32_e32 v1, 0x6000, v1
	global_load_lds_dwordx4 v[10:11], off
	v_lshl_add_u64 v[22:23], v[20:21], 0, v[140:141]
	s_mov_b32 m0, s0
	v_readfirstlane_b32 s0, v1
	global_load_lds_dwordx4 v[22:23], off
	v_lshl_add_u64 v[20:21], v[20:21], 0, v[144:145]
	s_mov_b32 m0, s0
	s_ashr_i32 s4, s2, 8
	global_load_lds_dwordx4 v[20:21], off
	s_cmp_eq_u32 s4, 1
	s_cselect_b64 s[0:1], -1, 0
	s_cmp_lg_u32 s4, 1
	s_cbranch_scc1 .LBB13_231
;     __device__ __forceinline__ size_t boff(const Unit& u) const { return (size_t)__builtin_amdgcn_readfirstlane(panel_e[u.pm]) * estride; }
; #define PG8_STAGE_A(bufoff, h, ptr, nsel) do { if constexpr (Sched::GATHER) { if (nsel) PG8_STAGE_X(bufoff, ptr, vAn[h], PG8_A_AUX); else PG8_STAGE_X(bufoff, ptr, vAc[h], PG8_A_AUX); } \
;         else PG8_STAGE_X(bufoff, (ptr) + (h) * hstep, voffA, PG8_A_AUX); } while (0)
; #define PG8_STAGE(bufoff, gbase, voff) PG8_STAGE_X(bufoff, gbase, voff, PG8_B_AUX)
; #define PG8_WAIT_V(n) asm volatile("s_waitcnt vmcnt(" #n ")" ::: "memory")
; #define PG8_BAR __builtin_amdgcn_s_barrier()
; template <class Epi, class Sched, bool ALIGN_EPI = false, bool SP2 = false>
; __device__ __forceinline__ void gemm_phase(PG8_LAS unsigned char* lds, const Gemm g, const Sched& S, const Epi& E) {
;     ...
;     const unsigned ldsw = (unsigned)wid * 1024u;
;     const int aoff = lds_byte(wr * 64 + fr, fq * 8), boff = lds_byte(wc * 32 + fr, fq * 8);
;     ...
;         if (wr == 1) PG8_BAR;
;         PG8_WAIT_V(2); PG8_BAR;
;         PG8_STAGE(PG8_SB(1, 0), cB + kstep, voffB); PG8_STAGE_A(PG8_SA(1, 0), 0, cA + kstep, false); PG8_STAGE(PG8_SB(1, 1), cB + hstep + kstep, voffB);
;         PG8_WAIT_V(6); PG8_BAR;
.LBB13_231:
	s_add_i32 s41, s3, 0x18000
	s_add_i32 s45, s41, s40
	s_and_b32 s7, s6, 3
	v_lshl_add_u64 v[4:5], v[4:5], 0, s[54:55]
	s_mov_b32 m0, s45
	s_add_i32 s46, s45, 0x2000
	s_add_i32 s47, s3, s40
	s_add_i32 s42, s3, 0x1c000
	s_ashr_i32 s43, s29, 31
	s_lshl_b32 s44, s4, 6
	s_lshl_b32 s9, s4, 13
	s_lshl_b32 s11, s7, 12
	s_waitcnt vmcnt(2)
	s_barrier
	global_load_lds_dwordx4 v[4:5], off
	v_lshl_add_u64 v[4:5], v[6:7], 0, s[54:55]
	s_mov_b32 m0, s46
	s_add_i32 s50, s47, 0x8000
	s_add_i32 s51, s47, 0xa000
	global_load_lds_dwordx4 v[4:5], off
	v_lshl_add_u64 v[4:5], v[8:9], 0, s[54:55]
	s_mov_b32 m0, s50
	s_add_u32 s4, s24, 0x40080
	global_load_lds_dwordx4 v[4:5], off
	v_lshl_add_u64 v[4:5], v[10:11], 0, s[54:55]
	s_mov_b32 m0, s51
	s_addc_u32 s5, s25, 0
	s_add_i32 s56, s42, s40
	global_load_lds_dwordx4 v[4:5], off
	v_lshl_add_u64 v[4:5], s[4:5], 0, v[142:143]
	s_mov_b32 m0, s56
	s_add_i32 s57, s56, 0x2000
	global_load_lds_dwordx4 v[4:5], off
	v_lshl_add_u64 v[4:5], s[4:5], 0, v[146:147]
	s_mov_b32 m0, s57
	s_cmpk_lt_u32 s2, 0x100
	global_load_lds_dwordx4 v[4:5], off
	s_mov_b64 s[4:5], 0x22800000
	s_cselect_b64 s[14:15], -1, 0
	s_cmp_lt_u32 s7, 2
	v_lshl_add_u64 v[148:149], v[2:3], 0, s[4:5]
	v_bfe_u32 v4, v12, 4, 2
	s_cselect_b64 s[4:5], -1, 0
	s_lshl_b32 s2, s6, 7
	v_lshlrev_b32_e32 v5, 3, v4
	s_and_b32 s76, s2, 0x80
	v_lshlrev_b32_e32 v6, 4, v4
	v_lshl_or_b32 v168, s7, 5, v5
	v_lshl_add_u64 v[2:3], v[2:3], 0, s[76:77]
	v_lshlrev_b32_e32 v4, 5, v4
	v_mov_b32_e32 v5, v98
	v_lshl_add_u64 v[2:3], v[2:3], 0, v[4:5]
	s_mov_b64 s[6:7], 0x250000
	v_lshl_add_u64 v[150:151], v[2:3], 0, s[6:7]
	v_lshlrev_b32_e32 v2, 14, v13
	v_and_b32_e32 v2, 0xffff8000, v2
	v_lshl_add_u32 v2, v14, 11, v2
	v_and_b32_e32 v3, 1, v13
	v_lshl_or_b32 v2, v3, 6, v2
	v_lshl_add_u32 v152, v15, 1, v2
	v_lshlrev_b32_e32 v2, 14, v16
	v_and_b32_e32 v1, 15, v12
	v_lshlrev_b32_e32 v7, 2, v12
	v_and_b32_e32 v2, 0xffff8000, v2
	v_lshl_or_b32 v6, v1, 6, v6
	v_and_b32_e32 v7, 32, v7
	s_waitcnt vmcnt(6)
	v_lshl_add_u32 v2, v17, 11, v2
	v_and_b32_e32 v3, 1, v16
	v_bitop3_b32 v8, v6, s9, v7 bitop3:0xde
	v_lshl_or_b32 v2, v3, 6, v2
	v_bitop3_b32 v99, v6, s11, v7 bitop3:0xde
	v_or_b32_e32 v169, 16, v1
	v_or_b32_e32 v170, 32, v1
	v_or_b32_e32 v171, 48, v1
	v_mov_b32_e32 v153, v98
	v_lshl_add_u32 v154, v18, 1, v2
	v_mov_b32_e32 v155, v98
	s_mov_b32 s58, 0
	v_add_u32_e32 v172, s3, v8
	s_barrier
	s_branch .LBB13_234

; #define PG8_STAGE_A(bufoff, h, ptr, nsel) do { if constexpr (Sched::GATHER) { if (nsel) PG8_STAGE_X(bufoff, ptr, vAn[h], PG8_A_AUX); else PG8_STAGE_X(bufoff, ptr, vAc[h], PG8_A_AUX); } \
;         else PG8_STAGE_X(bufoff, (ptr) + (h) * hstep, voffA, PG8_A_AUX); } while (0)
; #define PG8_LDA(dst, b, h) do { _Pragma("unroll") for (int m = 0; m < 4; ++m) _Pragma("unroll") for (int k = 0; k < 2; ++k) dst[m][k] = *(const PG8_LAS bf16x8*)(lds + PG8_SA(b, h) + aoff + m * 2048 + k * 1024); } while (0)
; #define PG8_LDB(dst, b, h) do { _Pragma("unroll") for (int n = 0; n < 2; ++n) _Pragma("unroll") for (int k = 0; k < 2; ++k) dst[n][k] = *(const PG8_LAS bf16x8*)(lds + PG8_SB(b, h) + boff + n * 2048 + k * 1024); } while (0)
; #define PG8_MMA(ai, bj, At, Bt) do { __builtin_amdgcn_s_setprio(1); _Pragma("unroll") for (int m = 0; m < 4; ++m) _Pragma("unroll") for (int n = 0; n < 2; ++n) _Pragma("unroll") for (int k = 0; k < 2; ++k) \
;         acc[ai][bj][m][n] = __builtin_amdgcn_mfma_f32_16x16x32_bf16(Bt[n][k], At[m][k], acc[ai][bj][m][n], 0, 0, 0); __builtin_amdgcn_s_setprio(0); } while (0)
; #define PG8_WAIT_V(n) asm volatile("s_waitcnt vmcnt(" #n ")" ::: "memory")
; #define PG8_WAIT_L(n) asm volatile("s_waitcnt lgkmcnt(" #n ")" ::: "memory")
; #define PG8_BAR __builtin_amdgcn_s_barrier()
; #define PG8_SCHED __builtin_amdgcn_sched_barrier(0)
; template <class Epi, class Sched, bool ALIGN_EPI = false, bool SP2 = false>
; __device__ __forceinline__ void gemm_phase(PG8_LAS unsigned char* lds, const Gemm g, const Sched& S, const Epi& E) {
;     ...
;             if constexpr (SP2) {
;             PG8_LDB(B0, 0, 0); PG8_LDB(B1, 0, 1); PG8_SCHED; PG8_LDA(At, 0, 0); PG8_STAGE_A(PG8_SA(1, 1), 1, a1, false);
;             PG8_WAIT_V(8); PG8_WAIT_L(0); PG8_BAR; PG8_MMA(0, 0, At, B0); PG8_MMA(0, 1, At, B1); PG8_BAR; PG8_SCHED;
;     ...
; #pragma unroll
;         for (int a = 0; a < 2; ++a)
; #pragma unroll
;             for (int b = 0; b < 2; ++b)
; #pragma unroll
;                 for (int m = 0; m < 4; ++m)
; #pragma unroll
;                     for (int n = 0; n < 2; ++n) acc[a][b][m][n] = (f32x4){0.f, 0.f, 0.f, 0.f};
.LBB13_240:
	s_ashr_i32 s19, s18, 31
	s_lshl_b64 s[2:3], s[18:19], 19
	s_add_u32 s20, s31, s2
	s_addc_u32 s21, s34, s3
	s_and_b64 s[2:3], s[6:7], exec
	s_cselect_b32 s2, s21, s13
	s_cselect_b32 s3, s20, s12
	s_ashr_i32 s17, s16, 31
	s_lshl_b64 s[22:23], s[16:17], 19
	s_add_u32 s22, s35, s22
	s_addc_u32 s23, s36, s23
	s_and_b64 s[26:27], s[6:7], exec
	s_cselect_b32 s9, s23, s25
	s_cselect_b32 s11, s22, s24
	s_add_u32 s12, s12, 0x40080
	s_addc_u32 s13, s13, 0
	s_add_u32 s17, s24, 0x100
	v_mov_b32_e32 v2, 0
	s_addc_u32 s19, s25, 0
	s_mov_b32 s38, -2
	v_mov_b32_e32 v3, v2
	v_mov_b64_e32 v[4:5], 0
	v_mov_b64_e32 v[6:7], 0
	v_mov_b64_e32 v[8:9], 0
	s_waitcnt vmcnt(0)
	v_mov_b64_e32 v[18:19], 0
	v_mov_b64_e32 v[20:21], 0
	v_mov_b64_e32 v[22:23], 0
	v_mov_b64_e32 v[24:25], 0
	v_mov_b64_e32 v[34:35], 0
	v_mov_b64_e32 v[36:37], 0
	v_mov_b64_e32 v[38:39], 0
	v_mov_b64_e32 v[40:41], 0
	v_mov_b64_e32 v[50:51], 0
	v_mov_b64_e32 v[52:53], 0
	v_mov_b64_e32 v[54:55], 0
	v_mov_b64_e32 v[56:57], 0
	v_mov_b64_e32 v[10:11], 0
	v_mov_b64_e32 v[12:13], 0
	v_mov_b64_e32 v[14:15], 0
	v_mov_b64_e32 v[16:17], 0
	v_mov_b64_e32 v[26:27], 0
	v_mov_b64_e32 v[28:29], 0
	v_mov_b64_e32 v[30:31], 0
	v_mov_b64_e32 v[32:33], 0
	v_mov_b64_e32 v[42:43], 0
	v_mov_b64_e32 v[44:45], 0
	v_mov_b64_e32 v[46:47], 0
	v_mov_b64_e32 v[48:49], 0
	v_mov_b64_e32 v[58:59], 0
	v_mov_b64_e32 v[60:61], 0
	v_mov_b64_e32 v[62:63], 0
	v_mov_b64_e32 v[64:65], 0
	v_mov_b64_e32 v[66:67], 0
	v_mov_b64_e32 v[68:69], 0
	v_mov_b64_e32 v[70:71], 0
	v_mov_b64_e32 v[72:73], 0
	v_mov_b64_e32 v[82:83], 0
	v_mov_b64_e32 v[84:85], 0
	v_mov_b64_e32 v[86:87], 0
	v_mov_b64_e32 v[88:89], 0
	v_mov_b64_e32 v[100:101], 0
	v_mov_b64_e32 v[102:103], 0
	v_mov_b64_e32 v[104:105], 0
	v_mov_b64_e32 v[106:107], 0
	v_mov_b64_e32 v[116:117], 0
	v_mov_b64_e32 v[118:119], 0
	v_mov_b64_e32 v[120:121], 0
	v_mov_b64_e32 v[122:123], 0
	v_mov_b64_e32 v[74:75], 0
	v_mov_b64_e32 v[76:77], 0
	v_mov_b64_e32 v[78:79], 0
	v_mov_b64_e32 v[80:81], 0
	v_mov_b64_e32 v[90:91], 0
	v_mov_b64_e32 v[92:93], 0
	v_mov_b64_e32 v[94:95], 0
	v_mov_b64_e32 v[96:97], 0
	v_mov_b64_e32 v[108:109], 0
	v_mov_b64_e32 v[110:111], 0
	v_mov_b64_e32 v[112:113], 0
	v_mov_b64_e32 v[114:115], 0
	v_mov_b64_e32 v[124:125], 0
	v_mov_b64_e32 v[126:127], 0
	v_mov_b64_e32 v[128:129], 0
	v_mov_b64_e32 v[130:131], 0
	s_and_b64 s[98:99], exec, s[14:15]
	s_cbranch_scc1 .Lrb_241
	s_barrier
.Lrb_241:
.LBB13_241:
	v_add_u32_e32 v160, s37, v99
	v_add_u32_e32 v173, s39, v99
	ds_read_b128 v[132:135], v160
	ds_read_b128 v[136:139], v160 offset:1024
	ds_read_b128 v[156:159], v160 offset:2048
	ds_read_b128 v[160:163], v160 offset:3072
	ds_read_b128 v[164:167], v173
	ds_read_b128 v[174:177], v173 offset:1024
	ds_read_b128 v[178:181], v173 offset:2048
	ds_read_b128 v[182:185], v173 offset:3072
	s_add_u32 s24, s12, 0xfffc0080
	s_addc_u32 s25, s13, -1
	s_cmp_eq_u32 s38, 12
	s_cselect_b32 s27, s2, s25
	s_cselect_b32 s26, s3, s24
	s_cselect_b32 s25, s9, s19
	s_cselect_b32 s24, s11, s17
	v_lshl_add_u64 v[198:199], s[12:13], 0, v[152:153]
	s_add_i32 m0, s47, 0xc000
	ds_read_b128 v[186:189], v172
	ds_read_b128 v[190:193], v172 offset:1024
	ds_read_b128 v[194:197], v172 offset:2048
	ds_read_b128 v[208:211], v172 offset:3072
	ds_read_b128 v[212:215], v172 offset:4096
	ds_read_b128 v[216:219], v172 offset:5120
	ds_read_b128 v[220:223], v172 offset:6144
	ds_read_b128 v[224:227], v172 offset:7168
	global_load_lds_dwordx4 v[198:199], off
	v_lshl_add_u64 v[198:199], s[12:13], 0, v[154:155]
	s_add_i32 m0, s47, 0xe000
	s_nop 0
	global_load_lds_dwordx4 v[198:199], off
	s_waitcnt vmcnt(8)
	s_waitcnt lgkmcnt(0)
	s_barrier
	s_setprio 1
	s_waitcnt lgkmcnt(0)
	v_mfma_f32_16x16x32_bf16 v[128:131], v[132:135], v[186:189], v[128:131]
	v_mfma_f32_16x16x32_bf16 v[124:127], v[156:159], v[186:189], v[124:127]
	v_mfma_f32_16x16x32_bf16 v[112:115], v[132:135], v[194:197], v[112:115]
	v_mfma_f32_16x16x32_bf16 v[108:111], v[156:159], v[194:197], v[108:111]
	v_mfma_f32_16x16x32_bf16 v[94:97], v[132:135], v[212:215], v[94:97]
	v_mfma_f32_16x16x32_bf16 v[90:93], v[156:159], v[212:215], v[90:93]
	v_mfma_f32_16x16x32_bf16 v[78:81], v[132:135], v[220:223], v[78:81]
	v_mfma_f32_16x16x32_bf16 v[74:77], v[156:159], v[220:223], v[74:77]
	v_mfma_f32_16x16x32_bf16 v[128:131], v[136:139], v[190:193], v[128:131]
	v_mfma_f32_16x16x32_bf16 v[124:127], v[160:163], v[190:193], v[124:127]
	v_mfma_f32_16x16x32_bf16 v[112:115], v[136:139], v[208:211], v[112:115]
	v_mfma_f32_16x16x32_bf16 v[108:111], v[160:163], v[208:211], v[108:111]
	v_mfma_f32_16x16x32_bf16 v[94:97], v[136:139], v[216:219], v[94:97]
	v_mfma_f32_16x16x32_bf16 v[90:93], v[160:163], v[216:219], v[90:93]
	v_mfma_f32_16x16x32_bf16 v[78:81], v[136:139], v[224:227], v[78:81]
	v_mfma_f32_16x16x32_bf16 v[74:77], v[160:163], v[224:227], v[74:77]
	s_setprio 0
	s_setprio 1
	v_mfma_f32_16x16x32_bf16 v[120:123], v[164:167], v[186:189], v[120:123]
	v_mfma_f32_16x16x32_bf16 v[116:119], v[178:181], v[186:189], v[116:119]
	v_mfma_f32_16x16x32_bf16 v[104:107], v[164:167], v[194:197], v[104:107]
	v_mfma_f32_16x16x32_bf16 v[100:103], v[178:181], v[194:197], v[100:103]
	v_mfma_f32_16x16x32_bf16 v[86:89], v[164:167], v[212:215], v[86:89]
	v_mfma_f32_16x16x32_bf16 v[82:85], v[178:181], v[212:215], v[82:85]
	v_mfma_f32_16x16x32_bf16 v[70:73], v[164:167], v[220:223], v[70:73]
	v_mfma_f32_16x16x32_bf16 v[66:69], v[178:181], v[220:223], v[66:69]
	v_mfma_f32_16x16x32_bf16 v[120:123], v[174:177], v[190:193], v[120:123]
	v_mfma_f32_16x16x32_bf16 v[116:119], v[182:185], v[190:193], v[116:119]
	v_mfma_f32_16x16x32_bf16 v[104:107], v[174:177], v[208:211], v[104:107]
	v_mfma_f32_16x16x32_bf16 v[100:103], v[182:185], v[208:211], v[100:103]
	v_mfma_f32_16x16x32_bf16 v[86:89], v[174:177], v[216:219], v[86:89]
	v_mfma_f32_16x16x32_bf16 v[82:85], v[182:185], v[216:219], v[82:85]
	v_mfma_f32_16x16x32_bf16 v[70:73], v[174:177], v[224:227], v[70:73]
	v_mfma_f32_16x16x32_bf16 v[66:69], v[182:185], v[224:227], v[66:69]
	s_setprio 0
	s_barrier
; #define PG8_STAGE_A(bufoff, h, ptr, nsel) do { if constexpr (Sched::GATHER) { if (nsel) PG8_STAGE_X(bufoff, ptr, vAn[h], PG8_A_AUX); else PG8_STAGE_X(bufoff, ptr, vAc[h], PG8_A_AUX); } \
;         else PG8_STAGE_X(bufoff, (ptr) + (h) * hstep, voffA, PG8_A_AUX); } while (0)
; #define PG8_STAGE(bufoff, gbase, voff) PG8_STAGE_X(bufoff, gbase, voff, PG8_B_AUX)
; #define PG8_LDA(dst, b, h) do { _Pragma("unroll") for (int m = 0; m < 4; ++m) _Pragma("unroll") for (int k = 0; k < 2; ++k) dst[m][k] = *(const PG8_LAS bf16x8*)(lds + PG8_SA(b, h) + aoff + m * 2048 + k * 1024); } while (0)
; #define PG8_LDB(dst, b, h) do { _Pragma("unroll") for (int n = 0; n < 2; ++n) _Pragma("unroll") for (int k = 0; k < 2; ++k) dst[n][k] = *(const PG8_LAS bf16x8*)(lds + PG8_SB(b, h) + boff + n * 2048 + k * 1024); } while (0)
; #define PG8_MMA(ai, bj, At, Bt) do { __builtin_amdgcn_s_setprio(1); _Pragma("unroll") for (int m = 0; m < 4; ++m) _Pragma("unroll") for (int n = 0; n < 2; ++n) _Pragma("unroll") for (int k = 0; k < 2; ++k) \
;         acc[ai][bj][m][n] = __builtin_amdgcn_mfma_f32_16x16x32_bf16(Bt[n][k], At[m][k], acc[ai][bj][m][n], 0, 0, 0); __builtin_amdgcn_s_setprio(0); } while (0)
; #define PG8_WAIT_V(n) asm volatile("s_waitcnt vmcnt(" #n ")" ::: "memory")
; #define PG8_WAIT_L(n) asm volatile("s_waitcnt lgkmcnt(" #n ")" ::: "memory")
; #define PG8_BAR __builtin_amdgcn_s_barrier()
; #define PG8_SCHED __builtin_amdgcn_sched_barrier(0)
; template <class Epi, class Sched, bool ALIGN_EPI = false, bool SP2 = false>
; __device__ __forceinline__ void gemm_phase(PG8_LAS unsigned char* lds, const Gemm g, const Sched& S, const Epi& E) {
;     ...
;             PG8_WAIT_V(8); PG8_WAIT_L(0); PG8_BAR; PG8_MMA(0, 0, At, B0); PG8_MMA(0, 1, At, B1); PG8_BAR; PG8_SCHED;
;             PG8_LDA(At, 0, 1); PG8_STAGE(PG8_SB(0, 0), b2, voffB); PG8_STAGE(PG8_SB(0, 1), b2 + hstep, voffB); PG8_STAGE_A(PG8_SA(0, 0), 0, a2, last);
;             PG8_WAIT_V(8); PG8_WAIT_L(0); PG8_BAR; PG8_MMA(1, 0, At, B0); PG8_MMA(1, 1, At, B1); PG8_BAR; PG8_SCHED;
;             PG8_LDB(B0, 1, 0); PG8_LDB(B1, 1, 1); PG8_SCHED; PG8_LDA(At, 1, 0); PG8_STAGE_A(PG8_SA(0, 1), 1, a2, last);
	s_add_i32 s48, s37, s40
	v_lshl_add_u64 v[198:199], s[24:25], 0, v[142:143]
	s_mov_b32 m0, s48
	ds_read_b128 v[186:189], v172 offset:16384
	ds_read_b128 v[190:193], v172 offset:17408
	ds_read_b128 v[194:197], v172 offset:18432
	ds_read_b128 v[208:211], v172 offset:19456
	ds_read_b128 v[212:215], v172 offset:20480
	ds_read_b128 v[216:219], v172 offset:21504
	ds_read_b128 v[220:223], v172 offset:22528
	ds_read_b128 v[224:227], v172 offset:23552
	global_load_lds_dwordx4 v[198:199], off
	s_add_i32 m0, s48, 0x2000
	s_add_u32 s48, s24, 0x40000
	v_lshl_add_u64 v[228:229], s[24:25], 0, v[146:147]
	s_addc_u32 s49, s25, 0
	s_add_i32 s52, s39, s40
	global_load_lds_dwordx4 v[228:229], off
	v_lshl_add_u64 v[230:231], s[48:49], 0, v[142:143]
	s_mov_b32 m0, s52
	v_lshl_add_u64 v[232:233], s[26:27], 0, v[144:145]
	global_load_lds_dwordx4 v[230:231], off
	v_lshl_add_u64 v[230:231], s[48:49], 0, v[146:147]
	s_add_i32 m0, s52, 0x2000
	s_nop 0
	global_load_lds_dwordx4 v[230:231], off
	v_lshl_add_u64 v[230:231], s[26:27], 0, v[140:141]
	s_mov_b32 m0, s47
	s_nop 0
	global_load_lds_dwordx4 v[230:231], off
	s_add_i32 m0, s47, 0x2000
	s_nop 0
	global_load_lds_dwordx4 v[232:233], off
	s_waitcnt vmcnt(8)
	s_waitcnt lgkmcnt(0)
	s_barrier
	s_setprio 1
	s_waitcnt lgkmcnt(0)
	v_mfma_f32_16x16x32_bf16 v[62:65], v[132:135], v[186:189], v[62:65]
	v_mfma_f32_16x16x32_bf16 v[58:61], v[156:159], v[186:189], v[58:61]
	v_mfma_f32_16x16x32_bf16 v[46:49], v[132:135], v[194:197], v[46:49]
	v_mfma_f32_16x16x32_bf16 v[42:45], v[156:159], v[194:197], v[42:45]
	v_mfma_f32_16x16x32_bf16 v[30:33], v[132:135], v[212:215], v[30:33]
	v_mfma_f32_16x16x32_bf16 v[26:29], v[156:159], v[212:215], v[26:29]
	v_mfma_f32_16x16x32_bf16 v[14:17], v[132:135], v[220:223], v[14:17]
	v_mfma_f32_16x16x32_bf16 v[10:13], v[156:159], v[220:223], v[10:13]
	v_mfma_f32_16x16x32_bf16 v[62:65], v[136:139], v[190:193], v[62:65]
	v_mfma_f32_16x16x32_bf16 v[58:61], v[160:163], v[190:193], v[58:61]
	v_mfma_f32_16x16x32_bf16 v[46:49], v[136:139], v[208:211], v[46:49]
	v_mfma_f32_16x16x32_bf16 v[42:45], v[160:163], v[208:211], v[42:45]
	v_mfma_f32_16x16x32_bf16 v[30:33], v[136:139], v[216:219], v[30:33]
	v_mfma_f32_16x16x32_bf16 v[26:29], v[160:163], v[216:219], v[26:29]
	v_mfma_f32_16x16x32_bf16 v[14:17], v[136:139], v[224:227], v[14:17]
	v_mfma_f32_16x16x32_bf16 v[10:13], v[160:163], v[224:227], v[10:13]
	s_setprio 0
	s_setprio 1
	v_mfma_f32_16x16x32_bf16 v[54:57], v[164:167], v[186:189], v[54:57]
	v_mfma_f32_16x16x32_bf16 v[50:53], v[178:181], v[186:189], v[50:53]
	v_mfma_f32_16x16x32_bf16 v[38:41], v[164:167], v[194:197], v[38:41]
	v_mfma_f32_16x16x32_bf16 v[34:37], v[178:181], v[194:197], v[34:37]
	v_mfma_f32_16x16x32_bf16 v[22:25], v[164:167], v[212:215], v[22:25]
	v_mfma_f32_16x16x32_bf16 v[18:21], v[178:181], v[212:215], v[18:21]
	v_mfma_f32_16x16x32_bf16 v[6:9], v[164:167], v[220:223], v[6:9]
	v_mfma_f32_16x16x32_bf16 v[2:5], v[178:181], v[220:223], v[2:5]
	v_mfma_f32_16x16x32_bf16 v[54:57], v[174:177], v[190:193], v[54:57]
	v_mfma_f32_16x16x32_bf16 v[50:53], v[182:185], v[190:193], v[50:53]
	v_mfma_f32_16x16x32_bf16 v[38:41], v[174:177], v[208:211], v[38:41]
	v_mfma_f32_16x16x32_bf16 v[34:37], v[182:185], v[208:211], v[34:37]
	v_mfma_f32_16x16x32_bf16 v[22:25], v[174:177], v[216:219], v[22:25]
	v_mfma_f32_16x16x32_bf16 v[18:21], v[182:185], v[216:219], v[18:21]
	v_mfma_f32_16x16x32_bf16 v[6:9], v[174:177], v[224:227], v[6:9]
	v_mfma_f32_16x16x32_bf16 v[2:5], v[182:185], v[224:227], v[2:5]
	s_setprio 0
	s_barrier
	v_add_u32_e32 v160, s41, v99
	v_add_u32_e32 v173, s42, v99
	ds_read_b128 v[132:135], v160
	ds_read_b128 v[136:139], v160 offset:1024
	ds_read_b128 v[156:159], v160 offset:2048
	ds_read_b128 v[160:163], v160 offset:3072
	ds_read_b128 v[164:167], v173
	ds_read_b128 v[174:177], v173 offset:1024
	ds_read_b128 v[178:181], v173 offset:2048
	ds_read_b128 v[182:185], v173 offset:3072
	s_add_u32 s26, s26, 0x40000
	s_addc_u32 s27, s27, 0
	v_lshl_add_u64 v[242:243], s[26:27], 0, v[140:141]
	s_add_i32 m0, s47, 0x4000
	ds_read_b128 v[186:189], v172 offset:32768
	ds_read_b128 v[190:193], v172 offset:33792
	ds_read_b128 v[194:197], v172 offset:34816
	ds_read_b128 v[208:211], v172 offset:35840
	ds_read_b128 v[212:215], v172 offset:36864
	ds_read_b128 v[216:219], v172 offset:37888
	ds_read_b128 v[220:223], v172 offset:38912
	ds_read_b128 v[224:227], v172 offset:39936
	global_load_lds_dwordx4 v[242:243], off
	v_lshl_add_u64 v[242:243], s[26:27], 0, v[144:145]
	s_add_i32 m0, s47, 0x6000
	s_nop 0
	global_load_lds_dwordx4 v[242:243], off
	s_waitcnt vmcnt(8)
	s_waitcnt lgkmcnt(0)
	s_barrier
; #define PG8_STAGE_A(bufoff, h, ptr, nsel) do { if constexpr (Sched::GATHER) { if (nsel) PG8_STAGE_X(bufoff, ptr, vAn[h], PG8_A_AUX); else PG8_STAGE_X(bufoff, ptr, vAc[h], PG8_A_AUX); } \
;         else PG8_STAGE_X(bufoff, (ptr) + (h) * hstep, voffA, PG8_A_AUX); } while (0)
; #define PG8_STAGE(bufoff, gbase, voff) PG8_STAGE_X(bufoff, gbase, voff, PG8_B_AUX)
; #define PG8_LDA(dst, b, h) do { _Pragma("unroll") for (int m = 0; m < 4; ++m) _Pragma("unroll") for (int k = 0; k < 2; ++k) dst[m][k] = *(const PG8_LAS bf16x8*)(lds + PG8_SA(b, h) + aoff + m * 2048 + k * 1024); } while (0)
; #define PG8_LDB(dst, b, h) do { _Pragma("unroll") for (int n = 0; n < 2; ++n) _Pragma("unroll") for (int k = 0; k < 2; ++k) dst[n][k] = *(const PG8_LAS bf16x8*)(lds + PG8_SB(b, h) + boff + n * 2048 + k * 1024); } while (0)
; #define PG8_MMA(ai, bj, At, Bt) do { __builtin_amdgcn_s_setprio(1); _Pragma("unroll") for (int m = 0; m < 4; ++m) _Pragma("unroll") for (int n = 0; n < 2; ++n) _Pragma("unroll") for (int k = 0; k < 2; ++k) \
;         acc[ai][bj][m][n] = __builtin_amdgcn_mfma_f32_16x16x32_bf16(Bt[n][k], At[m][k], acc[ai][bj][m][n], 0, 0, 0); __builtin_amdgcn_s_setprio(0); } while (0)
; #define PG8_WAIT_V(n) asm volatile("s_waitcnt vmcnt(" #n ")" ::: "memory")
; #define PG8_WAIT_L(n) asm volatile("s_waitcnt lgkmcnt(" #n ")" ::: "memory")
; #define PG8_BAR __builtin_amdgcn_s_barrier()
; #define PG8_SCHED __builtin_amdgcn_sched_barrier(0)
; template <class Epi, class Sched, bool ALIGN_EPI = false, bool SP2 = false>
; __device__ __forceinline__ void gemm_phase(PG8_LAS unsigned char* lds, const Gemm g, const Sched& S, const Epi& E) {
;     ...
;             PG8_WAIT_V(8); PG8_WAIT_L(0); PG8_BAR; PG8_MMA(1, 0, At, B0); PG8_MMA(1, 1, At, B1); PG8_BAR; PG8_SCHED;
;             PG8_LDB(B0, 1, 0); PG8_LDB(B1, 1, 1); PG8_SCHED; PG8_LDA(At, 1, 0); PG8_STAGE_A(PG8_SA(0, 1), 1, a2, last);
;             PG8_WAIT_V(8); PG8_WAIT_L(0); PG8_BAR; PG8_MMA(0, 0, At, B0); PG8_MMA(0, 1, At, B1); PG8_BAR; PG8_SCHED;
;             PG8_LDA(At, 1, 1); PG8_STAGE(PG8_SB(1, 0), b3, voffB); PG8_STAGE(PG8_SB(1, 1), b3 + hstep, voffB); PG8_STAGE_A(PG8_SA(1, 0), 0, a3, last);
;             PG8_WAIT_V(8); PG8_WAIT_L(0); PG8_BAR; PG8_MMA(1, 0, At, B0); PG8_MMA(1, 1, At, B1); PG8_BAR; PG8_SCHED;
;     ...
;         if constexpr (ALIGN_EPI) { if (wr == 0) PG8_BAR; }
	s_setprio 1
	s_waitcnt lgkmcnt(0)
	v_mfma_f32_16x16x32_bf16 v[128:131], v[132:135], v[186:189], v[128:131]
	v_mfma_f32_16x16x32_bf16 v[124:127], v[156:159], v[186:189], v[124:127]
	v_mfma_f32_16x16x32_bf16 v[112:115], v[132:135], v[194:197], v[112:115]
	v_mfma_f32_16x16x32_bf16 v[108:111], v[156:159], v[194:197], v[108:111]
	v_mfma_f32_16x16x32_bf16 v[94:97], v[132:135], v[212:215], v[94:97]
	v_mfma_f32_16x16x32_bf16 v[90:93], v[156:159], v[212:215], v[90:93]
	v_mfma_f32_16x16x32_bf16 v[78:81], v[132:135], v[220:223], v[78:81]
	v_mfma_f32_16x16x32_bf16 v[74:77], v[156:159], v[220:223], v[74:77]
	v_mfma_f32_16x16x32_bf16 v[128:131], v[136:139], v[190:193], v[128:131]
	v_mfma_f32_16x16x32_bf16 v[124:127], v[160:163], v[190:193], v[124:127]
	v_mfma_f32_16x16x32_bf16 v[112:115], v[136:139], v[208:211], v[112:115]
	v_mfma_f32_16x16x32_bf16 v[108:111], v[160:163], v[208:211], v[108:111]
	v_mfma_f32_16x16x32_bf16 v[94:97], v[136:139], v[216:219], v[94:97]
	v_mfma_f32_16x16x32_bf16 v[90:93], v[160:163], v[216:219], v[90:93]
	v_mfma_f32_16x16x32_bf16 v[78:81], v[136:139], v[224:227], v[78:81]
	v_mfma_f32_16x16x32_bf16 v[74:77], v[160:163], v[224:227], v[74:77]
	s_setprio 0
	s_setprio 1
	v_mfma_f32_16x16x32_bf16 v[120:123], v[164:167], v[186:189], v[120:123]
	v_mfma_f32_16x16x32_bf16 v[116:119], v[178:181], v[186:189], v[116:119]
	v_mfma_f32_16x16x32_bf16 v[104:107], v[164:167], v[194:197], v[104:107]
	v_mfma_f32_16x16x32_bf16 v[100:103], v[178:181], v[194:197], v[100:103]
	v_mfma_f32_16x16x32_bf16 v[86:89], v[164:167], v[212:215], v[86:89]
	v_mfma_f32_16x16x32_bf16 v[82:85], v[178:181], v[212:215], v[82:85]
	v_mfma_f32_16x16x32_bf16 v[70:73], v[164:167], v[220:223], v[70:73]
	v_mfma_f32_16x16x32_bf16 v[66:69], v[178:181], v[220:223], v[66:69]
	v_mfma_f32_16x16x32_bf16 v[120:123], v[174:177], v[190:193], v[120:123]
	v_mfma_f32_16x16x32_bf16 v[116:119], v[182:185], v[190:193], v[116:119]
	v_mfma_f32_16x16x32_bf16 v[104:107], v[174:177], v[208:211], v[104:107]
	v_mfma_f32_16x16x32_bf16 v[100:103], v[182:185], v[208:211], v[100:103]
	v_mfma_f32_16x16x32_bf16 v[86:89], v[174:177], v[216:219], v[86:89]
	v_mfma_f32_16x16x32_bf16 v[82:85], v[182:185], v[216:219], v[82:85]
	v_mfma_f32_16x16x32_bf16 v[70:73], v[174:177], v[224:227], v[70:73]
	v_mfma_f32_16x16x32_bf16 v[66:69], v[182:185], v[224:227], v[66:69]
	s_setprio 0
	s_barrier
	s_mov_b32 m0, s45
	v_lshl_add_u64 v[198:199], v[198:199], 0, s[54:55]
	s_add_u32 s24, s24, 0x40080
	ds_read_b128 v[186:189], v172 offset:49152
	ds_read_b128 v[190:193], v172 offset:50176
	ds_read_b128 v[194:197], v172 offset:51200
	ds_read_b128 v[208:211], v172 offset:52224
	ds_read_b128 v[212:215], v172 offset:53248
	ds_read_b128 v[216:219], v172 offset:54272
	ds_read_b128 v[220:223], v172 offset:55296
	ds_read_b128 v[224:227], v172 offset:56320
	global_load_lds_dwordx4 v[198:199], off
	v_lshl_add_u64 v[198:199], v[228:229], 0, s[54:55]
	s_mov_b32 m0, s46
	s_addc_u32 s25, s25, 0
	global_load_lds_dwordx4 v[198:199], off
	v_lshl_add_u64 v[198:199], s[24:25], 0, v[142:143]
	s_mov_b32 m0, s56
	s_nop 0
	global_load_lds_dwordx4 v[198:199], off
	v_lshl_add_u64 v[198:199], s[24:25], 0, v[146:147]
	s_mov_b32 m0, s57
	s_nop 0
	global_load_lds_dwordx4 v[198:199], off
	v_lshl_add_u64 v[198:199], v[230:231], 0, s[54:55]
	s_mov_b32 m0, s50
	s_nop 0
	global_load_lds_dwordx4 v[198:199], off
	v_lshl_add_u64 v[198:199], v[232:233], 0, s[54:55]
	s_mov_b32 m0, s51
	s_nop 0
	global_load_lds_dwordx4 v[198:199], off
	s_waitcnt vmcnt(8)
	s_waitcnt lgkmcnt(0)
	s_barrier
	s_setprio 1
	s_waitcnt lgkmcnt(0)
	v_mfma_f32_16x16x32_bf16 v[62:65], v[132:135], v[186:189], v[62:65]
	v_mfma_f32_16x16x32_bf16 v[58:61], v[156:159], v[186:189], v[58:61]
	v_mfma_f32_16x16x32_bf16 v[46:49], v[132:135], v[194:197], v[46:49]
	v_mfma_f32_16x16x32_bf16 v[42:45], v[156:159], v[194:197], v[42:45]
	v_mfma_f32_16x16x32_bf16 v[30:33], v[132:135], v[212:215], v[30:33]
	v_mfma_f32_16x16x32_bf16 v[26:29], v[156:159], v[212:215], v[26:29]
	v_mfma_f32_16x16x32_bf16 v[14:17], v[132:135], v[220:223], v[14:17]
	v_mfma_f32_16x16x32_bf16 v[10:13], v[156:159], v[220:223], v[10:13]
	v_mfma_f32_16x16x32_bf16 v[62:65], v[136:139], v[190:193], v[62:65]
	v_mfma_f32_16x16x32_bf16 v[58:61], v[160:163], v[190:193], v[58:61]
	v_mfma_f32_16x16x32_bf16 v[46:49], v[136:139], v[208:211], v[46:49]
	v_mfma_f32_16x16x32_bf16 v[42:45], v[160:163], v[208:211], v[42:45]
	v_mfma_f32_16x16x32_bf16 v[30:33], v[136:139], v[216:219], v[30:33]
	v_mfma_f32_16x16x32_bf16 v[26:29], v[160:163], v[216:219], v[26:29]
	v_mfma_f32_16x16x32_bf16 v[14:17], v[136:139], v[224:227], v[14:17]
	v_mfma_f32_16x16x32_bf16 v[10:13], v[160:163], v[224:227], v[10:13]
	s_setprio 0
	s_setprio 1
	v_mfma_f32_16x16x32_bf16 v[54:57], v[164:167], v[186:189], v[54:57]
	v_mfma_f32_16x16x32_bf16 v[50:53], v[178:181], v[186:189], v[50:53]
	v_mfma_f32_16x16x32_bf16 v[38:41], v[164:167], v[194:197], v[38:41]
	v_mfma_f32_16x16x32_bf16 v[34:37], v[178:181], v[194:197], v[34:37]
	v_mfma_f32_16x16x32_bf16 v[22:25], v[164:167], v[212:215], v[22:25]
	v_mfma_f32_16x16x32_bf16 v[18:21], v[178:181], v[212:215], v[18:21]
	v_mfma_f32_16x16x32_bf16 v[6:9], v[164:167], v[220:223], v[6:9]
	v_mfma_f32_16x16x32_bf16 v[2:5], v[178:181], v[220:223], v[2:5]
	v_mfma_f32_16x16x32_bf16 v[54:57], v[174:177], v[190:193], v[54:57]
	v_mfma_f32_16x16x32_bf16 v[50:53], v[182:185], v[190:193], v[50:53]
	v_mfma_f32_16x16x32_bf16 v[38:41], v[174:177], v[208:211], v[38:41]
	v_mfma_f32_16x16x32_bf16 v[34:37], v[182:185], v[208:211], v[34:37]
	v_mfma_f32_16x16x32_bf16 v[22:25], v[174:177], v[216:219], v[22:25]
	v_mfma_f32_16x16x32_bf16 v[18:21], v[182:185], v[216:219], v[18:21]
	v_mfma_f32_16x16x32_bf16 v[6:9], v[174:177], v[224:227], v[6:9]
	v_mfma_f32_16x16x32_bf16 v[2:5], v[182:185], v[224:227], v[2:5]
	s_setprio 0
	s_barrier
	s_add_i32 s38, s38, 2
	s_add_u32 s12, s12, 0x100
	s_addc_u32 s13, s13, 0
	s_add_u32 s17, s17, 0x100
	s_addc_u32 s19, s19, 0
	s_cmp_gt_u32 s38, 13
	s_cbranch_scc0 .LBB13_241
	s_and_b64 vcc, exec, s[14:15]
	s_cbranch_vccz .LBB13_244
	s_barrier

; __device__ __forceinline__ unsigned pk2(float lo, float hi) { f32x2 v = {lo, hi}; return __builtin_bit_cast(unsigned, __builtin_convertvector(v, bf2_t)); }
; template <int BIT = 0> __device__ __forceinline__ void st16w(void* p, u32x4 v) { if ((WT_STORES >> BIT) & 1) asm volatile("global_store_dwordx4 %0, %1, off sc1\n\ts_nop 1" :: "v"(p), "v"(v) : "memory"); else *(u32x4*)p = v; }
; #define PG8_LAS __attribute__((address_space(3)))
; #define PG8_BAR __builtin_amdgcn_s_barrier()
;     __device__ __forceinline__ void operator()(const f32x4 (&acc)[2][2][4][2], const Unit& u, int wr, int wc, int fr, int fq) const {
;     ...
;                     u32x4 w; w.x = pk2(v0[0], v0[1]); w.y = pk2(v0[2], v0[3]); w.z = pk2(v1[0], v1[1]); w.w = pk2(v1[2], v1[3]);
;                     st16w(rowp + bj * HALF, w);
; template <class Epi, class Sched, bool ALIGN_EPI = false, bool SP2 = false>
; __device__ __forceinline__ void gemm_phase(PG8_LAS unsigned char* lds, const Gemm g, const Sched& S, const Epi& E) {
;     ...
;         if constexpr (!Epi::AFTER_DRAIN) { E(acc, cur, wr, wc, fr, fq); S.done(cur); }
;         if (!has_next) break;
; #pragma unroll
;         for (int a = 0; a < 2; ++a)
; #pragma unroll
;             for (int b = 0; b < 2; ++b)
; #pragma unroll
;                 for (int m = 0; m < 4; ++m)
; #pragma unroll
;                     for (int n = 0; n < 2; ++n) acc[a][b][m][n] = (f32x4){0.f, 0.f, 0.f, 0.f};
;         cur = nxt; cA = nA; cB = nB; ++ui;
;         if constexpr (Sched::GATHER) { const u32x4 pv_ = *(const PG8_LAS u32x4*)(lds + STAGE_BYTES + tid * 16); vAc[0][0] = pv_.x; vAc[0][1] = pv_.y; vAc[1][0] = pv_.z; vAc[1][1] = pv_.w; }
;         if constexpr (ALIGN_EPI) { if (wr == 1) PG8_BAR; }
.LBB13_405:
	v_cvt_pk_bf16_f32 v2, v12, v13
	v_cvt_pk_bf16_f32 v3, v16, v17
	v_cvt_pk_bf16_f32 v4, v14, v15
	v_cvt_pk_bf16_f32 v5, v26, v27
	s_andn2_b64 vcc, exec, s[6:7]
	s_mov_b64 s[6:7], -1
	global_store_dwordx4 v[10:11], v[2:5], off offset:256
	s_cbranch_vccnz .LBB13_233
	s_andn2_b64 vcc, exec, s[0:1]
	s_cbranch_vccnz .LBB13_232
	s_branch .LBB13_232

; template <class Epi, class Sched, bool ALIGN_EPI = false, bool SP2 = false>
; __device__ __forceinline__ void gemm_phase(PG8_LAS unsigned char* lds, const Gemm g, const Sched& S, const Epi& E) {
;     ...
;     const int tid = tid_, wid = __builtin_amdgcn_readfirstlane(tid >> 6), lane = tid & 63, wr = wid >> 2, wc = wid & 3, fr = lane & 15, fq = lane >> 4;
;     const int K = g.K, nt = K / BK;
;     unsigned voffA[2], voffB[2];
; #pragma unroll
;     for (int i = 0; i < 2; ++i) { int R, C; stage_rc(tid * 16 + i * 8192, R, C); const int Rb = Epi::PERM ? ((R & ~31) + perm32(R & 31)) : R;
;         voffA[i] = (unsigned)(R * K + C) * 2u; voffB[i] = (unsigned)(Rb * K + C) * 2u; }
;     unsigned vAc[2][2] = {{0u, 0u}, {0u, 0u}}, vAn[2][2] = {{0u, 0u}, {0u, 0u}};
;     ...
;     const size_t kstep = (size_t)(BK * 2);
;     const size_t hstep = (size_t)HALF * K * 2;
;     const size_t tstep = 2 * hstep;
;     const unsigned ldsw = (unsigned)wid * 1024u;
;     const int aoff = lds_byte(wr * 64 + fr, fq * 8), boff = lds_byte(wc * 32 + fr, fq * 8);
;     ...
;     Unit cur, nxt; int ui = 0;
;     if (!S.next(0, cur)) return;
;     f32x4 acc[2][2][4][2];
; #pragma unroll
;     for (int a = 0; a < 2; ++a)
; #pragma unroll
;         for (int b = 0; b < 2; ++b)
; #pragma unroll
;             for (int m = 0; m < 4; ++m)
; #pragma unroll
;                 for (int n = 0; n < 2; ++n) acc[a][b][m][n] = (f32x4){0.f, 0.f, 0.f, 0.f};
;     bf16x8 At[4][2], B0[2][2], B1[2][2];
;     const char* cA = Sched::GATHER ? (const char*)g.A : (const char*)g.A + (size_t)cur.pm * tstep; PG8_SETA(vAc, cur); const char* cB = (const char*)g.Bt + S.boff(cur) + (size_t)cur.pn * tstep;
;     S.a_ready(cur);
;     if constexpr (SP2) {
;         PG8_STAGE(PG8_SB(0, 0), cB, voffB); PG8_STAGE(PG8_SB(0, 1), cB + hstep, voffB); PG8_STAGE_A(PG8_SA(0, 0), 0, cA, false); PG8_STAGE_A(PG8_SA(0, 1), 1, cA, false);
; __global__ void __launch_bounds__(NWAVES * 64, 2) mk_fwd(Args args) {
;     ...
;             pg8::StaticOrder S; S.init(ML, D, F.G, F.bx);
;             { pg8::Gemm g{(const bf16*)(ws + (MERGE_REC_FIRST ? WS_RECG : WS_ATT)), WO + (MERGE_REC_FIRST ? (size_t)D * D : 0), ML, D, D}; pg8::EpiMerge E{(const bf16*)(ws + WS_P), (bf16*)(ws + WS_T1), (bf16*)(ws + WS_MM), 0, MERGE_REC_FIRST ? OFF_GR : OFF_GA};
;               pg8::gemm_phase<pg8::EpiMerge, pg8::StaticOrder, true, true>(ring, g, S, E); }
.LBB13_809:
	s_waitcnt vmcnt(0)
	v_mov_b64_e32 v[2:3], s[4:5]
	v_readlane_b32 s4, v249, 1
	v_readlane_b32 s5, v249, 2
	s_load_dwordx2 s[4:5], s[4:5], 0xe8
	v_add_u32_e64 v8, 0, s1
	s_cmpk_lt_i32 s35, 0x100
	s_cselect_b64 s[10:11], -1, 0
	s_ashr_i32 s44, s30, 31
	s_waitcnt lgkmcnt(0)
	v_lshl_add_u64 v[2:3], s[4:5], 0, v[2:3]
	v_lshl_add_u64 v[4:5], s[76:77], 1, v[2:3]
	s_mov_b64 s[4:5], 0x3c00000
	v_lshl_add_u64 v[6:7], v[4:5], 0, s[4:5]
	s_mov_b64 s[4:5], 0x2ff00000
	v_readfirstlane_b32 s42, v6
	v_readfirstlane_b32 s43, v7
	v_lshl_add_u64 v[6:7], v[2:3], 0, s[4:5]
	s_mov_b64 s[4:5], 0x3e00000
	v_lshl_add_u64 v[4:5], v[4:5], 0, s[4:5]
	s_mov_b64 s[4:5], 0x22800000
	v_lshl_add_u64 v[132:133], v[2:3], 0, s[4:5]
	s_mov_b64 s[4:5], 0x32000000
	v_readfirstlane_b32 s3, v2
	v_lshl_add_u64 v[134:135], v[2:3], 0, s[4:5]
	v_add_u32_e32 v2, 0x10000, v8
	s_ashr_i32 s45, s35, 31
	v_readfirstlane_b32 s46, v2
	v_add_u32_e32 v2, 0x14000, v8
	s_cmp_lt_i32 s2, 0
	v_readfirstlane_b32 s47, v2
	v_add_u32_e32 v2, 0x18000, v8
	s_cselect_b64 s[8:9], -1, 0
	s_lshl_b32 s1, s2, 5
	v_readfirstlane_b32 s50, v2
	v_add_u32_e32 v2, 0x1c000, v8
	v_mov_b32_e32 v16, v0
	v_readfirstlane_b32 s48, v3
	v_readfirstlane_b32 s36, v8
	v_readfirstlane_b32 s37, v6
	v_readfirstlane_b32 s39, v7
	v_readfirstlane_b32 s40, v4
	v_readfirstlane_b32 s41, v5
	s_cmpk_gt_i32 s35, 0xff
	v_readfirstlane_b32 s51, v2
	s_mul_i32 s2, s2, 33
	s_nop 0
	v_readfirstlane_b32 s5, v16
	s_cbranch_scc1 .LBB13_829
	v_lshlrev_b32_e32 v2, 4, v16
	v_add_u32_e32 v3, 0x2000, v2
	v_ashrrev_i32_e32 v4, 31, v3
	v_lshrrev_b32_e32 v4, 22, v4
	v_add_u32_e32 v4, v3, v4
	v_ashrrev_i32_e32 v10, 10, v4
	v_mul_i32_i24_e32 v4, 0x400, v10
	v_sub_u32_e32 v3, v3, v4
	v_lshrrev_b32_e32 v4, 4, v3
	v_bitop3_b32 v3, v4, v3, 32 bitop3:0x6c
	v_ashrrev_i32_e32 v4, 31, v3
	v_lshrrev_b32_e32 v4, 26, v4
	v_add_u32_e32 v4, v3, v4
	v_lshlrev_b32_e32 v5, 3, v10
	v_ashrrev_i32_e32 v11, 6, v4
	v_and_b32_e32 v5, -16, v5
	v_add_u32_e32 v5, v11, v5
	v_and_b32_e32 v6, 3, v11
	s_mov_b32 s4, 0x1fffe0
	v_lshrrev_b32_e32 v7, 2, v5
	v_lshlrev_b32_e32 v8, 1, v5
	v_and_b32_e32 v4, 0xc0, v4
	v_and_or_b32 v6, v5, s4, v6
	v_and_b32_e32 v7, 4, v7
	v_and_b32_e32 v8, 24, v8
	v_sub_u32_e32 v3, v3, v4
	v_or3_b32 v6, v6, v7, v8
	v_lshlrev_b32_e32 v7, 5, v10
	v_ashrrev_i16_sdwa v3, v238, sext(v3) dst_sel:DWORD dst_unused:UNUSED_PAD src0_sel:DWORD src1_sel:BYTE_0
	v_and_b32_e32 v7, 32, v7
	v_bfe_i32 v12, v3, 0, 16
	v_add_lshl_u32 v3, v7, v12, 1
	v_lshl_add_u32 v136, v6, 11, v3
	v_lshl_add_u32 v138, v5, 11, v3
	v_bfe_i32 v3, v16, 27, 1
	v_lshrrev_b32_e32 v3, 22, v3
	v_add_u32_e32 v3, v2, v3
	v_and_b32_e32 v3, 0xfffffc00, v3
	v_sub_u32_e32 v2, v2, v3
	v_lshrrev_b32_e32 v3, 4, v2
	v_ashrrev_i32_e32 v4, 31, v16
	v_bitop3_b32 v2, v3, v2, 32 bitop3:0x6c
	v_lshrrev_b32_e32 v4, 26, v4
	v_ashrrev_i32_e32 v3, 31, v2
	v_add_u32_e32 v4, v16, v4
	v_lshrrev_b32_e32 v3, 26, v3
	v_ashrrev_i32_e32 v14, 6, v4
	s_ashr_i32 s13, s5, 6
	v_add_u32_e32 v3, v2, v3
	v_lshlrev_b32_e32 v4, 3, v14
	s_ashr_i32 s14, s5, 8
	s_lshl_b32 s12, s13, 10
	v_ashrrev_i32_e32 v13, 6, v3
	v_and_b32_e32 v4, -16, v4
	v_add_u32_e32 v4, v13, v4
	v_and_b32_e32 v5, 3, v13
	s_and_b64 s[6:7], s[8:9], exec
	v_and_or_b32 v5, v4, s4, v5
	s_cselect_b32 s4, s2, s1
	s_add_i32 s4, s4, s0
	s_ashr_i32 s6, s4, 31
	s_lshr_b32 s6, s6, 28
	s_add_i32 s6, s4, s6
	s_ashr_i32 s7, s6, 4
	s_and_b32 s6, s6, 0xfff0
	s_sub_i32 s6, s4, s6
	s_bfe_i32 s4, s6, 0x80000
	s_bfe_u32 s4, s4, 0x2000d
	s_add_i32 s15, s6, s4
	s_bfe_i32 s4, s15, 0x80000
	s_and_b32 s15, s15, 0xfc
	s_sub_i32 s6, s6, s15
	s_lshl_b32 s7, s7, 2
	s_sext_i32_i16 s4, s4
	s_sext_i32_i8 s6, s6
	s_lshr_b32 s4, s4, 2
	s_add_i32 s22, s7, s6
	s_ashr_i32 s23, s22, 31
	s_bfe_i64 s[16:17], s[4:5], 0x100000
	s_lshl_b64 s[6:7], s[22:23], 19
	s_lshl_b64 s[16:17], s[16:17], 19
	v_lshrrev_b32_e32 v6, 2, v4
	v_lshlrev_b32_e32 v7, 1, v4
	v_and_b32_e32 v3, 0xc0, v3
	s_add_u32 s26, s40, s16
	v_and_b32_e32 v6, 4, v6
	v_and_b32_e32 v7, 24, v7
	v_sub_u32_e32 v2, v2, v3
	s_addc_u32 s27, s41, s17
	s_add_i32 s49, s46, s12
	v_or3_b32 v5, v5, v6, v7
	v_lshlrev_b32_e32 v6, 5, v14
	v_ashrrev_i16_sdwa v2, v238, sext(v2) dst_sel:DWORD dst_unused:UNUSED_PAD src0_sel:DWORD src1_sel:BYTE_0
	s_add_i32 s53, s49, 0x2000
	v_and_b32_e32 v6, 32, v6
	v_bfe_i32 v15, v2, 0, 16
	s_add_u32 s16, s26, 0x40000
	v_add_lshl_u32 v2, v6, v15, 1
	s_addc_u32 s17, s27, 0
	s_add_i32 s56, s47, s12
	v_lshl_add_u32 v140, v5, 11, v2
	s_mov_b32 m0, s49
	s_add_i32 s57, s56, 0x2000
	global_load_lds_dwordx4 v140, s[26:27]
	s_mov_b32 m0, s53
	s_add_u32 s24, s37, s6
	global_load_lds_dwordx4 v136, s[26:27]
	s_mov_b32 m0, s56
	s_addc_u32 s25, s39, s7
	s_add_i32 s58, s36, s12
	global_load_lds_dwordx4 v140, s[16:17]
	s_mov_b32 m0, s57
	s_add_i32 s59, s58, 0x2000
	v_lshl_add_u32 v142, v4, 11, v2
	global_load_lds_dwordx4 v136, s[16:17]
	s_mov_b32 m0, s58
	s_add_u32 s6, s24, 0x40000
	global_load_lds_dwordx4 v142, s[24:25]
	s_mov_b32 m0, s59
	s_addc_u32 s7, s25, 0
	s_add_i32 s61, s58, 0x4000
	global_load_lds_dwordx4 v138, s[24:25]
	s_mov_b32 m0, s61
	s_add_i32 s68, s58, 0x6000
	global_load_lds_dwordx4 v142, s[6:7]
	s_mov_b32 m0, s68
	v_mov_b32_e32 v141, v98
	global_load_lds_dwordx4 v138, s[6:7]
	v_mov_b32_e32 v137, v98
	v_mov_b32_e32 v143, v98
	v_mov_b32_e32 v139, v98
	s_cmp_eq_u32 s14, 1
	v_lshl_add_u64 v[8:9], s[26:27], 0, v[140:141]
	v_lshl_add_u64 v[6:7], s[26:27], 0, v[136:137]
	v_lshl_add_u64 v[2:3], s[24:25], 0, v[142:143]
	s_cselect_b64 s[6:7], -1, 0
	s_cmp_lg_u32 s14, 1
	v_lshl_add_u64 v[4:5], s[24:25], 0, v[138:139]
	v_writelane_b32 v249, s94, 61
	s_cbranch_scc1 .LBB13_812
;     __device__ __forceinline__ size_t boff(const Unit& u) const { return (size_t)__builtin_amdgcn_readfirstlane(panel_e[u.pm]) * estride; }
; #define PG8_STAGE_A(bufoff, h, ptr, nsel) do { if constexpr (Sched::GATHER) { if (nsel) PG8_STAGE_X(bufoff, ptr, vAn[h], PG8_A_AUX); else PG8_STAGE_X(bufoff, ptr, vAc[h], PG8_A_AUX); } \
;         else PG8_STAGE_X(bufoff, (ptr) + (h) * hstep, voffA, PG8_A_AUX); } while (0)
; #define PG8_STAGE(bufoff, gbase, voff) PG8_STAGE_X(bufoff, gbase, voff, PG8_B_AUX)
; #define PG8_WAIT_V(n) asm volatile("s_waitcnt vmcnt(" #n ")" ::: "memory")
; #define PG8_BAR __builtin_amdgcn_s_barrier()
; template <class Epi, class Sched, bool ALIGN_EPI = false, bool SP2 = false>
; __device__ __forceinline__ void gemm_phase(PG8_LAS unsigned char* lds, const Gemm g, const Sched& S, const Epi& E) {
;     ...
;     const unsigned ldsw = (unsigned)wid * 1024u;
;     const int aoff = lds_byte(wr * 64 + fr, fq * 8), boff = lds_byte(wc * 32 + fr, fq * 8);
;     ...
;         if (wr == 1) PG8_BAR;
;         PG8_WAIT_V(2); PG8_BAR;
;         PG8_STAGE(PG8_SB(1, 0), cB + kstep, voffB); PG8_STAGE_A(PG8_SA(1, 0), 0, cA + kstep, false); PG8_STAGE(PG8_SB(1, 1), cB + hstep + kstep, voffB);
;         PG8_WAIT_V(6); PG8_BAR;
.LBB13_812:
	v_lshrrev_b32_e32 v18, 1, v16
	v_and_b32_e32 v18, 24, v18
	v_and_b32_e32 v17, 15, v16
	v_lshlrev_b32_e32 v19, 1, v18
	v_lshlrev_b32_e32 v16, 2, v16
	s_sext_i32_i8 s23, s4
	v_lshl_or_b32 v99, s14, 6, v17
	v_lshl_or_b32 v17, v17, 6, v19
	s_lshl_b32 s4, s14, 13
	v_and_b32_e32 v16, 32, v16
	v_bitop3_b32 v19, v17, s4, v16 bitop3:0xde
	s_lshl_b32 s4, s13, 5
	s_add_i32 s69, s50, s12
	s_and_b32 s4, s4, 0x60
	v_lshl_add_u64 v[8:9], v[8:9], 0, s[54:55]
	s_mov_b32 m0, s69
	s_add_i32 s88, s69, 0x2000
	s_lshl_b32 s13, s4, 7
	s_waitcnt vmcnt(2)
	s_barrier
	global_load_lds_dwordx4 v[8:9], off
	v_lshl_add_u64 v[6:7], v[6:7], 0, s[54:55]
	s_mov_b32 m0, s88
	s_add_i32 s89, s58, 0x8000
	s_add_i32 s94, s58, 0xa000
	global_load_lds_dwordx4 v[6:7], off
	v_lshl_add_u64 v[2:3], v[2:3], 0, s[54:55]
	s_mov_b32 m0, s89
	s_add_u32 s14, s26, 0x40080
	global_load_lds_dwordx4 v[2:3], off
	v_lshl_add_u64 v[2:3], v[4:5], 0, s[54:55]
	s_mov_b32 m0, s94
	s_addc_u32 s15, s27, 0
	s_add_i32 s38, s51, s12
	global_load_lds_dwordx4 v[2:3], off
	v_lshl_add_u64 v[2:3], s[14:15], 0, v[140:141]
	s_mov_b32 m0, s38
	s_add_i32 s95, s38, 0x2000
	global_load_lds_dwordx4 v[2:3], off
	v_lshl_add_u64 v[2:3], s[14:15], 0, v[136:137]
	s_mov_b32 m0, s95
	s_cmpk_lt_u32 s5, 0x100
	global_load_lds_dwordx4 v[2:3], off
	v_lshlrev_b32_e32 v2, 14, v14
	v_and_b32_e32 v2, 0xffff8000, v2
	v_lshl_add_u32 v2, v13, 11, v2
	v_and_b32_e32 v3, 1, v14
	v_lshl_or_b32 v2, v3, 6, v2
	v_lshl_add_u32 v144, v15, 1, v2
	v_lshlrev_b32_e32 v2, 14, v10
	v_and_b32_e32 v2, 0xffff8000, v2
	s_waitcnt vmcnt(6)
	v_lshl_add_u32 v2, v11, 11, v2
	v_and_b32_e32 v3, 1, v10
	v_lshl_or_b32 v2, v3, 6, v2
	v_bitop3_b32 v152, v17, s13, v16 bitop3:0xde
	s_cselect_b64 s[14:15], -1, 0
	v_or_b32_e32 v153, s4, v18
	v_mov_b32_e32 v145, v98
	v_lshl_add_u32 v146, v12, 1, v2
	v_mov_b32_e32 v147, v98
	s_mov_b32 s34, 0
	v_add_u32_e32 v154, s36, v19
	s_barrier
	s_branch .LBB13_815

; #define PG8_STAGE_A(bufoff, h, ptr, nsel) do { if constexpr (Sched::GATHER) { if (nsel) PG8_STAGE_X(bufoff, ptr, vAn[h], PG8_A_AUX); else PG8_STAGE_X(bufoff, ptr, vAc[h], PG8_A_AUX); } \
;         else PG8_STAGE_X(bufoff, (ptr) + (h) * hstep, voffA, PG8_A_AUX); } while (0)
; #define PG8_LDA(dst, b, h) do { _Pragma("unroll") for (int m = 0; m < 4; ++m) _Pragma("unroll") for (int k = 0; k < 2; ++k) dst[m][k] = *(const PG8_LAS bf16x8*)(lds + PG8_SA(b, h) + aoff + m * 2048 + k * 1024); } while (0)
; #define PG8_LDB(dst, b, h) do { _Pragma("unroll") for (int n = 0; n < 2; ++n) _Pragma("unroll") for (int k = 0; k < 2; ++k) dst[n][k] = *(const PG8_LAS bf16x8*)(lds + PG8_SB(b, h) + boff + n * 2048 + k * 1024); } while (0)
; #define PG8_MMA(ai, bj, At, Bt) do { __builtin_amdgcn_s_setprio(1); _Pragma("unroll") for (int m = 0; m < 4; ++m) _Pragma("unroll") for (int n = 0; n < 2; ++n) _Pragma("unroll") for (int k = 0; k < 2; ++k) \
;         acc[ai][bj][m][n] = __builtin_amdgcn_mfma_f32_16x16x32_bf16(Bt[n][k], At[m][k], acc[ai][bj][m][n], 0, 0, 0); __builtin_amdgcn_s_setprio(0); } while (0)
; #define PG8_WAIT_V(n) asm volatile("s_waitcnt vmcnt(" #n ")" ::: "memory")
; #define PG8_WAIT_L(n) asm volatile("s_waitcnt lgkmcnt(" #n ")" ::: "memory")
; #define PG8_BAR __builtin_amdgcn_s_barrier()
; #define PG8_SCHED __builtin_amdgcn_sched_barrier(0)
; template <class Epi, class Sched, bool ALIGN_EPI = false, bool SP2 = false>
; __device__ __forceinline__ void gemm_phase(PG8_LAS unsigned char* lds, const Gemm g, const Sched& S, const Epi& E) {
;     ...
;             if constexpr (SP2) {
;             PG8_LDB(B0, 0, 0); PG8_LDB(B1, 0, 1); PG8_SCHED; PG8_LDA(At, 0, 0); PG8_STAGE_A(PG8_SA(1, 1), 1, a1, false);
;             PG8_WAIT_V(8); PG8_WAIT_L(0); PG8_BAR; PG8_MMA(0, 0, At, B0); PG8_MMA(0, 1, At, B1); PG8_BAR; PG8_SCHED;
;     ...
; #pragma unroll
;         for (int a = 0; a < 2; ++a)
; #pragma unroll
;             for (int b = 0; b < 2; ++b)
; #pragma unroll
;                 for (int m = 0; m < 4; ++m)
; #pragma unroll
;                     for (int n = 0; n < 2; ++n) acc[a][b][m][n] = (f32x4){0.f, 0.f, 0.f, 0.f};
.LBB13_821:
	s_ashr_i32 s17, s16, 31
	s_lshl_b64 s[18:19], s[16:17], 19
	s_add_u32 s18, s37, s18
	s_addc_u32 s19, s39, s19
	s_and_b64 s[20:21], s[4:5], exec
	s_cselect_b32 s17, s19, s25
	s_cselect_b32 s52, s18, s24
	s_ashr_i32 s13, s12, 31
	s_lshl_b64 s[20:21], s[12:13], 19
	s_add_u32 s20, s40, s20
	s_addc_u32 s21, s41, s21
	s_and_b64 s[28:29], s[4:5], exec
	s_cselect_b32 s13, s21, s27
	s_cselect_b32 s60, s20, s26
	s_add_u32 s24, s24, 0x40080
	s_addc_u32 s25, s25, 0
	s_add_u32 s64, s26, 0x100
	v_mov_b32_e32 v2, 0
	s_addc_u32 s72, s27, 0
	s_mov_b32 s73, -2
	v_mov_b32_e32 v3, v2
	v_mov_b64_e32 v[4:5], 0
	v_mov_b64_e32 v[6:7], 0
	v_mov_b64_e32 v[8:9], 0
	v_mov_b64_e32 v[18:19], 0
	v_mov_b64_e32 v[20:21], 0
	v_mov_b64_e32 v[22:23], 0
	v_mov_b64_e32 v[24:25], 0
	v_mov_b64_e32 v[34:35], 0
	v_mov_b64_e32 v[36:37], 0
	v_mov_b64_e32 v[38:39], 0
	v_mov_b64_e32 v[40:41], 0
	v_mov_b64_e32 v[50:51], 0
	v_mov_b64_e32 v[52:53], 0
	v_mov_b64_e32 v[54:55], 0
	v_mov_b64_e32 v[56:57], 0
	v_mov_b64_e32 v[10:11], 0
	v_mov_b64_e32 v[12:13], 0
	v_mov_b64_e32 v[14:15], 0
	v_mov_b64_e32 v[16:17], 0
	v_mov_b64_e32 v[26:27], 0
	v_mov_b64_e32 v[28:29], 0
	v_mov_b64_e32 v[30:31], 0
	v_mov_b64_e32 v[32:33], 0
	v_mov_b64_e32 v[42:43], 0
	v_mov_b64_e32 v[44:45], 0
	v_mov_b64_e32 v[46:47], 0
	v_mov_b64_e32 v[48:49], 0
	v_mov_b64_e32 v[58:59], 0
	v_mov_b64_e32 v[60:61], 0
	v_mov_b64_e32 v[62:63], 0
	v_mov_b64_e32 v[64:65], 0
	v_mov_b64_e32 v[66:67], 0
	v_mov_b64_e32 v[68:69], 0
	v_mov_b64_e32 v[70:71], 0
	v_mov_b64_e32 v[72:73], 0
	v_mov_b64_e32 v[82:83], 0
	v_mov_b64_e32 v[84:85], 0
	v_mov_b64_e32 v[86:87], 0
	v_mov_b64_e32 v[88:89], 0
	v_mov_b64_e32 v[100:101], 0
	v_mov_b64_e32 v[102:103], 0
	v_mov_b64_e32 v[104:105], 0
	v_mov_b64_e32 v[106:107], 0
	v_mov_b64_e32 v[116:117], 0
	v_mov_b64_e32 v[118:119], 0
	v_mov_b64_e32 v[120:121], 0
	v_mov_b64_e32 v[122:123], 0
	v_mov_b64_e32 v[74:75], 0
	v_mov_b64_e32 v[76:77], 0
	v_mov_b64_e32 v[78:79], 0
	v_mov_b64_e32 v[80:81], 0
	v_mov_b64_e32 v[90:91], 0
	v_mov_b64_e32 v[92:93], 0
	v_mov_b64_e32 v[94:95], 0
	v_mov_b64_e32 v[96:97], 0
	v_mov_b64_e32 v[108:109], 0
	v_mov_b64_e32 v[110:111], 0
	v_mov_b64_e32 v[112:113], 0
	v_mov_b64_e32 v[114:115], 0
	v_mov_b64_e32 v[124:125], 0
	v_mov_b64_e32 v[126:127], 0
	v_mov_b64_e32 v[128:129], 0
	v_mov_b64_e32 v[130:131], 0
	s_and_b64 s[98:99], exec, s[14:15]
	s_cbranch_scc1 .Lrb_822
	s_barrier
.Lrb_822:
.LBB13_822:
	v_add_u32_e32 v155, s46, v152
	ds_read_b128 v[148:151], v155
	ds_read_b128 v[156:159], v155 offset:1024
	ds_read_b128 v[160:163], v155 offset:2048
	ds_read_b128 v[164:167], v155 offset:3072
	v_add_u32_e32 v155, s47, v152
	ds_read_b128 v[168:171], v155
	ds_read_b128 v[172:175], v155 offset:1024
	ds_read_b128 v[176:179], v155 offset:2048
	ds_read_b128 v[180:183], v155 offset:3072
	s_add_u32 s26, s24, 0xfffc0080
	s_addc_u32 s27, s25, -1
	s_cmp_eq_u32 s73, 12
	s_cselect_b32 s29, s17, s27
	s_cselect_b32 s28, s52, s26
	s_cselect_b32 s27, s13, s72
	s_cselect_b32 s26, s60, s64
	v_lshl_add_u64 v[224:225], s[24:25], 0, v[144:145]
	s_add_i32 m0, s58, 0xc000
	ds_read_b128 v[184:187], v154
	ds_read_b128 v[188:191], v154 offset:1024
	ds_read_b128 v[192:195], v154 offset:2048
	ds_read_b128 v[196:199], v154 offset:3072
	ds_read_b128 v[208:211], v154 offset:4096
	ds_read_b128 v[212:215], v154 offset:5120
	ds_read_b128 v[216:219], v154 offset:6144
	ds_read_b128 v[220:223], v154 offset:7168
	global_load_lds_dwordx4 v[224:225], off
	v_lshl_add_u64 v[224:225], s[24:25], 0, v[146:147]
	s_add_i32 m0, s58, 0xe000
	s_nop 0
	global_load_lds_dwordx4 v[224:225], off
	s_waitcnt vmcnt(8)
	s_waitcnt lgkmcnt(0)
	s_barrier
	s_setprio 1
	s_waitcnt lgkmcnt(0)
	v_mfma_f32_16x16x32_bf16 v[128:131], v[148:151], v[184:187], v[128:131]
	v_mfma_f32_16x16x32_bf16 v[124:127], v[160:163], v[184:187], v[124:127]
	v_mfma_f32_16x16x32_bf16 v[112:115], v[148:151], v[192:195], v[112:115]
	v_mfma_f32_16x16x32_bf16 v[108:111], v[160:163], v[192:195], v[108:111]
	v_mfma_f32_16x16x32_bf16 v[94:97], v[148:151], v[208:211], v[94:97]
	v_mfma_f32_16x16x32_bf16 v[90:93], v[160:163], v[208:211], v[90:93]
	v_mfma_f32_16x16x32_bf16 v[78:81], v[148:151], v[216:219], v[78:81]
	v_mfma_f32_16x16x32_bf16 v[74:77], v[160:163], v[216:219], v[74:77]
	v_mfma_f32_16x16x32_bf16 v[128:131], v[156:159], v[188:191], v[128:131]
	v_mfma_f32_16x16x32_bf16 v[124:127], v[164:167], v[188:191], v[124:127]
	v_mfma_f32_16x16x32_bf16 v[112:115], v[156:159], v[196:199], v[112:115]
	v_mfma_f32_16x16x32_bf16 v[108:111], v[164:167], v[196:199], v[108:111]
	v_mfma_f32_16x16x32_bf16 v[94:97], v[156:159], v[212:215], v[94:97]
	v_mfma_f32_16x16x32_bf16 v[90:93], v[164:167], v[212:215], v[90:93]
	v_mfma_f32_16x16x32_bf16 v[78:81], v[156:159], v[220:223], v[78:81]
	v_mfma_f32_16x16x32_bf16 v[74:77], v[164:167], v[220:223], v[74:77]
	s_setprio 0
	s_setprio 1
	v_mfma_f32_16x16x32_bf16 v[120:123], v[168:171], v[184:187], v[120:123]
	v_mfma_f32_16x16x32_bf16 v[116:119], v[176:179], v[184:187], v[116:119]
	v_mfma_f32_16x16x32_bf16 v[104:107], v[168:171], v[192:195], v[104:107]
	v_mfma_f32_16x16x32_bf16 v[100:103], v[176:179], v[192:195], v[100:103]
	v_mfma_f32_16x16x32_bf16 v[86:89], v[168:171], v[208:211], v[86:89]
	v_mfma_f32_16x16x32_bf16 v[82:85], v[176:179], v[208:211], v[82:85]
	v_mfma_f32_16x16x32_bf16 v[70:73], v[168:171], v[216:219], v[70:73]
	v_mfma_f32_16x16x32_bf16 v[66:69], v[176:179], v[216:219], v[66:69]
	v_mfma_f32_16x16x32_bf16 v[120:123], v[172:175], v[188:191], v[120:123]
	v_mfma_f32_16x16x32_bf16 v[116:119], v[180:183], v[188:191], v[116:119]
	v_mfma_f32_16x16x32_bf16 v[104:107], v[172:175], v[196:199], v[104:107]
	v_mfma_f32_16x16x32_bf16 v[100:103], v[180:183], v[196:199], v[100:103]
	v_mfma_f32_16x16x32_bf16 v[86:89], v[172:175], v[212:215], v[86:89]
	v_mfma_f32_16x16x32_bf16 v[82:85], v[180:183], v[212:215], v[82:85]
	v_mfma_f32_16x16x32_bf16 v[70:73], v[172:175], v[220:223], v[70:73]
	v_mfma_f32_16x16x32_bf16 v[66:69], v[180:183], v[220:223], v[66:69]
	s_setprio 0
	s_barrier
; #define PG8_STAGE_A(bufoff, h, ptr, nsel) do { if constexpr (Sched::GATHER) { if (nsel) PG8_STAGE_X(bufoff, ptr, vAn[h], PG8_A_AUX); else PG8_STAGE_X(bufoff, ptr, vAc[h], PG8_A_AUX); } \
;         else PG8_STAGE_X(bufoff, (ptr) + (h) * hstep, voffA, PG8_A_AUX); } while (0)
; #define PG8_STAGE(bufoff, gbase, voff) PG8_STAGE_X(bufoff, gbase, voff, PG8_B_AUX)
; #define PG8_LDA(dst, b, h) do { _Pragma("unroll") for (int m = 0; m < 4; ++m) _Pragma("unroll") for (int k = 0; k < 2; ++k) dst[m][k] = *(const PG8_LAS bf16x8*)(lds + PG8_SA(b, h) + aoff + m * 2048 + k * 1024); } while (0)
; #define PG8_LDB(dst, b, h) do { _Pragma("unroll") for (int n = 0; n < 2; ++n) _Pragma("unroll") for (int k = 0; k < 2; ++k) dst[n][k] = *(const PG8_LAS bf16x8*)(lds + PG8_SB(b, h) + boff + n * 2048 + k * 1024); } while (0)
; #define PG8_MMA(ai, bj, At, Bt) do { __builtin_amdgcn_s_setprio(1); _Pragma("unroll") for (int m = 0; m < 4; ++m) _Pragma("unroll") for (int n = 0; n < 2; ++n) _Pragma("unroll") for (int k = 0; k < 2; ++k) \
;         acc[ai][bj][m][n] = __builtin_amdgcn_mfma_f32_16x16x32_bf16(Bt[n][k], At[m][k], acc[ai][bj][m][n], 0, 0, 0); __builtin_amdgcn_s_setprio(0); } while (0)
; #define PG8_WAIT_V(n) asm volatile("s_waitcnt vmcnt(" #n ")" ::: "memory")
; #define PG8_WAIT_L(n) asm volatile("s_waitcnt lgkmcnt(" #n ")" ::: "memory")
; #define PG8_BAR __builtin_amdgcn_s_barrier()
; #define PG8_SCHED __builtin_amdgcn_sched_barrier(0)
; template <class Epi, class Sched, bool ALIGN_EPI = false, bool SP2 = false>
; __device__ __forceinline__ void gemm_phase(PG8_LAS unsigned char* lds, const Gemm g, const Sched& S, const Epi& E) {
;     ...
;             PG8_WAIT_V(8); PG8_WAIT_L(0); PG8_BAR; PG8_MMA(0, 0, At, B0); PG8_MMA(0, 1, At, B1); PG8_BAR; PG8_SCHED;
;             PG8_LDA(At, 0, 1); PG8_STAGE(PG8_SB(0, 0), b2, voffB); PG8_STAGE(PG8_SB(0, 1), b2 + hstep, voffB); PG8_STAGE_A(PG8_SA(0, 0), 0, a2, last);
;             PG8_WAIT_V(8); PG8_WAIT_L(0); PG8_BAR; PG8_MMA(1, 0, At, B0); PG8_MMA(1, 1, At, B1); PG8_BAR; PG8_SCHED;
;             PG8_LDB(B0, 1, 0); PG8_LDB(B1, 1, 1); PG8_SCHED; PG8_LDA(At, 1, 0); PG8_STAGE_A(PG8_SA(0, 1), 1, a2, last);
	s_mov_b32 m0, s49
	v_lshl_add_u64 v[224:225], s[26:27], 0, v[140:141]
	s_add_u32 s86, s26, 0x40000
	ds_read_b128 v[184:187], v154 offset:16384
	ds_read_b128 v[188:191], v154 offset:17408
	ds_read_b128 v[192:195], v154 offset:18432
	ds_read_b128 v[196:199], v154 offset:19456
	ds_read_b128 v[208:211], v154 offset:20480
	ds_read_b128 v[212:215], v154 offset:21504
	ds_read_b128 v[216:219], v154 offset:22528
	ds_read_b128 v[220:223], v154 offset:23552
	global_load_lds_dwordx4 v[224:225], off
	v_lshl_add_u64 v[226:227], s[26:27], 0, v[136:137]
	s_mov_b32 m0, s53
	s_addc_u32 s87, s27, 0
	global_load_lds_dwordx4 v[226:227], off
	v_lshl_add_u64 v[228:229], s[86:87], 0, v[140:141]
	s_mov_b32 m0, s56
	v_lshl_add_u64 v[230:231], s[28:29], 0, v[138:139]
	global_load_lds_dwordx4 v[228:229], off
	v_lshl_add_u64 v[228:229], s[86:87], 0, v[136:137]
	s_mov_b32 m0, s57
	s_nop 0
	global_load_lds_dwordx4 v[228:229], off
	v_lshl_add_u64 v[228:229], s[28:29], 0, v[142:143]
	s_mov_b32 m0, s58
	s_nop 0
	global_load_lds_dwordx4 v[228:229], off
	s_mov_b32 m0, s59
	s_nop 0
	global_load_lds_dwordx4 v[230:231], off
	s_waitcnt vmcnt(8)
	s_waitcnt lgkmcnt(0)
	s_barrier
	s_setprio 1
	s_waitcnt lgkmcnt(0)
	v_mfma_f32_16x16x32_bf16 v[62:65], v[148:151], v[184:187], v[62:65]
	v_mfma_f32_16x16x32_bf16 v[58:61], v[160:163], v[184:187], v[58:61]
	v_mfma_f32_16x16x32_bf16 v[46:49], v[148:151], v[192:195], v[46:49]
	v_mfma_f32_16x16x32_bf16 v[42:45], v[160:163], v[192:195], v[42:45]
	v_mfma_f32_16x16x32_bf16 v[30:33], v[148:151], v[208:211], v[30:33]
	v_mfma_f32_16x16x32_bf16 v[26:29], v[160:163], v[208:211], v[26:29]
	v_mfma_f32_16x16x32_bf16 v[14:17], v[148:151], v[216:219], v[14:17]
	v_mfma_f32_16x16x32_bf16 v[10:13], v[160:163], v[216:219], v[10:13]
	v_mfma_f32_16x16x32_bf16 v[62:65], v[156:159], v[188:191], v[62:65]
	v_mfma_f32_16x16x32_bf16 v[58:61], v[164:167], v[188:191], v[58:61]
	v_mfma_f32_16x16x32_bf16 v[46:49], v[156:159], v[196:199], v[46:49]
	v_mfma_f32_16x16x32_bf16 v[42:45], v[164:167], v[196:199], v[42:45]
	v_mfma_f32_16x16x32_bf16 v[30:33], v[156:159], v[212:215], v[30:33]
	v_mfma_f32_16x16x32_bf16 v[26:29], v[164:167], v[212:215], v[26:29]
	v_mfma_f32_16x16x32_bf16 v[14:17], v[156:159], v[220:223], v[14:17]
	v_mfma_f32_16x16x32_bf16 v[10:13], v[164:167], v[220:223], v[10:13]
	s_setprio 0
	s_setprio 1
	v_mfma_f32_16x16x32_bf16 v[54:57], v[168:171], v[184:187], v[54:57]
	v_mfma_f32_16x16x32_bf16 v[50:53], v[176:179], v[184:187], v[50:53]
	v_mfma_f32_16x16x32_bf16 v[38:41], v[168:171], v[192:195], v[38:41]
	v_mfma_f32_16x16x32_bf16 v[34:37], v[176:179], v[192:195], v[34:37]
	v_mfma_f32_16x16x32_bf16 v[22:25], v[168:171], v[208:211], v[22:25]
	v_mfma_f32_16x16x32_bf16 v[18:21], v[176:179], v[208:211], v[18:21]
	v_mfma_f32_16x16x32_bf16 v[6:9], v[168:171], v[216:219], v[6:9]
	v_mfma_f32_16x16x32_bf16 v[2:5], v[176:179], v[216:219], v[2:5]
	v_mfma_f32_16x16x32_bf16 v[54:57], v[172:175], v[188:191], v[54:57]
	v_mfma_f32_16x16x32_bf16 v[50:53], v[180:183], v[188:191], v[50:53]
	v_mfma_f32_16x16x32_bf16 v[38:41], v[172:175], v[196:199], v[38:41]
	v_mfma_f32_16x16x32_bf16 v[34:37], v[180:183], v[196:199], v[34:37]
	v_mfma_f32_16x16x32_bf16 v[22:25], v[172:175], v[212:215], v[22:25]
	v_mfma_f32_16x16x32_bf16 v[18:21], v[180:183], v[212:215], v[18:21]
	v_mfma_f32_16x16x32_bf16 v[6:9], v[172:175], v[220:223], v[6:9]
	v_mfma_f32_16x16x32_bf16 v[2:5], v[180:183], v[220:223], v[2:5]
	s_setprio 0
	s_barrier
	v_add_u32_e32 v155, s50, v152
	ds_read_b128 v[148:151], v155
	ds_read_b128 v[156:159], v155 offset:1024
	ds_read_b128 v[160:163], v155 offset:2048
	ds_read_b128 v[164:167], v155 offset:3072
	v_add_u32_e32 v155, s51, v152
	ds_read_b128 v[168:171], v155
	ds_read_b128 v[172:175], v155 offset:1024
	ds_read_b128 v[176:179], v155 offset:2048
	ds_read_b128 v[180:183], v155 offset:3072
	s_add_u32 s28, s28, 0x40000
	s_addc_u32 s29, s29, 0
	s_mov_b32 m0, s61
	v_lshl_add_u64 v[232:233], s[28:29], 0, v[142:143]
	ds_read_b128 v[184:187], v154 offset:32768
	ds_read_b128 v[188:191], v154 offset:33792
	ds_read_b128 v[192:195], v154 offset:34816
	ds_read_b128 v[196:199], v154 offset:35840
	ds_read_b128 v[208:211], v154 offset:36864
	ds_read_b128 v[212:215], v154 offset:37888
	ds_read_b128 v[216:219], v154 offset:38912
	ds_read_b128 v[220:223], v154 offset:39936
	global_load_lds_dwordx4 v[232:233], off
	v_lshl_add_u64 v[232:233], s[28:29], 0, v[138:139]
	s_mov_b32 m0, s68
	s_nop 0
	global_load_lds_dwordx4 v[232:233], off
	s_waitcnt vmcnt(8)
	s_waitcnt lgkmcnt(0)
	s_barrier
; #define PG8_STAGE_A(bufoff, h, ptr, nsel) do { if constexpr (Sched::GATHER) { if (nsel) PG8_STAGE_X(bufoff, ptr, vAn[h], PG8_A_AUX); else PG8_STAGE_X(bufoff, ptr, vAc[h], PG8_A_AUX); } \
;         else PG8_STAGE_X(bufoff, (ptr) + (h) * hstep, voffA, PG8_A_AUX); } while (0)
; #define PG8_STAGE(bufoff, gbase, voff) PG8_STAGE_X(bufoff, gbase, voff, PG8_B_AUX)
; #define PG8_LDA(dst, b, h) do { _Pragma("unroll") for (int m = 0; m < 4; ++m) _Pragma("unroll") for (int k = 0; k < 2; ++k) dst[m][k] = *(const PG8_LAS bf16x8*)(lds + PG8_SA(b, h) + aoff + m * 2048 + k * 1024); } while (0)
; #define PG8_LDB(dst, b, h) do { _Pragma("unroll") for (int n = 0; n < 2; ++n) _Pragma("unroll") for (int k = 0; k < 2; ++k) dst[n][k] = *(const PG8_LAS bf16x8*)(lds + PG8_SB(b, h) + boff + n * 2048 + k * 1024); } while (0)
; #define PG8_MMA(ai, bj, At, Bt) do { __builtin_amdgcn_s_setprio(1); _Pragma("unroll") for (int m = 0; m < 4; ++m) _Pragma("unroll") for (int n = 0; n < 2; ++n) _Pragma("unroll") for (int k = 0; k < 2; ++k) \
;         acc[ai][bj][m][n] = __builtin_amdgcn_mfma_f32_16x16x32_bf16(Bt[n][k], At[m][k], acc[ai][bj][m][n], 0, 0, 0); __builtin_amdgcn_s_setprio(0); } while (0)
; #define PG8_WAIT_V(n) asm volatile("s_waitcnt vmcnt(" #n ")" ::: "memory")
; #define PG8_WAIT_L(n) asm volatile("s_waitcnt lgkmcnt(" #n ")" ::: "memory")
; #define PG8_BAR __builtin_amdgcn_s_barrier()
; #define PG8_SCHED __builtin_amdgcn_sched_barrier(0)
; template <class Epi, class Sched, bool ALIGN_EPI = false, bool SP2 = false>
; __device__ __forceinline__ void gemm_phase(PG8_LAS unsigned char* lds, const Gemm g, const Sched& S, const Epi& E) {
;     ...
;             PG8_WAIT_V(8); PG8_WAIT_L(0); PG8_BAR; PG8_MMA(1, 0, At, B0); PG8_MMA(1, 1, At, B1); PG8_BAR; PG8_SCHED;
;             PG8_LDB(B0, 1, 0); PG8_LDB(B1, 1, 1); PG8_SCHED; PG8_LDA(At, 1, 0); PG8_STAGE_A(PG8_SA(0, 1), 1, a2, last);
;             PG8_WAIT_V(8); PG8_WAIT_L(0); PG8_BAR; PG8_MMA(0, 0, At, B0); PG8_MMA(0, 1, At, B1); PG8_BAR; PG8_SCHED;
;             PG8_LDA(At, 1, 1); PG8_STAGE(PG8_SB(1, 0), b3, voffB); PG8_STAGE(PG8_SB(1, 1), b3 + hstep, voffB); PG8_STAGE_A(PG8_SA(1, 0), 0, a3, last);
;             PG8_WAIT_V(8); PG8_WAIT_L(0); PG8_BAR; PG8_MMA(1, 0, At, B0); PG8_MMA(1, 1, At, B1); PG8_BAR; PG8_SCHED;
;     ...
;         if constexpr (ALIGN_EPI) { if (wr == 0) PG8_BAR; }
	s_setprio 1
	s_waitcnt lgkmcnt(0)
	v_mfma_f32_16x16x32_bf16 v[128:131], v[148:151], v[184:187], v[128:131]
	v_mfma_f32_16x16x32_bf16 v[124:127], v[160:163], v[184:187], v[124:127]
	v_mfma_f32_16x16x32_bf16 v[112:115], v[148:151], v[192:195], v[112:115]
	v_mfma_f32_16x16x32_bf16 v[108:111], v[160:163], v[192:195], v[108:111]
	v_mfma_f32_16x16x32_bf16 v[94:97], v[148:151], v[208:211], v[94:97]
	v_mfma_f32_16x16x32_bf16 v[90:93], v[160:163], v[208:211], v[90:93]
	v_mfma_f32_16x16x32_bf16 v[78:81], v[148:151], v[216:219], v[78:81]
	v_mfma_f32_16x16x32_bf16 v[74:77], v[160:163], v[216:219], v[74:77]
	v_mfma_f32_16x16x32_bf16 v[128:131], v[156:159], v[188:191], v[128:131]
	v_mfma_f32_16x16x32_bf16 v[124:127], v[164:167], v[188:191], v[124:127]
	v_mfma_f32_16x16x32_bf16 v[112:115], v[156:159], v[196:199], v[112:115]
	v_mfma_f32_16x16x32_bf16 v[108:111], v[164:167], v[196:199], v[108:111]
	v_mfma_f32_16x16x32_bf16 v[94:97], v[156:159], v[212:215], v[94:97]
	v_mfma_f32_16x16x32_bf16 v[90:93], v[164:167], v[212:215], v[90:93]
	v_mfma_f32_16x16x32_bf16 v[78:81], v[156:159], v[220:223], v[78:81]
	v_mfma_f32_16x16x32_bf16 v[74:77], v[164:167], v[220:223], v[74:77]
	s_setprio 0
	s_setprio 1
	v_mfma_f32_16x16x32_bf16 v[120:123], v[168:171], v[184:187], v[120:123]
	v_mfma_f32_16x16x32_bf16 v[116:119], v[176:179], v[184:187], v[116:119]
	v_mfma_f32_16x16x32_bf16 v[104:107], v[168:171], v[192:195], v[104:107]
	v_mfma_f32_16x16x32_bf16 v[100:103], v[176:179], v[192:195], v[100:103]
	v_mfma_f32_16x16x32_bf16 v[86:89], v[168:171], v[208:211], v[86:89]
	v_mfma_f32_16x16x32_bf16 v[82:85], v[176:179], v[208:211], v[82:85]
	v_mfma_f32_16x16x32_bf16 v[70:73], v[168:171], v[216:219], v[70:73]
	v_mfma_f32_16x16x32_bf16 v[66:69], v[176:179], v[216:219], v[66:69]
	v_mfma_f32_16x16x32_bf16 v[120:123], v[172:175], v[188:191], v[120:123]
	v_mfma_f32_16x16x32_bf16 v[116:119], v[180:183], v[188:191], v[116:119]
	v_mfma_f32_16x16x32_bf16 v[104:107], v[172:175], v[196:199], v[104:107]
	v_mfma_f32_16x16x32_bf16 v[100:103], v[180:183], v[196:199], v[100:103]
	v_mfma_f32_16x16x32_bf16 v[86:89], v[172:175], v[212:215], v[86:89]
	v_mfma_f32_16x16x32_bf16 v[82:85], v[180:183], v[212:215], v[82:85]
	v_mfma_f32_16x16x32_bf16 v[70:73], v[172:175], v[220:223], v[70:73]
	v_mfma_f32_16x16x32_bf16 v[66:69], v[180:183], v[220:223], v[66:69]
	s_setprio 0
	s_barrier
	s_mov_b32 m0, s69
	v_lshl_add_u64 v[224:225], v[224:225], 0, s[54:55]
	s_add_u32 s26, s26, 0x40080
	ds_read_b128 v[184:187], v154 offset:49152
	ds_read_b128 v[188:191], v154 offset:50176
	ds_read_b128 v[192:195], v154 offset:51200
	ds_read_b128 v[196:199], v154 offset:52224
	ds_read_b128 v[208:211], v154 offset:53248
	ds_read_b128 v[212:215], v154 offset:54272
	ds_read_b128 v[216:219], v154 offset:55296
	ds_read_b128 v[220:223], v154 offset:56320
	global_load_lds_dwordx4 v[224:225], off
	v_lshl_add_u64 v[224:225], v[226:227], 0, s[54:55]
	s_mov_b32 m0, s88
	s_addc_u32 s27, s27, 0
	global_load_lds_dwordx4 v[224:225], off
	v_lshl_add_u64 v[224:225], s[26:27], 0, v[140:141]
	s_mov_b32 m0, s38
	s_nop 0
	global_load_lds_dwordx4 v[224:225], off
	v_lshl_add_u64 v[224:225], s[26:27], 0, v[136:137]
	s_mov_b32 m0, s95
	s_nop 0
	global_load_lds_dwordx4 v[224:225], off
	v_lshl_add_u64 v[224:225], v[228:229], 0, s[54:55]
	s_mov_b32 m0, s89
	s_nop 0
	global_load_lds_dwordx4 v[224:225], off
	v_lshl_add_u64 v[224:225], v[230:231], 0, s[54:55]
	s_mov_b32 m0, s94
	s_nop 0
	global_load_lds_dwordx4 v[224:225], off
	s_waitcnt vmcnt(8)
	s_waitcnt lgkmcnt(0)
	s_barrier
	s_setprio 1
	s_waitcnt lgkmcnt(0)
	v_mfma_f32_16x16x32_bf16 v[62:65], v[148:151], v[184:187], v[62:65]
	v_mfma_f32_16x16x32_bf16 v[58:61], v[160:163], v[184:187], v[58:61]
	v_mfma_f32_16x16x32_bf16 v[46:49], v[148:151], v[192:195], v[46:49]
	v_mfma_f32_16x16x32_bf16 v[42:45], v[160:163], v[192:195], v[42:45]
	v_mfma_f32_16x16x32_bf16 v[30:33], v[148:151], v[208:211], v[30:33]
	v_mfma_f32_16x16x32_bf16 v[26:29], v[160:163], v[208:211], v[26:29]
	v_mfma_f32_16x16x32_bf16 v[14:17], v[148:151], v[216:219], v[14:17]
	v_mfma_f32_16x16x32_bf16 v[10:13], v[160:163], v[216:219], v[10:13]
	v_mfma_f32_16x16x32_bf16 v[62:65], v[156:159], v[188:191], v[62:65]
	v_mfma_f32_16x16x32_bf16 v[58:61], v[164:167], v[188:191], v[58:61]
	v_mfma_f32_16x16x32_bf16 v[46:49], v[156:159], v[196:199], v[46:49]
	v_mfma_f32_16x16x32_bf16 v[42:45], v[164:167], v[196:199], v[42:45]
	v_mfma_f32_16x16x32_bf16 v[30:33], v[156:159], v[212:215], v[30:33]
	v_mfma_f32_16x16x32_bf16 v[26:29], v[164:167], v[212:215], v[26:29]
	v_mfma_f32_16x16x32_bf16 v[14:17], v[156:159], v[220:223], v[14:17]
	v_mfma_f32_16x16x32_bf16 v[10:13], v[164:167], v[220:223], v[10:13]
	s_setprio 0
	s_setprio 1
	v_mfma_f32_16x16x32_bf16 v[54:57], v[168:171], v[184:187], v[54:57]
	v_mfma_f32_16x16x32_bf16 v[50:53], v[176:179], v[184:187], v[50:53]
	v_mfma_f32_16x16x32_bf16 v[38:41], v[168:171], v[192:195], v[38:41]
	v_mfma_f32_16x16x32_bf16 v[34:37], v[176:179], v[192:195], v[34:37]
	v_mfma_f32_16x16x32_bf16 v[22:25], v[168:171], v[208:211], v[22:25]
	v_mfma_f32_16x16x32_bf16 v[18:21], v[176:179], v[208:211], v[18:21]
	v_mfma_f32_16x16x32_bf16 v[6:9], v[168:171], v[216:219], v[6:9]
	v_mfma_f32_16x16x32_bf16 v[2:5], v[176:179], v[216:219], v[2:5]
	v_mfma_f32_16x16x32_bf16 v[54:57], v[172:175], v[188:191], v[54:57]
	v_mfma_f32_16x16x32_bf16 v[50:53], v[180:183], v[188:191], v[50:53]
	v_mfma_f32_16x16x32_bf16 v[38:41], v[172:175], v[196:199], v[38:41]
	v_mfma_f32_16x16x32_bf16 v[34:37], v[180:183], v[196:199], v[34:37]
	v_mfma_f32_16x16x32_bf16 v[22:25], v[172:175], v[212:215], v[22:25]
	v_mfma_f32_16x16x32_bf16 v[18:21], v[180:183], v[212:215], v[18:21]
	v_mfma_f32_16x16x32_bf16 v[6:9], v[172:175], v[220:223], v[6:9]
	v_mfma_f32_16x16x32_bf16 v[2:5], v[180:183], v[220:223], v[2:5]
	s_setprio 0
	s_barrier
	s_add_i32 s73, s73, 2
	s_add_u32 s24, s24, 0x100
	s_addc_u32 s25, s25, 0
	s_add_u32 s64, s64, 0x100
	s_addc_u32 s72, s72, 0
	s_cmp_gt_u32 s73, 13
	s_cbranch_scc0 .LBB13_822
	s_and_b64 vcc, exec, s[14:15]
	s_mov_b32 s64, 0x18000
	s_cbranch_vccz .LBB13_825
	s_barrier
; __device__ __forceinline__ unsigned pk2(float lo, float hi) { f32x2 v = {lo, hi}; return __builtin_bit_cast(unsigned, __builtin_convertvector(v, bf2_t)); }
; template <int BIT = 0> __device__ __forceinline__ void st16w(void* p, u32x4 v) { if ((WT_STORES >> BIT) & 1) asm volatile("global_store_dwordx4 %0, %1, off sc1\n\ts_nop 1" :: "v"(p), "v"(v) : "memory"); else *(u32x4*)p = v; }
; __device__ __forceinline__ float bflo(unsigned u) { return __uint_as_float(u << 16); }
; __device__ __forceinline__ float bfhi(unsigned u) { return __uint_as_float(u & 0xffff0000u); }
;     __device__ __forceinline__ void operator()(const f32x4 (&acc)[2][2][4][2], const Unit& u, int wr, int wc, int fr, int fq) const {
;         const int row0 = u.pm * BM + wr * 64 + fr, col0 = u.pn * BM + wc * 32 + 8 * fq;
; #pragma unroll
;         for (int ai = 0; ai < 2; ++ai)
; #pragma unroll
;             for (int m = 0; m < 4; ++m) {
;                 const size_t row = (size_t)(row0 + ai * HALF + m * 16);
; #pragma unroll
;                 for (int bj = 0; bj < 2; ++bj) {
;                     const int col = col0 + bj * HALF;
;                     const u32x4 g = *(const u32x4*)(P + row * INC + goff + col);
;                     const f32x4 a0 = acc[ai][bj][m][0], a1 = acc[ai][bj][m][1];
;                     float o[8] = {bflo(g.x) * a0[0], bfhi(g.x) * a0[1], bflo(g.y) * a0[2], bfhi(g.y) * a0[3], bflo(g.z) * a1[0], bfhi(g.z) * a1[1], bflo(g.w) * a1[2], bfhi(g.w) * a1[3]};
;                     if (mode) { const u32x4 t = *(const u32x4*)(T1 + row * D + col);
;                         o[0] += bflo(t.x); o[1] += bfhi(t.x); o[2] += bflo(t.y); o[3] += bfhi(t.y); o[4] += bflo(t.z); o[5] += bfhi(t.z); o[6] += bflo(t.w); o[7] += bfhi(t.w); }
;                     u32x4 w; w.x = pk2(o[0], o[1]); w.y = pk2(o[2], o[3]); w.z = pk2(o[4], o[5]); w.w = pk2(o[6], o[7]);
;                     if (mode) st16w(MM + row * D + col, w); else *(u32x4*)(T1 + row * D + col) = w;
.LBB13_825:
	v_readfirstlane_b32 s98, v132
	v_readfirstlane_b32 s99, v133
	v_readfirstlane_b32 s24, v134
	v_readfirstlane_b32 s25, v135
	v_lshl_add_u32 v158, s22, 8, v99
	v_lshl_or_b32 v159, s23, 8, v153
	s_mov_b64 s[22:23], -1
	s_andn2_b64 vcc, exec, s[4:5]
	s_mov_b32 s87, 0x8000
	s_movk_i32 s86, 0x1c00
	v_mul_u32_u24_e32 v156, 0x2c00, v158
	v_lshl_add_u32 v156, v159, 1, v156
	v_add_u32_e32 v156, 0x2400, v156
	v_lshlrev_b32_e32 v157, 11, v158
	v_lshl_add_u32 v157, v159, 1, v157
	global_load_dwordx4 v[160:163], v156, s[98:99]
	global_load_dwordx4 v[164:167], v156, s[98:99] offset:256
	v_add_u32_e32 v158, 0x2c000, v156
	global_load_dwordx4 v[168:171], v158, s[98:99]
	v_add_u32_e32 v158, 0x2c000, v156
	global_load_dwordx4 v[172:175], v158, s[98:99] offset:256
	v_add_u32_e32 v158, 0x58000, v156
	global_load_dwordx4 v[176:179], v158, s[98:99]
	v_add_u32_e32 v158, 0x58000, v156
	global_load_dwordx4 v[180:183], v158, s[98:99] offset:256
	v_add_u32_e32 v158, 0x84000, v156
	global_load_dwordx4 v[184:187], v158, s[98:99]
	v_add_u32_e32 v158, 0x84000, v156
	global_load_dwordx4 v[188:191], v158, s[98:99] offset:256
	v_add_u32_e32 v158, 0x160000, v156
	global_load_dwordx4 v[192:195], v158, s[98:99]
	v_add_u32_e32 v158, 0x160000, v156
	global_load_dwordx4 v[196:199], v158, s[98:99] offset:256
	v_add_u32_e32 v158, 0x18c000, v156
	global_load_dwordx4 v[208:211], v158, s[98:99]
	v_add_u32_e32 v158, 0x18c000, v156
	global_load_dwordx4 v[212:215], v158, s[98:99] offset:256
	v_add_u32_e32 v158, 0x1b8000, v156
	global_load_dwordx4 v[216:219], v158, s[98:99]
	v_add_u32_e32 v158, 0x1b8000, v156
	global_load_dwordx4 v[220:223], v158, s[98:99] offset:256
	s_waitcnt vmcnt(13)
	v_lshlrev_b32_e32 v148, 16, v160
	v_and_b32_e32 v149, 0xffff0000, v160
	v_pk_mul_f32 v[128:129], v[128:129], v[148:149]
	v_lshlrev_b32_e32 v150, 16, v161
	v_and_b32_e32 v151, 0xffff0000, v161
	v_pk_mul_f32 v[130:131], v[130:131], v[150:151]
	v_lshlrev_b32_e32 v148, 16, v162
	v_and_b32_e32 v149, 0xffff0000, v162
	v_pk_mul_f32 v[124:125], v[124:125], v[148:149]
	v_lshlrev_b32_e32 v150, 16, v163
	v_and_b32_e32 v151, 0xffff0000, v163
	v_pk_mul_f32 v[126:127], v[126:127], v[150:151]
	v_cvt_pk_bf16_f32 v128, v128, v129
	v_cvt_pk_bf16_f32 v129, v130, v131
	v_cvt_pk_bf16_f32 v130, v124, v125
	v_cvt_pk_bf16_f32 v131, v126, v127
	global_store_dwordx4 v157, v[128:131], s[24:25]
	v_add_u32_e32 v158, 0x1e4000, v156
	global_load_dwordx4 v[160:163], v158, s[98:99]
	v_add_u32_e32 v158, 0x1e4000, v156
	global_load_dwordx4 v[124:127], v158, s[98:99] offset:256
	s_waitcnt vmcnt(15)
	v_lshlrev_b32_e32 v148, 16, v164
	v_and_b32_e32 v149, 0xffff0000, v164
	v_pk_mul_f32 v[120:121], v[120:121], v[148:149]
	v_lshlrev_b32_e32 v150, 16, v165
	v_and_b32_e32 v151, 0xffff0000, v165
	v_pk_mul_f32 v[122:123], v[122:123], v[150:151]
	v_lshlrev_b32_e32 v148, 16, v166
	v_and_b32_e32 v149, 0xffff0000, v166
	v_pk_mul_f32 v[116:117], v[116:117], v[148:149]
	v_lshlrev_b32_e32 v150, 16, v167
	v_and_b32_e32 v151, 0xffff0000, v167
	v_pk_mul_f32 v[118:119], v[118:119], v[150:151]
	v_cvt_pk_bf16_f32 v120, v120, v121
	v_cvt_pk_bf16_f32 v121, v122, v123
	v_cvt_pk_bf16_f32 v122, v116, v117
	v_cvt_pk_bf16_f32 v123, v118, v119
	global_store_dwordx4 v157, v[120:123], s[24:25] offset:256
	s_waitcnt vmcnt(15)
	v_lshlrev_b32_e32 v148, 16, v168
	v_and_b32_e32 v149, 0xffff0000, v168
	v_pk_mul_f32 v[112:113], v[112:113], v[148:149]
	v_lshlrev_b32_e32 v150, 16, v169
	v_and_b32_e32 v151, 0xffff0000, v169
	v_pk_mul_f32 v[114:115], v[114:115], v[150:151]
	v_lshlrev_b32_e32 v148, 16, v170
	v_and_b32_e32 v149, 0xffff0000, v170
	v_pk_mul_f32 v[108:109], v[108:109], v[148:149]
	v_lshlrev_b32_e32 v150, 16, v171
	v_and_b32_e32 v151, 0xffff0000, v171
	v_pk_mul_f32 v[110:111], v[110:111], v[150:151]
	v_cvt_pk_bf16_f32 v112, v112, v113
	v_cvt_pk_bf16_f32 v113, v114, v115
	v_cvt_pk_bf16_f32 v114, v108, v109
	v_cvt_pk_bf16_f32 v115, v110, v111
	v_add_u32_e32 v159, 0x8000, v157
	global_store_dwordx4 v159, v[112:115], s[24:25]
	s_waitcnt vmcnt(15)
	v_lshlrev_b32_e32 v148, 16, v172
	v_and_b32_e32 v149, 0xffff0000, v172
	v_pk_mul_f32 v[104:105], v[104:105], v[148:149]
	v_lshlrev_b32_e32 v150, 16, v173
	v_and_b32_e32 v151, 0xffff0000, v173
	v_pk_mul_f32 v[106:107], v[106:107], v[150:151]
	v_lshlrev_b32_e32 v148, 16, v174
	v_and_b32_e32 v149, 0xffff0000, v174
	v_pk_mul_f32 v[100:101], v[100:101], v[148:149]
	v_lshlrev_b32_e32 v150, 16, v175
	v_and_b32_e32 v151, 0xffff0000, v175
	v_pk_mul_f32 v[102:103], v[102:103], v[150:151]
	v_cvt_pk_bf16_f32 v104, v104, v105
	v_cvt_pk_bf16_f32 v105, v106, v107
	v_cvt_pk_bf16_f32 v106, v100, v101
	v_cvt_pk_bf16_f32 v107, v102, v103
	v_add_u32_e32 v159, 0x8000, v157
	global_store_dwordx4 v159, v[104:107], s[24:25] offset:256
	s_waitcnt vmcnt(15)
	v_lshlrev_b32_e32 v148, 16, v176
	v_and_b32_e32 v149, 0xffff0000, v176
	v_pk_mul_f32 v[94:95], v[94:95], v[148:149]
	v_lshlrev_b32_e32 v150, 16, v177
	v_and_b32_e32 v151, 0xffff0000, v177
	v_pk_mul_f32 v[96:97], v[96:97], v[150:151]
	v_lshlrev_b32_e32 v148, 16, v178
	v_and_b32_e32 v149, 0xffff0000, v178
	v_pk_mul_f32 v[90:91], v[90:91], v[148:149]
	v_lshlrev_b32_e32 v150, 16, v179
	v_and_b32_e32 v151, 0xffff0000, v179
	v_pk_mul_f32 v[92:93], v[92:93], v[150:151]
	v_cvt_pk_bf16_f32 v94, v94, v95
	v_cvt_pk_bf16_f32 v95, v96, v97
	v_cvt_pk_bf16_f32 v96, v90, v91
	v_cvt_pk_bf16_f32 v97, v92, v93
	v_add_u32_e32 v159, 0x10000, v157
	global_store_dwordx4 v159, v[94:97], s[24:25]
	s_waitcnt vmcnt(15)
; __device__ __forceinline__ unsigned pk2(float lo, float hi) { f32x2 v = {lo, hi}; return __builtin_bit_cast(unsigned, __builtin_convertvector(v, bf2_t)); }
; template <int BIT = 0> __device__ __forceinline__ void st16w(void* p, u32x4 v) { if ((WT_STORES >> BIT) & 1) asm volatile("global_store_dwordx4 %0, %1, off sc1\n\ts_nop 1" :: "v"(p), "v"(v) : "memory"); else *(u32x4*)p = v; }
; __device__ __forceinline__ float bflo(unsigned u) { return __uint_as_float(u << 16); }
; __device__ __forceinline__ float bfhi(unsigned u) { return __uint_as_float(u & 0xffff0000u); }
;     __device__ __forceinline__ void operator()(const f32x4 (&acc)[2][2][4][2], const Unit& u, int wr, int wc, int fr, int fq) const {
;     ...
; #pragma unroll
;                 for (int bj = 0; bj < 2; ++bj) {
;                     const int col = col0 + bj * HALF;
;                     const u32x4 g = *(const u32x4*)(P + row * INC + goff + col);
;                     const f32x4 a0 = acc[ai][bj][m][0], a1 = acc[ai][bj][m][1];
;                     float o[8] = {bflo(g.x) * a0[0], bfhi(g.x) * a0[1], bflo(g.y) * a0[2], bfhi(g.y) * a0[3], bflo(g.z) * a1[0], bfhi(g.z) * a1[1], bflo(g.w) * a1[2], bfhi(g.w) * a1[3]};
;                     if (mode) { const u32x4 t = *(const u32x4*)(T1 + row * D + col);
;                         o[0] += bflo(t.x); o[1] += bfhi(t.x); o[2] += bflo(t.y); o[3] += bfhi(t.y); o[4] += bflo(t.z); o[5] += bfhi(t.z); o[6] += bflo(t.w); o[7] += bfhi(t.w); }
;                     u32x4 w; w.x = pk2(o[0], o[1]); w.y = pk2(o[2], o[3]); w.z = pk2(o[4], o[5]); w.w = pk2(o[6], o[7]);
;                     if (mode) st16w(MM + row * D + col, w); else *(u32x4*)(T1 + row * D + col) = w;
	v_lshlrev_b32_e32 v148, 16, v180
	v_and_b32_e32 v149, 0xffff0000, v180
	v_pk_mul_f32 v[86:87], v[86:87], v[148:149]
	v_lshlrev_b32_e32 v150, 16, v181
	v_and_b32_e32 v151, 0xffff0000, v181
	v_pk_mul_f32 v[88:89], v[88:89], v[150:151]
	v_lshlrev_b32_e32 v148, 16, v182
	v_and_b32_e32 v149, 0xffff0000, v182
	v_pk_mul_f32 v[82:83], v[82:83], v[148:149]
	v_lshlrev_b32_e32 v150, 16, v183
	v_and_b32_e32 v151, 0xffff0000, v183
	v_pk_mul_f32 v[84:85], v[84:85], v[150:151]
	v_cvt_pk_bf16_f32 v86, v86, v87
	v_cvt_pk_bf16_f32 v87, v88, v89
	v_cvt_pk_bf16_f32 v88, v82, v83
	v_cvt_pk_bf16_f32 v89, v84, v85
	v_add_u32_e32 v159, 0x10000, v157
	global_store_dwordx4 v159, v[86:89], s[24:25] offset:256
	s_waitcnt vmcnt(15)
	v_lshlrev_b32_e32 v148, 16, v184
	v_and_b32_e32 v149, 0xffff0000, v184
	v_pk_mul_f32 v[78:79], v[78:79], v[148:149]
	v_lshlrev_b32_e32 v150, 16, v185
	v_and_b32_e32 v151, 0xffff0000, v185
	v_pk_mul_f32 v[80:81], v[80:81], v[150:151]
	v_lshlrev_b32_e32 v148, 16, v186
	v_and_b32_e32 v149, 0xffff0000, v186
	v_pk_mul_f32 v[74:75], v[74:75], v[148:149]
	v_lshlrev_b32_e32 v150, 16, v187
	v_and_b32_e32 v151, 0xffff0000, v187
	v_pk_mul_f32 v[76:77], v[76:77], v[150:151]
	v_cvt_pk_bf16_f32 v78, v78, v79
	v_cvt_pk_bf16_f32 v79, v80, v81
	v_cvt_pk_bf16_f32 v80, v74, v75
	v_cvt_pk_bf16_f32 v81, v76, v77
	v_add_u32_e32 v159, 0x18000, v157
	global_store_dwordx4 v159, v[78:81], s[24:25]
	s_waitcnt vmcnt(15)
	v_lshlrev_b32_e32 v148, 16, v188
	v_and_b32_e32 v149, 0xffff0000, v188
	v_pk_mul_f32 v[70:71], v[70:71], v[148:149]
	v_lshlrev_b32_e32 v150, 16, v189
	v_and_b32_e32 v151, 0xffff0000, v189
	v_pk_mul_f32 v[72:73], v[72:73], v[150:151]
	v_lshlrev_b32_e32 v148, 16, v190
	v_and_b32_e32 v149, 0xffff0000, v190
	v_pk_mul_f32 v[66:67], v[66:67], v[148:149]
	v_lshlrev_b32_e32 v150, 16, v191
	v_and_b32_e32 v151, 0xffff0000, v191
	v_pk_mul_f32 v[68:69], v[68:69], v[150:151]
	v_cvt_pk_bf16_f32 v70, v70, v71
	v_cvt_pk_bf16_f32 v71, v72, v73
	v_cvt_pk_bf16_f32 v72, v66, v67
	v_cvt_pk_bf16_f32 v73, v68, v69
	v_add_u32_e32 v159, 0x18000, v157
	global_store_dwordx4 v159, v[70:73], s[24:25] offset:256
	s_waitcnt vmcnt(15)
	v_lshlrev_b32_e32 v148, 16, v192
	v_and_b32_e32 v149, 0xffff0000, v192
	v_pk_mul_f32 v[62:63], v[62:63], v[148:149]
	v_lshlrev_b32_e32 v150, 16, v193
	v_and_b32_e32 v151, 0xffff0000, v193
	v_pk_mul_f32 v[64:65], v[64:65], v[150:151]
	v_lshlrev_b32_e32 v148, 16, v194
	v_and_b32_e32 v149, 0xffff0000, v194
	v_pk_mul_f32 v[58:59], v[58:59], v[148:149]
	v_lshlrev_b32_e32 v150, 16, v195
	v_and_b32_e32 v151, 0xffff0000, v195
	v_pk_mul_f32 v[60:61], v[60:61], v[150:151]
	v_cvt_pk_bf16_f32 v62, v62, v63
	v_cvt_pk_bf16_f32 v63, v64, v65
	v_cvt_pk_bf16_f32 v64, v58, v59
	v_cvt_pk_bf16_f32 v65, v60, v61
	v_add_u32_e32 v159, 0x40000, v157
	global_store_dwordx4 v159, v[62:65], s[24:25]
	s_waitcnt vmcnt(15)
	v_lshlrev_b32_e32 v148, 16, v196
	v_and_b32_e32 v149, 0xffff0000, v196
	v_pk_mul_f32 v[54:55], v[54:55], v[148:149]
	v_lshlrev_b32_e32 v150, 16, v197
	v_and_b32_e32 v151, 0xffff0000, v197
	v_pk_mul_f32 v[56:57], v[56:57], v[150:151]
	v_lshlrev_b32_e32 v148, 16, v198
	v_and_b32_e32 v149, 0xffff0000, v198
	v_pk_mul_f32 v[50:51], v[50:51], v[148:149]
	v_lshlrev_b32_e32 v150, 16, v199
	v_and_b32_e32 v151, 0xffff0000, v199
	v_pk_mul_f32 v[52:53], v[52:53], v[150:151]
	v_cvt_pk_bf16_f32 v54, v54, v55
	v_cvt_pk_bf16_f32 v55, v56, v57
	v_cvt_pk_bf16_f32 v56, v50, v51
	v_cvt_pk_bf16_f32 v57, v52, v53
	v_add_u32_e32 v159, 0x40000, v157
	global_store_dwordx4 v159, v[54:57], s[24:25] offset:256
	s_waitcnt vmcnt(15)
	v_lshlrev_b32_e32 v148, 16, v208
	v_and_b32_e32 v149, 0xffff0000, v208
	v_pk_mul_f32 v[46:47], v[46:47], v[148:149]
	v_lshlrev_b32_e32 v150, 16, v209
	v_and_b32_e32 v151, 0xffff0000, v209
	v_pk_mul_f32 v[48:49], v[48:49], v[150:151]
	v_lshlrev_b32_e32 v148, 16, v210
	v_and_b32_e32 v149, 0xffff0000, v210
	v_pk_mul_f32 v[42:43], v[42:43], v[148:149]
	v_lshlrev_b32_e32 v150, 16, v211
	v_and_b32_e32 v151, 0xffff0000, v211
	v_pk_mul_f32 v[44:45], v[44:45], v[150:151]
	v_cvt_pk_bf16_f32 v46, v46, v47
	v_cvt_pk_bf16_f32 v47, v48, v49
	v_cvt_pk_bf16_f32 v48, v42, v43
	v_cvt_pk_bf16_f32 v49, v44, v45
	v_add_u32_e32 v159, 0x48000, v157
	global_store_dwordx4 v159, v[46:49], s[24:25]
	s_waitcnt vmcnt(15)
; __device__ __forceinline__ unsigned pk2(float lo, float hi) { f32x2 v = {lo, hi}; return __builtin_bit_cast(unsigned, __builtin_convertvector(v, bf2_t)); }
; template <int BIT = 0> __device__ __forceinline__ void st16w(void* p, u32x4 v) { if ((WT_STORES >> BIT) & 1) asm volatile("global_store_dwordx4 %0, %1, off sc1\n\ts_nop 1" :: "v"(p), "v"(v) : "memory"); else *(u32x4*)p = v; }
;     __device__ __forceinline__ void operator()(const f32x4 (&acc)[2][2][4][2], const Unit& u, int wr, int wc, int fr, int fq) const {
;     ...
; #pragma unroll
;                 for (int bj = 0; bj < 2; ++bj) {
;                     const int col = col0 + bj * HALF;
;                     const u32x4 g = *(const u32x4*)(P + row * INC + goff + col);
;                     const f32x4 a0 = acc[ai][bj][m][0], a1 = acc[ai][bj][m][1];
;                     float o[8] = {bflo(g.x) * a0[0], bfhi(g.x) * a0[1], bflo(g.y) * a0[2], bfhi(g.y) * a0[3], bflo(g.z) * a1[0], bfhi(g.z) * a1[1], bflo(g.w) * a1[2], bfhi(g.w) * a1[3]};
;                     if (mode) { const u32x4 t = *(const u32x4*)(T1 + row * D + col);
;                         o[0] += bflo(t.x); o[1] += bfhi(t.x); o[2] += bflo(t.y); o[3] += bfhi(t.y); o[4] += bflo(t.z); o[5] += bfhi(t.z); o[6] += bflo(t.w); o[7] += bfhi(t.w); }
;                     u32x4 w; w.x = pk2(o[0], o[1]); w.y = pk2(o[2], o[3]); w.z = pk2(o[4], o[5]); w.w = pk2(o[6], o[7]);
;                     if (mode) st16w(MM + row * D + col, w); else *(u32x4*)(T1 + row * D + col) = w;
; template <class Epi, class Sched, bool ALIGN_EPI = false, bool SP2 = false>
; __device__ __forceinline__ void gemm_phase(PG8_LAS unsigned char* lds, const Gemm g, const Sched& S, const Epi& E) {
;     ...
;         if constexpr (!Epi::AFTER_DRAIN) { E(acc, cur, wr, wc, fr, fq); S.done(cur); }
;         if (!has_next) break;
; #pragma unroll
;         for (int a = 0; a < 2; ++a)
; #pragma unroll
;             for (int b = 0; b < 2; ++b)
; #pragma unroll
;                 for (int m = 0; m < 4; ++m)
; #pragma unroll
;                     for (int n = 0; n < 2; ++n) acc[a][b][m][n] = (f32x4){0.f, 0.f, 0.f, 0.f};
;         cur = nxt; cA = nA; cB = nB; ++ui;
;         if constexpr (Sched::GATHER) { const u32x4 pv_ = *(const PG8_LAS u32x4*)(lds + STAGE_BYTES + tid * 16); vAc[0][0] = pv_.x; vAc[0][1] = pv_.y; vAc[1][0] = pv_.z; vAc[1][1] = pv_.w; }
;         if constexpr (ALIGN_EPI) { if (wr == 1) PG8_BAR; }
	v_lshlrev_b32_e32 v148, 16, v212
	v_and_b32_e32 v149, 0xffff0000, v212
	v_pk_mul_f32 v[38:39], v[38:39], v[148:149]
	v_lshlrev_b32_e32 v150, 16, v213
	v_and_b32_e32 v151, 0xffff0000, v213
	v_pk_mul_f32 v[40:41], v[40:41], v[150:151]
	v_lshlrev_b32_e32 v148, 16, v214
	v_and_b32_e32 v149, 0xffff0000, v214
	v_pk_mul_f32 v[34:35], v[34:35], v[148:149]
	v_lshlrev_b32_e32 v150, 16, v215
	v_and_b32_e32 v151, 0xffff0000, v215
	v_pk_mul_f32 v[36:37], v[36:37], v[150:151]
	v_cvt_pk_bf16_f32 v38, v38, v39
	v_cvt_pk_bf16_f32 v39, v40, v41
	v_cvt_pk_bf16_f32 v40, v34, v35
	v_cvt_pk_bf16_f32 v41, v36, v37
	v_add_u32_e32 v159, 0x48000, v157
	global_store_dwordx4 v159, v[38:41], s[24:25] offset:256
	s_waitcnt vmcnt(15)
	v_lshlrev_b32_e32 v148, 16, v216
	v_and_b32_e32 v149, 0xffff0000, v216
	v_pk_mul_f32 v[30:31], v[30:31], v[148:149]
	v_lshlrev_b32_e32 v150, 16, v217
	v_and_b32_e32 v151, 0xffff0000, v217
	v_pk_mul_f32 v[32:33], v[32:33], v[150:151]
	v_lshlrev_b32_e32 v148, 16, v218
	v_and_b32_e32 v149, 0xffff0000, v218
	v_pk_mul_f32 v[26:27], v[26:27], v[148:149]
	v_lshlrev_b32_e32 v150, 16, v219
	v_and_b32_e32 v151, 0xffff0000, v219
	v_pk_mul_f32 v[28:29], v[28:29], v[150:151]
	v_cvt_pk_bf16_f32 v30, v30, v31
	v_cvt_pk_bf16_f32 v31, v32, v33
	v_cvt_pk_bf16_f32 v32, v26, v27
	v_cvt_pk_bf16_f32 v33, v28, v29
	v_add_u32_e32 v159, 0x50000, v157
	global_store_dwordx4 v159, v[30:33], s[24:25]
	s_waitcnt vmcnt(15)
	v_lshlrev_b32_e32 v148, 16, v220
	v_and_b32_e32 v149, 0xffff0000, v220
	v_pk_mul_f32 v[22:23], v[22:23], v[148:149]
	v_lshlrev_b32_e32 v150, 16, v221
	v_and_b32_e32 v151, 0xffff0000, v221
	v_pk_mul_f32 v[24:25], v[24:25], v[150:151]
	v_lshlrev_b32_e32 v148, 16, v222
	v_and_b32_e32 v149, 0xffff0000, v222
	v_pk_mul_f32 v[18:19], v[18:19], v[148:149]
	v_lshlrev_b32_e32 v150, 16, v223
	v_and_b32_e32 v151, 0xffff0000, v223
	v_pk_mul_f32 v[20:21], v[20:21], v[150:151]
	v_cvt_pk_bf16_f32 v22, v22, v23
	v_cvt_pk_bf16_f32 v23, v24, v25
	v_cvt_pk_bf16_f32 v24, v18, v19
	v_cvt_pk_bf16_f32 v25, v20, v21
	v_add_u32_e32 v159, 0x50000, v157
	global_store_dwordx4 v159, v[22:25], s[24:25] offset:256
	s_waitcnt vmcnt(14)
	v_lshlrev_b32_e32 v148, 16, v160
	v_and_b32_e32 v149, 0xffff0000, v160
	v_pk_mul_f32 v[14:15], v[14:15], v[148:149]
	v_lshlrev_b32_e32 v150, 16, v161
	v_and_b32_e32 v151, 0xffff0000, v161
	v_pk_mul_f32 v[16:17], v[16:17], v[150:151]
	v_lshlrev_b32_e32 v148, 16, v162
	v_and_b32_e32 v149, 0xffff0000, v162
	v_pk_mul_f32 v[10:11], v[10:11], v[148:149]
	v_lshlrev_b32_e32 v150, 16, v163
	v_and_b32_e32 v151, 0xffff0000, v163
	v_pk_mul_f32 v[12:13], v[12:13], v[150:151]
	v_cvt_pk_bf16_f32 v14, v14, v15
	v_cvt_pk_bf16_f32 v15, v16, v17
	v_cvt_pk_bf16_f32 v16, v10, v11
	v_cvt_pk_bf16_f32 v17, v12, v13
	v_add_u32_e32 v159, 0x58000, v157
	global_store_dwordx4 v159, v[14:17], s[24:25]
	s_waitcnt vmcnt(14)
	v_lshlrev_b32_e32 v148, 16, v124
	v_and_b32_e32 v149, 0xffff0000, v124
	v_pk_mul_f32 v[6:7], v[6:7], v[148:149]
	v_lshlrev_b32_e32 v150, 16, v125
	v_and_b32_e32 v151, 0xffff0000, v125
	v_pk_mul_f32 v[8:9], v[8:9], v[150:151]
	v_lshlrev_b32_e32 v148, 16, v126
	v_and_b32_e32 v149, 0xffff0000, v126
	v_pk_mul_f32 v[2:3], v[2:3], v[148:149]
	v_lshlrev_b32_e32 v150, 16, v127
	v_and_b32_e32 v151, 0xffff0000, v127
	v_pk_mul_f32 v[4:5], v[4:5], v[150:151]
	v_cvt_pk_bf16_f32 v6, v6, v7
	v_cvt_pk_bf16_f32 v7, v8, v9
	v_cvt_pk_bf16_f32 v8, v2, v3
	v_cvt_pk_bf16_f32 v9, v4, v5
	v_add_u32_e32 v159, 0x58000, v157
	global_store_dwordx4 v159, v[6:9], s[24:25] offset:256
	s_nop 1
	s_mov_b64 s[24:25], 0x2400
	s_cbranch_vccnz .LBB13_814
	s_andn2_b64 vcc, exec, s[6:7]
	s_cbranch_vccnz .LBB13_813
	s_branch .LBB13_813

;     __device__ __forceinline__ size_t boff(const Unit& u) const { return (size_t)__builtin_amdgcn_readfirstlane(panel_e[u.pm]) * estride; }
; #define PG8_STAGE(bufoff, gbase, voff) PG8_STAGE_X(bufoff, gbase, voff, PG8_B_AUX)
; #define PG8_BAR __builtin_amdgcn_s_barrier()
; template <class Epi, class Sched, bool ALIGN_EPI = false, bool SP2 = false>
; __device__ __forceinline__ void gemm_phase(PG8_LAS unsigned char* lds, const Gemm g, const Sched& S, const Epi& E) {
;     ...
;     const int tid = tid_, wid = __builtin_amdgcn_readfirstlane(tid >> 6), lane = tid & 63, wr = wid >> 2, wc = wid & 3, fr = lane & 15, fq = lane >> 4;
;     const int K = g.K, nt = K / BK;
;     unsigned voffA[2], voffB[2];
; #pragma unroll
;     for (int i = 0; i < 2; ++i) { int R, C; stage_rc(tid * 16 + i * 8192, R, C); const int Rb = Epi::PERM ? ((R & ~31) + perm32(R & 31)) : R;
;         voffA[i] = (unsigned)(R * K + C) * 2u; voffB[i] = (unsigned)(Rb * K + C) * 2u; }
;     unsigned vAc[2][2] = {{0u, 0u}, {0u, 0u}}, vAn[2][2] = {{0u, 0u}, {0u, 0u}};
;     ...
;     const size_t kstep = (size_t)(BK * 2);
;     const size_t hstep = (size_t)HALF * K * 2;
;     const size_t tstep = 2 * hstep;
;     const unsigned ldsw = (unsigned)wid * 1024u;
;     const int aoff = lds_byte(wr * 64 + fr, fq * 8), boff = lds_byte(wc * 32 + fr, fq * 8);
;     ...
;     Unit cur, nxt; int ui = 0;
;     if (!S.next(0, cur)) return;
;     f32x4 acc[2][2][4][2];
; #pragma unroll
;     for (int a = 0; a < 2; ++a)
; #pragma unroll
;         for (int b = 0; b < 2; ++b)
; #pragma unroll
;             for (int m = 0; m < 4; ++m)
; #pragma unroll
;                 for (int n = 0; n < 2; ++n) acc[a][b][m][n] = (f32x4){0.f, 0.f, 0.f, 0.f};
;     bf16x8 At[4][2], B0[2][2], B1[2][2];
;     const char* cA = Sched::GATHER ? (const char*)g.A : (const char*)g.A + (size_t)cur.pm * tstep; PG8_SETA(vAc, cur); const char* cB = (const char*)g.Bt + S.boff(cur) + (size_t)cur.pn * tstep;
;     S.a_ready(cur);
;     if constexpr (SP2) {
;         PG8_STAGE(PG8_SB(0, 0), cB, voffB); PG8_STAGE(PG8_SB(0, 1), cB + hstep, voffB); PG8_STAGE_A(PG8_SA(0, 0), 0, cA, false); PG8_STAGE_A(PG8_SA(0, 1), 1, cA, false);
;         if (wr == 1) PG8_BAR;
;         PG8_WAIT_V(2); PG8_BAR;
;         PG8_STAGE(PG8_SB(1, 0), cB + kstep, voffB); PG8_STAGE_A(PG8_SA(1, 0), 0, cA + kstep, false); PG8_STAGE(PG8_SB(1, 1), cB + hstep + kstep, voffB);
;         PG8_WAIT_V(6); PG8_BAR;
.LBB13_831:
	s_or_b64 exec, exec, s[4:5]
	s_add_u32 s6, s3, 0x34100000
	s_addc_u32 s7, s48, 0
	s_add_u32 s28, s3, 0x2de00000
	v_mov_b32_e32 v16, v0
	s_addc_u32 s29, s48, 0
	s_barrier
	s_andn2_b64 vcc, exec, s[10:11]
	v_readfirstlane_b32 s5, v16
	s_cbranch_vccnz .LBB13_851
	v_lshlrev_b32_e32 v2, 4, v16
	v_add_u32_e32 v3, 0x2000, v2
	v_ashrrev_i32_e32 v4, 31, v3
	v_lshrrev_b32_e32 v4, 22, v4
	v_add_u32_e32 v4, v3, v4
	v_ashrrev_i32_e32 v10, 10, v4
	v_mul_i32_i24_e32 v4, 0x400, v10
	v_sub_u32_e32 v3, v3, v4
	v_lshrrev_b32_e32 v4, 4, v3
	v_bitop3_b32 v3, v4, v3, 32 bitop3:0x6c
	v_ashrrev_i32_e32 v4, 31, v3
	v_lshrrev_b32_e32 v4, 26, v4
	v_add_u32_e32 v4, v3, v4
	v_lshlrev_b32_e32 v5, 3, v10
	v_ashrrev_i32_e32 v11, 6, v4
	v_and_b32_e32 v5, -16, v5
	v_add_u32_e32 v5, v11, v5
	v_and_b32_e32 v6, 3, v11
	s_mov_b32 s3, 0x1fffe0
	v_lshrrev_b32_e32 v7, 2, v5
	v_lshlrev_b32_e32 v8, 1, v5
	v_and_b32_e32 v4, 0xc0, v4
	v_and_or_b32 v6, v5, s3, v6
	v_and_b32_e32 v7, 4, v7
	v_and_b32_e32 v8, 24, v8
	v_sub_u32_e32 v3, v3, v4
	v_or3_b32 v6, v6, v7, v8
	v_lshlrev_b32_e32 v7, 5, v10
	v_ashrrev_i16_sdwa v3, v238, sext(v3) dst_sel:DWORD dst_unused:UNUSED_PAD src0_sel:DWORD src1_sel:BYTE_0
	v_and_b32_e32 v7, 32, v7
	v_bfe_i32 v12, v3, 0, 16
	s_ashr_i32 s11, s5, 6
	v_add_lshl_u32 v3, v7, v12, 1
	s_ashr_i32 s14, s5, 8
	s_lshl_b32 s10, s11, 10
	v_lshl_add_u32 v136, v6, 11, v3
	v_lshl_add_u32 v138, v5, 11, v3
	v_bfe_i32 v3, v16, 27, 1
	v_lshrrev_b32_e32 v3, 22, v3
	s_and_b64 s[8:9], s[8:9], exec
	v_add_u32_e32 v3, v2, v3
	s_cselect_b32 s1, s2, s1
	v_and_b32_e32 v3, 0xfffffc00, v3
	s_add_i32 s0, s1, s0
	v_sub_u32_e32 v2, v2, v3
	s_ashr_i32 s1, s0, 31
	v_lshrrev_b32_e32 v3, 4, v2
	v_ashrrev_i32_e32 v4, 31, v16
	s_lshr_b32 s1, s1, 28
	v_bitop3_b32 v2, v3, v2, 32 bitop3:0x6c
	v_lshrrev_b32_e32 v4, 26, v4
	s_add_i32 s1, s0, s1
	v_ashrrev_i32_e32 v3, 31, v2
	v_add_u32_e32 v4, v16, v4
	s_ashr_i32 s2, s1, 4
	s_and_b32 s1, s1, 0xfff0
	v_lshrrev_b32_e32 v3, 26, v3
	v_ashrrev_i32_e32 v14, 6, v4
	s_sub_i32 s0, s0, s1
	v_add_u32_e32 v3, v2, v3
	v_lshlrev_b32_e32 v4, 3, v14
	s_bfe_i32 s1, s0, 0x80000
	v_ashrrev_i32_e32 v13, 6, v3
	v_and_b32_e32 v4, -16, v4
	s_bfe_u32 s1, s1, 0x2000d
	v_add_u32_e32 v4, v13, v4
	v_and_b32_e32 v5, 3, v13
	s_add_i32 s1, s0, s1
	v_and_or_b32 v5, v4, s3, v5
	s_bfe_i32 s3, s1, 0x80000
	s_and_b32 s1, s1, 0xfc
	s_sub_i32 s0, s0, s1
	s_lshl_b32 s2, s2, 2
	s_sext_i32_i16 s3, s3
	s_sext_i32_i8 s0, s0
	s_lshr_b32 s4, s3, 2
	s_add_i32 s12, s2, s0
	s_ashr_i32 s13, s12, 31
	s_bfe_i64 s[0:1], s[4:5], 0x100000
	s_lshl_b64 s[8:9], s[12:13], 19
	s_lshl_b64 s[0:1], s[0:1], 19
	v_lshrrev_b32_e32 v6, 2, v4
	v_lshlrev_b32_e32 v7, 1, v4
	v_and_b32_e32 v3, 0xc0, v3
	s_add_u32 s24, s42, s0
	v_and_b32_e32 v6, 4, v6
	v_and_b32_e32 v7, 24, v7
	v_sub_u32_e32 v2, v2, v3
	s_addc_u32 s25, s43, s1
	s_add_i32 s0, s46, s10
	v_or3_b32 v5, v5, v6, v7
	v_lshlrev_b32_e32 v6, 5, v14
	v_ashrrev_i16_sdwa v2, v238, sext(v2) dst_sel:DWORD dst_unused:UNUSED_PAD src0_sel:DWORD src1_sel:BYTE_0
	s_add_i32 s1, s0, 0x2000
	v_and_b32_e32 v6, 32, v6
	v_bfe_i32 v15, v2, 0, 16
	s_add_u32 s16, s24, 0x40000
	v_add_lshl_u32 v2, v6, v15, 1
	s_addc_u32 s17, s25, 0
	s_add_i32 s2, s47, s10
	v_lshl_add_u32 v140, v5, 11, v2
	s_mov_b32 m0, s0
	s_add_i32 s3, s2, 0x2000
	global_load_lds_dwordx4 v140, s[24:25]
	s_mov_b32 m0, s1
	s_add_u32 s22, s28, s8
	global_load_lds_dwordx4 v136, s[24:25]
	s_mov_b32 m0, s2
	s_addc_u32 s23, s29, s9
	s_add_i32 s48, s36, s10
	global_load_lds_dwordx4 v140, s[16:17]
	s_mov_b32 m0, s3
	s_add_i32 s49, s48, 0x2000
	v_lshl_add_u32 v142, v4, 11, v2
	global_load_lds_dwordx4 v136, s[16:17]
	s_mov_b32 m0, s48
	s_add_u32 s8, s22, 0x40000
	global_load_lds_dwordx4 v142, s[22:23]
	s_mov_b32 m0, s49
	s_addc_u32 s9, s23, 0
	s_add_i32 s53, s48, 0x4000
	global_load_lds_dwordx4 v138, s[22:23]
	s_mov_b32 m0, s53
	s_add_i32 s56, s48, 0x6000
	global_load_lds_dwordx4 v142, s[8:9]
	s_mov_b32 m0, s56
	v_mov_b32_e32 v141, v98
	global_load_lds_dwordx4 v138, s[8:9]
	v_mov_b32_e32 v137, v98
	v_mov_b32_e32 v143, v98
	v_mov_b32_e32 v139, v98
	s_cmp_eq_u32 s14, 1
	v_lshl_add_u64 v[8:9], s[24:25], 0, v[140:141]
	v_lshl_add_u64 v[6:7], s[24:25], 0, v[136:137]
	v_lshl_add_u64 v[2:3], s[22:23], 0, v[142:143]
	s_cselect_b64 s[8:9], -1, 0
	s_cmp_lg_u32 s14, 1
	v_lshl_add_u64 v[4:5], s[22:23], 0, v[138:139]
	s_cbranch_scc1 .LBB13_834
.LBB13_834:
	v_lshrrev_b32_e32 v18, 1, v16
	v_and_b32_e32 v18, 24, v18
	v_and_b32_e32 v17, 15, v16
	v_lshlrev_b32_e32 v19, 1, v18
	v_lshlrev_b32_e32 v16, 2, v16
	s_sext_i32_i8 s13, s4
	v_lshl_or_b32 v99, s14, 6, v17
	v_lshl_or_b32 v17, v17, 6, v19
	s_lshl_b32 s4, s14, 13
	v_and_b32_e32 v16, 32, v16
	v_bitop3_b32 v19, v17, s4, v16 bitop3:0xde
	s_lshl_b32 s4, s11, 5
	s_add_i32 s57, s50, s10
	s_and_b32 s4, s4, 0x60
	v_lshl_add_u64 v[8:9], v[8:9], 0, s[54:55]
	s_mov_b32 m0, s57
	s_add_i32 s58, s57, 0x2000
	s_lshl_b32 s11, s4, 7
	s_waitcnt vmcnt(2)
	s_barrier
	global_load_lds_dwordx4 v[8:9], off
	v_lshl_add_u64 v[6:7], v[6:7], 0, s[54:55]
	s_mov_b32 m0, s58
	s_add_i32 s59, s48, 0x8000
	s_add_i32 s61, s48, 0xa000
	global_load_lds_dwordx4 v[6:7], off
	v_lshl_add_u64 v[2:3], v[2:3], 0, s[54:55]
	s_mov_b32 m0, s59
	s_add_u32 s14, s24, 0x40080
	global_load_lds_dwordx4 v[2:3], off
	v_lshl_add_u64 v[2:3], v[4:5], 0, s[54:55]
	s_mov_b32 m0, s61
	s_addc_u32 s15, s25, 0
	s_add_i32 s68, s51, s10
	global_load_lds_dwordx4 v[2:3], off
	v_lshl_add_u64 v[2:3], s[14:15], 0, v[140:141]
	s_mov_b32 m0, s68
	s_add_i32 s69, s68, 0x2000
	global_load_lds_dwordx4 v[2:3], off
	v_lshl_add_u64 v[2:3], s[14:15], 0, v[136:137]
	s_mov_b32 m0, s69
	s_cmpk_lt_u32 s5, 0x100
	global_load_lds_dwordx4 v[2:3], off
	v_lshlrev_b32_e32 v2, 14, v14
	v_and_b32_e32 v2, 0xffff8000, v2
	v_lshl_add_u32 v2, v13, 11, v2
	v_and_b32_e32 v3, 1, v14
	v_lshl_or_b32 v2, v3, 6, v2
	v_lshl_add_u32 v144, v15, 1, v2
	v_lshlrev_b32_e32 v2, 14, v10
	v_and_b32_e32 v2, 0xffff8000, v2
	s_waitcnt vmcnt(6)
	v_lshl_add_u32 v2, v11, 11, v2
	v_and_b32_e32 v3, 1, v10
	v_lshl_or_b32 v2, v3, 6, v2
	v_bitop3_b32 v152, v17, s11, v16 bitop3:0xde
	s_cselect_b64 s[10:11], -1, 0
	v_or_b32_e32 v153, s4, v18
	v_mov_b32_e32 v145, v98
	v_lshl_add_u32 v146, v12, 1, v2
	v_mov_b32_e32 v147, v98
	s_mov_b32 s88, 0
	v_add_u32_e32 v154, s36, v19
	s_barrier
	s_branch .LBB13_837

; #define PG8_LAS __attribute__((address_space(3)))
; #define PG8_STAGE_A(bufoff, h, ptr, nsel) do { if constexpr (Sched::GATHER) { if (nsel) PG8_STAGE_X(bufoff, ptr, vAn[h], PG8_A_AUX); else PG8_STAGE_X(bufoff, ptr, vAc[h], PG8_A_AUX); } \
;         else PG8_STAGE_X(bufoff, (ptr) + (h) * hstep, voffA, PG8_A_AUX); } while (0)
; #define PG8_STAGE(bufoff, gbase, voff) PG8_STAGE_X(bufoff, gbase, voff, PG8_B_AUX)
; #define PG8_LDA(dst, b, h) do { _Pragma("unroll") for (int m = 0; m < 4; ++m) _Pragma("unroll") for (int k = 0; k < 2; ++k) dst[m][k] = *(const PG8_LAS bf16x8*)(lds + PG8_SA(b, h) + aoff + m * 2048 + k * 1024); } while (0)
; #define PG8_LDB(dst, b, h) do { _Pragma("unroll") for (int n = 0; n < 2; ++n) _Pragma("unroll") for (int k = 0; k < 2; ++k) dst[n][k] = *(const PG8_LAS bf16x8*)(lds + PG8_SB(b, h) + boff + n * 2048 + k * 1024); } while (0)
; #define PG8_WAIT_V(n) asm volatile("s_waitcnt vmcnt(" #n ")" ::: "memory")
; #define PG8_WAIT_L(n) asm volatile("s_waitcnt lgkmcnt(" #n ")" ::: "memory")
; #define PG8_BAR __builtin_amdgcn_s_barrier()
; template <class Epi, class Sched, bool ALIGN_EPI = false, bool SP2 = false>
; __device__ __forceinline__ void gemm_phase(PG8_LAS unsigned char* lds, const Gemm g, const Sched& S, const Epi& E) {
;     ...
;             PG8_LDB(B0, 0, 0); PG8_LDB(B1, 0, 1); PG8_SCHED; PG8_LDA(At, 0, 0); PG8_STAGE_A(PG8_SA(1, 1), 1, a1, false);
;             PG8_WAIT_V(8); PG8_WAIT_L(0); PG8_BAR; PG8_MMA(0, 0, At, B0); PG8_MMA(0, 1, At, B1); PG8_BAR; PG8_SCHED;
;             PG8_LDA(At, 0, 1); PG8_STAGE(PG8_SB(0, 0), b2, voffB); PG8_STAGE(PG8_SB(0, 1), b2 + hstep, voffB); PG8_STAGE_A(PG8_SA(0, 0), 0, a2, last);
;             PG8_WAIT_V(8); PG8_WAIT_L(0); PG8_BAR; PG8_MMA(1, 0, At, B0); PG8_MMA(1, 1, At, B1); PG8_BAR; PG8_SCHED;
;     ...
; #pragma unroll
;         for (int a = 0; a < 2; ++a)
; #pragma unroll
;             for (int b = 0; b < 2; ++b)
; #pragma unroll
;                 for (int m = 0; m < 4; ++m)
; #pragma unroll
;                     for (int n = 0; n < 2; ++n) acc[a][b][m][n] = (f32x4){0.f, 0.f, 0.f, 0.f};
;         cur = nxt; cA = nA; cB = nB; ++ui;
;         if constexpr (Sched::GATHER) { const u32x4 pv_ = *(const PG8_LAS u32x4*)(lds + STAGE_BYTES + tid * 16); vAc[0][0] = pv_.x; vAc[0][1] = pv_.y; vAc[1][0] = pv_.z; vAc[1][1] = pv_.w; }
;         if constexpr (ALIGN_EPI) { if (wr == 1) PG8_BAR; }
.LBB13_843:
	s_ashr_i32 s17, s16, 31
	s_lshl_b64 s[18:19], s[16:17], 19
	s_add_u32 s18, s28, s18
	s_addc_u32 s19, s29, s19
	s_and_b64 s[20:21], s[4:5], exec
	s_cselect_b32 s17, s19, s23
	s_cselect_b32 s34, s18, s22
	s_ashr_i32 s15, s14, 31
	s_lshl_b64 s[20:21], s[14:15], 19
	s_add_u32 s20, s42, s20
	s_addc_u32 s21, s43, s21
	s_and_b64 s[26:27], s[4:5], exec
	s_cselect_b32 s15, s21, s25
	s_cselect_b32 s38, s20, s24
	s_add_u32 s22, s22, 0x40080
	s_addc_u32 s23, s23, 0
	s_add_u32 s52, s24, 0x100
	v_mov_b32_e32 v2, 0
	s_addc_u32 s60, s25, 0
	s_mov_b32 s64, -2
	v_mov_b32_e32 v3, v2
	v_mov_b64_e32 v[4:5], 0
	v_mov_b64_e32 v[6:7], 0
	v_mov_b64_e32 v[8:9], 0
	v_mov_b64_e32 v[18:19], 0
	v_mov_b64_e32 v[20:21], 0
	v_mov_b64_e32 v[22:23], 0
	v_mov_b64_e32 v[24:25], 0
	v_mov_b64_e32 v[34:35], 0
	v_mov_b64_e32 v[36:37], 0
	v_mov_b64_e32 v[38:39], 0
	v_mov_b64_e32 v[40:41], 0
	v_mov_b64_e32 v[50:51], 0
	v_mov_b64_e32 v[52:53], 0
	v_mov_b64_e32 v[54:55], 0
	v_mov_b64_e32 v[56:57], 0
	v_mov_b64_e32 v[10:11], 0
	v_mov_b64_e32 v[12:13], 0
	v_mov_b64_e32 v[14:15], 0
	v_mov_b64_e32 v[16:17], 0
	v_mov_b64_e32 v[26:27], 0
	v_mov_b64_e32 v[28:29], 0
	v_mov_b64_e32 v[30:31], 0
	v_mov_b64_e32 v[32:33], 0
	v_mov_b64_e32 v[42:43], 0
	v_mov_b64_e32 v[44:45], 0
	v_mov_b64_e32 v[46:47], 0
	v_mov_b64_e32 v[48:49], 0
	v_mov_b64_e32 v[58:59], 0
	v_mov_b64_e32 v[60:61], 0
	v_mov_b64_e32 v[62:63], 0
	v_mov_b64_e32 v[64:65], 0
	v_mov_b64_e32 v[66:67], 0
	v_mov_b64_e32 v[68:69], 0
	v_mov_b64_e32 v[70:71], 0
	v_mov_b64_e32 v[72:73], 0
	v_mov_b64_e32 v[82:83], 0
	v_mov_b64_e32 v[84:85], 0
	v_mov_b64_e32 v[86:87], 0
	v_mov_b64_e32 v[88:89], 0
	v_mov_b64_e32 v[100:101], 0
	v_mov_b64_e32 v[102:103], 0
	v_mov_b64_e32 v[104:105], 0
	v_mov_b64_e32 v[106:107], 0
	v_mov_b64_e32 v[116:117], 0
	v_mov_b64_e32 v[118:119], 0
	v_mov_b64_e32 v[120:121], 0
	v_mov_b64_e32 v[122:123], 0
	v_mov_b64_e32 v[74:75], 0
	v_mov_b64_e32 v[76:77], 0
	v_mov_b64_e32 v[78:79], 0
	v_mov_b64_e32 v[80:81], 0
	v_mov_b64_e32 v[90:91], 0
	v_mov_b64_e32 v[92:93], 0
	v_mov_b64_e32 v[94:95], 0
	v_mov_b64_e32 v[96:97], 0
	v_mov_b64_e32 v[108:109], 0
	v_mov_b64_e32 v[110:111], 0
	v_mov_b64_e32 v[112:113], 0
	v_mov_b64_e32 v[114:115], 0
	v_mov_b64_e32 v[124:125], 0
	v_mov_b64_e32 v[126:127], 0
	v_mov_b64_e32 v[128:129], 0
	v_mov_b64_e32 v[130:131], 0
	s_and_b64 s[98:99], exec, s[10:11]
	s_cbranch_scc1 .Lrb_844
	s_barrier
.Lrb_844:
.LBB13_844:
	v_add_u32_e32 v155, s46, v152
	ds_read_b128 v[148:151], v155
	ds_read_b128 v[156:159], v155 offset:1024
	ds_read_b128 v[160:163], v155 offset:2048
	ds_read_b128 v[164:167], v155 offset:3072
	v_add_u32_e32 v155, s47, v152
	ds_read_b128 v[168:171], v155
	ds_read_b128 v[172:175], v155 offset:1024
	ds_read_b128 v[176:179], v155 offset:2048
	ds_read_b128 v[180:183], v155 offset:3072
	s_add_u32 s24, s22, 0xfffc0080
	s_addc_u32 s25, s23, -1
	s_cmp_eq_u32 s64, 12
	s_cselect_b32 s27, s17, s25
	s_cselect_b32 s26, s34, s24
	s_cselect_b32 s25, s15, s60
	s_cselect_b32 s24, s38, s52
	v_lshl_add_u64 v[224:225], s[22:23], 0, v[144:145]
	s_add_i32 m0, s48, 0xc000
	ds_read_b128 v[184:187], v154
	ds_read_b128 v[188:191], v154 offset:1024
	ds_read_b128 v[192:195], v154 offset:2048
	ds_read_b128 v[196:199], v154 offset:3072
	ds_read_b128 v[208:211], v154 offset:4096
	ds_read_b128 v[212:215], v154 offset:5120
	ds_read_b128 v[216:219], v154 offset:6144
	ds_read_b128 v[220:223], v154 offset:7168
	global_load_lds_dwordx4 v[224:225], off
	v_lshl_add_u64 v[224:225], s[22:23], 0, v[146:147]
	s_add_i32 m0, s48, 0xe000
	s_nop 0
	global_load_lds_dwordx4 v[224:225], off
	s_waitcnt vmcnt(8)
	s_waitcnt lgkmcnt(0)
	s_barrier
	s_setprio 1
	s_waitcnt lgkmcnt(0)
	v_mfma_f32_16x16x32_bf16 v[128:131], v[148:151], v[184:187], v[128:131]
	v_mfma_f32_16x16x32_bf16 v[124:127], v[160:163], v[184:187], v[124:127]
	v_mfma_f32_16x16x32_bf16 v[112:115], v[148:151], v[192:195], v[112:115]
	v_mfma_f32_16x16x32_bf16 v[108:111], v[160:163], v[192:195], v[108:111]
	v_mfma_f32_16x16x32_bf16 v[94:97], v[148:151], v[208:211], v[94:97]
	v_mfma_f32_16x16x32_bf16 v[90:93], v[160:163], v[208:211], v[90:93]
	v_mfma_f32_16x16x32_bf16 v[78:81], v[148:151], v[216:219], v[78:81]
	v_mfma_f32_16x16x32_bf16 v[74:77], v[160:163], v[216:219], v[74:77]
	v_mfma_f32_16x16x32_bf16 v[128:131], v[156:159], v[188:191], v[128:131]
	v_mfma_f32_16x16x32_bf16 v[124:127], v[164:167], v[188:191], v[124:127]
	v_mfma_f32_16x16x32_bf16 v[112:115], v[156:159], v[196:199], v[112:115]
	v_mfma_f32_16x16x32_bf16 v[108:111], v[164:167], v[196:199], v[108:111]
	v_mfma_f32_16x16x32_bf16 v[94:97], v[156:159], v[212:215], v[94:97]
	v_mfma_f32_16x16x32_bf16 v[90:93], v[164:167], v[212:215], v[90:93]
	v_mfma_f32_16x16x32_bf16 v[78:81], v[156:159], v[220:223], v[78:81]
	v_mfma_f32_16x16x32_bf16 v[74:77], v[164:167], v[220:223], v[74:77]
	s_setprio 0
	s_setprio 1
	v_mfma_f32_16x16x32_bf16 v[120:123], v[168:171], v[184:187], v[120:123]
	v_mfma_f32_16x16x32_bf16 v[116:119], v[176:179], v[184:187], v[116:119]
	v_mfma_f32_16x16x32_bf16 v[104:107], v[168:171], v[192:195], v[104:107]
	v_mfma_f32_16x16x32_bf16 v[100:103], v[176:179], v[192:195], v[100:103]
	v_mfma_f32_16x16x32_bf16 v[86:89], v[168:171], v[208:211], v[86:89]
	v_mfma_f32_16x16x32_bf16 v[82:85], v[176:179], v[208:211], v[82:85]
	v_mfma_f32_16x16x32_bf16 v[70:73], v[168:171], v[216:219], v[70:73]
	v_mfma_f32_16x16x32_bf16 v[66:69], v[176:179], v[216:219], v[66:69]
	v_mfma_f32_16x16x32_bf16 v[120:123], v[172:175], v[188:191], v[120:123]
	v_mfma_f32_16x16x32_bf16 v[116:119], v[180:183], v[188:191], v[116:119]
	v_mfma_f32_16x16x32_bf16 v[104:107], v[172:175], v[196:199], v[104:107]
	v_mfma_f32_16x16x32_bf16 v[100:103], v[180:183], v[196:199], v[100:103]
	v_mfma_f32_16x16x32_bf16 v[86:89], v[172:175], v[212:215], v[86:89]
	v_mfma_f32_16x16x32_bf16 v[82:85], v[180:183], v[212:215], v[82:85]
	v_mfma_f32_16x16x32_bf16 v[70:73], v[172:175], v[220:223], v[70:73]
	v_mfma_f32_16x16x32_bf16 v[66:69], v[180:183], v[220:223], v[66:69]
	s_setprio 0
	s_barrier
; #define PG8_STAGE_A(bufoff, h, ptr, nsel) do { if constexpr (Sched::GATHER) { if (nsel) PG8_STAGE_X(bufoff, ptr, vAn[h], PG8_A_AUX); else PG8_STAGE_X(bufoff, ptr, vAc[h], PG8_A_AUX); } \
;         else PG8_STAGE_X(bufoff, (ptr) + (h) * hstep, voffA, PG8_A_AUX); } while (0)
; #define PG8_STAGE(bufoff, gbase, voff) PG8_STAGE_X(bufoff, gbase, voff, PG8_B_AUX)
; #define PG8_LDA(dst, b, h) do { _Pragma("unroll") for (int m = 0; m < 4; ++m) _Pragma("unroll") for (int k = 0; k < 2; ++k) dst[m][k] = *(const PG8_LAS bf16x8*)(lds + PG8_SA(b, h) + aoff + m * 2048 + k * 1024); } while (0)
; #define PG8_LDB(dst, b, h) do { _Pragma("unroll") for (int n = 0; n < 2; ++n) _Pragma("unroll") for (int k = 0; k < 2; ++k) dst[n][k] = *(const PG8_LAS bf16x8*)(lds + PG8_SB(b, h) + boff + n * 2048 + k * 1024); } while (0)
; #define PG8_MMA(ai, bj, At, Bt) do { __builtin_amdgcn_s_setprio(1); _Pragma("unroll") for (int m = 0; m < 4; ++m) _Pragma("unroll") for (int n = 0; n < 2; ++n) _Pragma("unroll") for (int k = 0; k < 2; ++k) \
;         acc[ai][bj][m][n] = __builtin_amdgcn_mfma_f32_16x16x32_bf16(Bt[n][k], At[m][k], acc[ai][bj][m][n], 0, 0, 0); __builtin_amdgcn_s_setprio(0); } while (0)
; #define PG8_WAIT_V(n) asm volatile("s_waitcnt vmcnt(" #n ")" ::: "memory")
; #define PG8_WAIT_L(n) asm volatile("s_waitcnt lgkmcnt(" #n ")" ::: "memory")
; #define PG8_BAR __builtin_amdgcn_s_barrier()
; #define PG8_SCHED __builtin_amdgcn_sched_barrier(0)
; template <class Epi, class Sched, bool ALIGN_EPI = false, bool SP2 = false>
; __device__ __forceinline__ void gemm_phase(PG8_LAS unsigned char* lds, const Gemm g, const Sched& S, const Epi& E) {
;     ...
;             PG8_WAIT_V(8); PG8_WAIT_L(0); PG8_BAR; PG8_MMA(0, 0, At, B0); PG8_MMA(0, 1, At, B1); PG8_BAR; PG8_SCHED;
;             PG8_LDA(At, 0, 1); PG8_STAGE(PG8_SB(0, 0), b2, voffB); PG8_STAGE(PG8_SB(0, 1), b2 + hstep, voffB); PG8_STAGE_A(PG8_SA(0, 0), 0, a2, last);
;             PG8_WAIT_V(8); PG8_WAIT_L(0); PG8_BAR; PG8_MMA(1, 0, At, B0); PG8_MMA(1, 1, At, B1); PG8_BAR; PG8_SCHED;
;             PG8_LDB(B0, 1, 0); PG8_LDB(B1, 1, 1); PG8_SCHED; PG8_LDA(At, 1, 0); PG8_STAGE_A(PG8_SA(0, 1), 1, a2, last);
;             PG8_WAIT_V(8); PG8_WAIT_L(0); PG8_BAR; PG8_MMA(0, 0, At, B0); PG8_MMA(0, 1, At, B1); PG8_BAR; PG8_SCHED;
	s_mov_b32 m0, s0
	v_lshl_add_u64 v[224:225], s[24:25], 0, v[140:141]
	s_add_u32 s72, s24, 0x40000
	ds_read_b128 v[184:187], v154 offset:16384
	ds_read_b128 v[188:191], v154 offset:17408
	ds_read_b128 v[192:195], v154 offset:18432
	ds_read_b128 v[196:199], v154 offset:19456
	ds_read_b128 v[208:211], v154 offset:20480
	ds_read_b128 v[212:215], v154 offset:21504
	ds_read_b128 v[216:219], v154 offset:22528
	ds_read_b128 v[220:223], v154 offset:23552
	global_load_lds_dwordx4 v[224:225], off
	v_lshl_add_u64 v[226:227], s[24:25], 0, v[136:137]
	s_mov_b32 m0, s1
	s_addc_u32 s73, s25, 0
	global_load_lds_dwordx4 v[226:227], off
	v_lshl_add_u64 v[228:229], s[72:73], 0, v[140:141]
	s_mov_b32 m0, s2
	v_lshl_add_u64 v[230:231], s[26:27], 0, v[138:139]
	global_load_lds_dwordx4 v[228:229], off
	v_lshl_add_u64 v[228:229], s[72:73], 0, v[136:137]
	s_mov_b32 m0, s3
	s_nop 0
	global_load_lds_dwordx4 v[228:229], off
	v_lshl_add_u64 v[228:229], s[26:27], 0, v[142:143]
	s_mov_b32 m0, s48
	s_nop 0
	global_load_lds_dwordx4 v[228:229], off
	s_mov_b32 m0, s49
	s_nop 0
	global_load_lds_dwordx4 v[230:231], off
	s_waitcnt vmcnt(8)
	s_waitcnt lgkmcnt(0)
	s_barrier
	s_setprio 1
	s_waitcnt lgkmcnt(0)
	v_mfma_f32_16x16x32_bf16 v[62:65], v[148:151], v[184:187], v[62:65]
	v_mfma_f32_16x16x32_bf16 v[58:61], v[160:163], v[184:187], v[58:61]
	v_mfma_f32_16x16x32_bf16 v[46:49], v[148:151], v[192:195], v[46:49]
	v_mfma_f32_16x16x32_bf16 v[42:45], v[160:163], v[192:195], v[42:45]
	v_mfma_f32_16x16x32_bf16 v[30:33], v[148:151], v[208:211], v[30:33]
	v_mfma_f32_16x16x32_bf16 v[26:29], v[160:163], v[208:211], v[26:29]
	v_mfma_f32_16x16x32_bf16 v[14:17], v[148:151], v[216:219], v[14:17]
	v_mfma_f32_16x16x32_bf16 v[10:13], v[160:163], v[216:219], v[10:13]
	v_mfma_f32_16x16x32_bf16 v[62:65], v[156:159], v[188:191], v[62:65]
	v_mfma_f32_16x16x32_bf16 v[58:61], v[164:167], v[188:191], v[58:61]
	v_mfma_f32_16x16x32_bf16 v[46:49], v[156:159], v[196:199], v[46:49]
	v_mfma_f32_16x16x32_bf16 v[42:45], v[164:167], v[196:199], v[42:45]
	v_mfma_f32_16x16x32_bf16 v[30:33], v[156:159], v[212:215], v[30:33]
	v_mfma_f32_16x16x32_bf16 v[26:29], v[164:167], v[212:215], v[26:29]
	v_mfma_f32_16x16x32_bf16 v[14:17], v[156:159], v[220:223], v[14:17]
	v_mfma_f32_16x16x32_bf16 v[10:13], v[164:167], v[220:223], v[10:13]
	s_setprio 0
	s_setprio 1
	v_mfma_f32_16x16x32_bf16 v[54:57], v[168:171], v[184:187], v[54:57]
	v_mfma_f32_16x16x32_bf16 v[50:53], v[176:179], v[184:187], v[50:53]
	v_mfma_f32_16x16x32_bf16 v[38:41], v[168:171], v[192:195], v[38:41]
	v_mfma_f32_16x16x32_bf16 v[34:37], v[176:179], v[192:195], v[34:37]
	v_mfma_f32_16x16x32_bf16 v[22:25], v[168:171], v[208:211], v[22:25]
	v_mfma_f32_16x16x32_bf16 v[18:21], v[176:179], v[208:211], v[18:21]
	v_mfma_f32_16x16x32_bf16 v[6:9], v[168:171], v[216:219], v[6:9]
	v_mfma_f32_16x16x32_bf16 v[2:5], v[176:179], v[216:219], v[2:5]
	v_mfma_f32_16x16x32_bf16 v[54:57], v[172:175], v[188:191], v[54:57]
	v_mfma_f32_16x16x32_bf16 v[50:53], v[180:183], v[188:191], v[50:53]
	v_mfma_f32_16x16x32_bf16 v[38:41], v[172:175], v[196:199], v[38:41]
	v_mfma_f32_16x16x32_bf16 v[34:37], v[180:183], v[196:199], v[34:37]
	v_mfma_f32_16x16x32_bf16 v[22:25], v[172:175], v[212:215], v[22:25]
	v_mfma_f32_16x16x32_bf16 v[18:21], v[180:183], v[212:215], v[18:21]
	v_mfma_f32_16x16x32_bf16 v[6:9], v[172:175], v[220:223], v[6:9]
	v_mfma_f32_16x16x32_bf16 v[2:5], v[180:183], v[220:223], v[2:5]
	s_setprio 0
	s_barrier
	v_add_u32_e32 v155, s50, v152
	ds_read_b128 v[148:151], v155
	ds_read_b128 v[156:159], v155 offset:1024
	ds_read_b128 v[160:163], v155 offset:2048
	ds_read_b128 v[164:167], v155 offset:3072
	v_add_u32_e32 v155, s51, v152
	ds_read_b128 v[168:171], v155
	ds_read_b128 v[172:175], v155 offset:1024
	ds_read_b128 v[176:179], v155 offset:2048
	ds_read_b128 v[180:183], v155 offset:3072
	s_add_u32 s26, s26, 0x40000
	s_addc_u32 s27, s27, 0
	s_mov_b32 m0, s53
	v_lshl_add_u64 v[232:233], s[26:27], 0, v[142:143]
	ds_read_b128 v[184:187], v154 offset:32768
	ds_read_b128 v[188:191], v154 offset:33792
	ds_read_b128 v[192:195], v154 offset:34816
	ds_read_b128 v[196:199], v154 offset:35840
	ds_read_b128 v[208:211], v154 offset:36864
	ds_read_b128 v[212:215], v154 offset:37888
	ds_read_b128 v[216:219], v154 offset:38912
	ds_read_b128 v[220:223], v154 offset:39936
	global_load_lds_dwordx4 v[232:233], off
	v_lshl_add_u64 v[232:233], s[26:27], 0, v[138:139]
	s_mov_b32 m0, s56
	s_nop 0
	global_load_lds_dwordx4 v[232:233], off
	s_waitcnt vmcnt(8)
	s_waitcnt lgkmcnt(0)
	s_barrier
; #define PG8_STAGE_A(bufoff, h, ptr, nsel) do { if constexpr (Sched::GATHER) { if (nsel) PG8_STAGE_X(bufoff, ptr, vAn[h], PG8_A_AUX); else PG8_STAGE_X(bufoff, ptr, vAc[h], PG8_A_AUX); } \
;         else PG8_STAGE_X(bufoff, (ptr) + (h) * hstep, voffA, PG8_A_AUX); } while (0)
; #define PG8_STAGE(bufoff, gbase, voff) PG8_STAGE_X(bufoff, gbase, voff, PG8_B_AUX)
; #define PG8_LDA(dst, b, h) do { _Pragma("unroll") for (int m = 0; m < 4; ++m) _Pragma("unroll") for (int k = 0; k < 2; ++k) dst[m][k] = *(const PG8_LAS bf16x8*)(lds + PG8_SA(b, h) + aoff + m * 2048 + k * 1024); } while (0)
; #define PG8_MMA(ai, bj, At, Bt) do { __builtin_amdgcn_s_setprio(1); _Pragma("unroll") for (int m = 0; m < 4; ++m) _Pragma("unroll") for (int n = 0; n < 2; ++n) _Pragma("unroll") for (int k = 0; k < 2; ++k) \
;         acc[ai][bj][m][n] = __builtin_amdgcn_mfma_f32_16x16x32_bf16(Bt[n][k], At[m][k], acc[ai][bj][m][n], 0, 0, 0); __builtin_amdgcn_s_setprio(0); } while (0)
; #define PG8_WAIT_V(n) asm volatile("s_waitcnt vmcnt(" #n ")" ::: "memory")
; #define PG8_WAIT_L(n) asm volatile("s_waitcnt lgkmcnt(" #n ")" ::: "memory")
; #define PG8_BAR __builtin_amdgcn_s_barrier()
; #define PG8_SCHED __builtin_amdgcn_sched_barrier(0)
; template <class Epi, class Sched, bool ALIGN_EPI = false, bool SP2 = false>
; __device__ __forceinline__ void gemm_phase(PG8_LAS unsigned char* lds, const Gemm g, const Sched& S, const Epi& E) {
;     ...
;             PG8_WAIT_V(8); PG8_WAIT_L(0); PG8_BAR; PG8_MMA(0, 0, At, B0); PG8_MMA(0, 1, At, B1); PG8_BAR; PG8_SCHED;
;             PG8_LDA(At, 1, 1); PG8_STAGE(PG8_SB(1, 0), b3, voffB); PG8_STAGE(PG8_SB(1, 1), b3 + hstep, voffB); PG8_STAGE_A(PG8_SA(1, 0), 0, a3, last);
;             PG8_WAIT_V(8); PG8_WAIT_L(0); PG8_BAR; PG8_MMA(1, 0, At, B0); PG8_MMA(1, 1, At, B1); PG8_BAR; PG8_SCHED;
;     ...
;         if constexpr (ALIGN_EPI) { if (wr == 0) PG8_BAR; }
	s_setprio 1
	s_waitcnt lgkmcnt(0)
	v_mfma_f32_16x16x32_bf16 v[128:131], v[148:151], v[184:187], v[128:131]
	v_mfma_f32_16x16x32_bf16 v[124:127], v[160:163], v[184:187], v[124:127]
	v_mfma_f32_16x16x32_bf16 v[112:115], v[148:151], v[192:195], v[112:115]
	v_mfma_f32_16x16x32_bf16 v[108:111], v[160:163], v[192:195], v[108:111]
	v_mfma_f32_16x16x32_bf16 v[94:97], v[148:151], v[208:211], v[94:97]
	v_mfma_f32_16x16x32_bf16 v[90:93], v[160:163], v[208:211], v[90:93]
	v_mfma_f32_16x16x32_bf16 v[78:81], v[148:151], v[216:219], v[78:81]
	v_mfma_f32_16x16x32_bf16 v[74:77], v[160:163], v[216:219], v[74:77]
	v_mfma_f32_16x16x32_bf16 v[128:131], v[156:159], v[188:191], v[128:131]
	v_mfma_f32_16x16x32_bf16 v[124:127], v[164:167], v[188:191], v[124:127]
	v_mfma_f32_16x16x32_bf16 v[112:115], v[156:159], v[196:199], v[112:115]
	v_mfma_f32_16x16x32_bf16 v[108:111], v[164:167], v[196:199], v[108:111]
	v_mfma_f32_16x16x32_bf16 v[94:97], v[156:159], v[212:215], v[94:97]
	v_mfma_f32_16x16x32_bf16 v[90:93], v[164:167], v[212:215], v[90:93]
	v_mfma_f32_16x16x32_bf16 v[78:81], v[156:159], v[220:223], v[78:81]
	v_mfma_f32_16x16x32_bf16 v[74:77], v[164:167], v[220:223], v[74:77]
	s_setprio 0
	s_setprio 1
	v_mfma_f32_16x16x32_bf16 v[120:123], v[168:171], v[184:187], v[120:123]
	v_mfma_f32_16x16x32_bf16 v[116:119], v[176:179], v[184:187], v[116:119]
	v_mfma_f32_16x16x32_bf16 v[104:107], v[168:171], v[192:195], v[104:107]
	v_mfma_f32_16x16x32_bf16 v[100:103], v[176:179], v[192:195], v[100:103]
	v_mfma_f32_16x16x32_bf16 v[86:89], v[168:171], v[208:211], v[86:89]
	v_mfma_f32_16x16x32_bf16 v[82:85], v[176:179], v[208:211], v[82:85]
	v_mfma_f32_16x16x32_bf16 v[70:73], v[168:171], v[216:219], v[70:73]
	v_mfma_f32_16x16x32_bf16 v[66:69], v[176:179], v[216:219], v[66:69]
	v_mfma_f32_16x16x32_bf16 v[120:123], v[172:175], v[188:191], v[120:123]
	v_mfma_f32_16x16x32_bf16 v[116:119], v[180:183], v[188:191], v[116:119]
	v_mfma_f32_16x16x32_bf16 v[104:107], v[172:175], v[196:199], v[104:107]
	v_mfma_f32_16x16x32_bf16 v[100:103], v[180:183], v[196:199], v[100:103]
	v_mfma_f32_16x16x32_bf16 v[86:89], v[172:175], v[212:215], v[86:89]
	v_mfma_f32_16x16x32_bf16 v[82:85], v[180:183], v[212:215], v[82:85]
	v_mfma_f32_16x16x32_bf16 v[70:73], v[172:175], v[220:223], v[70:73]
	v_mfma_f32_16x16x32_bf16 v[66:69], v[180:183], v[220:223], v[66:69]
	s_setprio 0
	s_barrier
	s_mov_b32 m0, s57
	v_lshl_add_u64 v[224:225], v[224:225], 0, s[54:55]
	s_add_u32 s24, s24, 0x40080
	ds_read_b128 v[184:187], v154 offset:49152
	ds_read_b128 v[188:191], v154 offset:50176
	ds_read_b128 v[192:195], v154 offset:51200
	ds_read_b128 v[196:199], v154 offset:52224
	ds_read_b128 v[208:211], v154 offset:53248
	ds_read_b128 v[212:215], v154 offset:54272
	ds_read_b128 v[216:219], v154 offset:55296
	ds_read_b128 v[220:223], v154 offset:56320
	global_load_lds_dwordx4 v[224:225], off
	v_lshl_add_u64 v[224:225], v[226:227], 0, s[54:55]
	s_mov_b32 m0, s58
	s_addc_u32 s25, s25, 0
	global_load_lds_dwordx4 v[224:225], off
	v_lshl_add_u64 v[224:225], s[24:25], 0, v[140:141]
	s_mov_b32 m0, s68
	s_nop 0
	global_load_lds_dwordx4 v[224:225], off
	v_lshl_add_u64 v[224:225], s[24:25], 0, v[136:137]
	s_mov_b32 m0, s69
	s_nop 0
	global_load_lds_dwordx4 v[224:225], off
	v_lshl_add_u64 v[224:225], v[228:229], 0, s[54:55]
	s_mov_b32 m0, s59
	s_nop 0
	global_load_lds_dwordx4 v[224:225], off
	v_lshl_add_u64 v[224:225], v[230:231], 0, s[54:55]
	s_mov_b32 m0, s61
	s_nop 0
	global_load_lds_dwordx4 v[224:225], off
	s_waitcnt vmcnt(8)
	s_waitcnt lgkmcnt(0)
	s_barrier
	s_setprio 1
	s_waitcnt lgkmcnt(0)
	v_mfma_f32_16x16x32_bf16 v[62:65], v[148:151], v[184:187], v[62:65]
	v_mfma_f32_16x16x32_bf16 v[58:61], v[160:163], v[184:187], v[58:61]
	v_mfma_f32_16x16x32_bf16 v[46:49], v[148:151], v[192:195], v[46:49]
	v_mfma_f32_16x16x32_bf16 v[42:45], v[160:163], v[192:195], v[42:45]
	v_mfma_f32_16x16x32_bf16 v[30:33], v[148:151], v[208:211], v[30:33]
	v_mfma_f32_16x16x32_bf16 v[26:29], v[160:163], v[208:211], v[26:29]
	v_mfma_f32_16x16x32_bf16 v[14:17], v[148:151], v[216:219], v[14:17]
	v_mfma_f32_16x16x32_bf16 v[10:13], v[160:163], v[216:219], v[10:13]
	v_mfma_f32_16x16x32_bf16 v[62:65], v[156:159], v[188:191], v[62:65]
	v_mfma_f32_16x16x32_bf16 v[58:61], v[164:167], v[188:191], v[58:61]
	v_mfma_f32_16x16x32_bf16 v[46:49], v[156:159], v[196:199], v[46:49]
	v_mfma_f32_16x16x32_bf16 v[42:45], v[164:167], v[196:199], v[42:45]
	v_mfma_f32_16x16x32_bf16 v[30:33], v[156:159], v[212:215], v[30:33]
	v_mfma_f32_16x16x32_bf16 v[26:29], v[164:167], v[212:215], v[26:29]
	v_mfma_f32_16x16x32_bf16 v[14:17], v[156:159], v[220:223], v[14:17]
	v_mfma_f32_16x16x32_bf16 v[10:13], v[164:167], v[220:223], v[10:13]
	s_setprio 0
	s_setprio 1
	v_mfma_f32_16x16x32_bf16 v[54:57], v[168:171], v[184:187], v[54:57]
	v_mfma_f32_16x16x32_bf16 v[50:53], v[176:179], v[184:187], v[50:53]
	v_mfma_f32_16x16x32_bf16 v[38:41], v[168:171], v[192:195], v[38:41]
	v_mfma_f32_16x16x32_bf16 v[34:37], v[176:179], v[192:195], v[34:37]
	v_mfma_f32_16x16x32_bf16 v[22:25], v[168:171], v[208:211], v[22:25]
	v_mfma_f32_16x16x32_bf16 v[18:21], v[176:179], v[208:211], v[18:21]
	v_mfma_f32_16x16x32_bf16 v[6:9], v[168:171], v[216:219], v[6:9]
	v_mfma_f32_16x16x32_bf16 v[2:5], v[176:179], v[216:219], v[2:5]
	v_mfma_f32_16x16x32_bf16 v[54:57], v[172:175], v[188:191], v[54:57]
	v_mfma_f32_16x16x32_bf16 v[50:53], v[180:183], v[188:191], v[50:53]
	v_mfma_f32_16x16x32_bf16 v[38:41], v[172:175], v[196:199], v[38:41]
	v_mfma_f32_16x16x32_bf16 v[34:37], v[180:183], v[196:199], v[34:37]
	v_mfma_f32_16x16x32_bf16 v[22:25], v[172:175], v[212:215], v[22:25]
	v_mfma_f32_16x16x32_bf16 v[18:21], v[180:183], v[212:215], v[18:21]
	v_mfma_f32_16x16x32_bf16 v[6:9], v[172:175], v[220:223], v[6:9]
	v_mfma_f32_16x16x32_bf16 v[2:5], v[180:183], v[220:223], v[2:5]
	s_setprio 0
	s_barrier
	s_add_i32 s64, s64, 2
	s_add_u32 s22, s22, 0x100
	s_addc_u32 s23, s23, 0
	s_add_u32 s52, s52, 0x100
	s_addc_u32 s60, s60, 0
	s_cmp_gt_u32 s64, 13
	s_cbranch_scc0 .LBB13_844
	s_and_b64 vcc, exec, s[10:11]
	s_mov_b32 s64, 0x18000
	s_cbranch_vccz .LBB13_847
	s_barrier
; __device__ __forceinline__ unsigned pk2(float lo, float hi) { f32x2 v = {lo, hi}; return __builtin_bit_cast(unsigned, __builtin_convertvector(v, bf2_t)); }
; template <int BIT = 0> __device__ __forceinline__ void st16w(void* p, u32x4 v) { if ((WT_STORES >> BIT) & 1) asm volatile("global_store_dwordx4 %0, %1, off sc1\n\ts_nop 1" :: "v"(p), "v"(v) : "memory"); else *(u32x4*)p = v; }
; __device__ __forceinline__ float bflo(unsigned u) { return __uint_as_float(u << 16); }
; __device__ __forceinline__ float bfhi(unsigned u) { return __uint_as_float(u & 0xffff0000u); }
;     __device__ __forceinline__ void operator()(const f32x4 (&acc)[2][2][4][2], const Unit& u, int wr, int wc, int fr, int fq) const {
;         const int row0 = u.pm * BM + wr * 64 + fr, col0 = u.pn * BM + wc * 32 + 8 * fq;
; #pragma unroll
;         for (int ai = 0; ai < 2; ++ai)
; #pragma unroll
;             for (int m = 0; m < 4; ++m) {
;                 const size_t row = (size_t)(row0 + ai * HALF + m * 16);
; #pragma unroll
;                 for (int bj = 0; bj < 2; ++bj) {
;                     const int col = col0 + bj * HALF;
;                     const u32x4 g = *(const u32x4*)(P + row * INC + goff + col);
;                     const f32x4 a0 = acc[ai][bj][m][0], a1 = acc[ai][bj][m][1];
;                     float o[8] = {bflo(g.x) * a0[0], bfhi(g.x) * a0[1], bflo(g.y) * a0[2], bfhi(g.y) * a0[3], bflo(g.z) * a1[0], bfhi(g.z) * a1[1], bflo(g.w) * a1[2], bfhi(g.w) * a1[3]};
;                     if (mode) { const u32x4 t = *(const u32x4*)(T1 + row * D + col);
;                         o[0] += bflo(t.x); o[1] += bfhi(t.x); o[2] += bflo(t.y); o[3] += bfhi(t.y); o[4] += bflo(t.z); o[5] += bfhi(t.z); o[6] += bflo(t.w); o[7] += bfhi(t.w); }
;                     u32x4 w; w.x = pk2(o[0], o[1]); w.y = pk2(o[2], o[3]); w.z = pk2(o[4], o[5]); w.w = pk2(o[6], o[7]);
;                     if (mode) st16w(MM + row * D + col, w); else *(u32x4*)(T1 + row * D + col) = w;
.LBB13_847:
	v_readfirstlane_b32 s98, v132
	v_readfirstlane_b32 s99, v133
	v_readfirstlane_b32 s22, v134
	v_readfirstlane_b32 s23, v135
	v_lshl_add_u32 v158, s12, 8, v99
	v_lshl_or_b32 v159, s13, 8, v153
	s_mov_b64 s[12:13], -1
	s_andn2_b64 vcc, exec, s[4:5]
	v_mul_u32_u24_e32 v156, 0x2c00, v158
	v_lshl_add_u32 v156, v159, 1, v156
	v_add_u32_e32 v156, 0x1c00, v156
	v_lshlrev_b32_e32 v157, 11, v158
	v_lshl_add_u32 v157, v159, 1, v157
	global_load_dwordx4 v[160:163], v156, s[98:99]
	global_load_dwordx4 v[164:167], v157, s[22:23]
	global_load_dwordx4 v[168:171], v156, s[98:99] offset:256
	global_load_dwordx4 v[172:175], v157, s[22:23] offset:256
	v_add_u32_e32 v158, 0x2c000, v156
	global_load_dwordx4 v[176:179], v158, s[98:99]
	v_add_u32_e32 v159, 0x8000, v157
	global_load_dwordx4 v[180:183], v159, s[22:23]
	v_add_u32_e32 v158, 0x2c000, v156
	global_load_dwordx4 v[184:187], v158, s[98:99] offset:256
	v_add_u32_e32 v159, 0x8000, v157
	global_load_dwordx4 v[188:191], v159, s[22:23] offset:256
	v_add_u32_e32 v158, 0x58000, v156
	global_load_dwordx4 v[192:195], v158, s[98:99]
	v_add_u32_e32 v159, 0x10000, v157
	global_load_dwordx4 v[196:199], v159, s[22:23]
	v_add_u32_e32 v158, 0x58000, v156
	global_load_dwordx4 v[208:211], v158, s[98:99] offset:256
	v_add_u32_e32 v159, 0x10000, v157
	global_load_dwordx4 v[212:215], v159, s[22:23] offset:256
	v_add_u32_e32 v158, 0x84000, v156
	global_load_dwordx4 v[216:219], v158, s[98:99]
	v_add_u32_e32 v159, 0x18000, v157
	global_load_dwordx4 v[220:223], v159, s[22:23]
	s_waitcnt vmcnt(12)
	v_lshlrev_b32_e32 v148, 16, v160
	v_and_b32_e32 v149, 0xffff0000, v160
	v_lshlrev_b32_e32 v150, 16, v164
	v_and_b32_e32 v151, 0xffff0000, v164
	v_pk_fma_f32 v[128:129], v[128:129], v[148:149], v[150:151]
	v_lshlrev_b32_e32 v148, 16, v161
	v_and_b32_e32 v149, 0xffff0000, v161
	v_lshlrev_b32_e32 v150, 16, v165
	v_and_b32_e32 v151, 0xffff0000, v165
	v_pk_fma_f32 v[130:131], v[130:131], v[148:149], v[150:151]
	v_lshlrev_b32_e32 v148, 16, v162
	v_and_b32_e32 v149, 0xffff0000, v162
	v_lshlrev_b32_e32 v150, 16, v166
	v_and_b32_e32 v151, 0xffff0000, v166
	v_pk_fma_f32 v[124:125], v[124:125], v[148:149], v[150:151]
	v_lshlrev_b32_e32 v148, 16, v163
	v_and_b32_e32 v149, 0xffff0000, v163
	v_lshlrev_b32_e32 v150, 16, v167
	v_and_b32_e32 v151, 0xffff0000, v167
	v_pk_fma_f32 v[126:127], v[126:127], v[148:149], v[150:151]
	v_cvt_pk_bf16_f32 v128, v128, v129
	v_cvt_pk_bf16_f32 v129, v130, v131
	v_cvt_pk_bf16_f32 v130, v124, v125
	v_cvt_pk_bf16_f32 v131, v126, v127
	global_store_dwordx4 v157, v[128:131], s[6:7]
	v_add_u32_e32 v158, 0x84000, v156
	global_load_dwordx4 v[160:163], v158, s[98:99] offset:256
	v_add_u32_e32 v159, 0x18000, v157
	global_load_dwordx4 v[164:167], v159, s[22:23] offset:256
	s_waitcnt vmcnt(13)
	v_lshlrev_b32_e32 v148, 16, v168
	v_and_b32_e32 v149, 0xffff0000, v168
	v_lshlrev_b32_e32 v150, 16, v172
	v_and_b32_e32 v151, 0xffff0000, v172
	v_pk_fma_f32 v[120:121], v[120:121], v[148:149], v[150:151]
	v_lshlrev_b32_e32 v148, 16, v169
	v_and_b32_e32 v149, 0xffff0000, v169
	v_lshlrev_b32_e32 v150, 16, v173
	v_and_b32_e32 v151, 0xffff0000, v173
	v_pk_fma_f32 v[122:123], v[122:123], v[148:149], v[150:151]
	v_lshlrev_b32_e32 v148, 16, v170
	v_and_b32_e32 v149, 0xffff0000, v170
	v_lshlrev_b32_e32 v150, 16, v174
	v_and_b32_e32 v151, 0xffff0000, v174
	v_pk_fma_f32 v[116:117], v[116:117], v[148:149], v[150:151]
	v_lshlrev_b32_e32 v148, 16, v171
	v_and_b32_e32 v149, 0xffff0000, v171
	v_lshlrev_b32_e32 v150, 16, v175
	v_and_b32_e32 v151, 0xffff0000, v175
	v_pk_fma_f32 v[118:119], v[118:119], v[148:149], v[150:151]
	v_cvt_pk_bf16_f32 v120, v120, v121
	v_cvt_pk_bf16_f32 v121, v122, v123
	v_cvt_pk_bf16_f32 v122, v116, v117
	v_cvt_pk_bf16_f32 v123, v118, v119
	global_store_dwordx4 v157, v[120:123], s[6:7] offset:256
	v_add_u32_e32 v158, 0x160000, v156
	global_load_dwordx4 v[124:127], v158, s[98:99]
	v_add_u32_e32 v159, 0x40000, v157
	global_load_dwordx4 v[168:171], v159, s[22:23]
	v_add_u32_e32 v158, 0x160000, v156
	global_load_dwordx4 v[172:175], v158, s[98:99] offset:256
	v_add_u32_e32 v159, 0x40000, v157
	global_load_dwordx4 v[116:119], v159, s[22:23] offset:256
	s_waitcnt vmcnt(16)
	v_lshlrev_b32_e32 v148, 16, v176
	v_and_b32_e32 v149, 0xffff0000, v176
	v_lshlrev_b32_e32 v150, 16, v180
	v_and_b32_e32 v151, 0xffff0000, v180
	v_pk_fma_f32 v[112:113], v[112:113], v[148:149], v[150:151]
	v_lshlrev_b32_e32 v148, 16, v177
	v_and_b32_e32 v149, 0xffff0000, v177
	v_lshlrev_b32_e32 v150, 16, v181
	v_and_b32_e32 v151, 0xffff0000, v181
	v_pk_fma_f32 v[114:115], v[114:115], v[148:149], v[150:151]
	v_lshlrev_b32_e32 v148, 16, v178
	v_and_b32_e32 v149, 0xffff0000, v178
	v_lshlrev_b32_e32 v150, 16, v182
	v_and_b32_e32 v151, 0xffff0000, v182
	v_pk_fma_f32 v[108:109], v[108:109], v[148:149], v[150:151]
	v_lshlrev_b32_e32 v148, 16, v179
	v_and_b32_e32 v149, 0xffff0000, v179
	v_lshlrev_b32_e32 v150, 16, v183
	v_and_b32_e32 v151, 0xffff0000, v183
	v_pk_fma_f32 v[110:111], v[110:111], v[148:149], v[150:151]
	v_cvt_pk_bf16_f32 v112, v112, v113
	v_cvt_pk_bf16_f32 v113, v114, v115
	v_cvt_pk_bf16_f32 v114, v108, v109
	v_cvt_pk_bf16_f32 v115, v110, v111
	v_add_u32_e32 v159, 0x8000, v157
	global_store_dwordx4 v159, v[112:115], s[6:7]
	v_add_u32_e32 v158, 0x18c000, v156
	global_load_dwordx4 v[176:179], v158, s[98:99]
	v_add_u32_e32 v159, 0x48000, v157
	global_load_dwordx4 v[180:183], v159, s[22:23]
	s_waitcnt vmcnt(17)
; __device__ __forceinline__ unsigned pk2(float lo, float hi) { f32x2 v = {lo, hi}; return __builtin_bit_cast(unsigned, __builtin_convertvector(v, bf2_t)); }
; template <int BIT = 0> __device__ __forceinline__ void st16w(void* p, u32x4 v) { if ((WT_STORES >> BIT) & 1) asm volatile("global_store_dwordx4 %0, %1, off sc1\n\ts_nop 1" :: "v"(p), "v"(v) : "memory"); else *(u32x4*)p = v; }
; __device__ __forceinline__ float bflo(unsigned u) { return __uint_as_float(u << 16); }
; __device__ __forceinline__ float bfhi(unsigned u) { return __uint_as_float(u & 0xffff0000u); }
;     __device__ __forceinline__ void operator()(const f32x4 (&acc)[2][2][4][2], const Unit& u, int wr, int wc, int fr, int fq) const {
;     ...
;                     const u32x4 g = *(const u32x4*)(P + row * INC + goff + col);
;                     const f32x4 a0 = acc[ai][bj][m][0], a1 = acc[ai][bj][m][1];
;                     float o[8] = {bflo(g.x) * a0[0], bfhi(g.x) * a0[1], bflo(g.y) * a0[2], bfhi(g.y) * a0[3], bflo(g.z) * a1[0], bfhi(g.z) * a1[1], bflo(g.w) * a1[2], bfhi(g.w) * a1[3]};
;                     if (mode) { const u32x4 t = *(const u32x4*)(T1 + row * D + col);
;                         o[0] += bflo(t.x); o[1] += bfhi(t.x); o[2] += bflo(t.y); o[3] += bfhi(t.y); o[4] += bflo(t.z); o[5] += bfhi(t.z); o[6] += bflo(t.w); o[7] += bfhi(t.w); }
;                     u32x4 w; w.x = pk2(o[0], o[1]); w.y = pk2(o[2], o[3]); w.z = pk2(o[4], o[5]); w.w = pk2(o[6], o[7]);
;                     if (mode) st16w(MM + row * D + col, w); else *(u32x4*)(T1 + row * D + col) = w;
	v_lshlrev_b32_e32 v148, 16, v184
	v_and_b32_e32 v149, 0xffff0000, v184
	v_lshlrev_b32_e32 v150, 16, v188
	v_and_b32_e32 v151, 0xffff0000, v188
	v_pk_fma_f32 v[104:105], v[104:105], v[148:149], v[150:151]
	v_lshlrev_b32_e32 v148, 16, v185
	v_and_b32_e32 v149, 0xffff0000, v185
	v_lshlrev_b32_e32 v150, 16, v189
	v_and_b32_e32 v151, 0xffff0000, v189
	v_pk_fma_f32 v[106:107], v[106:107], v[148:149], v[150:151]
	v_lshlrev_b32_e32 v148, 16, v186
	v_and_b32_e32 v149, 0xffff0000, v186
	v_lshlrev_b32_e32 v150, 16, v190
	v_and_b32_e32 v151, 0xffff0000, v190
	v_pk_fma_f32 v[100:101], v[100:101], v[148:149], v[150:151]
	v_lshlrev_b32_e32 v148, 16, v187
	v_and_b32_e32 v149, 0xffff0000, v187
	v_lshlrev_b32_e32 v150, 16, v191
	v_and_b32_e32 v151, 0xffff0000, v191
	v_pk_fma_f32 v[102:103], v[102:103], v[148:149], v[150:151]
	v_cvt_pk_bf16_f32 v104, v104, v105
	v_cvt_pk_bf16_f32 v105, v106, v107
	v_cvt_pk_bf16_f32 v106, v100, v101
	v_cvt_pk_bf16_f32 v107, v102, v103
	v_add_u32_e32 v159, 0x8000, v157
	global_store_dwordx4 v159, v[104:107], s[6:7] offset:256
	v_add_u32_e32 v158, 0x18c000, v156
	global_load_dwordx4 v[108:111], v158, s[98:99] offset:256
	v_add_u32_e32 v159, 0x48000, v157
	global_load_dwordx4 v[184:187], v159, s[22:23] offset:256
	v_add_u32_e32 v158, 0x1b8000, v156
	global_load_dwordx4 v[188:191], v158, s[98:99]
	v_add_u32_e32 v159, 0x50000, v157
	global_load_dwordx4 v[100:103], v159, s[22:23]
	s_waitcnt vmcnt(20)
	v_lshlrev_b32_e32 v148, 16, v192
	v_and_b32_e32 v149, 0xffff0000, v192
	v_lshlrev_b32_e32 v150, 16, v196
	v_and_b32_e32 v151, 0xffff0000, v196
	v_pk_fma_f32 v[94:95], v[94:95], v[148:149], v[150:151]
	v_lshlrev_b32_e32 v148, 16, v193
	v_and_b32_e32 v149, 0xffff0000, v193
	v_lshlrev_b32_e32 v150, 16, v197
	v_and_b32_e32 v151, 0xffff0000, v197
	v_pk_fma_f32 v[96:97], v[96:97], v[148:149], v[150:151]
	v_lshlrev_b32_e32 v148, 16, v194
	v_and_b32_e32 v149, 0xffff0000, v194
	v_lshlrev_b32_e32 v150, 16, v198
	v_and_b32_e32 v151, 0xffff0000, v198
	v_pk_fma_f32 v[90:91], v[90:91], v[148:149], v[150:151]
	v_lshlrev_b32_e32 v148, 16, v195
	v_and_b32_e32 v149, 0xffff0000, v195
	v_lshlrev_b32_e32 v150, 16, v199
	v_and_b32_e32 v151, 0xffff0000, v199
	v_pk_fma_f32 v[92:93], v[92:93], v[148:149], v[150:151]
	v_cvt_pk_bf16_f32 v94, v94, v95
	v_cvt_pk_bf16_f32 v95, v96, v97
	v_cvt_pk_bf16_f32 v96, v90, v91
	v_cvt_pk_bf16_f32 v97, v92, v93
	v_add_u32_e32 v159, 0x10000, v157
	global_store_dwordx4 v159, v[94:97], s[6:7]
	v_add_u32_e32 v158, 0x1b8000, v156
	global_load_dwordx4 v[192:195], v158, s[98:99] offset:256
	v_add_u32_e32 v159, 0x50000, v157
	global_load_dwordx4 v[196:199], v159, s[22:23] offset:256
	s_waitcnt vmcnt(21)
	v_lshlrev_b32_e32 v148, 16, v208
	v_and_b32_e32 v149, 0xffff0000, v208
	v_lshlrev_b32_e32 v150, 16, v212
	v_and_b32_e32 v151, 0xffff0000, v212
	v_pk_fma_f32 v[86:87], v[86:87], v[148:149], v[150:151]
	v_lshlrev_b32_e32 v148, 16, v209
	v_and_b32_e32 v149, 0xffff0000, v209
	v_lshlrev_b32_e32 v150, 16, v213
	v_and_b32_e32 v151, 0xffff0000, v213
	v_pk_fma_f32 v[88:89], v[88:89], v[148:149], v[150:151]
	v_lshlrev_b32_e32 v148, 16, v210
	v_and_b32_e32 v149, 0xffff0000, v210
	v_lshlrev_b32_e32 v150, 16, v214
	v_and_b32_e32 v151, 0xffff0000, v214
	v_pk_fma_f32 v[82:83], v[82:83], v[148:149], v[150:151]
	v_lshlrev_b32_e32 v148, 16, v211
	v_and_b32_e32 v149, 0xffff0000, v211
	v_lshlrev_b32_e32 v150, 16, v215
	v_and_b32_e32 v151, 0xffff0000, v215
	v_pk_fma_f32 v[84:85], v[84:85], v[148:149], v[150:151]
	v_cvt_pk_bf16_f32 v86, v86, v87
	v_cvt_pk_bf16_f32 v87, v88, v89
	v_cvt_pk_bf16_f32 v88, v82, v83
	v_cvt_pk_bf16_f32 v89, v84, v85
	v_add_u32_e32 v159, 0x10000, v157
	global_store_dwordx4 v159, v[86:89], s[6:7] offset:256
	v_add_u32_e32 v158, 0x1e4000, v156
	global_load_dwordx4 v[90:93], v158, s[98:99]
	v_add_u32_e32 v159, 0x58000, v157
	global_load_dwordx4 v[208:211], v159, s[22:23]
	v_add_u32_e32 v158, 0x1e4000, v156
	global_load_dwordx4 v[212:215], v158, s[98:99] offset:256
	v_add_u32_e32 v159, 0x58000, v157
	global_load_dwordx4 v[82:85], v159, s[22:23] offset:256
	s_waitcnt vmcnt(24)
	v_lshlrev_b32_e32 v148, 16, v216
	v_and_b32_e32 v149, 0xffff0000, v216
	v_lshlrev_b32_e32 v150, 16, v220
	v_and_b32_e32 v151, 0xffff0000, v220
	v_pk_fma_f32 v[78:79], v[78:79], v[148:149], v[150:151]
	v_lshlrev_b32_e32 v148, 16, v217
	v_and_b32_e32 v149, 0xffff0000, v217
	v_lshlrev_b32_e32 v150, 16, v221
	v_and_b32_e32 v151, 0xffff0000, v221
	v_pk_fma_f32 v[80:81], v[80:81], v[148:149], v[150:151]
	v_lshlrev_b32_e32 v148, 16, v218
	v_and_b32_e32 v149, 0xffff0000, v218
	v_lshlrev_b32_e32 v150, 16, v222
	v_and_b32_e32 v151, 0xffff0000, v222
	v_pk_fma_f32 v[74:75], v[74:75], v[148:149], v[150:151]
	v_lshlrev_b32_e32 v148, 16, v219
	v_and_b32_e32 v149, 0xffff0000, v219
	v_lshlrev_b32_e32 v150, 16, v223
	v_and_b32_e32 v151, 0xffff0000, v223
	v_pk_fma_f32 v[76:77], v[76:77], v[148:149], v[150:151]
	v_cvt_pk_bf16_f32 v78, v78, v79
	v_cvt_pk_bf16_f32 v79, v80, v81
	v_cvt_pk_bf16_f32 v80, v74, v75
	v_cvt_pk_bf16_f32 v81, v76, v77
	v_add_u32_e32 v159, 0x18000, v157
	global_store_dwordx4 v159, v[78:81], s[6:7]
	s_waitcnt vmcnt(22)
	v_lshlrev_b32_e32 v148, 16, v160
	v_and_b32_e32 v149, 0xffff0000, v160
	v_lshlrev_b32_e32 v150, 16, v164
	v_and_b32_e32 v151, 0xffff0000, v164
	v_pk_fma_f32 v[70:71], v[70:71], v[148:149], v[150:151]
	v_lshlrev_b32_e32 v148, 16, v161
	v_and_b32_e32 v149, 0xffff0000, v161
	v_lshlrev_b32_e32 v150, 16, v165
	v_and_b32_e32 v151, 0xffff0000, v165
	v_pk_fma_f32 v[72:73], v[72:73], v[148:149], v[150:151]
	v_lshlrev_b32_e32 v148, 16, v162
	v_and_b32_e32 v149, 0xffff0000, v162
	v_lshlrev_b32_e32 v150, 16, v166
	v_and_b32_e32 v151, 0xffff0000, v166
	v_pk_fma_f32 v[66:67], v[66:67], v[148:149], v[150:151]
	v_lshlrev_b32_e32 v148, 16, v163
	v_and_b32_e32 v149, 0xffff0000, v163
	v_lshlrev_b32_e32 v150, 16, v167
	v_and_b32_e32 v151, 0xffff0000, v167
	v_pk_fma_f32 v[68:69], v[68:69], v[148:149], v[150:151]
	v_cvt_pk_bf16_f32 v70, v70, v71
	v_cvt_pk_bf16_f32 v71, v72, v73
	v_cvt_pk_bf16_f32 v72, v66, v67
	v_cvt_pk_bf16_f32 v73, v68, v69
	v_add_u32_e32 v159, 0x18000, v157
	global_store_dwordx4 v159, v[70:73], s[6:7] offset:256
	s_waitcnt vmcnt(20)
; __device__ __forceinline__ unsigned pk2(float lo, float hi) { f32x2 v = {lo, hi}; return __builtin_bit_cast(unsigned, __builtin_convertvector(v, bf2_t)); }
; template <int BIT = 0> __device__ __forceinline__ void st16w(void* p, u32x4 v) { if ((WT_STORES >> BIT) & 1) asm volatile("global_store_dwordx4 %0, %1, off sc1\n\ts_nop 1" :: "v"(p), "v"(v) : "memory"); else *(u32x4*)p = v; }
; __device__ __forceinline__ float bflo(unsigned u) { return __uint_as_float(u << 16); }
; __device__ __forceinline__ float bfhi(unsigned u) { return __uint_as_float(u & 0xffff0000u); }
;     __device__ __forceinline__ void operator()(const f32x4 (&acc)[2][2][4][2], const Unit& u, int wr, int wc, int fr, int fq) const {
;     ...
;                     const u32x4 g = *(const u32x4*)(P + row * INC + goff + col);
;                     const f32x4 a0 = acc[ai][bj][m][0], a1 = acc[ai][bj][m][1];
;                     float o[8] = {bflo(g.x) * a0[0], bfhi(g.x) * a0[1], bflo(g.y) * a0[2], bfhi(g.y) * a0[3], bflo(g.z) * a1[0], bfhi(g.z) * a1[1], bflo(g.w) * a1[2], bfhi(g.w) * a1[3]};
;                     if (mode) { const u32x4 t = *(const u32x4*)(T1 + row * D + col);
;                         o[0] += bflo(t.x); o[1] += bfhi(t.x); o[2] += bflo(t.y); o[3] += bfhi(t.y); o[4] += bflo(t.z); o[5] += bfhi(t.z); o[6] += bflo(t.w); o[7] += bfhi(t.w); }
;                     u32x4 w; w.x = pk2(o[0], o[1]); w.y = pk2(o[2], o[3]); w.z = pk2(o[4], o[5]); w.w = pk2(o[6], o[7]);
;                     if (mode) st16w(MM + row * D + col, w); else *(u32x4*)(T1 + row * D + col) = w;
	v_lshlrev_b32_e32 v148, 16, v124
	v_and_b32_e32 v149, 0xffff0000, v124
	v_lshlrev_b32_e32 v150, 16, v168
	v_and_b32_e32 v151, 0xffff0000, v168
	v_pk_fma_f32 v[62:63], v[62:63], v[148:149], v[150:151]
	v_lshlrev_b32_e32 v148, 16, v125
	v_and_b32_e32 v149, 0xffff0000, v125
	v_lshlrev_b32_e32 v150, 16, v169
	v_and_b32_e32 v151, 0xffff0000, v169
	v_pk_fma_f32 v[64:65], v[64:65], v[148:149], v[150:151]
	v_lshlrev_b32_e32 v148, 16, v126
	v_and_b32_e32 v149, 0xffff0000, v126
	v_lshlrev_b32_e32 v150, 16, v170
	v_and_b32_e32 v151, 0xffff0000, v170
	v_pk_fma_f32 v[58:59], v[58:59], v[148:149], v[150:151]
	v_lshlrev_b32_e32 v148, 16, v127
	v_and_b32_e32 v149, 0xffff0000, v127
	v_lshlrev_b32_e32 v150, 16, v171
	v_and_b32_e32 v151, 0xffff0000, v171
	v_pk_fma_f32 v[60:61], v[60:61], v[148:149], v[150:151]
	v_cvt_pk_bf16_f32 v62, v62, v63
	v_cvt_pk_bf16_f32 v63, v64, v65
	v_cvt_pk_bf16_f32 v64, v58, v59
	v_cvt_pk_bf16_f32 v65, v60, v61
	v_add_u32_e32 v159, 0x40000, v157
	global_store_dwordx4 v159, v[62:65], s[6:7]
	s_waitcnt vmcnt(19)
	v_lshlrev_b32_e32 v148, 16, v172
	v_and_b32_e32 v149, 0xffff0000, v172
	v_lshlrev_b32_e32 v150, 16, v116
	v_and_b32_e32 v151, 0xffff0000, v116
	v_pk_fma_f32 v[54:55], v[54:55], v[148:149], v[150:151]
	v_lshlrev_b32_e32 v148, 16, v173
	v_and_b32_e32 v149, 0xffff0000, v173
	v_lshlrev_b32_e32 v150, 16, v117
	v_and_b32_e32 v151, 0xffff0000, v117
	v_pk_fma_f32 v[56:57], v[56:57], v[148:149], v[150:151]
	v_lshlrev_b32_e32 v148, 16, v174
	v_and_b32_e32 v149, 0xffff0000, v174
	v_lshlrev_b32_e32 v150, 16, v118
	v_and_b32_e32 v151, 0xffff0000, v118
	v_pk_fma_f32 v[50:51], v[50:51], v[148:149], v[150:151]
	v_lshlrev_b32_e32 v148, 16, v175
	v_and_b32_e32 v149, 0xffff0000, v175
	v_lshlrev_b32_e32 v150, 16, v119
	v_and_b32_e32 v151, 0xffff0000, v119
	v_pk_fma_f32 v[52:53], v[52:53], v[148:149], v[150:151]
	v_cvt_pk_bf16_f32 v54, v54, v55
	v_cvt_pk_bf16_f32 v55, v56, v57
	v_cvt_pk_bf16_f32 v56, v50, v51
	v_cvt_pk_bf16_f32 v57, v52, v53
	v_add_u32_e32 v159, 0x40000, v157
	global_store_dwordx4 v159, v[54:57], s[6:7] offset:256
	s_waitcnt vmcnt(17)
	v_lshlrev_b32_e32 v148, 16, v176
	v_and_b32_e32 v149, 0xffff0000, v176
	v_lshlrev_b32_e32 v150, 16, v180
	v_and_b32_e32 v151, 0xffff0000, v180
	v_pk_fma_f32 v[46:47], v[46:47], v[148:149], v[150:151]
	v_lshlrev_b32_e32 v148, 16, v177
	v_and_b32_e32 v149, 0xffff0000, v177
	v_lshlrev_b32_e32 v150, 16, v181
	v_and_b32_e32 v151, 0xffff0000, v181
	v_pk_fma_f32 v[48:49], v[48:49], v[148:149], v[150:151]
	v_lshlrev_b32_e32 v148, 16, v178
	v_and_b32_e32 v149, 0xffff0000, v178
	v_lshlrev_b32_e32 v150, 16, v182
	v_and_b32_e32 v151, 0xffff0000, v182
	v_pk_fma_f32 v[42:43], v[42:43], v[148:149], v[150:151]
	v_lshlrev_b32_e32 v148, 16, v179
	v_and_b32_e32 v149, 0xffff0000, v179
	v_lshlrev_b32_e32 v150, 16, v183
	v_and_b32_e32 v151, 0xffff0000, v183
	v_pk_fma_f32 v[44:45], v[44:45], v[148:149], v[150:151]
	v_cvt_pk_bf16_f32 v46, v46, v47
	v_cvt_pk_bf16_f32 v47, v48, v49
	v_cvt_pk_bf16_f32 v48, v42, v43
	v_cvt_pk_bf16_f32 v49, v44, v45
	v_add_u32_e32 v159, 0x48000, v157
	global_store_dwordx4 v159, v[46:49], s[6:7]
	s_waitcnt vmcnt(15)
	v_lshlrev_b32_e32 v148, 16, v108
	v_and_b32_e32 v149, 0xffff0000, v108
	v_lshlrev_b32_e32 v150, 16, v184
	v_and_b32_e32 v151, 0xffff0000, v184
	v_pk_fma_f32 v[38:39], v[38:39], v[148:149], v[150:151]
	v_lshlrev_b32_e32 v148, 16, v109
	v_and_b32_e32 v149, 0xffff0000, v109
	v_lshlrev_b32_e32 v150, 16, v185
	v_and_b32_e32 v151, 0xffff0000, v185
	v_pk_fma_f32 v[40:41], v[40:41], v[148:149], v[150:151]
	v_lshlrev_b32_e32 v148, 16, v110
	v_and_b32_e32 v149, 0xffff0000, v110
	v_lshlrev_b32_e32 v150, 16, v186
	v_and_b32_e32 v151, 0xffff0000, v186
	v_pk_fma_f32 v[34:35], v[34:35], v[148:149], v[150:151]
	v_lshlrev_b32_e32 v148, 16, v111
	v_and_b32_e32 v149, 0xffff0000, v111
	v_lshlrev_b32_e32 v150, 16, v187
	v_and_b32_e32 v151, 0xffff0000, v187
	v_pk_fma_f32 v[36:37], v[36:37], v[148:149], v[150:151]
	v_cvt_pk_bf16_f32 v38, v38, v39
	v_cvt_pk_bf16_f32 v39, v40, v41
	v_cvt_pk_bf16_f32 v40, v34, v35
	v_cvt_pk_bf16_f32 v41, v36, v37
	v_add_u32_e32 v159, 0x48000, v157
	global_store_dwordx4 v159, v[38:41], s[6:7] offset:256
	s_waitcnt vmcnt(14)
; __device__ __forceinline__ unsigned pk2(float lo, float hi) { f32x2 v = {lo, hi}; return __builtin_bit_cast(unsigned, __builtin_convertvector(v, bf2_t)); }
; template <int BIT = 0> __device__ __forceinline__ void st16w(void* p, u32x4 v) { if ((WT_STORES >> BIT) & 1) asm volatile("global_store_dwordx4 %0, %1, off sc1\n\ts_nop 1" :: "v"(p), "v"(v) : "memory"); else *(u32x4*)p = v; }
; __device__ __forceinline__ float bflo(unsigned u) { return __uint_as_float(u << 16); }
; __device__ __forceinline__ float bfhi(unsigned u) { return __uint_as_float(u & 0xffff0000u); }
;     __device__ __forceinline__ void operator()(const f32x4 (&acc)[2][2][4][2], const Unit& u, int wr, int wc, int fr, int fq) const {
;     ...
;                     const u32x4 g = *(const u32x4*)(P + row * INC + goff + col);
;                     const f32x4 a0 = acc[ai][bj][m][0], a1 = acc[ai][bj][m][1];
;                     float o[8] = {bflo(g.x) * a0[0], bfhi(g.x) * a0[1], bflo(g.y) * a0[2], bfhi(g.y) * a0[3], bflo(g.z) * a1[0], bfhi(g.z) * a1[1], bflo(g.w) * a1[2], bfhi(g.w) * a1[3]};
;                     if (mode) { const u32x4 t = *(const u32x4*)(T1 + row * D + col);
;                         o[0] += bflo(t.x); o[1] += bfhi(t.x); o[2] += bflo(t.y); o[3] += bfhi(t.y); o[4] += bflo(t.z); o[5] += bfhi(t.z); o[6] += bflo(t.w); o[7] += bfhi(t.w); }
;                     u32x4 w; w.x = pk2(o[0], o[1]); w.y = pk2(o[2], o[3]); w.z = pk2(o[4], o[5]); w.w = pk2(o[6], o[7]);
;                     if (mode) st16w(MM + row * D + col, w); else *(u32x4*)(T1 + row * D + col) = w;
; template <class Epi, class Sched, bool ALIGN_EPI = false, bool SP2 = false>
; __device__ __forceinline__ void gemm_phase(PG8_LAS unsigned char* lds, const Gemm g, const Sched& S, const Epi& E) {
;     ...
;         if (!has_next) break;
; #pragma unroll
;         for (int a = 0; a < 2; ++a)
; #pragma unroll
;             for (int b = 0; b < 2; ++b)
; #pragma unroll
;                 for (int m = 0; m < 4; ++m)
; #pragma unroll
;                     for (int n = 0; n < 2; ++n) acc[a][b][m][n] = (f32x4){0.f, 0.f, 0.f, 0.f};
;         cur = nxt; cA = nA; cB = nB; ++ui;
;         if constexpr (Sched::GATHER) { const u32x4 pv_ = *(const PG8_LAS u32x4*)(lds + STAGE_BYTES + tid * 16); vAc[0][0] = pv_.x; vAc[0][1] = pv_.y; vAc[1][0] = pv_.z; vAc[1][1] = pv_.w; }
;         if constexpr (ALIGN_EPI) { if (wr == 1) PG8_BAR; }
	v_lshlrev_b32_e32 v148, 16, v188
	v_and_b32_e32 v149, 0xffff0000, v188
	v_lshlrev_b32_e32 v150, 16, v100
	v_and_b32_e32 v151, 0xffff0000, v100
	v_pk_fma_f32 v[30:31], v[30:31], v[148:149], v[150:151]
	v_lshlrev_b32_e32 v148, 16, v189
	v_and_b32_e32 v149, 0xffff0000, v189
	v_lshlrev_b32_e32 v150, 16, v101
	v_and_b32_e32 v151, 0xffff0000, v101
	v_pk_fma_f32 v[32:33], v[32:33], v[148:149], v[150:151]
	v_lshlrev_b32_e32 v148, 16, v190
	v_and_b32_e32 v149, 0xffff0000, v190
	v_lshlrev_b32_e32 v150, 16, v102
	v_and_b32_e32 v151, 0xffff0000, v102
	v_pk_fma_f32 v[26:27], v[26:27], v[148:149], v[150:151]
	v_lshlrev_b32_e32 v148, 16, v191
	v_and_b32_e32 v149, 0xffff0000, v191
	v_lshlrev_b32_e32 v150, 16, v103
	v_and_b32_e32 v151, 0xffff0000, v103
	v_pk_fma_f32 v[28:29], v[28:29], v[148:149], v[150:151]
	v_cvt_pk_bf16_f32 v30, v30, v31
	v_cvt_pk_bf16_f32 v31, v32, v33
	v_cvt_pk_bf16_f32 v32, v26, v27
	v_cvt_pk_bf16_f32 v33, v28, v29
	v_add_u32_e32 v159, 0x50000, v157
	global_store_dwordx4 v159, v[30:33], s[6:7]
	s_waitcnt vmcnt(12)
	v_lshlrev_b32_e32 v148, 16, v192
	v_and_b32_e32 v149, 0xffff0000, v192
	v_lshlrev_b32_e32 v150, 16, v196
	v_and_b32_e32 v151, 0xffff0000, v196
	v_pk_fma_f32 v[22:23], v[22:23], v[148:149], v[150:151]
	v_lshlrev_b32_e32 v148, 16, v193
	v_and_b32_e32 v149, 0xffff0000, v193
	v_lshlrev_b32_e32 v150, 16, v197
	v_and_b32_e32 v151, 0xffff0000, v197
	v_pk_fma_f32 v[24:25], v[24:25], v[148:149], v[150:151]
	v_lshlrev_b32_e32 v148, 16, v194
	v_and_b32_e32 v149, 0xffff0000, v194
	v_lshlrev_b32_e32 v150, 16, v198
	v_and_b32_e32 v151, 0xffff0000, v198
	v_pk_fma_f32 v[18:19], v[18:19], v[148:149], v[150:151]
	v_lshlrev_b32_e32 v148, 16, v195
	v_and_b32_e32 v149, 0xffff0000, v195
	v_lshlrev_b32_e32 v150, 16, v199
	v_and_b32_e32 v151, 0xffff0000, v199
	v_pk_fma_f32 v[20:21], v[20:21], v[148:149], v[150:151]
	v_cvt_pk_bf16_f32 v22, v22, v23
	v_cvt_pk_bf16_f32 v23, v24, v25
	v_cvt_pk_bf16_f32 v24, v18, v19
	v_cvt_pk_bf16_f32 v25, v20, v21
	v_add_u32_e32 v159, 0x50000, v157
	global_store_dwordx4 v159, v[22:25], s[6:7] offset:256
	s_waitcnt vmcnt(10)
	v_lshlrev_b32_e32 v148, 16, v90
	v_and_b32_e32 v149, 0xffff0000, v90
	v_lshlrev_b32_e32 v150, 16, v208
	v_and_b32_e32 v151, 0xffff0000, v208
	v_pk_fma_f32 v[14:15], v[14:15], v[148:149], v[150:151]
	v_lshlrev_b32_e32 v148, 16, v91
	v_and_b32_e32 v149, 0xffff0000, v91
	v_lshlrev_b32_e32 v150, 16, v209
	v_and_b32_e32 v151, 0xffff0000, v209
	v_pk_fma_f32 v[16:17], v[16:17], v[148:149], v[150:151]
	v_lshlrev_b32_e32 v148, 16, v92
	v_and_b32_e32 v149, 0xffff0000, v92
	v_lshlrev_b32_e32 v150, 16, v210
	v_and_b32_e32 v151, 0xffff0000, v210
	v_pk_fma_f32 v[10:11], v[10:11], v[148:149], v[150:151]
	v_lshlrev_b32_e32 v148, 16, v93
	v_and_b32_e32 v149, 0xffff0000, v93
	v_lshlrev_b32_e32 v150, 16, v211
	v_and_b32_e32 v151, 0xffff0000, v211
	v_pk_fma_f32 v[12:13], v[12:13], v[148:149], v[150:151]
	v_cvt_pk_bf16_f32 v14, v14, v15
	v_cvt_pk_bf16_f32 v15, v16, v17
	v_cvt_pk_bf16_f32 v16, v10, v11
	v_cvt_pk_bf16_f32 v17, v12, v13
	v_add_u32_e32 v159, 0x58000, v157
	global_store_dwordx4 v159, v[14:17], s[6:7]
	s_waitcnt vmcnt(9)
	v_lshlrev_b32_e32 v148, 16, v212
	v_and_b32_e32 v149, 0xffff0000, v212
	v_lshlrev_b32_e32 v150, 16, v82
	v_and_b32_e32 v151, 0xffff0000, v82
	v_pk_fma_f32 v[6:7], v[6:7], v[148:149], v[150:151]
	v_lshlrev_b32_e32 v148, 16, v213
	v_and_b32_e32 v149, 0xffff0000, v213
	v_lshlrev_b32_e32 v150, 16, v83
	v_and_b32_e32 v151, 0xffff0000, v83
	v_pk_fma_f32 v[8:9], v[8:9], v[148:149], v[150:151]
	v_lshlrev_b32_e32 v148, 16, v214
	v_and_b32_e32 v149, 0xffff0000, v214
	v_lshlrev_b32_e32 v150, 16, v84
	v_and_b32_e32 v151, 0xffff0000, v84
	v_pk_fma_f32 v[2:3], v[2:3], v[148:149], v[150:151]
	v_lshlrev_b32_e32 v148, 16, v215
	v_and_b32_e32 v149, 0xffff0000, v215
	v_lshlrev_b32_e32 v150, 16, v85
	v_and_b32_e32 v151, 0xffff0000, v85
	v_pk_fma_f32 v[4:5], v[4:5], v[148:149], v[150:151]
	v_cvt_pk_bf16_f32 v6, v6, v7
	v_cvt_pk_bf16_f32 v7, v8, v9
	v_cvt_pk_bf16_f32 v8, v2, v3
	v_cvt_pk_bf16_f32 v9, v4, v5
	v_add_u32_e32 v159, 0x58000, v157
	global_store_dwordx4 v159, v[6:9], s[6:7] offset:256
	s_nop 1
	s_mov_b64 s[22:23], 0x1c00
	s_cbranch_vccnz .LBB13_836
	s_andn2_b64 vcc, exec, s[8:9]
	s_cbranch_vccnz .LBB13_835
	s_branch .LBB13_835

; template <class Epi, class Sched, bool ALIGN_EPI = false, bool SP2 = false>
; __device__ __forceinline__ void gemm_phase(PG8_LAS unsigned char* lds, const Gemm g, const Sched& S, const Epi& E) {
;     ...
;     const int tid = tid_, wid = __builtin_amdgcn_readfirstlane(tid >> 6), lane = tid & 63, wr = wid >> 2, wc = wid & 3, fr = lane & 15, fq = lane >> 4;
;     const int K = g.K, nt = K / BK;
;     unsigned voffA[2], voffB[2];
; #pragma unroll
;     for (int i = 0; i < 2; ++i) { int R, C; stage_rc(tid * 16 + i * 8192, R, C); const int Rb = Epi::PERM ? ((R & ~31) + perm32(R & 31)) : R;
;         voffA[i] = (unsigned)(R * K + C) * 2u; voffB[i] = (unsigned)(Rb * K + C) * 2u; }
;     unsigned vAc[2][2] = {{0u, 0u}, {0u, 0u}}, vAn[2][2] = {{0u, 0u}, {0u, 0u}};
;     ...
;     const size_t kstep = (size_t)(BK * 2);
;     const size_t hstep = (size_t)HALF * K * 2;
;     const size_t tstep = 2 * hstep;
;     const unsigned ldsw = (unsigned)wid * 1024u;
;     const int aoff = lds_byte(wr * 64 + fr, fq * 8), boff = lds_byte(wc * 32 + fr, fq * 8);
;     ...
;     Unit cur, nxt; int ui = 0;
;     if (!S.next(0, cur)) return;
;     f32x4 acc[2][2][4][2];
; #pragma unroll
;     for (int a = 0; a < 2; ++a)
; #pragma unroll
;         for (int b = 0; b < 2; ++b)
; #pragma unroll
;             for (int m = 0; m < 4; ++m)
; #pragma unroll
;                 for (int n = 0; n < 2; ++n) acc[a][b][m][n] = (f32x4){0.f, 0.f, 0.f, 0.f};
;     bf16x8 At[4][2], B0[2][2], B1[2][2];
;     const char* cA = Sched::GATHER ? (const char*)g.A : (const char*)g.A + (size_t)cur.pm * tstep; PG8_SETA(vAc, cur); const char* cB = (const char*)g.Bt + S.boff(cur) + (size_t)cur.pn * tstep;
;     S.a_ready(cur);
;     if constexpr (SP2) {
; __global__ void __launch_bounds__(NWAVES * 64, 2) mk_fwd(Args args) {
;     ...
;             const bf16* WOUT = (const bf16*)(ws + WS_WO) + (size_t)(l * 3 + 2) * D * D; const float* g1 = (const float*)(ws + WS_MOD) + (size_t)l * 18 * D + 2 * D;
;             pg8::Gemm g{(const bf16*)(ws + WS_MM), WOUT, ML, D, D}; pg8::StaticOrder S; S.init(ML, D, F.G, F.bx);
;             pg8::EpiResid E{(bf16*)(ws + WS_H), g1, (const bf16*)(ws + WS_H), l == 0 ? args.in[0] + F.zo : nullptr};
;             pg8::gemm_phase<pg8::EpiResid, pg8::StaticOrder, true, true>(ring, g, S, E);
.LBB13_913:
	v_readlane_b32 s4, v249, 1
	v_readlane_b32 s5, v249, 2
	s_load_dwordx2 s[4:5], s[4:5], 0xe8
	v_mov_b64_e32 v[2:3], s[10:11]
	s_cmp_eq_u32 s68, 0
	s_waitcnt lgkmcnt(0)
	v_lshl_add_u64 v[2:3], s[4:5], 0, v[2:3]
	v_lshl_add_u64 v[4:5], s[76:77], 1, v[2:3]
	s_mov_b64 s[4:5], 0x4000000
	v_lshl_add_u64 v[4:5], v[4:5], 0, s[4:5]
	s_mov_b64 s[4:5], 0x34100000
	v_readfirstlane_b32 s38, v4
	v_readfirstlane_b32 s39, v5
	s_mul_i32 s76, s68, 0x4800
	v_lshl_add_u64 v[4:5], v[2:3], 0, s[4:5]
	s_mov_b64 s[4:5], 0x1c500000
	v_lshl_add_u64 v[158:159], s[76:77], 2, v[2:3]
	v_lshl_add_u64 v[156:157], v[2:3], 0, s[4:5]
	s_cselect_b64 s[4:5], -1, 0
	s_cmp_lg_u32 s68, 0
	v_add_u32_e64 v2, 0, s7
	v_readfirstlane_b32 s41, v4
	v_readfirstlane_b32 s42, v5
	s_cselect_b64 s[8:9], -1, 0
	s_andn2_b64 vcc, exec, s[12:13]
	v_readfirstlane_b32 s40, v2
	s_cbranch_vccnz .LBB13_998
	v_ashrrev_i32_e32 v3, 31, v10
	v_lshrrev_b32_e32 v3, 26, v3
	v_add_u32_e32 v3, v10, v3
	v_ashrrev_i32_e32 v11, 6, v3
	v_bfe_i32 v3, v10, 27, 1
	v_lshlrev_b32_e32 v2, 4, v10
	v_lshrrev_b32_e32 v3, 22, v3
	v_add_u32_e32 v3, v2, v3
	v_and_b32_e32 v3, 0xfffffc00, v3
	v_sub_u32_e32 v3, v2, v3
	v_lshrrev_b32_e32 v4, 4, v3
	v_bitop3_b32 v3, v4, v3, 32 bitop3:0x6c
	v_ashrrev_i32_e32 v5, 31, v3
	v_lshrrev_b32_e32 v5, 26, v5
	v_add_u32_e32 v5, v3, v5
	v_lshlrev_b32_e32 v4, 3, v11
	v_ashrrev_i32_e32 v12, 6, v5
	v_and_b32_e32 v5, 0xc0, v5
	v_and_b32_e32 v4, -16, v4
	v_sub_u32_e32 v3, v3, v5
	v_add_u32_e32 v4, v12, v4
	v_ashrrev_i16_sdwa v3, v238, sext(v3) dst_sel:DWORD dst_unused:UNUSED_PAD src0_sel:DWORD src1_sel:BYTE_0
	v_lshlrev_b32_e32 v6, 5, v11
	v_bfe_i32 v13, v3, 0, 16
	v_lshlrev_b32_e32 v3, 1, v4
	v_lshrrev_b32_e32 v5, 2, v4
	v_and_b32_e32 v7, 3, v12
	s_mov_b32 s7, 0x1fffe0
	v_and_b32_e32 v6, 32, v6
	v_and_b32_e32 v3, 24, v3
	v_and_b32_e32 v5, 4, v5
	v_and_or_b32 v7, v4, s7, v7
	v_or3_b32 v3, v7, v5, v3
	v_add_lshl_u32 v5, v6, v13, 1
	v_add_u32_e32 v2, 0x2000, v2
	v_lshl_add_u32 v162, v3, 11, v5
	v_ashrrev_i32_e32 v3, 31, v2
	v_lshrrev_b32_e32 v3, 22, v3
	v_add_u32_e32 v3, v2, v3
	v_ashrrev_i32_e32 v14, 10, v3
	v_mul_i32_i24_e32 v3, 0x400, v14
	v_sub_u32_e32 v2, v2, v3
	v_lshrrev_b32_e32 v3, 4, v2
	v_bitop3_b32 v2, v3, v2, 32 bitop3:0x6c
	v_lshl_add_u32 v160, v4, 11, v5
	v_ashrrev_i32_e32 v4, 31, v2
	v_lshrrev_b32_e32 v4, 26, v4
	v_lshlrev_b32_e32 v3, 3, v14
	v_add_u32_e32 v4, v2, v4
	v_and_b32_e32 v3, -16, v3
	v_ashrrev_i32_e32 v15, 6, v4
	v_add_u32_e32 v3, v15, v3
	v_and_b32_e32 v6, 3, v15
	s_ashr_i32 s17, s16, 6
	v_and_or_b32 v6, v3, s7, v6
	s_ashr_i32 s7, s6, 31
	s_ashr_i32 s29, s28, 31
	s_ashr_i32 s18, s16, 8
	s_lshl_b32 s19, s17, 10
	s_lshl_b64 s[12:13], s[6:7], 19
	s_lshl_b64 s[14:15], s[28:29], 19
	s_add_u32 s34, s38, s14
	s_addc_u32 s35, s39, s15
	s_add_i32 s43, s40, 0x10000
	v_and_b32_e32 v4, 0xc0, v4
	s_add_i32 s44, s43, s19
	v_sub_u32_e32 v2, v2, v4
	s_add_i32 s45, s44, 0x2000
	v_ashrrev_i16_sdwa v2, v238, sext(v2) dst_sel:DWORD dst_unused:UNUSED_PAD src0_sel:DWORD src1_sel:BYTE_0
	s_add_u32 s14, s34, 0x40000
	v_lshlrev_b32_e32 v5, 5, v14
	v_bfe_i32 v16, v2, 0, 16
	v_lshlrev_b32_e32 v2, 1, v3
	v_lshrrev_b32_e32 v4, 2, v3
	s_addc_u32 s15, s35, 0
	s_add_i32 s46, s40, 0x14000
	v_and_b32_e32 v5, 32, v5
	v_and_b32_e32 v2, 24, v2
	v_and_b32_e32 v4, 4, v4
	s_add_i32 s47, s46, s19
	v_or3_b32 v2, v6, v4, v2
	v_add_lshl_u32 v4, v5, v16, 1
	s_mov_b32 m0, s44
	s_add_i32 s48, s47, 0x2000
	v_lshl_add_u32 v166, v2, 11, v4
	global_load_lds_dwordx4 v162, s[34:35]
	s_mov_b32 m0, s45
	s_add_u32 s30, s41, s12
	global_load_lds_dwordx4 v166, s[34:35]
	s_mov_b32 m0, s47
	s_addc_u32 s31, s42, s13
	s_add_i32 s49, s40, s19
	global_load_lds_dwordx4 v162, s[14:15]
	s_mov_b32 m0, s48
	s_add_i32 s50, s49, 0x2000
	global_load_lds_dwordx4 v166, s[14:15]
	s_mov_b32 m0, s49
	s_add_u32 s12, s30, 0x40000
	v_lshl_add_u32 v164, v3, 11, v4
	global_load_lds_dwordx4 v160, s[30:31]
	s_mov_b32 m0, s50
	s_addc_u32 s13, s31, 0
	s_add_i32 s51, s49, 0x4000
	global_load_lds_dwordx4 v164, s[30:31]
	s_mov_b32 m0, s51
	s_add_i32 s52, s49, 0x6000
	global_load_lds_dwordx4 v160, s[12:13]
	s_mov_b32 m0, s52
	v_mov_b32_e32 v163, v98
	global_load_lds_dwordx4 v164, s[12:13]
	v_mov_b32_e32 v167, v98
	v_mov_b32_e32 v161, v98
	v_mov_b32_e32 v165, v98
	s_cmp_eq_u32 s18, 1
	v_lshl_add_u64 v[8:9], s[34:35], 0, v[162:163]
	v_lshl_add_u64 v[6:7], s[34:35], 0, v[166:167]
	v_lshl_add_u64 v[2:3], s[30:31], 0, v[160:161]
	s_cselect_b64 s[12:13], -1, 0
	s_cmp_lg_u32 s18, 1
	v_lshl_add_u64 v[4:5], s[30:31], 0, v[164:165]
	s_cbranch_scc1 .LBB13_916
.LBB13_916:
	s_lshl_b64 s[14:15], s[10:11], 2
	v_readlane_b32 s20, v249, 39
	v_readlane_b32 s21, v249, 40
	s_add_u32 s7, s20, s14
	s_addc_u32 s14, s21, s15
	s_and_b64 s[4:5], s[4:5], exec
	s_cselect_b32 s15, s14, 0
	s_cselect_b32 s14, s7, 0
	s_lshl_b32 s4, s17, 5
	s_add_i32 s53, s40, 0x18000
	s_and_b32 s20, s4, 0x60
	s_add_i32 s56, s53, s19
	s_lshl_b32 s7, s18, 13
	s_lshl_b32 s17, s20, 7
	v_lshl_add_u64 v[8:9], v[8:9], 0, s[54:55]
	s_mov_b32 m0, s56
	s_add_i32 s57, s56, 0x2000
	s_add_i32 s58, s49, 0x8000
	s_add_i32 s59, s49, 0xa000
	s_waitcnt vmcnt(2)
	s_barrier
	global_load_lds_dwordx4 v[8:9], off
	v_lshl_add_u64 v[6:7], v[6:7], 0, s[54:55]
	s_mov_b32 m0, s57
	s_add_u32 s4, s34, 0x40080
	global_load_lds_dwordx4 v[6:7], off
	v_lshl_add_u64 v[2:3], v[2:3], 0, s[54:55]
	s_mov_b32 m0, s58
	s_addc_u32 s5, s35, 0
	s_add_i32 s60, s40, 0x1c000
	global_load_lds_dwordx4 v[2:3], off
	v_lshl_add_u64 v[2:3], v[4:5], 0, s[54:55]
	s_mov_b32 m0, s59
	s_add_i32 s61, s60, s19
	global_load_lds_dwordx4 v[2:3], off
	v_lshl_add_u64 v[2:3], s[4:5], 0, v[162:163]
	s_mov_b32 m0, s61
	s_add_i32 s64, s61, 0x2000
	global_load_lds_dwordx4 v[2:3], off
	v_lshl_add_u64 v[2:3], s[4:5], 0, v[166:167]
	s_mov_b32 m0, s64
	s_cmpk_lt_u32 s16, 0x100
	global_load_lds_dwordx4 v[2:3], off
	v_lshrrev_b32_e32 v3, 1, v10
	v_and_b32_e32 v3, 24, v3
	v_and_b32_e32 v2, 15, v10
	v_lshlrev_b32_e32 v4, 1, v3
	v_lshl_or_b32 v99, s18, 6, v2
	v_lshl_or_b32 v2, v2, 6, v4
	v_lshlrev_b32_e32 v4, 2, v10
	v_and_b32_e32 v4, 32, v4
	v_bitop3_b32 v5, v2, s7, v4 bitop3:0xde
	v_bitop3_b32 v184, v2, s17, v4 bitop3:0xde
	v_lshlrev_b32_e32 v2, 14, v11
	v_and_b32_e32 v2, 0xffff8000, v2
	v_or_b32_e32 v185, s20, v3
	v_lshl_add_u32 v2, v12, 11, v2
	v_and_b32_e32 v3, 1, v11
	v_lshl_or_b32 v2, v3, 6, v2
	v_lshl_add_u32 v170, v13, 1, v2
	v_lshlrev_b32_e32 v2, 14, v14
	v_and_b32_e32 v2, 0xffff8000, v2
	s_waitcnt vmcnt(6)
	s_cselect_b64 s[16:17], -1, 0
	s_ashr_i32 s69, s0, 31
	s_ashr_i32 s72, s3, 31
	v_lshl_add_u32 v2, v15, 11, v2
	v_and_b32_e32 v3, 1, v14
	s_mov_b64 s[4:5], 0x202000
	s_cmp_lg_u64 s[14:15], 0
	v_lshl_or_b32 v2, v3, 6, v2
	v_lshl_add_u64 v[168:169], v[158:159], 0, s[4:5]
	s_mov_b32 s68, 0
	s_cselect_b64 s[18:19], -1, 0
	v_mov_b32_e32 v171, v98
	v_lshl_add_u32 v172, v16, 1, v2
	v_mov_b32_e32 v173, v98
	v_add_u32_e32 v186, s40, v5
	s_barrier
	s_branch .LBB13_919

; #define PG8_LAS __attribute__((address_space(3)))
; #define PG8_STAGE_A(bufoff, h, ptr, nsel) do { if constexpr (Sched::GATHER) { if (nsel) PG8_STAGE_X(bufoff, ptr, vAn[h], PG8_A_AUX); else PG8_STAGE_X(bufoff, ptr, vAc[h], PG8_A_AUX); } \
;         else PG8_STAGE_X(bufoff, (ptr) + (h) * hstep, voffA, PG8_A_AUX); } while (0)
; #define PG8_STAGE(bufoff, gbase, voff) PG8_STAGE_X(bufoff, gbase, voff, PG8_B_AUX)
; #define PG8_LDA(dst, b, h) do { _Pragma("unroll") for (int m = 0; m < 4; ++m) _Pragma("unroll") for (int k = 0; k < 2; ++k) dst[m][k] = *(const PG8_LAS bf16x8*)(lds + PG8_SA(b, h) + aoff + m * 2048 + k * 1024); } while (0)
; #define PG8_LDB(dst, b, h) do { _Pragma("unroll") for (int n = 0; n < 2; ++n) _Pragma("unroll") for (int k = 0; k < 2; ++k) dst[n][k] = *(const PG8_LAS bf16x8*)(lds + PG8_SB(b, h) + boff + n * 2048 + k * 1024); } while (0)
; #define PG8_WAIT_V(n) asm volatile("s_waitcnt vmcnt(" #n ")" ::: "memory")
; #define PG8_WAIT_L(n) asm volatile("s_waitcnt lgkmcnt(" #n ")" ::: "memory")
; #define PG8_BAR __builtin_amdgcn_s_barrier()
; template <class Epi, class Sched, bool ALIGN_EPI = false, bool SP2 = false>
; __device__ __forceinline__ void gemm_phase(PG8_LAS unsigned char* lds, const Gemm g, const Sched& S, const Epi& E) {
;     ...
;             PG8_LDB(B0, 0, 0); PG8_LDB(B1, 0, 1); PG8_SCHED; PG8_LDA(At, 0, 0); PG8_STAGE_A(PG8_SA(1, 1), 1, a1, false);
;             PG8_WAIT_V(8); PG8_WAIT_L(0); PG8_BAR; PG8_MMA(0, 0, At, B0); PG8_MMA(0, 1, At, B1); PG8_BAR; PG8_SCHED;
;             PG8_LDA(At, 0, 1); PG8_STAGE(PG8_SB(0, 0), b2, voffB); PG8_STAGE(PG8_SB(0, 1), b2 + hstep, voffB); PG8_STAGE_A(PG8_SA(0, 0), 0, a2, last);
;             PG8_WAIT_V(8); PG8_WAIT_L(0); PG8_BAR; PG8_MMA(1, 0, At, B0); PG8_MMA(1, 1, At, B1); PG8_BAR; PG8_SCHED;
;     ...
; #pragma unroll
;         for (int a = 0; a < 2; ++a)
; #pragma unroll
;             for (int b = 0; b < 2; ++b)
; #pragma unroll
;                 for (int m = 0; m < 4; ++m)
; #pragma unroll
;                     for (int n = 0; n < 2; ++n) acc[a][b][m][n] = (f32x4){0.f, 0.f, 0.f, 0.f};
;         cur = nxt; cA = nA; cB = nB; ++ui;
;         if constexpr (Sched::GATHER) { const u32x4 pv_ = *(const PG8_LAS u32x4*)(lds + STAGE_BYTES + tid * 16); vAc[0][0] = pv_.x; vAc[0][1] = pv_.y; vAc[1][0] = pv_.z; vAc[1][1] = pv_.w; }
;         if constexpr (ALIGN_EPI) { if (wr == 1) PG8_BAR; }
.LBB13_925:
	s_ashr_i32 s23, s22, 31
	s_lshl_b64 s[24:25], s[22:23], 19
	s_add_u32 s24, s41, s24
	s_addc_u32 s25, s42, s25
	s_and_b64 s[26:27], s[4:5], exec
	s_cselect_b32 s7, s25, s31
	s_cselect_b32 s23, s24, s30
	s_ashr_i32 s21, s20, 31
	s_lshl_b64 s[26:27], s[20:21], 19
	s_add_u32 s26, s38, s26
	s_addc_u32 s27, s39, s27
	s_and_b64 s[36:37], s[4:5], exec
	s_cselect_b32 s21, s27, s35
	s_cselect_b32 s29, s26, s34
	s_add_u32 s30, s30, 0x40080
	s_addc_u32 s31, s31, 0
	s_add_u32 s73, s34, 0x100
	v_mov_b32_e32 v2, 0
	s_addc_u32 s76, s35, 0
	s_mov_b32 s86, -2
	v_mov_b32_e32 v3, v2
	v_mov_b64_e32 v[4:5], 0
	v_mov_b64_e32 v[6:7], 0
	v_mov_b64_e32 v[8:9], 0
	v_mov_b64_e32 v[18:19], 0
	v_mov_b64_e32 v[20:21], 0
	v_mov_b64_e32 v[22:23], 0
	v_mov_b64_e32 v[24:25], 0
	v_mov_b64_e32 v[34:35], 0
	v_mov_b64_e32 v[36:37], 0
	v_mov_b64_e32 v[38:39], 0
	v_mov_b64_e32 v[40:41], 0
	v_mov_b64_e32 v[50:51], 0
	v_mov_b64_e32 v[52:53], 0
	v_mov_b64_e32 v[54:55], 0
	v_mov_b64_e32 v[56:57], 0
	v_mov_b64_e32 v[10:11], 0
	v_mov_b64_e32 v[12:13], 0
	v_mov_b64_e32 v[14:15], 0
	v_mov_b64_e32 v[16:17], 0
	v_mov_b64_e32 v[26:27], 0
	v_mov_b64_e32 v[28:29], 0
	v_mov_b64_e32 v[30:31], 0
	v_mov_b64_e32 v[32:33], 0
	v_mov_b64_e32 v[42:43], 0
	v_mov_b64_e32 v[44:45], 0
	v_mov_b64_e32 v[46:47], 0
	v_mov_b64_e32 v[48:49], 0
	v_mov_b64_e32 v[58:59], 0
	v_mov_b64_e32 v[60:61], 0
	v_mov_b64_e32 v[62:63], 0
	v_mov_b64_e32 v[64:65], 0
	v_mov_b64_e32 v[66:67], 0
	v_mov_b64_e32 v[68:69], 0
	v_mov_b64_e32 v[70:71], 0
	v_mov_b64_e32 v[72:73], 0
	v_mov_b64_e32 v[100:101], 0
	v_mov_b64_e32 v[102:103], 0
	v_mov_b64_e32 v[104:105], 0
	v_mov_b64_e32 v[106:107], 0
	v_mov_b64_e32 v[116:117], 0
	v_mov_b64_e32 v[118:119], 0
	v_mov_b64_e32 v[120:121], 0
	v_mov_b64_e32 v[122:123], 0
	v_mov_b64_e32 v[132:133], 0
	v_mov_b64_e32 v[134:135], 0
	v_mov_b64_e32 v[136:137], 0
	v_mov_b64_e32 v[138:139], 0
	v_mov_b64_e32 v[86:87], 0
	v_mov_b64_e32 v[88:89], 0
	v_mov_b64_e32 v[94:95], 0
	v_mov_b64_e32 v[96:97], 0
	v_mov_b64_e32 v[108:109], 0
	v_mov_b64_e32 v[110:111], 0
	v_mov_b64_e32 v[112:113], 0
	v_mov_b64_e32 v[114:115], 0
	v_mov_b64_e32 v[124:125], 0
	v_mov_b64_e32 v[126:127], 0
	v_mov_b64_e32 v[128:129], 0
	v_mov_b64_e32 v[130:131], 0
	v_mov_b64_e32 v[140:141], 0
	v_mov_b64_e32 v[142:143], 0
	v_mov_b64_e32 v[144:145], 0
	v_mov_b64_e32 v[146:147], 0
	s_and_b64 s[98:99], exec, s[16:17]
	s_cbranch_scc1 .Lrb_926
	s_barrier
.Lrb_926:
.LBB13_926:
	v_add_u32_e32 v90, s43, v184
	v_add_u32_e32 v178, s46, v184
	ds_read_b128 v[74:77], v90
	ds_read_b128 v[78:81], v90 offset:1024
	ds_read_b128 v[82:85], v90 offset:2048
	ds_read_b128 v[90:93], v90 offset:3072
	ds_read_b128 v[148:151], v178
	ds_read_b128 v[152:155], v178 offset:1024
	ds_read_b128 v[174:177], v178 offset:2048
	ds_read_b128 v[178:181], v178 offset:3072
	s_add_u32 s34, s30, 0xfffc0080
	s_addc_u32 s35, s31, -1
	s_cmp_eq_u32 s86, 12
	s_cselect_b32 s37, s7, s35
	s_cselect_b32 s36, s23, s34
	s_cselect_b32 s35, s21, s76
	s_cselect_b32 s34, s29, s73
	v_lshl_add_u64 v[182:183], s[30:31], 0, v[170:171]
	s_add_i32 m0, s49, 0xc000
	ds_read_b128 v[188:191], v186
	ds_read_b128 v[192:195], v186 offset:1024
	ds_read_b128 v[196:199], v186 offset:2048
	ds_read_b128 v[208:211], v186 offset:3072
	ds_read_b128 v[212:215], v186 offset:4096
	ds_read_b128 v[216:219], v186 offset:5120
	ds_read_b128 v[220:223], v186 offset:6144
	ds_read_b128 v[224:227], v186 offset:7168
	global_load_lds_dwordx4 v[182:183], off
	v_lshl_add_u64 v[182:183], s[30:31], 0, v[172:173]
	s_add_i32 m0, s49, 0xe000
	s_nop 0
	global_load_lds_dwordx4 v[182:183], off
	s_waitcnt vmcnt(8)
	s_waitcnt lgkmcnt(0)
	s_barrier
	s_setprio 1
	s_waitcnt lgkmcnt(0)
	v_mfma_f32_16x16x32_bf16 v[144:147], v[74:77], v[188:191], v[144:147]
	v_mfma_f32_16x16x32_bf16 v[140:143], v[82:85], v[188:191], v[140:143]
	v_mfma_f32_16x16x32_bf16 v[128:131], v[74:77], v[196:199], v[128:131]
	v_mfma_f32_16x16x32_bf16 v[124:127], v[82:85], v[196:199], v[124:127]
	v_mfma_f32_16x16x32_bf16 v[112:115], v[74:77], v[212:215], v[112:115]
	v_mfma_f32_16x16x32_bf16 v[108:111], v[82:85], v[212:215], v[108:111]
	v_mfma_f32_16x16x32_bf16 v[94:97], v[74:77], v[220:223], v[94:97]
	v_mfma_f32_16x16x32_bf16 v[86:89], v[82:85], v[220:223], v[86:89]
	v_mfma_f32_16x16x32_bf16 v[144:147], v[78:81], v[192:195], v[144:147]
	v_mfma_f32_16x16x32_bf16 v[140:143], v[90:93], v[192:195], v[140:143]
	v_mfma_f32_16x16x32_bf16 v[128:131], v[78:81], v[208:211], v[128:131]
	v_mfma_f32_16x16x32_bf16 v[124:127], v[90:93], v[208:211], v[124:127]
	v_mfma_f32_16x16x32_bf16 v[112:115], v[78:81], v[216:219], v[112:115]
	v_mfma_f32_16x16x32_bf16 v[108:111], v[90:93], v[216:219], v[108:111]
	v_mfma_f32_16x16x32_bf16 v[94:97], v[78:81], v[224:227], v[94:97]
	v_mfma_f32_16x16x32_bf16 v[86:89], v[90:93], v[224:227], v[86:89]
	s_setprio 0
	s_setprio 1
	v_mfma_f32_16x16x32_bf16 v[136:139], v[148:151], v[188:191], v[136:139]
	v_mfma_f32_16x16x32_bf16 v[132:135], v[174:177], v[188:191], v[132:135]
	v_mfma_f32_16x16x32_bf16 v[120:123], v[148:151], v[196:199], v[120:123]
	v_mfma_f32_16x16x32_bf16 v[116:119], v[174:177], v[196:199], v[116:119]
	v_mfma_f32_16x16x32_bf16 v[104:107], v[148:151], v[212:215], v[104:107]
	v_mfma_f32_16x16x32_bf16 v[100:103], v[174:177], v[212:215], v[100:103]
	v_mfma_f32_16x16x32_bf16 v[70:73], v[148:151], v[220:223], v[70:73]
	v_mfma_f32_16x16x32_bf16 v[66:69], v[174:177], v[220:223], v[66:69]
	v_mfma_f32_16x16x32_bf16 v[136:139], v[152:155], v[192:195], v[136:139]
	v_mfma_f32_16x16x32_bf16 v[132:135], v[178:181], v[192:195], v[132:135]
	v_mfma_f32_16x16x32_bf16 v[120:123], v[152:155], v[208:211], v[120:123]
	v_mfma_f32_16x16x32_bf16 v[116:119], v[178:181], v[208:211], v[116:119]
	v_mfma_f32_16x16x32_bf16 v[104:107], v[152:155], v[216:219], v[104:107]
	v_mfma_f32_16x16x32_bf16 v[100:103], v[178:181], v[216:219], v[100:103]
	v_mfma_f32_16x16x32_bf16 v[70:73], v[152:155], v[224:227], v[70:73]
	v_mfma_f32_16x16x32_bf16 v[66:69], v[178:181], v[224:227], v[66:69]
	s_setprio 0
	s_barrier
; #define PG8_STAGE_A(bufoff, h, ptr, nsel) do { if constexpr (Sched::GATHER) { if (nsel) PG8_STAGE_X(bufoff, ptr, vAn[h], PG8_A_AUX); else PG8_STAGE_X(bufoff, ptr, vAc[h], PG8_A_AUX); } \
;         else PG8_STAGE_X(bufoff, (ptr) + (h) * hstep, voffA, PG8_A_AUX); } while (0)
; #define PG8_STAGE(bufoff, gbase, voff) PG8_STAGE_X(bufoff, gbase, voff, PG8_B_AUX)
; #define PG8_LDA(dst, b, h) do { _Pragma("unroll") for (int m = 0; m < 4; ++m) _Pragma("unroll") for (int k = 0; k < 2; ++k) dst[m][k] = *(const PG8_LAS bf16x8*)(lds + PG8_SA(b, h) + aoff + m * 2048 + k * 1024); } while (0)
; #define PG8_LDB(dst, b, h) do { _Pragma("unroll") for (int n = 0; n < 2; ++n) _Pragma("unroll") for (int k = 0; k < 2; ++k) dst[n][k] = *(const PG8_LAS bf16x8*)(lds + PG8_SB(b, h) + boff + n * 2048 + k * 1024); } while (0)
; #define PG8_MMA(ai, bj, At, Bt) do { __builtin_amdgcn_s_setprio(1); _Pragma("unroll") for (int m = 0; m < 4; ++m) _Pragma("unroll") for (int n = 0; n < 2; ++n) _Pragma("unroll") for (int k = 0; k < 2; ++k) \
;         acc[ai][bj][m][n] = __builtin_amdgcn_mfma_f32_16x16x32_bf16(Bt[n][k], At[m][k], acc[ai][bj][m][n], 0, 0, 0); __builtin_amdgcn_s_setprio(0); } while (0)
; #define PG8_WAIT_V(n) asm volatile("s_waitcnt vmcnt(" #n ")" ::: "memory")
; #define PG8_WAIT_L(n) asm volatile("s_waitcnt lgkmcnt(" #n ")" ::: "memory")
; #define PG8_BAR __builtin_amdgcn_s_barrier()
; #define PG8_SCHED __builtin_amdgcn_sched_barrier(0)
; template <class Epi, class Sched, bool ALIGN_EPI = false, bool SP2 = false>
; __device__ __forceinline__ void gemm_phase(PG8_LAS unsigned char* lds, const Gemm g, const Sched& S, const Epi& E) {
;     ...
;             PG8_WAIT_V(8); PG8_WAIT_L(0); PG8_BAR; PG8_MMA(0, 0, At, B0); PG8_MMA(0, 1, At, B1); PG8_BAR; PG8_SCHED;
;             PG8_LDA(At, 0, 1); PG8_STAGE(PG8_SB(0, 0), b2, voffB); PG8_STAGE(PG8_SB(0, 1), b2 + hstep, voffB); PG8_STAGE_A(PG8_SA(0, 0), 0, a2, last);
;             PG8_WAIT_V(8); PG8_WAIT_L(0); PG8_BAR; PG8_MMA(1, 0, At, B0); PG8_MMA(1, 1, At, B1); PG8_BAR; PG8_SCHED;
;             PG8_LDB(B0, 1, 0); PG8_LDB(B1, 1, 1); PG8_SCHED; PG8_LDA(At, 1, 0); PG8_STAGE_A(PG8_SA(0, 1), 1, a2, last);
;             PG8_WAIT_V(8); PG8_WAIT_L(0); PG8_BAR; PG8_MMA(0, 0, At, B0); PG8_MMA(0, 1, At, B1); PG8_BAR; PG8_SCHED;
	s_mov_b32 m0, s44
	v_lshl_add_u64 v[182:183], s[34:35], 0, v[162:163]
	s_add_u32 s88, s34, 0x40000
	ds_read_b128 v[188:191], v186 offset:16384
	ds_read_b128 v[192:195], v186 offset:17408
	ds_read_b128 v[196:199], v186 offset:18432
	ds_read_b128 v[208:211], v186 offset:19456
	ds_read_b128 v[212:215], v186 offset:20480
	ds_read_b128 v[216:219], v186 offset:21504
	ds_read_b128 v[220:223], v186 offset:22528
	ds_read_b128 v[224:227], v186 offset:23552
	global_load_lds_dwordx4 v[182:183], off
	v_lshl_add_u64 v[228:229], s[34:35], 0, v[166:167]
	s_mov_b32 m0, s45
	s_addc_u32 s89, s35, 0
	global_load_lds_dwordx4 v[228:229], off
	v_lshl_add_u64 v[230:231], s[88:89], 0, v[162:163]
	s_mov_b32 m0, s47
	v_lshl_add_u64 v[232:233], s[36:37], 0, v[164:165]
	global_load_lds_dwordx4 v[230:231], off
	v_lshl_add_u64 v[230:231], s[88:89], 0, v[166:167]
	s_mov_b32 m0, s48
	s_nop 0
	global_load_lds_dwordx4 v[230:231], off
	v_lshl_add_u64 v[230:231], s[36:37], 0, v[160:161]
	s_mov_b32 m0, s49
	s_nop 0
	global_load_lds_dwordx4 v[230:231], off
	s_mov_b32 m0, s50
	s_nop 0
	global_load_lds_dwordx4 v[232:233], off
	s_waitcnt vmcnt(8)
	s_waitcnt lgkmcnt(0)
	s_barrier
	s_setprio 1
	s_waitcnt lgkmcnt(0)
	v_mfma_f32_16x16x32_bf16 v[62:65], v[74:77], v[188:191], v[62:65]
	v_mfma_f32_16x16x32_bf16 v[58:61], v[82:85], v[188:191], v[58:61]
	v_mfma_f32_16x16x32_bf16 v[46:49], v[74:77], v[196:199], v[46:49]
	v_mfma_f32_16x16x32_bf16 v[42:45], v[82:85], v[196:199], v[42:45]
	v_mfma_f32_16x16x32_bf16 v[30:33], v[74:77], v[212:215], v[30:33]
	v_mfma_f32_16x16x32_bf16 v[26:29], v[82:85], v[212:215], v[26:29]
	v_mfma_f32_16x16x32_bf16 v[14:17], v[74:77], v[220:223], v[14:17]
	v_mfma_f32_16x16x32_bf16 v[10:13], v[82:85], v[220:223], v[10:13]
	v_mfma_f32_16x16x32_bf16 v[62:65], v[78:81], v[192:195], v[62:65]
	v_mfma_f32_16x16x32_bf16 v[58:61], v[90:93], v[192:195], v[58:61]
	v_mfma_f32_16x16x32_bf16 v[46:49], v[78:81], v[208:211], v[46:49]
	v_mfma_f32_16x16x32_bf16 v[42:45], v[90:93], v[208:211], v[42:45]
	v_mfma_f32_16x16x32_bf16 v[30:33], v[78:81], v[216:219], v[30:33]
	v_mfma_f32_16x16x32_bf16 v[26:29], v[90:93], v[216:219], v[26:29]
	v_mfma_f32_16x16x32_bf16 v[14:17], v[78:81], v[224:227], v[14:17]
	v_mfma_f32_16x16x32_bf16 v[10:13], v[90:93], v[224:227], v[10:13]
	s_setprio 0
	s_setprio 1
	v_mfma_f32_16x16x32_bf16 v[54:57], v[148:151], v[188:191], v[54:57]
	v_mfma_f32_16x16x32_bf16 v[50:53], v[174:177], v[188:191], v[50:53]
	v_mfma_f32_16x16x32_bf16 v[38:41], v[148:151], v[196:199], v[38:41]
	v_mfma_f32_16x16x32_bf16 v[34:37], v[174:177], v[196:199], v[34:37]
	v_mfma_f32_16x16x32_bf16 v[22:25], v[148:151], v[212:215], v[22:25]
	v_mfma_f32_16x16x32_bf16 v[18:21], v[174:177], v[212:215], v[18:21]
	v_mfma_f32_16x16x32_bf16 v[6:9], v[148:151], v[220:223], v[6:9]
	v_mfma_f32_16x16x32_bf16 v[2:5], v[174:177], v[220:223], v[2:5]
	v_mfma_f32_16x16x32_bf16 v[54:57], v[152:155], v[192:195], v[54:57]
	v_mfma_f32_16x16x32_bf16 v[50:53], v[178:181], v[192:195], v[50:53]
	v_mfma_f32_16x16x32_bf16 v[38:41], v[152:155], v[208:211], v[38:41]
	v_mfma_f32_16x16x32_bf16 v[34:37], v[178:181], v[208:211], v[34:37]
	v_mfma_f32_16x16x32_bf16 v[22:25], v[152:155], v[216:219], v[22:25]
	v_mfma_f32_16x16x32_bf16 v[18:21], v[178:181], v[216:219], v[18:21]
	v_mfma_f32_16x16x32_bf16 v[6:9], v[152:155], v[224:227], v[6:9]
	v_mfma_f32_16x16x32_bf16 v[2:5], v[178:181], v[224:227], v[2:5]
	s_setprio 0
	s_barrier
	v_add_u32_e32 v90, s53, v184
	v_add_u32_e32 v178, s60, v184
	ds_read_b128 v[74:77], v90
	ds_read_b128 v[78:81], v90 offset:1024
	ds_read_b128 v[82:85], v90 offset:2048
	ds_read_b128 v[90:93], v90 offset:3072
	ds_read_b128 v[148:151], v178
	ds_read_b128 v[152:155], v178 offset:1024
	ds_read_b128 v[174:177], v178 offset:2048
	ds_read_b128 v[178:181], v178 offset:3072
	s_add_u32 s36, s36, 0x40000
	s_addc_u32 s37, s37, 0
	s_mov_b32 m0, s51
	v_lshl_add_u64 v[242:243], s[36:37], 0, v[160:161]
	ds_read_b128 v[188:191], v186 offset:32768
	ds_read_b128 v[192:195], v186 offset:33792
	ds_read_b128 v[196:199], v186 offset:34816
	ds_read_b128 v[208:211], v186 offset:35840
	ds_read_b128 v[212:215], v186 offset:36864
	ds_read_b128 v[216:219], v186 offset:37888
	ds_read_b128 v[220:223], v186 offset:38912
	ds_read_b128 v[224:227], v186 offset:39936
	global_load_lds_dwordx4 v[242:243], off
	v_lshl_add_u64 v[242:243], s[36:37], 0, v[164:165]
	s_mov_b32 m0, s52
	s_nop 0
	global_load_lds_dwordx4 v[242:243], off
	s_waitcnt vmcnt(8)
	s_waitcnt lgkmcnt(0)
	s_barrier
; #define PG8_STAGE_A(bufoff, h, ptr, nsel) do { if constexpr (Sched::GATHER) { if (nsel) PG8_STAGE_X(bufoff, ptr, vAn[h], PG8_A_AUX); else PG8_STAGE_X(bufoff, ptr, vAc[h], PG8_A_AUX); } \
;         else PG8_STAGE_X(bufoff, (ptr) + (h) * hstep, voffA, PG8_A_AUX); } while (0)
; #define PG8_STAGE(bufoff, gbase, voff) PG8_STAGE_X(bufoff, gbase, voff, PG8_B_AUX)
; #define PG8_LDA(dst, b, h) do { _Pragma("unroll") for (int m = 0; m < 4; ++m) _Pragma("unroll") for (int k = 0; k < 2; ++k) dst[m][k] = *(const PG8_LAS bf16x8*)(lds + PG8_SA(b, h) + aoff + m * 2048 + k * 1024); } while (0)
; #define PG8_MMA(ai, bj, At, Bt) do { __builtin_amdgcn_s_setprio(1); _Pragma("unroll") for (int m = 0; m < 4; ++m) _Pragma("unroll") for (int n = 0; n < 2; ++n) _Pragma("unroll") for (int k = 0; k < 2; ++k) \
;         acc[ai][bj][m][n] = __builtin_amdgcn_mfma_f32_16x16x32_bf16(Bt[n][k], At[m][k], acc[ai][bj][m][n], 0, 0, 0); __builtin_amdgcn_s_setprio(0); } while (0)
; #define PG8_WAIT_V(n) asm volatile("s_waitcnt vmcnt(" #n ")" ::: "memory")
; #define PG8_WAIT_L(n) asm volatile("s_waitcnt lgkmcnt(" #n ")" ::: "memory")
; #define PG8_BAR __builtin_amdgcn_s_barrier()
; #define PG8_SCHED __builtin_amdgcn_sched_barrier(0)
; template <class Epi, class Sched, bool ALIGN_EPI = false, bool SP2 = false>
; __device__ __forceinline__ void gemm_phase(PG8_LAS unsigned char* lds, const Gemm g, const Sched& S, const Epi& E) {
;     ...
;             PG8_WAIT_V(8); PG8_WAIT_L(0); PG8_BAR; PG8_MMA(0, 0, At, B0); PG8_MMA(0, 1, At, B1); PG8_BAR; PG8_SCHED;
;             PG8_LDA(At, 1, 1); PG8_STAGE(PG8_SB(1, 0), b3, voffB); PG8_STAGE(PG8_SB(1, 1), b3 + hstep, voffB); PG8_STAGE_A(PG8_SA(1, 0), 0, a3, last);
;             PG8_WAIT_V(8); PG8_WAIT_L(0); PG8_BAR; PG8_MMA(1, 0, At, B0); PG8_MMA(1, 1, At, B1); PG8_BAR; PG8_SCHED;
;     ...
;         if constexpr (ALIGN_EPI) { if (wr == 0) PG8_BAR; }
	s_setprio 1
	s_waitcnt lgkmcnt(0)
	v_mfma_f32_16x16x32_bf16 v[144:147], v[74:77], v[188:191], v[144:147]
	v_mfma_f32_16x16x32_bf16 v[140:143], v[82:85], v[188:191], v[140:143]
	v_mfma_f32_16x16x32_bf16 v[128:131], v[74:77], v[196:199], v[128:131]
	v_mfma_f32_16x16x32_bf16 v[124:127], v[82:85], v[196:199], v[124:127]
	v_mfma_f32_16x16x32_bf16 v[112:115], v[74:77], v[212:215], v[112:115]
	v_mfma_f32_16x16x32_bf16 v[108:111], v[82:85], v[212:215], v[108:111]
	v_mfma_f32_16x16x32_bf16 v[94:97], v[74:77], v[220:223], v[94:97]
	v_mfma_f32_16x16x32_bf16 v[86:89], v[82:85], v[220:223], v[86:89]
	v_mfma_f32_16x16x32_bf16 v[144:147], v[78:81], v[192:195], v[144:147]
	v_mfma_f32_16x16x32_bf16 v[140:143], v[90:93], v[192:195], v[140:143]
	v_mfma_f32_16x16x32_bf16 v[128:131], v[78:81], v[208:211], v[128:131]
	v_mfma_f32_16x16x32_bf16 v[124:127], v[90:93], v[208:211], v[124:127]
	v_mfma_f32_16x16x32_bf16 v[112:115], v[78:81], v[216:219], v[112:115]
	v_mfma_f32_16x16x32_bf16 v[108:111], v[90:93], v[216:219], v[108:111]
	v_mfma_f32_16x16x32_bf16 v[94:97], v[78:81], v[224:227], v[94:97]
	v_mfma_f32_16x16x32_bf16 v[86:89], v[90:93], v[224:227], v[86:89]
	s_setprio 0
	s_setprio 1
	v_mfma_f32_16x16x32_bf16 v[136:139], v[148:151], v[188:191], v[136:139]
	v_mfma_f32_16x16x32_bf16 v[132:135], v[174:177], v[188:191], v[132:135]
	v_mfma_f32_16x16x32_bf16 v[120:123], v[148:151], v[196:199], v[120:123]
	v_mfma_f32_16x16x32_bf16 v[116:119], v[174:177], v[196:199], v[116:119]
	v_mfma_f32_16x16x32_bf16 v[104:107], v[148:151], v[212:215], v[104:107]
	v_mfma_f32_16x16x32_bf16 v[100:103], v[174:177], v[212:215], v[100:103]
	v_mfma_f32_16x16x32_bf16 v[70:73], v[148:151], v[220:223], v[70:73]
	v_mfma_f32_16x16x32_bf16 v[66:69], v[174:177], v[220:223], v[66:69]
	v_mfma_f32_16x16x32_bf16 v[136:139], v[152:155], v[192:195], v[136:139]
	v_mfma_f32_16x16x32_bf16 v[132:135], v[178:181], v[192:195], v[132:135]
	v_mfma_f32_16x16x32_bf16 v[120:123], v[152:155], v[208:211], v[120:123]
	v_mfma_f32_16x16x32_bf16 v[116:119], v[178:181], v[208:211], v[116:119]
	v_mfma_f32_16x16x32_bf16 v[104:107], v[152:155], v[216:219], v[104:107]
	v_mfma_f32_16x16x32_bf16 v[100:103], v[178:181], v[216:219], v[100:103]
	v_mfma_f32_16x16x32_bf16 v[70:73], v[152:155], v[224:227], v[70:73]
	v_mfma_f32_16x16x32_bf16 v[66:69], v[178:181], v[224:227], v[66:69]
	s_setprio 0
	s_barrier
	s_mov_b32 m0, s56
	v_lshl_add_u64 v[182:183], v[182:183], 0, s[54:55]
	s_add_u32 s34, s34, 0x40080
	ds_read_b128 v[188:191], v186 offset:49152
	ds_read_b128 v[192:195], v186 offset:50176
	ds_read_b128 v[196:199], v186 offset:51200
	ds_read_b128 v[208:211], v186 offset:52224
	ds_read_b128 v[212:215], v186 offset:53248
	ds_read_b128 v[216:219], v186 offset:54272
	ds_read_b128 v[220:223], v186 offset:55296
	ds_read_b128 v[224:227], v186 offset:56320
	global_load_lds_dwordx4 v[182:183], off
	v_lshl_add_u64 v[182:183], v[228:229], 0, s[54:55]
	s_mov_b32 m0, s57
	s_addc_u32 s35, s35, 0
	global_load_lds_dwordx4 v[182:183], off
	v_lshl_add_u64 v[182:183], s[34:35], 0, v[162:163]
	s_mov_b32 m0, s61
	s_nop 0
	global_load_lds_dwordx4 v[182:183], off
	v_lshl_add_u64 v[182:183], s[34:35], 0, v[166:167]
	s_mov_b32 m0, s64
	s_nop 0
	global_load_lds_dwordx4 v[182:183], off
	v_lshl_add_u64 v[182:183], v[230:231], 0, s[54:55]
	s_mov_b32 m0, s58
	s_nop 0
	global_load_lds_dwordx4 v[182:183], off
	v_lshl_add_u64 v[182:183], v[232:233], 0, s[54:55]
	s_mov_b32 m0, s59
	s_nop 0
	global_load_lds_dwordx4 v[182:183], off
	s_waitcnt vmcnt(8)
	s_waitcnt lgkmcnt(0)
	s_barrier
	s_setprio 1
	s_waitcnt lgkmcnt(0)
	v_mfma_f32_16x16x32_bf16 v[62:65], v[74:77], v[188:191], v[62:65]
	v_mfma_f32_16x16x32_bf16 v[58:61], v[82:85], v[188:191], v[58:61]
	v_mfma_f32_16x16x32_bf16 v[46:49], v[74:77], v[196:199], v[46:49]
	v_mfma_f32_16x16x32_bf16 v[42:45], v[82:85], v[196:199], v[42:45]
	v_mfma_f32_16x16x32_bf16 v[30:33], v[74:77], v[212:215], v[30:33]
	v_mfma_f32_16x16x32_bf16 v[26:29], v[82:85], v[212:215], v[26:29]
	v_mfma_f32_16x16x32_bf16 v[14:17], v[74:77], v[220:223], v[14:17]
	v_mfma_f32_16x16x32_bf16 v[10:13], v[82:85], v[220:223], v[10:13]
	v_mfma_f32_16x16x32_bf16 v[62:65], v[78:81], v[192:195], v[62:65]
	v_mfma_f32_16x16x32_bf16 v[58:61], v[90:93], v[192:195], v[58:61]
	v_mfma_f32_16x16x32_bf16 v[46:49], v[78:81], v[208:211], v[46:49]
	v_mfma_f32_16x16x32_bf16 v[42:45], v[90:93], v[208:211], v[42:45]
	v_mfma_f32_16x16x32_bf16 v[30:33], v[78:81], v[216:219], v[30:33]
	v_mfma_f32_16x16x32_bf16 v[26:29], v[90:93], v[216:219], v[26:29]
	v_mfma_f32_16x16x32_bf16 v[14:17], v[78:81], v[224:227], v[14:17]
	v_mfma_f32_16x16x32_bf16 v[10:13], v[90:93], v[224:227], v[10:13]
	s_setprio 0
	s_setprio 1
	v_mfma_f32_16x16x32_bf16 v[54:57], v[148:151], v[188:191], v[54:57]
	v_mfma_f32_16x16x32_bf16 v[50:53], v[174:177], v[188:191], v[50:53]
	v_mfma_f32_16x16x32_bf16 v[38:41], v[148:151], v[196:199], v[38:41]
	v_mfma_f32_16x16x32_bf16 v[34:37], v[174:177], v[196:199], v[34:37]
	v_mfma_f32_16x16x32_bf16 v[22:25], v[148:151], v[212:215], v[22:25]
	v_mfma_f32_16x16x32_bf16 v[18:21], v[174:177], v[212:215], v[18:21]
	v_mfma_f32_16x16x32_bf16 v[6:9], v[148:151], v[220:223], v[6:9]
	v_mfma_f32_16x16x32_bf16 v[2:5], v[174:177], v[220:223], v[2:5]
	v_mfma_f32_16x16x32_bf16 v[54:57], v[152:155], v[192:195], v[54:57]
	v_mfma_f32_16x16x32_bf16 v[50:53], v[178:181], v[192:195], v[50:53]
	v_mfma_f32_16x16x32_bf16 v[38:41], v[152:155], v[208:211], v[38:41]
	v_mfma_f32_16x16x32_bf16 v[34:37], v[178:181], v[208:211], v[34:37]
	v_mfma_f32_16x16x32_bf16 v[22:25], v[152:155], v[216:219], v[22:25]
	v_mfma_f32_16x16x32_bf16 v[18:21], v[178:181], v[216:219], v[18:21]
	v_mfma_f32_16x16x32_bf16 v[6:9], v[152:155], v[224:227], v[6:9]
	v_mfma_f32_16x16x32_bf16 v[2:5], v[178:181], v[224:227], v[2:5]
	s_setprio 0
	s_barrier
	s_add_i32 s86, s86, 2
	s_add_u32 s30, s30, 0x100
	s_addc_u32 s31, s31, 0
	s_add_u32 s73, s73, 0x100
	s_addc_u32 s76, s76, 0
	s_cmp_gt_u32 s86, 13
	s_cbranch_scc0 .LBB13_926
	s_and_b64 vcc, exec, s[16:17]
	s_cbranch_vccz .LBB13_929
	s_barrier

; #define PG8_LAS __attribute__((address_space(3)))
; #define PG8_BAR __builtin_amdgcn_s_barrier()
; template <class Epi, class Sched, bool ALIGN_EPI = false, bool SP2 = false>
; __device__ __forceinline__ void gemm_phase(PG8_LAS unsigned char* lds, const Gemm g, const Sched& S, const Epi& E) {
;     ...
;         if (!has_next) break;
; #pragma unroll
;         for (int a = 0; a < 2; ++a)
; #pragma unroll
;             for (int b = 0; b < 2; ++b)
; #pragma unroll
;                 for (int m = 0; m < 4; ++m)
; #pragma unroll
;                     for (int n = 0; n < 2; ++n) acc[a][b][m][n] = (f32x4){0.f, 0.f, 0.f, 0.f};
;         cur = nxt; cA = nA; cB = nB; ++ui;
;         if constexpr (Sched::GATHER) { const u32x4 pv_ = *(const PG8_LAS u32x4*)(lds + STAGE_BYTES + tid * 16); vAc[0][0] = pv_.x; vAc[0][1] = pv_.y; vAc[1][0] = pv_.z; vAc[1][1] = pv_.w; }
;         if constexpr (ALIGN_EPI) { if (wr == 1) PG8_BAR; }
.Lresid_out_done:
	s_mov_b64 s[28:29], 0x2c000
	s_andn2_b64 vcc, exec, s[4:5]
	s_mov_b64 s[4:5], -1
	s_cbranch_vccnz .LBB13_918
	s_andn2_b64 vcc, exec, s[12:13]
	s_cbranch_vccnz .LBB13_917
	s_branch .LBB13_917

;     __host__ __device__ bool next(int i, Unit& u) const {
;         const long L = (long)i * G + c; if (L >= nwg) return false;
;         int wgid = (int)L; { const int q = nwg / NXCD, r = nwg % NXCD, xcd = wgid % NXCD; int off = wgid / NXCD; if (rev & 2) off = (xcd < r ? q + 1 : q) - 1 - off;
;             wgid = (xcd < r ? xcd * (q + 1) : r * (q + 1) + (xcd - r) * q) + off; }
;         const int nig = wgm * nN, gid = wgid / nig, fm = gid * wgm, gsz = (nM - fm) < wgm ? (nM - fm) : wgm;
;         u.pm = fm + ((wgid % nig) % gsz); u.pn = (wgid % nig) / gsz; if (rev & 1) u.pn = nN - 1 - u.pn; return true;
;     }
; template <class Epi, class Sched, bool ALIGN_EPI = false, bool SP2 = false>
; __device__ __forceinline__ void gemm_phase(PG8_LAS unsigned char* lds, const Gemm g, const Sched& S, const Epi& E) {
;     ...
;     const int tid = tid_, wid = __builtin_amdgcn_readfirstlane(tid >> 6), lane = tid & 63, wr = wid >> 2, wc = wid & 3, fr = lane & 15, fq = lane >> 4;
;     const int K = g.K, nt = K / BK;
;     unsigned voffA[2], voffB[2];
; #pragma unroll
;     for (int i = 0; i < 2; ++i) { int R, C; stage_rc(tid * 16 + i * 8192, R, C); const int Rb = Epi::PERM ? ((R & ~31) + perm32(R & 31)) : R;
;         voffA[i] = (unsigned)(R * K + C) * 2u; voffB[i] = (unsigned)(Rb * K + C) * 2u; }
;     unsigned vAc[2][2] = {{0u, 0u}, {0u, 0u}}, vAn[2][2] = {{0u, 0u}, {0u, 0u}};
;     ...
;     const size_t kstep = (size_t)(BK * 2);
;     const size_t hstep = (size_t)HALF * K * 2;
;     const size_t tstep = 2 * hstep;
;     const unsigned ldsw = (unsigned)wid * 1024u;
;     const int aoff = lds_byte(wr * 64 + fr, fq * 8), boff = lds_byte(wc * 32 + fr, fq * 8);
;     ...
;     Unit cur, nxt; int ui = 0;
;     if (!S.next(0, cur)) return;
;     f32x4 acc[2][2][4][2];
; #pragma unroll
;     for (int a = 0; a < 2; ++a)
; #pragma unroll
;         for (int b = 0; b < 2; ++b)
; #pragma unroll
;             for (int m = 0; m < 4; ++m)
; #pragma unroll
;                 for (int n = 0; n < 2; ++n) acc[a][b][m][n] = (f32x4){0.f, 0.f, 0.f, 0.f};
;     bf16x8 At[4][2], B0[2][2], B1[2][2];
;     const char* cA = Sched::GATHER ? (const char*)g.A : (const char*)g.A + (size_t)cur.pm * tstep; PG8_SETA(vAc, cur); const char* cB = (const char*)g.Bt + S.boff(cur) + (size_t)cur.pn * tstep;
;     S.a_ready(cur);
;     if constexpr (SP2) {
.LBB13_1397:
	v_cndmask_b32_e64 v1, 0, 1, s[38:39]
	s_andn2_b64 vcc, exec, s[4:5]
	v_cmp_ne_u32_e64 s[42:43], 1, v1
	s_cbranch_vccnz .LBB13_1513
	v_readlane_b32 s2, v249, 1
	v_readlane_b32 s3, v249, 2
	s_load_dwordx2 s[2:3], s[2:3], 0xe8
	s_mov_b32 s0, s77
	v_mov_b32_e32 v1, v0
	s_mov_b64 s[8:9], 0
	s_waitcnt lgkmcnt(0)
	s_add_u32 s10, s2, s8
	s_addc_u32 s11, s3, s9
	s_add_i32 s2, s0, 0
	s_add_u32 s14, s10, 0x20700000
	s_addc_u32 s15, s11, 0
	s_lshr_b32 s38, s68, 1
	s_mov_b32 s44, s56
	v_readlane_b32 s45, v249, 0
	s_add_u32 s16, s10, 0x22800000
	s_addc_u32 s17, s11, 0
	s_ashr_i32 s46, s45, 31
	s_lshr_b32 s0, s46, 29
	s_add_i32 s0, s45, s0
	s_ashr_i32 s39, s0, 3
	s_and_b32 s0, s0, -8
	s_sub_i32 s40, s45, s0
	s_add_i32 s47, s2, 0x10000
	s_add_i32 s50, s2, 0x14000
	s_add_i32 s51, s2, 0x18000
	s_add_i32 s56, s2, 0x1c000
	s_ashr_i32 s57, s44, 31
	s_and_b64 vcc, exec, s[42:43]
	s_mov_b64 s[6:7], -1
	s_cbranch_vccnz .LBB13_1420
	v_readlane_b32 s0, v249, 59
	v_readlane_b32 s1, v249, 60
	s_and_b64 s[0:1], s[0:1], exec
	s_cselect_b32 s3, 64, 0x42
	s_mul_i32 s76, s3, 22
	s_waitcnt vmcnt(0)
	v_mov_b32_e32 v8, v0
	s_cmp_ge_i32 s45, s76
	s_nop 0
	v_readfirstlane_b32 s6, v8
	s_cbranch_scc1 .LBB13_1419
	v_lshlrev_b32_e32 v1, 4, v8
	v_add_u32_e32 v3, 0x2000, v1
	v_ashrrev_i32_e32 v2, 31, v3
	v_lshrrev_b32_e32 v2, 22, v2
	v_add_u32_e32 v2, v3, v2
	v_ashrrev_i32_e32 v2, 10, v2
	v_mul_i32_i24_e32 v4, 0x400, v2
	v_sub_u32_e32 v3, v3, v4
	v_lshrrev_b32_e32 v4, 4, v3
	v_bitop3_b32 v4, v4, v3, 32 bitop3:0x6c
	v_ashrrev_i32_e32 v3, 31, v4
	v_lshrrev_b32_e32 v3, 26, v3
	v_add_u32_e32 v5, v4, v3
	v_lshlrev_b32_e32 v6, 3, v2
	v_ashrrev_i32_e32 v3, 6, v5
	v_and_b32_e32 v6, -16, v6
	v_add_u32_e32 v6, v3, v6
	v_and_b32_e32 v7, 3, v3
	s_mov_b32 s4, 0x1fffe0
	v_lshrrev_b32_e32 v9, 2, v6
	v_lshlrev_b32_e32 v10, 1, v6
	v_and_b32_e32 v5, 0xc0, v5
	v_and_or_b32 v7, v6, s4, v7
	v_and_b32_e32 v9, 4, v9
	v_and_b32_e32 v10, 24, v10
	v_sub_u32_e32 v4, v4, v5
	v_or3_b32 v7, v7, v9, v10
	v_lshlrev_b32_e32 v9, 5, v2
	v_ashrrev_i16_sdwa v4, v238, sext(v4) dst_sel:DWORD dst_unused:UNUSED_PAD src0_sel:DWORD src1_sel:BYTE_0
	v_and_b32_e32 v9, 32, v9
	v_bfe_i32 v4, v4, 0, 16
	s_ashr_i32 s12, s6, 6
	v_add_lshl_u32 v5, v9, v4, 1
	s_ashr_i32 s13, s6, 8
	s_lshl_b32 s7, s12, 10
	s_mul_i32 s0, s38, 0x1080000
	v_lshl_add_u32 v132, v7, 11, v5
	v_lshl_add_u32 v134, v6, 11, v5
	v_bfe_i32 v5, v8, 27, 1
	s_add_u32 s0, s10, s0
	v_lshrrev_b32_e32 v5, 22, v5
	s_addc_u32 s1, s11, 0
	v_add_u32_e32 v5, v1, v5
	v_writelane_b32 v249, s42, 55
	s_add_u32 s41, s0, 0x5400000
	v_and_b32_e32 v5, 0xfffffc00, v5
	v_writelane_b32 v249, s43, 56
	s_addc_u32 s42, s1, 0
	s_lshr_b32 s43, s76, 3
	s_and_b32 s48, s76, 4
	v_sub_u32_e32 v1, v1, v5
	s_add_i32 s49, s43, 1
	s_sub_i32 s0, s40, s48
	v_lshrrev_b32_e32 v5, 4, v1
	v_ashrrev_i32_e32 v6, 31, v8
	s_mul_i32 s53, s49, s48
	s_mul_i32 s0, s0, s43
	v_bitop3_b32 v1, v5, v1, 32 bitop3:0x6c
	v_lshrrev_b32_e32 v6, 26, v6
	s_add_i32 s0, s0, s53
	v_ashrrev_i32_e32 v5, 31, v1
	v_add_u32_e32 v6, v8, v6
	s_cmp_lt_i32 s40, s48
	s_mul_i32 s1, s40, s49
	v_lshrrev_b32_e32 v5, 26, v5
	v_ashrrev_i32_e32 v6, 6, v6
	v_add_u32_e32 v7, v1, v5
	v_lshlrev_b32_e32 v9, 3, v6
	s_cselect_b32 s0, s1, s0
	v_ashrrev_i32_e32 v5, 6, v7
	v_and_b32_e32 v9, -16, v9
	s_add_i32 s0, s0, s39
	v_add_u32_e32 v9, v5, v9
	v_and_b32_e32 v10, 3, v5
	s_mul_hi_i32 s1, s0, 0x2e8ba2e9
	v_and_or_b32 v10, v9, s4, v10
	s_lshr_b32 s4, s1, 31
	s_ashr_i32 s1, s1, 3
	s_add_i32 s1, s1, s4
	s_lshl_b32 s4, s1, 1
	v_and_b32_e32 v7, 0xc0, v7
	s_sub_i32 s5, s3, s4
	v_sub_u32_e32 v1, v1, v7
	s_min_i32 s5, s5, 2
	v_ashrrev_i16_sdwa v1, v238, sext(v1) dst_sel:DWORD dst_unused:UNUSED_PAD src0_sel:DWORD src1_sel:BYTE_0
	s_abs_i32 s18, s5
	v_bfe_i32 v7, v1, 0, 16
	v_cvt_f32_u32_e32 v1, s18
	s_sub_i32 s20, 0, s18
	s_mul_i32 s1, s1, 44
	s_sub_i32 s0, s0, s1
	v_rcp_iflag_f32_e32 v1, v1
	s_abs_i32 s19, s0
	s_xor_b32 s1, s0, s5
	s_ashr_i32 s1, s1, 31
	v_mul_f32_e32 v1, 0x4f7ffffe, v1
	v_cvt_u32_f32_e32 v1, v1
	v_lshrrev_b32_e32 v11, 2, v9
	v_lshlrev_b32_e32 v12, 1, v9
	v_and_b32_e32 v11, 4, v11
	v_readfirstlane_b32 s21, v1
	s_mul_i32 s20, s20, s21
	s_mul_hi_u32 s20, s21, s20
	s_add_i32 s21, s21, s20
	s_mul_hi_u32 s20, s19, s21
	s_mul_i32 s21, s20, s18
	s_sub_i32 s19, s19, s21
	s_add_i32 s21, s20, 1
	s_sub_i32 s22, s19, s18
	s_cmp_ge_u32 s19, s18
	s_cselect_b32 s20, s21, s20
	s_cselect_b32 s19, s22, s19
	s_add_i32 s21, s20, 1
	s_cmp_ge_u32 s19, s18
	s_cselect_b32 s18, s21, s20
	s_xor_b32 s18, s18, s1
	s_sub_i32 s26, s18, s1
	s_mul_i32 s1, s26, s5
	s_sub_i32 s0, s0, s1
	s_add_i32 s28, s4, s0
	s_ashr_i32 s29, s28, 31
	s_lshl_b64 s[0:1], s[28:29], 19
	s_add_u32 s30, s14, s0
	s_addc_u32 s31, s15, s1
	s_ashr_i32 s27, s26, 31
	v_and_b32_e32 v12, 24, v12
	s_lshl_b64 s[0:1], s[26:27], 19
	v_or3_b32 v10, v10, v11, v12
	v_lshlrev_b32_e32 v11, 5, v6
	s_add_u32 s34, s41, s0
	v_and_b32_e32 v11, 32, v11
	s_addc_u32 s35, s42, s1
	s_add_i32 s4, s47, s7
	v_add_lshl_u32 v11, v11, v7, 1
	s_add_i32 s5, s4, 0x2000
	v_lshl_add_u32 v136, v10, 11, v11
	s_mov_b32 m0, s4
	s_add_u32 s0, s34, 0x40000
	global_load_lds_dwordx4 v136, s[34:35]
	s_mov_b32 m0, s5
	s_addc_u32 s1, s35, 0
	s_add_i32 s29, s50, s7
	global_load_lds_dwordx4 v132, s[34:35]
	s_mov_b32 m0, s29
	s_add_i32 s52, s29, 0x2000
	s_add_i32 s58, s2, s7
	global_load_lds_dwordx4 v136, s[0:1]
	s_mov_b32 m0, s52
	s_add_i32 s59, s58, 0x2000
	v_lshl_add_u32 v138, v9, 11, v11
	global_load_lds_dwordx4 v132, s[0:1]
	s_mov_b32 m0, s58
	s_add_u32 s0, s30, 0x40000
	global_load_lds_dwordx4 v138, s[30:31]
	s_mov_b32 m0, s59
	s_addc_u32 s1, s31, 0
	s_add_i32 s60, s58, 0x4000
	global_load_lds_dwordx4 v134, s[30:31]
	s_mov_b32 m0, s60
	s_add_i32 s61, s58, 0x6000
	global_load_lds_dwordx4 v138, s[0:1]
	s_mov_b32 m0, s61
	s_cmp_eq_u32 s13, 1
	global_load_lds_dwordx4 v134, s[0:1]
	s_cselect_b64 s[0:1], -1, 0
	s_cmp_lg_u32 s13, 1
	s_cbranch_scc1 .LBB13_1402
; #define PG8_STAGE_A(bufoff, h, ptr, nsel) do { if constexpr (Sched::GATHER) { if (nsel) PG8_STAGE_X(bufoff, ptr, vAn[h], PG8_A_AUX); else PG8_STAGE_X(bufoff, ptr, vAc[h], PG8_A_AUX); } \
;         else PG8_STAGE_X(bufoff, (ptr) + (h) * hstep, voffA, PG8_A_AUX); } while (0)
; #define PG8_STAGE(bufoff, gbase, voff) PG8_STAGE_X(bufoff, gbase, voff, PG8_B_AUX)
; #define PG8_WAIT_V(n) asm volatile("s_waitcnt vmcnt(" #n ")" ::: "memory")
; #define PG8_BAR __builtin_amdgcn_s_barrier()
; template <class Epi, class Sched, bool ALIGN_EPI = false, bool SP2 = false>
; __device__ __forceinline__ void gemm_phase(PG8_LAS unsigned char* lds, const Gemm g, const Sched& S, const Epi& E) {
;     ...
;         PG8_STAGE(PG8_SB(0, 0), cB, voffB); PG8_STAGE(PG8_SB(0, 1), cB + hstep, voffB); PG8_STAGE_A(PG8_SA(0, 0), 0, cA, false); PG8_STAGE_A(PG8_SA(0, 1), 1, cA, false);
;         if (wr == 1) PG8_BAR;
;         PG8_WAIT_V(2); PG8_BAR;
;         PG8_STAGE(PG8_SB(1, 0), cB + kstep, voffB); PG8_STAGE_A(PG8_SA(1, 0), 0, cA + kstep, false); PG8_STAGE(PG8_SB(1, 1), cB + hstep + kstep, voffB);
;         PG8_WAIT_V(6); PG8_BAR;
.LBB13_1402:
	v_lshrrev_b32_e32 v18, 1, v8
	v_and_b32_e32 v18, 24, v18
	s_lshl_b32 s12, s12, 5
	v_mov_b32_e32 v137, v98
	v_and_b32_e32 v9, 15, v8
	v_lshlrev_b32_e32 v19, 1, v18
	v_lshlrev_b32_e32 v8, 2, v8
	s_and_b32 s18, s12, 0x60
	v_lshl_add_u64 v[10:11], s[34:35], 0, v[136:137]
	v_mov_b32_e32 v133, v98
	v_lshl_or_b32 v1, s13, 6, v9
	v_lshl_or_b32 v9, v9, 6, v19
	s_lshl_b32 s13, s13, 13
	v_and_b32_e32 v8, 32, v8
	s_lshl_b32 s12, s18, 7
	s_add_i32 s64, s51, s7
	v_lshl_add_u64 v[12:13], s[34:35], 0, v[132:133]
	v_mov_b32_e32 v139, v98
	v_bitop3_b32 v19, v9, s13, v8 bitop3:0xde
	v_bitop3_b32 v99, v9, s12, v8 bitop3:0xde
	v_lshl_add_u64 v[8:9], v[10:11], 0, s[54:55]
	s_mov_b32 m0, s64
	s_add_i32 s68, s64, 0x2000
	v_lshl_add_u64 v[14:15], s[30:31], 0, v[138:139]
	v_mov_b32_e32 v135, v98
	s_waitcnt vmcnt(2)
	s_barrier
	global_load_lds_dwordx4 v[8:9], off
	v_lshl_add_u64 v[8:9], v[12:13], 0, s[54:55]
	s_mov_b32 m0, s68
	s_add_i32 s69, s58, 0x8000
	s_add_i32 s72, s58, 0xa000
	v_lshl_add_u64 v[16:17], s[30:31], 0, v[134:135]
	global_load_lds_dwordx4 v[8:9], off
	v_lshl_add_u64 v[8:9], v[14:15], 0, s[54:55]
	s_mov_b32 m0, s69
	s_add_u32 s12, s34, 0x40080
	global_load_lds_dwordx4 v[8:9], off
	v_lshl_add_u64 v[8:9], v[16:17], 0, s[54:55]
	s_mov_b32 m0, s72
	s_addc_u32 s13, s35, 0
	s_add_i32 s73, s56, s7
	global_load_lds_dwordx4 v[8:9], off
	v_lshl_add_u64 v[8:9], s[12:13], 0, v[136:137]
	s_mov_b32 m0, s73
	s_add_i32 s86, s73, 0x2000
	global_load_lds_dwordx4 v[8:9], off
	v_lshl_add_u64 v[8:9], s[12:13], 0, v[132:133]
	s_mov_b32 m0, s86
	s_cmpk_lt_u32 s6, 0x100
	global_load_lds_dwordx4 v[8:9], off
	v_lshlrev_b32_e32 v8, 14, v6
	v_and_b32_e32 v8, 0xffff8000, v8
	v_lshl_add_u32 v5, v5, 11, v8
	v_and_b32_e32 v6, 1, v6
	v_lshl_or_b32 v5, v6, 6, v5
	v_lshl_add_u32 v140, v7, 1, v5
	v_lshlrev_b32_e32 v5, 14, v2
	v_and_b32_e32 v5, 0xffff8000, v5
	s_waitcnt vmcnt(6)
	v_lshl_add_u32 v3, v3, 11, v5
	v_and_b32_e32 v2, 1, v2
	v_lshl_or_b32 v2, v2, 6, v3
	s_cselect_b64 s[12:13], -1, 0
	v_or_b32_e32 v144, s18, v18
	v_mov_b32_e32 v141, v98
	v_lshl_add_u32 v142, v4, 1, v2
	v_mov_b32_e32 v143, v98
	s_mov_b32 s87, 0
	v_add_u32_e32 v145, s2, v19
	s_barrier
	s_branch .LBB13_1405

; #define PG8_LAS __attribute__((address_space(3)))
; #define PG8_STAGE_A(bufoff, h, ptr, nsel) do { if constexpr (Sched::GATHER) { if (nsel) PG8_STAGE_X(bufoff, ptr, vAn[h], PG8_A_AUX); else PG8_STAGE_X(bufoff, ptr, vAc[h], PG8_A_AUX); } \
;         else PG8_STAGE_X(bufoff, (ptr) + (h) * hstep, voffA, PG8_A_AUX); } while (0)
; #define PG8_STAGE(bufoff, gbase, voff) PG8_STAGE_X(bufoff, gbase, voff, PG8_B_AUX)
; #define PG8_LDA(dst, b, h) do { _Pragma("unroll") for (int m = 0; m < 4; ++m) _Pragma("unroll") for (int k = 0; k < 2; ++k) dst[m][k] = *(const PG8_LAS bf16x8*)(lds + PG8_SA(b, h) + aoff + m * 2048 + k * 1024); } while (0)
; #define PG8_LDB(dst, b, h) do { _Pragma("unroll") for (int n = 0; n < 2; ++n) _Pragma("unroll") for (int k = 0; k < 2; ++k) dst[n][k] = *(const PG8_LAS bf16x8*)(lds + PG8_SB(b, h) + boff + n * 2048 + k * 1024); } while (0)
; #define PG8_WAIT_V(n) asm volatile("s_waitcnt vmcnt(" #n ")" ::: "memory")
; #define PG8_WAIT_L(n) asm volatile("s_waitcnt lgkmcnt(" #n ")" ::: "memory")
; #define PG8_BAR __builtin_amdgcn_s_barrier()
; template <class Epi, class Sched, bool ALIGN_EPI = false, bool SP2 = false>
; __device__ __forceinline__ void gemm_phase(PG8_LAS unsigned char* lds, const Gemm g, const Sched& S, const Epi& E) {
;     ...
;             PG8_LDB(B0, 0, 0); PG8_LDB(B1, 0, 1); PG8_SCHED; PG8_LDA(At, 0, 0); PG8_STAGE_A(PG8_SA(1, 1), 1, a1, false);
;             PG8_WAIT_V(8); PG8_WAIT_L(0); PG8_BAR; PG8_MMA(0, 0, At, B0); PG8_MMA(0, 1, At, B1); PG8_BAR; PG8_SCHED;
;             PG8_LDA(At, 0, 1); PG8_STAGE(PG8_SB(0, 0), b2, voffB); PG8_STAGE(PG8_SB(0, 1), b2 + hstep, voffB); PG8_STAGE_A(PG8_SA(0, 0), 0, a2, last);
;             PG8_WAIT_V(8); PG8_WAIT_L(0); PG8_BAR; PG8_MMA(1, 0, At, B0); PG8_MMA(1, 1, At, B1); PG8_BAR; PG8_SCHED;
;     ...
; #pragma unroll
;         for (int a = 0; a < 2; ++a)
; #pragma unroll
;             for (int b = 0; b < 2; ++b)
; #pragma unroll
;                 for (int m = 0; m < 4; ++m)
; #pragma unroll
;                     for (int n = 0; n < 2; ++n) acc[a][b][m][n] = (f32x4){0.f, 0.f, 0.f, 0.f};
;         cur = nxt; cA = nA; cB = nB; ++ui;
;         if constexpr (Sched::GATHER) { const u32x4 pv_ = *(const PG8_LAS u32x4*)(lds + STAGE_BYTES + tid * 16); vAc[0][0] = pv_.x; vAc[0][1] = pv_.y; vAc[1][0] = pv_.z; vAc[1][1] = pv_.w; }
;         if constexpr (ALIGN_EPI) { if (wr == 1) PG8_BAR; }
.LBB13_1411:
	s_ashr_i32 s21, s20, 31
	s_lshl_b64 s[22:23], s[20:21], 19
	s_add_u32 s22, s14, s22
	s_addc_u32 s23, s15, s23
	s_and_b64 s[24:25], s[6:7], exec
	s_cselect_b32 s21, s23, s31
	s_cselect_b32 s27, s22, s30
	s_ashr_i32 s19, s18, 31
	s_lshl_b64 s[24:25], s[18:19], 19
	s_add_u32 s24, s41, s24
	s_addc_u32 s25, s42, s25
	s_and_b64 s[36:37], s[6:7], exec
	s_cselect_b32 s19, s25, s35
	s_cselect_b32 s88, s24, s34
	s_add_u32 s30, s30, 0x40080
	s_addc_u32 s31, s31, 0
	s_add_u32 s89, s34, 0x100
	v_mov_b32_e32 v2, 0
	s_addc_u32 s90, s35, 0
	s_mov_b32 s94, -2
	v_mov_b32_e32 v3, v2
	v_mov_b64_e32 v[4:5], 0
	v_mov_b64_e32 v[10:11], 0
	v_mov_b64_e32 v[12:13], 0
	v_mov_b64_e32 v[18:19], 0
	v_mov_b64_e32 v[20:21], 0
	v_mov_b64_e32 v[26:27], 0
	v_mov_b64_e32 v[28:29], 0
	v_mov_b64_e32 v[34:35], 0
	v_mov_b64_e32 v[36:37], 0
	v_mov_b64_e32 v[42:43], 0
	v_mov_b64_e32 v[44:45], 0
	v_mov_b64_e32 v[50:51], 0
	v_mov_b64_e32 v[52:53], 0
	v_mov_b64_e32 v[58:59], 0
	v_mov_b64_e32 v[60:61], 0
	v_mov_b64_e32 v[6:7], 0
	v_mov_b64_e32 v[8:9], 0
	v_mov_b64_e32 v[14:15], 0
	v_mov_b64_e32 v[16:17], 0
	v_mov_b64_e32 v[22:23], 0
	v_mov_b64_e32 v[24:25], 0
	v_mov_b64_e32 v[30:31], 0
	v_mov_b64_e32 v[32:33], 0
	v_mov_b64_e32 v[38:39], 0
	v_mov_b64_e32 v[40:41], 0
	v_mov_b64_e32 v[46:47], 0
	v_mov_b64_e32 v[48:49], 0
	v_mov_b64_e32 v[54:55], 0
	v_mov_b64_e32 v[56:57], 0
	v_mov_b64_e32 v[62:63], 0
	v_mov_b64_e32 v[64:65], 0
	v_mov_b64_e32 v[66:67], 0
	v_mov_b64_e32 v[68:69], 0
	v_mov_b64_e32 v[74:75], 0
	v_mov_b64_e32 v[76:77], 0
	v_mov_b64_e32 v[82:83], 0
	v_mov_b64_e32 v[84:85], 0
	v_mov_b64_e32 v[90:91], 0
	v_mov_b64_e32 v[92:93], 0
	v_mov_b64_e32 v[100:101], 0
	v_mov_b64_e32 v[102:103], 0
	v_mov_b64_e32 v[108:109], 0
	v_mov_b64_e32 v[110:111], 0
	v_mov_b64_e32 v[116:117], 0
	v_mov_b64_e32 v[118:119], 0
	v_mov_b64_e32 v[124:125], 0
	v_mov_b64_e32 v[126:127], 0
	v_mov_b64_e32 v[70:71], 0
	v_mov_b64_e32 v[72:73], 0
	v_mov_b64_e32 v[78:79], 0
	v_mov_b64_e32 v[80:81], 0
	v_mov_b64_e32 v[86:87], 0
	v_mov_b64_e32 v[88:89], 0
	v_mov_b64_e32 v[94:95], 0
	v_mov_b64_e32 v[96:97], 0
	v_mov_b64_e32 v[104:105], 0
	v_mov_b64_e32 v[106:107], 0
	v_mov_b64_e32 v[112:113], 0
	v_mov_b64_e32 v[114:115], 0
	v_mov_b64_e32 v[120:121], 0
	v_mov_b64_e32 v[122:123], 0
	v_mov_b64_e32 v[128:129], 0
	v_mov_b64_e32 v[130:131], 0
	s_and_b64 s[98:99], exec, s[12:13]
	s_cbranch_scc1 .Lrb_1412
	s_barrier
.Lrb_1412:
.LBB13_1412:
	v_add_u32_e32 v158, s47, v99
	v_add_u32_e32 v174, s50, v99
	ds_read_b128 v[146:149], v158
	ds_read_b128 v[150:153], v158 offset:1024
	ds_read_b128 v[154:157], v158 offset:2048
	ds_read_b128 v[158:161], v158 offset:3072
	ds_read_b128 v[162:165], v174
	ds_read_b128 v[166:169], v174 offset:1024
	ds_read_b128 v[170:173], v174 offset:2048
	ds_read_b128 v[174:177], v174 offset:3072
	s_add_u32 s34, s30, 0xfffc0080
	s_addc_u32 s35, s31, -1
	s_cmp_eq_u32 s94, 12
	s_cselect_b32 s37, s21, s35
	s_cselect_b32 s36, s27, s34
	s_cselect_b32 s35, s19, s90
	s_cselect_b32 s34, s88, s89
	v_lshl_add_u64 v[198:199], s[30:31], 0, v[140:141]
	s_add_i32 m0, s58, 0xc000
	ds_read_b128 v[178:181], v145
	ds_read_b128 v[182:185], v145 offset:1024
	ds_read_b128 v[186:189], v145 offset:2048
	ds_read_b128 v[190:193], v145 offset:3072
	ds_read_b128 v[194:197], v145 offset:4096
	ds_read_b128 v[208:211], v145 offset:5120
	ds_read_b128 v[212:215], v145 offset:6144
	ds_read_b128 v[216:219], v145 offset:7168
	global_load_lds_dwordx4 v[198:199], off
	v_lshl_add_u64 v[198:199], s[30:31], 0, v[142:143]
	s_add_i32 m0, s58, 0xe000
	s_nop 0
	global_load_lds_dwordx4 v[198:199], off
	s_waitcnt vmcnt(8)
	s_waitcnt lgkmcnt(0)
	s_barrier
	s_setprio 1
	s_waitcnt lgkmcnt(0)
	v_mfma_f32_16x16x32_bf16 v[128:131], v[146:149], v[178:181], v[128:131]
	v_mfma_f32_16x16x32_bf16 v[120:123], v[154:157], v[178:181], v[120:123]
	v_mfma_f32_16x16x32_bf16 v[112:115], v[146:149], v[186:189], v[112:115]
	v_mfma_f32_16x16x32_bf16 v[104:107], v[154:157], v[186:189], v[104:107]
	v_mfma_f32_16x16x32_bf16 v[94:97], v[146:149], v[194:197], v[94:97]
	v_mfma_f32_16x16x32_bf16 v[86:89], v[154:157], v[194:197], v[86:89]
	v_mfma_f32_16x16x32_bf16 v[78:81], v[146:149], v[212:215], v[78:81]
	v_mfma_f32_16x16x32_bf16 v[70:73], v[154:157], v[212:215], v[70:73]
	v_mfma_f32_16x16x32_bf16 v[128:131], v[150:153], v[182:185], v[128:131]
	v_mfma_f32_16x16x32_bf16 v[120:123], v[158:161], v[182:185], v[120:123]
	v_mfma_f32_16x16x32_bf16 v[112:115], v[150:153], v[190:193], v[112:115]
	v_mfma_f32_16x16x32_bf16 v[104:107], v[158:161], v[190:193], v[104:107]
	v_mfma_f32_16x16x32_bf16 v[94:97], v[150:153], v[208:211], v[94:97]
	v_mfma_f32_16x16x32_bf16 v[86:89], v[158:161], v[208:211], v[86:89]
	v_mfma_f32_16x16x32_bf16 v[78:81], v[150:153], v[216:219], v[78:81]
	v_mfma_f32_16x16x32_bf16 v[70:73], v[158:161], v[216:219], v[70:73]
	s_setprio 0
	s_setprio 1
	v_mfma_f32_16x16x32_bf16 v[124:127], v[162:165], v[178:181], v[124:127]
	v_mfma_f32_16x16x32_bf16 v[116:119], v[170:173], v[178:181], v[116:119]
	v_mfma_f32_16x16x32_bf16 v[108:111], v[162:165], v[186:189], v[108:111]
	v_mfma_f32_16x16x32_bf16 v[100:103], v[170:173], v[186:189], v[100:103]
	v_mfma_f32_16x16x32_bf16 v[90:93], v[162:165], v[194:197], v[90:93]
	v_mfma_f32_16x16x32_bf16 v[82:85], v[170:173], v[194:197], v[82:85]
	v_mfma_f32_16x16x32_bf16 v[74:77], v[162:165], v[212:215], v[74:77]
	v_mfma_f32_16x16x32_bf16 v[66:69], v[170:173], v[212:215], v[66:69]
	v_mfma_f32_16x16x32_bf16 v[124:127], v[166:169], v[182:185], v[124:127]
	v_mfma_f32_16x16x32_bf16 v[116:119], v[174:177], v[182:185], v[116:119]
	v_mfma_f32_16x16x32_bf16 v[108:111], v[166:169], v[190:193], v[108:111]
	v_mfma_f32_16x16x32_bf16 v[100:103], v[174:177], v[190:193], v[100:103]
	v_mfma_f32_16x16x32_bf16 v[90:93], v[166:169], v[208:211], v[90:93]
	v_mfma_f32_16x16x32_bf16 v[82:85], v[174:177], v[208:211], v[82:85]
	v_mfma_f32_16x16x32_bf16 v[74:77], v[166:169], v[216:219], v[74:77]
	v_mfma_f32_16x16x32_bf16 v[66:69], v[174:177], v[216:219], v[66:69]
	s_setprio 0
	s_barrier
; #define PG8_STAGE_A(bufoff, h, ptr, nsel) do { if constexpr (Sched::GATHER) { if (nsel) PG8_STAGE_X(bufoff, ptr, vAn[h], PG8_A_AUX); else PG8_STAGE_X(bufoff, ptr, vAc[h], PG8_A_AUX); } \
;         else PG8_STAGE_X(bufoff, (ptr) + (h) * hstep, voffA, PG8_A_AUX); } while (0)
; #define PG8_STAGE(bufoff, gbase, voff) PG8_STAGE_X(bufoff, gbase, voff, PG8_B_AUX)
; #define PG8_LDA(dst, b, h) do { _Pragma("unroll") for (int m = 0; m < 4; ++m) _Pragma("unroll") for (int k = 0; k < 2; ++k) dst[m][k] = *(const PG8_LAS bf16x8*)(lds + PG8_SA(b, h) + aoff + m * 2048 + k * 1024); } while (0)
; #define PG8_LDB(dst, b, h) do { _Pragma("unroll") for (int n = 0; n < 2; ++n) _Pragma("unroll") for (int k = 0; k < 2; ++k) dst[n][k] = *(const PG8_LAS bf16x8*)(lds + PG8_SB(b, h) + boff + n * 2048 + k * 1024); } while (0)
; #define PG8_MMA(ai, bj, At, Bt) do { __builtin_amdgcn_s_setprio(1); _Pragma("unroll") for (int m = 0; m < 4; ++m) _Pragma("unroll") for (int n = 0; n < 2; ++n) _Pragma("unroll") for (int k = 0; k < 2; ++k) \
;         acc[ai][bj][m][n] = __builtin_amdgcn_mfma_f32_16x16x32_bf16(Bt[n][k], At[m][k], acc[ai][bj][m][n], 0, 0, 0); __builtin_amdgcn_s_setprio(0); } while (0)
; #define PG8_WAIT_V(n) asm volatile("s_waitcnt vmcnt(" #n ")" ::: "memory")
; #define PG8_WAIT_L(n) asm volatile("s_waitcnt lgkmcnt(" #n ")" ::: "memory")
; #define PG8_BAR __builtin_amdgcn_s_barrier()
; #define PG8_SCHED __builtin_amdgcn_sched_barrier(0)
; template <class Epi, class Sched, bool ALIGN_EPI = false, bool SP2 = false>
; __device__ __forceinline__ void gemm_phase(PG8_LAS unsigned char* lds, const Gemm g, const Sched& S, const Epi& E) {
;     ...
;             PG8_WAIT_V(8); PG8_WAIT_L(0); PG8_BAR; PG8_MMA(0, 0, At, B0); PG8_MMA(0, 1, At, B1); PG8_BAR; PG8_SCHED;
;             PG8_LDA(At, 0, 1); PG8_STAGE(PG8_SB(0, 0), b2, voffB); PG8_STAGE(PG8_SB(0, 1), b2 + hstep, voffB); PG8_STAGE_A(PG8_SA(0, 0), 0, a2, last);
;             PG8_WAIT_V(8); PG8_WAIT_L(0); PG8_BAR; PG8_MMA(1, 0, At, B0); PG8_MMA(1, 1, At, B1); PG8_BAR; PG8_SCHED;
;             PG8_LDB(B0, 1, 0); PG8_LDB(B1, 1, 1); PG8_SCHED; PG8_LDA(At, 1, 0); PG8_STAGE_A(PG8_SA(0, 1), 1, a2, last);
;             PG8_WAIT_V(8); PG8_WAIT_L(0); PG8_BAR; PG8_MMA(0, 0, At, B0); PG8_MMA(0, 1, At, B1); PG8_BAR; PG8_SCHED;
	s_mov_b32 m0, s4
	v_lshl_add_u64 v[198:199], s[34:35], 0, v[136:137]
	s_add_u32 vcc_lo, s34, 0x40000
	ds_read_b128 v[178:181], v145 offset:16384
	ds_read_b128 v[182:185], v145 offset:17408
	ds_read_b128 v[186:189], v145 offset:18432
	ds_read_b128 v[190:193], v145 offset:19456
	ds_read_b128 v[194:197], v145 offset:20480
	ds_read_b128 v[208:211], v145 offset:21504
	ds_read_b128 v[212:215], v145 offset:22528
	ds_read_b128 v[216:219], v145 offset:23552
	global_load_lds_dwordx4 v[198:199], off
	v_lshl_add_u64 v[220:221], s[34:35], 0, v[132:133]
	s_mov_b32 m0, s5
	s_addc_u32 vcc_hi, s35, 0
	global_load_lds_dwordx4 v[220:221], off
	v_lshl_add_u64 v[222:223], vcc, 0, v[136:137]
	s_mov_b32 m0, s29
	v_lshl_add_u64 v[224:225], s[36:37], 0, v[134:135]
	global_load_lds_dwordx4 v[222:223], off
	v_lshl_add_u64 v[222:223], vcc, 0, v[132:133]
	s_mov_b32 m0, s52
	s_nop 0
	global_load_lds_dwordx4 v[222:223], off
	v_lshl_add_u64 v[222:223], s[36:37], 0, v[138:139]
	s_mov_b32 m0, s58
	s_nop 0
	global_load_lds_dwordx4 v[222:223], off
	s_mov_b32 m0, s59
	s_nop 0
	global_load_lds_dwordx4 v[224:225], off
	s_waitcnt vmcnt(8)
	s_waitcnt lgkmcnt(0)
	s_barrier
	s_setprio 1
	s_waitcnt lgkmcnt(0)
	v_mfma_f32_16x16x32_bf16 v[62:65], v[146:149], v[178:181], v[62:65]
	v_mfma_f32_16x16x32_bf16 v[54:57], v[154:157], v[178:181], v[54:57]
	v_mfma_f32_16x16x32_bf16 v[46:49], v[146:149], v[186:189], v[46:49]
	v_mfma_f32_16x16x32_bf16 v[38:41], v[154:157], v[186:189], v[38:41]
	v_mfma_f32_16x16x32_bf16 v[30:33], v[146:149], v[194:197], v[30:33]
	v_mfma_f32_16x16x32_bf16 v[22:25], v[154:157], v[194:197], v[22:25]
	v_mfma_f32_16x16x32_bf16 v[14:17], v[146:149], v[212:215], v[14:17]
	v_mfma_f32_16x16x32_bf16 v[6:9], v[154:157], v[212:215], v[6:9]
	v_mfma_f32_16x16x32_bf16 v[62:65], v[150:153], v[182:185], v[62:65]
	v_mfma_f32_16x16x32_bf16 v[54:57], v[158:161], v[182:185], v[54:57]
	v_mfma_f32_16x16x32_bf16 v[46:49], v[150:153], v[190:193], v[46:49]
	v_mfma_f32_16x16x32_bf16 v[38:41], v[158:161], v[190:193], v[38:41]
	v_mfma_f32_16x16x32_bf16 v[30:33], v[150:153], v[208:211], v[30:33]
	v_mfma_f32_16x16x32_bf16 v[22:25], v[158:161], v[208:211], v[22:25]
	v_mfma_f32_16x16x32_bf16 v[14:17], v[150:153], v[216:219], v[14:17]
	v_mfma_f32_16x16x32_bf16 v[6:9], v[158:161], v[216:219], v[6:9]
	s_setprio 0
	s_setprio 1
	v_mfma_f32_16x16x32_bf16 v[58:61], v[162:165], v[178:181], v[58:61]
	v_mfma_f32_16x16x32_bf16 v[50:53], v[170:173], v[178:181], v[50:53]
	v_mfma_f32_16x16x32_bf16 v[42:45], v[162:165], v[186:189], v[42:45]
	v_mfma_f32_16x16x32_bf16 v[34:37], v[170:173], v[186:189], v[34:37]
	v_mfma_f32_16x16x32_bf16 v[26:29], v[162:165], v[194:197], v[26:29]
	v_mfma_f32_16x16x32_bf16 v[18:21], v[170:173], v[194:197], v[18:21]
	v_mfma_f32_16x16x32_bf16 v[10:13], v[162:165], v[212:215], v[10:13]
	v_mfma_f32_16x16x32_bf16 v[2:5], v[170:173], v[212:215], v[2:5]
	v_mfma_f32_16x16x32_bf16 v[58:61], v[166:169], v[182:185], v[58:61]
	v_mfma_f32_16x16x32_bf16 v[50:53], v[174:177], v[182:185], v[50:53]
	v_mfma_f32_16x16x32_bf16 v[42:45], v[166:169], v[190:193], v[42:45]
	v_mfma_f32_16x16x32_bf16 v[34:37], v[174:177], v[190:193], v[34:37]
	v_mfma_f32_16x16x32_bf16 v[26:29], v[166:169], v[208:211], v[26:29]
	v_mfma_f32_16x16x32_bf16 v[18:21], v[174:177], v[208:211], v[18:21]
	v_mfma_f32_16x16x32_bf16 v[10:13], v[166:169], v[216:219], v[10:13]
	v_mfma_f32_16x16x32_bf16 v[2:5], v[174:177], v[216:219], v[2:5]
	s_setprio 0
	s_barrier
	v_add_u32_e32 v158, s51, v99
	v_add_u32_e32 v174, s56, v99
	ds_read_b128 v[146:149], v158
	ds_read_b128 v[150:153], v158 offset:1024
	ds_read_b128 v[154:157], v158 offset:2048
	ds_read_b128 v[158:161], v158 offset:3072
	ds_read_b128 v[162:165], v174
	ds_read_b128 v[166:169], v174 offset:1024
	ds_read_b128 v[170:173], v174 offset:2048
	ds_read_b128 v[174:177], v174 offset:3072
	s_add_u32 s36, s36, 0x40000
	s_addc_u32 s37, s37, 0
	s_mov_b32 m0, s60
	v_lshl_add_u64 v[226:227], s[36:37], 0, v[138:139]
	ds_read_b128 v[178:181], v145 offset:32768
	ds_read_b128 v[182:185], v145 offset:33792
	ds_read_b128 v[186:189], v145 offset:34816
	ds_read_b128 v[190:193], v145 offset:35840
	ds_read_b128 v[194:197], v145 offset:36864
	ds_read_b128 v[208:211], v145 offset:37888
	ds_read_b128 v[212:215], v145 offset:38912
	ds_read_b128 v[216:219], v145 offset:39936
	global_load_lds_dwordx4 v[226:227], off
	v_lshl_add_u64 v[226:227], s[36:37], 0, v[134:135]
	s_mov_b32 m0, s61
	s_nop 0
	global_load_lds_dwordx4 v[226:227], off
	s_waitcnt vmcnt(8)
	s_waitcnt lgkmcnt(0)
	s_barrier
; #define PG8_STAGE_A(bufoff, h, ptr, nsel) do { if constexpr (Sched::GATHER) { if (nsel) PG8_STAGE_X(bufoff, ptr, vAn[h], PG8_A_AUX); else PG8_STAGE_X(bufoff, ptr, vAc[h], PG8_A_AUX); } \
;         else PG8_STAGE_X(bufoff, (ptr) + (h) * hstep, voffA, PG8_A_AUX); } while (0)
; #define PG8_STAGE(bufoff, gbase, voff) PG8_STAGE_X(bufoff, gbase, voff, PG8_B_AUX)
; #define PG8_LDA(dst, b, h) do { _Pragma("unroll") for (int m = 0; m < 4; ++m) _Pragma("unroll") for (int k = 0; k < 2; ++k) dst[m][k] = *(const PG8_LAS bf16x8*)(lds + PG8_SA(b, h) + aoff + m * 2048 + k * 1024); } while (0)
; #define PG8_MMA(ai, bj, At, Bt) do { __builtin_amdgcn_s_setprio(1); _Pragma("unroll") for (int m = 0; m < 4; ++m) _Pragma("unroll") for (int n = 0; n < 2; ++n) _Pragma("unroll") for (int k = 0; k < 2; ++k) \
;         acc[ai][bj][m][n] = __builtin_amdgcn_mfma_f32_16x16x32_bf16(Bt[n][k], At[m][k], acc[ai][bj][m][n], 0, 0, 0); __builtin_amdgcn_s_setprio(0); } while (0)
; #define PG8_WAIT_V(n) asm volatile("s_waitcnt vmcnt(" #n ")" ::: "memory")
; #define PG8_WAIT_L(n) asm volatile("s_waitcnt lgkmcnt(" #n ")" ::: "memory")
; #define PG8_BAR __builtin_amdgcn_s_barrier()
; #define PG8_SCHED __builtin_amdgcn_sched_barrier(0)
; template <class Epi, class Sched, bool ALIGN_EPI = false, bool SP2 = false>
; __device__ __forceinline__ void gemm_phase(PG8_LAS unsigned char* lds, const Gemm g, const Sched& S, const Epi& E) {
;     ...
;             PG8_WAIT_V(8); PG8_WAIT_L(0); PG8_BAR; PG8_MMA(0, 0, At, B0); PG8_MMA(0, 1, At, B1); PG8_BAR; PG8_SCHED;
;             PG8_LDA(At, 1, 1); PG8_STAGE(PG8_SB(1, 0), b3, voffB); PG8_STAGE(PG8_SB(1, 1), b3 + hstep, voffB); PG8_STAGE_A(PG8_SA(1, 0), 0, a3, last);
;             PG8_WAIT_V(8); PG8_WAIT_L(0); PG8_BAR; PG8_MMA(1, 0, At, B0); PG8_MMA(1, 1, At, B1); PG8_BAR; PG8_SCHED;
;     ...
;         if constexpr (ALIGN_EPI) { if (wr == 0) PG8_BAR; }
	s_setprio 1
	s_waitcnt lgkmcnt(0)
	v_mfma_f32_16x16x32_bf16 v[128:131], v[146:149], v[178:181], v[128:131]
	v_mfma_f32_16x16x32_bf16 v[120:123], v[154:157], v[178:181], v[120:123]
	v_mfma_f32_16x16x32_bf16 v[112:115], v[146:149], v[186:189], v[112:115]
	v_mfma_f32_16x16x32_bf16 v[104:107], v[154:157], v[186:189], v[104:107]
	v_mfma_f32_16x16x32_bf16 v[94:97], v[146:149], v[194:197], v[94:97]
	v_mfma_f32_16x16x32_bf16 v[86:89], v[154:157], v[194:197], v[86:89]
	v_mfma_f32_16x16x32_bf16 v[78:81], v[146:149], v[212:215], v[78:81]
	v_mfma_f32_16x16x32_bf16 v[70:73], v[154:157], v[212:215], v[70:73]
	v_mfma_f32_16x16x32_bf16 v[128:131], v[150:153], v[182:185], v[128:131]
	v_mfma_f32_16x16x32_bf16 v[120:123], v[158:161], v[182:185], v[120:123]
	v_mfma_f32_16x16x32_bf16 v[112:115], v[150:153], v[190:193], v[112:115]
	v_mfma_f32_16x16x32_bf16 v[104:107], v[158:161], v[190:193], v[104:107]
	v_mfma_f32_16x16x32_bf16 v[94:97], v[150:153], v[208:211], v[94:97]
	v_mfma_f32_16x16x32_bf16 v[86:89], v[158:161], v[208:211], v[86:89]
	v_mfma_f32_16x16x32_bf16 v[78:81], v[150:153], v[216:219], v[78:81]
	v_mfma_f32_16x16x32_bf16 v[70:73], v[158:161], v[216:219], v[70:73]
	s_setprio 0
	s_setprio 1
	v_mfma_f32_16x16x32_bf16 v[124:127], v[162:165], v[178:181], v[124:127]
	v_mfma_f32_16x16x32_bf16 v[116:119], v[170:173], v[178:181], v[116:119]
	v_mfma_f32_16x16x32_bf16 v[108:111], v[162:165], v[186:189], v[108:111]
	v_mfma_f32_16x16x32_bf16 v[100:103], v[170:173], v[186:189], v[100:103]
	v_mfma_f32_16x16x32_bf16 v[90:93], v[162:165], v[194:197], v[90:93]
	v_mfma_f32_16x16x32_bf16 v[82:85], v[170:173], v[194:197], v[82:85]
	v_mfma_f32_16x16x32_bf16 v[74:77], v[162:165], v[212:215], v[74:77]
	v_mfma_f32_16x16x32_bf16 v[66:69], v[170:173], v[212:215], v[66:69]
	v_mfma_f32_16x16x32_bf16 v[124:127], v[166:169], v[182:185], v[124:127]
	v_mfma_f32_16x16x32_bf16 v[116:119], v[174:177], v[182:185], v[116:119]
	v_mfma_f32_16x16x32_bf16 v[108:111], v[166:169], v[190:193], v[108:111]
	v_mfma_f32_16x16x32_bf16 v[100:103], v[174:177], v[190:193], v[100:103]
	v_mfma_f32_16x16x32_bf16 v[90:93], v[166:169], v[208:211], v[90:93]
	v_mfma_f32_16x16x32_bf16 v[82:85], v[174:177], v[208:211], v[82:85]
	v_mfma_f32_16x16x32_bf16 v[74:77], v[166:169], v[216:219], v[74:77]
	v_mfma_f32_16x16x32_bf16 v[66:69], v[174:177], v[216:219], v[66:69]
	s_setprio 0
	s_barrier
	s_mov_b32 m0, s64
	v_lshl_add_u64 v[198:199], v[198:199], 0, s[54:55]
	s_add_u32 s34, s34, 0x40080
	ds_read_b128 v[178:181], v145 offset:49152
	ds_read_b128 v[182:185], v145 offset:50176
	ds_read_b128 v[186:189], v145 offset:51200
	ds_read_b128 v[190:193], v145 offset:52224
	ds_read_b128 v[194:197], v145 offset:53248
	ds_read_b128 v[208:211], v145 offset:54272
	ds_read_b128 v[212:215], v145 offset:55296
	ds_read_b128 v[216:219], v145 offset:56320
	global_load_lds_dwordx4 v[198:199], off
	v_lshl_add_u64 v[198:199], v[220:221], 0, s[54:55]
	s_mov_b32 m0, s68
	s_addc_u32 s35, s35, 0
	global_load_lds_dwordx4 v[198:199], off
	v_lshl_add_u64 v[198:199], s[34:35], 0, v[136:137]
	s_mov_b32 m0, s73
	s_nop 0
	global_load_lds_dwordx4 v[198:199], off
	v_lshl_add_u64 v[198:199], s[34:35], 0, v[132:133]
	s_mov_b32 m0, s86
	s_nop 0
	global_load_lds_dwordx4 v[198:199], off
	v_lshl_add_u64 v[198:199], v[222:223], 0, s[54:55]
	s_mov_b32 m0, s69
	s_nop 0
	global_load_lds_dwordx4 v[198:199], off
	v_lshl_add_u64 v[198:199], v[224:225], 0, s[54:55]
	s_mov_b32 m0, s72
	s_nop 0
	global_load_lds_dwordx4 v[198:199], off
	s_waitcnt vmcnt(8)
	s_waitcnt lgkmcnt(0)
	s_barrier
	s_setprio 1
	s_waitcnt lgkmcnt(0)
	v_mfma_f32_16x16x32_bf16 v[62:65], v[146:149], v[178:181], v[62:65]
	v_mfma_f32_16x16x32_bf16 v[54:57], v[154:157], v[178:181], v[54:57]
	v_mfma_f32_16x16x32_bf16 v[46:49], v[146:149], v[186:189], v[46:49]
	v_mfma_f32_16x16x32_bf16 v[38:41], v[154:157], v[186:189], v[38:41]
	v_mfma_f32_16x16x32_bf16 v[30:33], v[146:149], v[194:197], v[30:33]
	v_mfma_f32_16x16x32_bf16 v[22:25], v[154:157], v[194:197], v[22:25]
	v_mfma_f32_16x16x32_bf16 v[14:17], v[146:149], v[212:215], v[14:17]
	v_mfma_f32_16x16x32_bf16 v[6:9], v[154:157], v[212:215], v[6:9]
	v_mfma_f32_16x16x32_bf16 v[62:65], v[150:153], v[182:185], v[62:65]
	v_mfma_f32_16x16x32_bf16 v[54:57], v[158:161], v[182:185], v[54:57]
	v_mfma_f32_16x16x32_bf16 v[46:49], v[150:153], v[190:193], v[46:49]
	v_mfma_f32_16x16x32_bf16 v[38:41], v[158:161], v[190:193], v[38:41]
	v_mfma_f32_16x16x32_bf16 v[30:33], v[150:153], v[208:211], v[30:33]
	v_mfma_f32_16x16x32_bf16 v[22:25], v[158:161], v[208:211], v[22:25]
	v_mfma_f32_16x16x32_bf16 v[14:17], v[150:153], v[216:219], v[14:17]
	v_mfma_f32_16x16x32_bf16 v[6:9], v[158:161], v[216:219], v[6:9]
	s_setprio 0
	s_setprio 1
	v_mfma_f32_16x16x32_bf16 v[58:61], v[162:165], v[178:181], v[58:61]
	v_mfma_f32_16x16x32_bf16 v[50:53], v[170:173], v[178:181], v[50:53]
	v_mfma_f32_16x16x32_bf16 v[42:45], v[162:165], v[186:189], v[42:45]
	v_mfma_f32_16x16x32_bf16 v[34:37], v[170:173], v[186:189], v[34:37]
	v_mfma_f32_16x16x32_bf16 v[26:29], v[162:165], v[194:197], v[26:29]
	v_mfma_f32_16x16x32_bf16 v[18:21], v[170:173], v[194:197], v[18:21]
	v_mfma_f32_16x16x32_bf16 v[10:13], v[162:165], v[212:215], v[10:13]
	v_mfma_f32_16x16x32_bf16 v[2:5], v[170:173], v[212:215], v[2:5]
	v_mfma_f32_16x16x32_bf16 v[58:61], v[166:169], v[182:185], v[58:61]
	v_mfma_f32_16x16x32_bf16 v[50:53], v[174:177], v[182:185], v[50:53]
	v_mfma_f32_16x16x32_bf16 v[42:45], v[166:169], v[190:193], v[42:45]
	v_mfma_f32_16x16x32_bf16 v[34:37], v[174:177], v[190:193], v[34:37]
	v_mfma_f32_16x16x32_bf16 v[26:29], v[166:169], v[208:211], v[26:29]
	v_mfma_f32_16x16x32_bf16 v[18:21], v[174:177], v[208:211], v[18:21]
	v_mfma_f32_16x16x32_bf16 v[10:13], v[166:169], v[216:219], v[10:13]
	v_mfma_f32_16x16x32_bf16 v[2:5], v[174:177], v[216:219], v[2:5]
	s_setprio 0
	s_barrier
	s_add_i32 s94, s94, 2
	s_add_u32 s30, s30, 0x100
	s_addc_u32 s31, s31, 0
	s_add_u32 s89, s89, 0x100
	s_addc_u32 s90, s90, 0
	s_cmp_gt_u32 s94, 13
	s_cbranch_scc0 .LBB13_1412
	s_and_b64 vcc, exec, s[12:13]
	s_mov_b32 s90, 0x1c000
	s_mov_b32 s88, 0x16000
	s_cbranch_vccz .LBB13_1415
	s_barrier
; __device__ __forceinline__ unsigned pk2(float lo, float hi) { f32x2 v = {lo, hi}; return __builtin_bit_cast(unsigned, __builtin_convertvector(v, bf2_t)); }
; template <int BIT = 0> __device__ __forceinline__ void st16w(void* p, u32x4 v) { if ((WT_STORES >> BIT) & 1) asm volatile("global_store_dwordx4 %0, %1, off sc1\n\ts_nop 1" :: "v"(p), "v"(v) : "memory"); else *(u32x4*)p = v; }
; __device__ __forceinline__ float fsilu(float x) { return x * fsigm(x); }
;     __device__ __forceinline__ void operator()(const f32x4 (&acc)[2][2][4][2], const Unit& u, int wr, int wc, int fr, int fq) const {
;         const int row0 = u.pm * BM + wr * 64 + fr, col0 = u.pn * HALF + wc * 32 + 8 * fq;
; #pragma unroll
;         for (int ai = 0; ai < 2; ++ai)
; #pragma unroll
;             for (int m = 0; m < 4; ++m) {
;                 const f32x4 g0 = acc[ai][0][m][0], g1 = acc[ai][0][m][1], u0 = acc[ai][1][m][0], u1 = acc[ai][1][m][1];
;                 u32x4 w; w.x = pk2(fsilu(g0[0]) * u0[0], fsilu(g0[1]) * u0[1]); w.y = pk2(fsilu(g0[2]) * u0[2], fsilu(g0[3]) * u0[3]);
;                 w.z = pk2(fsilu(g1[0]) * u1[0], fsilu(g1[1]) * u1[1]); w.w = pk2(fsilu(g1[2]) * u1[2], fsilu(g1[3]) * u1[3]);
;                 bf16* dst = HID + (size_t)(row0 + ai * HALF + m * 16) * ldh + col0;
;                 if (wt) asm volatile("global_store_dwordx4 %0, %1, off sc1\n\ts_nop 1" :: "v"(dst), "v"(w) : "memory");
;                 else st16w(dst, w);
;             }
;     }
.LBB13_1415:
	v_mul_f32_e32 v147, 0xbfb8aa3b, v128
	v_exp_f32_e32 v147, v147
	v_lshl_or_b32 v148, s26, 7, v144
	v_lshl_add_u32 v146, s28, 8, v1
	v_ashrrev_i32_e32 v149, 31, v148
	v_add_f32_e32 v147, 1.0, v147
	v_rcp_f32_e32 v150, v147
	v_mul_f32_e32 v147, 0xbfb8aa3b, v129
	v_exp_f32_e32 v147, v147
	s_movk_i32 s89, 0x1600
	s_andn2_b64 vcc, exec, s[6:7]
	v_add_f32_e32 v147, 1.0, v147
	v_rcp_f32_e32 v151, v147
	s_nop 0
	v_pk_mul_f32 v[128:129], v[128:129], v[150:151]
	s_nop 0
	v_pk_mul_f32 v[124:125], v[128:129], v[124:125]
	s_nop 0
	v_cvt_pk_bf16_f32 v124, v124, v125
	v_mul_f32_e32 v125, 0xbfb8aa3b, v130
	v_exp_f32_e32 v125, v125
	s_nop 0
	v_add_f32_e32 v125, 1.0, v125
	v_rcp_f32_e32 v128, v125
	v_mul_f32_e32 v125, 0xbfb8aa3b, v131
	v_exp_f32_e32 v125, v125
	s_nop 0
	v_add_f32_e32 v125, 1.0, v125
	v_rcp_f32_e32 v129, v125
	s_nop 0
	v_pk_mul_f32 v[128:129], v[130:131], v[128:129]
	s_nop 0
	v_pk_mul_f32 v[126:127], v[128:129], v[126:127]
	s_nop 0
	v_cvt_pk_bf16_f32 v125, v126, v127
	v_mul_f32_e32 v126, 0xbfb8aa3b, v120
	v_mul_f32_e32 v127, 0xbfb8aa3b, v121
	v_exp_f32_e32 v126, v126
	v_exp_f32_e32 v127, v127
	v_add_f32_e32 v126, 1.0, v126
	v_add_f32_e32 v127, 1.0, v127
	v_rcp_f32_e32 v126, v126
	v_rcp_f32_e32 v127, v127
	s_nop 0
	v_pk_mul_f32 v[120:121], v[120:121], v[126:127]
	s_nop 0
	v_pk_mul_f32 v[116:117], v[120:121], v[116:117]
	s_nop 0
	v_cvt_pk_bf16_f32 v126, v116, v117
	v_mul_f32_e32 v116, 0xbfb8aa3b, v122
	v_mul_f32_e32 v117, 0xbfb8aa3b, v123
	v_exp_f32_e32 v116, v116
	v_exp_f32_e32 v117, v117
	v_add_f32_e32 v116, 1.0, v116
	v_add_f32_e32 v117, 1.0, v117
	v_rcp_f32_e32 v116, v116
	v_rcp_f32_e32 v117, v117
	s_nop 0
	v_pk_mul_f32 v[116:117], v[122:123], v[116:117]
	s_nop 0
	v_pk_mul_f32 v[116:117], v[116:117], v[118:119]
	v_lshlrev_b64 v[118:119], 1, v[148:149]
	v_cvt_pk_bf16_f32 v127, v116, v117
	v_mov_b64_e32 v[116:117], s[16:17]
	v_mad_i64_i32 v[120:121], s[26:27], v146, s89, v[116:117]
	v_lshl_add_u64 v[120:121], v[120:121], 0, v[118:119]
	global_store_dwordx4 v[120:121], v[124:127], off
	v_mul_f32_e32 v120, 0xbfb8aa3b, v112
	v_mul_f32_e32 v121, 0xbfb8aa3b, v113
	v_exp_f32_e32 v120, v120
	v_exp_f32_e32 v121, v121
	v_add_f32_e32 v120, 1.0, v120
	v_add_f32_e32 v121, 1.0, v121
	v_rcp_f32_e32 v120, v120
	v_rcp_f32_e32 v121, v121
	s_nop 0
	v_pk_mul_f32 v[112:113], v[112:113], v[120:121]
	s_nop 0
	v_pk_mul_f32 v[108:109], v[112:113], v[108:109]
	s_nop 0
	v_cvt_pk_bf16_f32 v108, v108, v109
	v_mul_f32_e32 v109, 0xbfb8aa3b, v114
	v_exp_f32_e32 v109, v109
	s_nop 0
	v_add_f32_e32 v109, 1.0, v109
	v_rcp_f32_e32 v112, v109
	v_mul_f32_e32 v109, 0xbfb8aa3b, v115
	v_exp_f32_e32 v109, v109
	s_nop 0
	v_add_f32_e32 v109, 1.0, v109
	v_rcp_f32_e32 v113, v109
	s_nop 0
	v_pk_mul_f32 v[112:113], v[114:115], v[112:113]
	s_nop 0
	v_pk_mul_f32 v[110:111], v[112:113], v[110:111]
	s_nop 0
	v_cvt_pk_bf16_f32 v109, v110, v111
	v_mul_f32_e32 v110, 0xbfb8aa3b, v104
	v_mul_f32_e32 v111, 0xbfb8aa3b, v105
	v_exp_f32_e32 v110, v110
	v_exp_f32_e32 v111, v111
	v_add_f32_e32 v110, 1.0, v110
	v_add_f32_e32 v111, 1.0, v111
	v_rcp_f32_e32 v110, v110
	v_rcp_f32_e32 v111, v111
	s_nop 0
	v_pk_mul_f32 v[104:105], v[104:105], v[110:111]
	s_nop 0
	v_pk_mul_f32 v[100:101], v[104:105], v[100:101]
	s_nop 0
	v_cvt_pk_bf16_f32 v110, v100, v101
	v_mul_f32_e32 v100, 0xbfb8aa3b, v106
	v_mul_f32_e32 v101, 0xbfb8aa3b, v107
	v_exp_f32_e32 v100, v100
	v_exp_f32_e32 v101, v101
	v_add_f32_e32 v100, 1.0, v100
	v_add_f32_e32 v101, 1.0, v101
	v_rcp_f32_e32 v100, v100
	v_rcp_f32_e32 v101, v101
	s_nop 0
	v_pk_mul_f32 v[100:101], v[106:107], v[100:101]
	s_nop 0
	v_pk_mul_f32 v[100:101], v[100:101], v[102:103]
	s_nop 0
	v_cvt_pk_bf16_f32 v111, v100, v101
	v_or_b32_e32 v100, 16, v146
	v_mad_i64_i32 v[100:101], s[26:27], v100, s89, v[116:117]
	v_lshl_add_u64 v[100:101], v[100:101], 0, v[118:119]
	global_store_dwordx4 v[100:101], v[108:111], off
	v_mul_f32_e32 v100, 0xbfb8aa3b, v94
	v_mul_f32_e32 v101, 0xbfb8aa3b, v95
	v_exp_f32_e32 v100, v100
	v_exp_f32_e32 v101, v101
	v_add_f32_e32 v100, 1.0, v100
	v_add_f32_e32 v101, 1.0, v101
	v_rcp_f32_e32 v100, v100
	v_rcp_f32_e32 v101, v101
	s_nop 0
	v_pk_mul_f32 v[94:95], v[94:95], v[100:101]
	s_nop 0
	v_pk_mul_f32 v[90:91], v[94:95], v[90:91]
	s_nop 0
	v_cvt_pk_bf16_f32 v90, v90, v91
	v_mul_f32_e32 v91, 0xbfb8aa3b, v96
	v_exp_f32_e32 v91, v91
	s_nop 0
	v_add_f32_e32 v91, 1.0, v91
	v_rcp_f32_e32 v94, v91
	v_mul_f32_e32 v91, 0xbfb8aa3b, v97
	v_exp_f32_e32 v91, v91
	s_nop 0
	v_add_f32_e32 v91, 1.0, v91
	v_rcp_f32_e32 v95, v91
	s_nop 0
	v_pk_mul_f32 v[94:95], v[96:97], v[94:95]
	s_nop 0
	v_pk_mul_f32 v[92:93], v[94:95], v[92:93]
	s_nop 0
	v_cvt_pk_bf16_f32 v91, v92, v93
	v_mul_f32_e32 v92, 0xbfb8aa3b, v86
	v_mul_f32_e32 v93, 0xbfb8aa3b, v87
	v_exp_f32_e32 v92, v92
	v_exp_f32_e32 v93, v93
	v_add_f32_e32 v92, 1.0, v92
	v_add_f32_e32 v93, 1.0, v93
	v_rcp_f32_e32 v92, v92
	v_rcp_f32_e32 v93, v93
	s_nop 0
	v_pk_mul_f32 v[86:87], v[86:87], v[92:93]
	s_nop 0
	v_pk_mul_f32 v[82:83], v[86:87], v[82:83]
	s_nop 0
	v_cvt_pk_bf16_f32 v92, v82, v83
	v_mul_f32_e32 v82, 0xbfb8aa3b, v88
	v_mul_f32_e32 v83, 0xbfb8aa3b, v89
	v_exp_f32_e32 v82, v82
	v_exp_f32_e32 v83, v83
	v_add_f32_e32 v82, 1.0, v82
	v_add_f32_e32 v83, 1.0, v83
	v_rcp_f32_e32 v82, v82
	v_rcp_f32_e32 v83, v83
	s_nop 0
	v_pk_mul_f32 v[82:83], v[88:89], v[82:83]
	s_nop 0
	v_pk_mul_f32 v[82:83], v[82:83], v[84:85]
	s_nop 0
	v_cvt_pk_bf16_f32 v93, v82, v83
	v_or_b32_e32 v82, 32, v146
	v_mad_i64_i32 v[82:83], s[26:27], v82, s89, v[116:117]
	v_lshl_add_u64 v[82:83], v[82:83], 0, v[118:119]
	global_store_dwordx4 v[82:83], v[90:93], off
	v_mul_f32_e32 v82, 0xbfb8aa3b, v78
	v_mul_f32_e32 v83, 0xbfb8aa3b, v79
	v_exp_f32_e32 v82, v82
; __device__ __forceinline__ unsigned pk2(float lo, float hi) { f32x2 v = {lo, hi}; return __builtin_bit_cast(unsigned, __builtin_convertvector(v, bf2_t)); }
; template <int BIT = 0> __device__ __forceinline__ void st16w(void* p, u32x4 v) { if ((WT_STORES >> BIT) & 1) asm volatile("global_store_dwordx4 %0, %1, off sc1\n\ts_nop 1" :: "v"(p), "v"(v) : "memory"); else *(u32x4*)p = v; }
; __device__ __forceinline__ float fsilu(float x) { return x * fsigm(x); }
;     __device__ __forceinline__ void operator()(const f32x4 (&acc)[2][2][4][2], const Unit& u, int wr, int wc, int fr, int fq) const {
;     ...
;                 u32x4 w; w.x = pk2(fsilu(g0[0]) * u0[0], fsilu(g0[1]) * u0[1]); w.y = pk2(fsilu(g0[2]) * u0[2], fsilu(g0[3]) * u0[3]);
;                 w.z = pk2(fsilu(g1[0]) * u1[0], fsilu(g1[1]) * u1[1]); w.w = pk2(fsilu(g1[2]) * u1[2], fsilu(g1[3]) * u1[3]);
;                 bf16* dst = HID + (size_t)(row0 + ai * HALF + m * 16) * ldh + col0;
;                 if (wt) asm volatile("global_store_dwordx4 %0, %1, off sc1\n\ts_nop 1" :: "v"(dst), "v"(w) : "memory");
;                 else st16w(dst, w);
;             }
	v_exp_f32_e32 v83, v83
	v_add_f32_e32 v82, 1.0, v82
	v_add_f32_e32 v83, 1.0, v83
	v_rcp_f32_e32 v82, v82
	v_rcp_f32_e32 v83, v83
	s_nop 0
	v_pk_mul_f32 v[78:79], v[78:79], v[82:83]
	s_nop 0
	v_pk_mul_f32 v[74:75], v[78:79], v[74:75]
	s_nop 0
	v_cvt_pk_bf16_f32 v74, v74, v75
	v_mul_f32_e32 v75, 0xbfb8aa3b, v80
	v_exp_f32_e32 v75, v75
	s_nop 0
	v_add_f32_e32 v75, 1.0, v75
	v_rcp_f32_e32 v78, v75
	v_mul_f32_e32 v75, 0xbfb8aa3b, v81
	v_exp_f32_e32 v75, v75
	s_nop 0
	v_add_f32_e32 v75, 1.0, v75
	v_rcp_f32_e32 v79, v75
	s_nop 0
	v_pk_mul_f32 v[78:79], v[80:81], v[78:79]
	s_nop 0
	v_pk_mul_f32 v[76:77], v[78:79], v[76:77]
	s_nop 0
	v_cvt_pk_bf16_f32 v75, v76, v77
	v_mul_f32_e32 v76, 0xbfb8aa3b, v70
	v_mul_f32_e32 v77, 0xbfb8aa3b, v71
	v_exp_f32_e32 v76, v76
	v_exp_f32_e32 v77, v77
	v_add_f32_e32 v76, 1.0, v76
	v_add_f32_e32 v77, 1.0, v77
	v_rcp_f32_e32 v76, v76
	v_rcp_f32_e32 v77, v77
	s_nop 0
	v_pk_mul_f32 v[70:71], v[70:71], v[76:77]
	s_nop 0
	v_pk_mul_f32 v[66:67], v[70:71], v[66:67]
	s_nop 0
	v_cvt_pk_bf16_f32 v76, v66, v67
	v_mul_f32_e32 v66, 0xbfb8aa3b, v72
	v_mul_f32_e32 v67, 0xbfb8aa3b, v73
	v_exp_f32_e32 v66, v66
	v_exp_f32_e32 v67, v67
	v_add_f32_e32 v66, 1.0, v66
	v_add_f32_e32 v67, 1.0, v67
	v_rcp_f32_e32 v66, v66
	v_rcp_f32_e32 v67, v67
	s_nop 0
	v_pk_mul_f32 v[66:67], v[72:73], v[66:67]
	s_nop 0
	v_pk_mul_f32 v[66:67], v[66:67], v[68:69]
	v_add_u32_e32 v68, 0x80, v146
	v_cvt_pk_bf16_f32 v77, v66, v67
	v_or_b32_e32 v66, 48, v146
	v_mad_i64_i32 v[66:67], s[26:27], v66, s89, v[116:117]
	v_lshl_add_u64 v[66:67], v[66:67], 0, v[118:119]
	global_store_dwordx4 v[66:67], v[74:77], off
	v_mul_f32_e32 v66, 0xbfb8aa3b, v62
	v_mul_f32_e32 v67, 0xbfb8aa3b, v63
	v_exp_f32_e32 v66, v66
	v_exp_f32_e32 v67, v67
	v_add_f32_e32 v66, 1.0, v66
	v_add_f32_e32 v67, 1.0, v67
	v_rcp_f32_e32 v66, v66
	v_rcp_f32_e32 v67, v67
	s_nop 0
	v_pk_mul_f32 v[62:63], v[62:63], v[66:67]
	s_nop 0
	v_pk_mul_f32 v[58:59], v[62:63], v[58:59]
	s_nop 0
	v_cvt_pk_bf16_f32 v58, v58, v59
	v_mul_f32_e32 v59, 0xbfb8aa3b, v64
	v_exp_f32_e32 v59, v59
	s_nop 0
	v_add_f32_e32 v59, 1.0, v59
	v_rcp_f32_e32 v62, v59
	v_mul_f32_e32 v59, 0xbfb8aa3b, v65
	v_exp_f32_e32 v59, v59
	s_nop 0
	v_add_f32_e32 v59, 1.0, v59
	v_rcp_f32_e32 v63, v59
	s_nop 0
	v_pk_mul_f32 v[62:63], v[64:65], v[62:63]
	s_nop 0
	v_pk_mul_f32 v[60:61], v[62:63], v[60:61]
	s_nop 0
	v_cvt_pk_bf16_f32 v59, v60, v61
	v_mul_f32_e32 v60, 0xbfb8aa3b, v54
	v_mul_f32_e32 v61, 0xbfb8aa3b, v55
	v_exp_f32_e32 v60, v60
	v_exp_f32_e32 v61, v61
	v_add_f32_e32 v60, 1.0, v60
	v_add_f32_e32 v61, 1.0, v61
	v_rcp_f32_e32 v60, v60
	v_rcp_f32_e32 v61, v61
	s_nop 0
	v_pk_mul_f32 v[54:55], v[54:55], v[60:61]
	s_nop 0
	v_pk_mul_f32 v[50:51], v[54:55], v[50:51]
	s_nop 0
	v_cvt_pk_bf16_f32 v60, v50, v51
	v_mul_f32_e32 v50, 0xbfb8aa3b, v56
	v_mul_f32_e32 v51, 0xbfb8aa3b, v57
	v_exp_f32_e32 v50, v50
	v_exp_f32_e32 v51, v51
	v_add_f32_e32 v50, 1.0, v50
	v_add_f32_e32 v51, 1.0, v51
	v_rcp_f32_e32 v50, v50
	v_rcp_f32_e32 v51, v51
	s_nop 0
	v_pk_mul_f32 v[50:51], v[56:57], v[50:51]
	s_nop 0
	v_pk_mul_f32 v[50:51], v[50:51], v[52:53]
	s_nop 0
	v_cvt_pk_bf16_f32 v61, v50, v51
	v_mad_i64_i32 v[50:51], s[26:27], v68, s89, v[116:117]
	v_lshl_add_u64 v[50:51], v[50:51], 0, v[118:119]
	global_store_dwordx4 v[50:51], v[58:61], off
	v_mul_f32_e32 v50, 0xbfb8aa3b, v46
	v_mul_f32_e32 v51, 0xbfb8aa3b, v47
	v_exp_f32_e32 v50, v50
	v_exp_f32_e32 v51, v51
	v_add_f32_e32 v50, 1.0, v50
	v_add_f32_e32 v51, 1.0, v51
	v_rcp_f32_e32 v50, v50
	v_rcp_f32_e32 v51, v51
	s_nop 0
	v_pk_mul_f32 v[46:47], v[46:47], v[50:51]
	s_nop 0
	v_pk_mul_f32 v[42:43], v[46:47], v[42:43]
	s_nop 0
	v_cvt_pk_bf16_f32 v42, v42, v43
	v_mul_f32_e32 v43, 0xbfb8aa3b, v48
	v_exp_f32_e32 v43, v43
	s_nop 0
	v_add_f32_e32 v43, 1.0, v43
	v_rcp_f32_e32 v46, v43
	v_mul_f32_e32 v43, 0xbfb8aa3b, v49
	v_exp_f32_e32 v43, v43
	s_nop 0
	v_add_f32_e32 v43, 1.0, v43
	v_rcp_f32_e32 v47, v43
	s_nop 0
	v_pk_mul_f32 v[46:47], v[48:49], v[46:47]
	s_nop 0
	v_pk_mul_f32 v[44:45], v[46:47], v[44:45]
	s_nop 0
	v_cvt_pk_bf16_f32 v43, v44, v45
	v_mul_f32_e32 v44, 0xbfb8aa3b, v38
	v_mul_f32_e32 v45, 0xbfb8aa3b, v39
	v_exp_f32_e32 v44, v44
	v_exp_f32_e32 v45, v45
	v_add_f32_e32 v44, 1.0, v44
	v_add_f32_e32 v45, 1.0, v45
; __device__ __forceinline__ unsigned pk2(float lo, float hi) { f32x2 v = {lo, hi}; return __builtin_bit_cast(unsigned, __builtin_convertvector(v, bf2_t)); }
; template <int BIT = 0> __device__ __forceinline__ void st16w(void* p, u32x4 v) { if ((WT_STORES >> BIT) & 1) asm volatile("global_store_dwordx4 %0, %1, off sc1\n\ts_nop 1" :: "v"(p), "v"(v) : "memory"); else *(u32x4*)p = v; }
; __device__ __forceinline__ float fsilu(float x) { return x * fsigm(x); }
; #define PG8_LAS __attribute__((address_space(3)))
; #define PG8_BAR __builtin_amdgcn_s_barrier()
;     __device__ __forceinline__ void operator()(const f32x4 (&acc)[2][2][4][2], const Unit& u, int wr, int wc, int fr, int fq) const {
;     ...
;                 u32x4 w; w.x = pk2(fsilu(g0[0]) * u0[0], fsilu(g0[1]) * u0[1]); w.y = pk2(fsilu(g0[2]) * u0[2], fsilu(g0[3]) * u0[3]);
;                 w.z = pk2(fsilu(g1[0]) * u1[0], fsilu(g1[1]) * u1[1]); w.w = pk2(fsilu(g1[2]) * u1[2], fsilu(g1[3]) * u1[3]);
;                 bf16* dst = HID + (size_t)(row0 + ai * HALF + m * 16) * ldh + col0;
;                 if (wt) asm volatile("global_store_dwordx4 %0, %1, off sc1\n\ts_nop 1" :: "v"(dst), "v"(w) : "memory");
;                 else st16w(dst, w);
;             }
; template <class Epi, class Sched, bool ALIGN_EPI = false, bool SP2 = false>
; __device__ __forceinline__ void gemm_phase(PG8_LAS unsigned char* lds, const Gemm g, const Sched& S, const Epi& E) {
;     ...
;         if (!has_next) break;
; #pragma unroll
;         for (int a = 0; a < 2; ++a)
; #pragma unroll
;             for (int b = 0; b < 2; ++b)
; #pragma unroll
;                 for (int m = 0; m < 4; ++m)
; #pragma unroll
;                     for (int n = 0; n < 2; ++n) acc[a][b][m][n] = (f32x4){0.f, 0.f, 0.f, 0.f};
;         cur = nxt; cA = nA; cB = nB; ++ui;
;         if constexpr (Sched::GATHER) { const u32x4 pv_ = *(const PG8_LAS u32x4*)(lds + STAGE_BYTES + tid * 16); vAc[0][0] = pv_.x; vAc[0][1] = pv_.y; vAc[1][0] = pv_.z; vAc[1][1] = pv_.w; }
;         if constexpr (ALIGN_EPI) { if (wr == 1) PG8_BAR; }
	v_rcp_f32_e32 v44, v44
	v_rcp_f32_e32 v45, v45
	s_nop 0
	v_pk_mul_f32 v[38:39], v[38:39], v[44:45]
	s_nop 0
	v_pk_mul_f32 v[34:35], v[38:39], v[34:35]
	s_nop 0
	v_cvt_pk_bf16_f32 v44, v34, v35
	v_mul_f32_e32 v34, 0xbfb8aa3b, v40
	v_mul_f32_e32 v35, 0xbfb8aa3b, v41
	v_exp_f32_e32 v34, v34
	v_exp_f32_e32 v35, v35
	v_add_f32_e32 v34, 1.0, v34
	v_add_f32_e32 v35, 1.0, v35
	v_rcp_f32_e32 v34, v34
	v_rcp_f32_e32 v35, v35
	s_nop 0
	v_pk_mul_f32 v[34:35], v[40:41], v[34:35]
	s_nop 0
	v_pk_mul_f32 v[34:35], v[34:35], v[36:37]
	s_nop 0
	v_cvt_pk_bf16_f32 v45, v34, v35
	v_add_u32_e32 v34, 0x90, v146
	v_mad_i64_i32 v[34:35], s[26:27], v34, s89, v[116:117]
	v_lshl_add_u64 v[34:35], v[34:35], 0, v[118:119]
	global_store_dwordx4 v[34:35], v[42:45], off
	v_mul_f32_e32 v34, 0xbfb8aa3b, v30
	v_mul_f32_e32 v35, 0xbfb8aa3b, v31
	v_exp_f32_e32 v34, v34
	v_exp_f32_e32 v35, v35
	v_add_f32_e32 v34, 1.0, v34
	v_add_f32_e32 v35, 1.0, v35
	v_rcp_f32_e32 v34, v34
	v_rcp_f32_e32 v35, v35
	s_nop 0
	v_pk_mul_f32 v[30:31], v[30:31], v[34:35]
	s_nop 0
	v_pk_mul_f32 v[26:27], v[30:31], v[26:27]
	s_nop 0
	v_cvt_pk_bf16_f32 v26, v26, v27
	v_mul_f32_e32 v27, 0xbfb8aa3b, v32
	v_exp_f32_e32 v27, v27
	s_nop 0
	v_add_f32_e32 v27, 1.0, v27
	v_rcp_f32_e32 v30, v27
	v_mul_f32_e32 v27, 0xbfb8aa3b, v33
	v_exp_f32_e32 v27, v27
	s_nop 0
	v_add_f32_e32 v27, 1.0, v27
	v_rcp_f32_e32 v31, v27
	s_nop 0
	v_pk_mul_f32 v[30:31], v[32:33], v[30:31]
	s_nop 0
	v_pk_mul_f32 v[28:29], v[30:31], v[28:29]
	s_nop 0
	v_cvt_pk_bf16_f32 v27, v28, v29
	v_mul_f32_e32 v28, 0xbfb8aa3b, v22
	v_mul_f32_e32 v29, 0xbfb8aa3b, v23
	v_exp_f32_e32 v28, v28
	v_exp_f32_e32 v29, v29
	v_add_f32_e32 v28, 1.0, v28
	v_add_f32_e32 v29, 1.0, v29
	v_rcp_f32_e32 v28, v28
	v_rcp_f32_e32 v29, v29
	s_nop 0
	v_pk_mul_f32 v[22:23], v[22:23], v[28:29]
	s_nop 0
	v_pk_mul_f32 v[18:19], v[22:23], v[18:19]
	s_nop 0
	v_cvt_pk_bf16_f32 v28, v18, v19
	v_mul_f32_e32 v18, 0xbfb8aa3b, v24
	v_mul_f32_e32 v19, 0xbfb8aa3b, v25
	v_exp_f32_e32 v18, v18
	v_exp_f32_e32 v19, v19
	v_add_f32_e32 v18, 1.0, v18
	v_add_f32_e32 v19, 1.0, v19
	v_rcp_f32_e32 v18, v18
	v_rcp_f32_e32 v19, v19
	s_nop 0
	v_pk_mul_f32 v[18:19], v[24:25], v[18:19]
	s_nop 0
	v_pk_mul_f32 v[18:19], v[18:19], v[20:21]
	s_nop 0
	v_cvt_pk_bf16_f32 v29, v18, v19
	v_add_u32_e32 v18, 0xa0, v146
	v_mad_i64_i32 v[18:19], s[26:27], v18, s89, v[116:117]
	v_lshl_add_u64 v[18:19], v[18:19], 0, v[118:119]
	global_store_dwordx4 v[18:19], v[26:29], off
	v_mul_f32_e32 v18, 0xbfb8aa3b, v14
	v_mul_f32_e32 v19, 0xbfb8aa3b, v15
	v_exp_f32_e32 v18, v18
	v_exp_f32_e32 v19, v19
	v_add_f32_e32 v18, 1.0, v18
	v_add_f32_e32 v19, 1.0, v19
	v_rcp_f32_e32 v18, v18
	v_rcp_f32_e32 v19, v19
	s_nop 0
	v_pk_mul_f32 v[14:15], v[14:15], v[18:19]
	s_nop 0
	v_pk_mul_f32 v[10:11], v[14:15], v[10:11]
	s_nop 0
	v_cvt_pk_bf16_f32 v10, v10, v11
	v_mul_f32_e32 v11, 0xbfb8aa3b, v16
	v_exp_f32_e32 v11, v11
	s_nop 0
	v_add_f32_e32 v11, 1.0, v11
	v_rcp_f32_e32 v14, v11
	v_mul_f32_e32 v11, 0xbfb8aa3b, v17
	v_exp_f32_e32 v11, v11
	s_nop 0
	v_add_f32_e32 v11, 1.0, v11
	v_rcp_f32_e32 v15, v11
	s_nop 0
	v_pk_mul_f32 v[14:15], v[16:17], v[14:15]
	s_nop 0
	v_pk_mul_f32 v[12:13], v[14:15], v[12:13]
	s_nop 0
	v_cvt_pk_bf16_f32 v11, v12, v13
	v_mul_f32_e32 v12, 0xbfb8aa3b, v6
	v_mul_f32_e32 v13, 0xbfb8aa3b, v7
	v_exp_f32_e32 v12, v12
	v_exp_f32_e32 v13, v13
	v_add_f32_e32 v12, 1.0, v12
	v_add_f32_e32 v13, 1.0, v13
	v_rcp_f32_e32 v12, v12
	v_rcp_f32_e32 v13, v13
	s_nop 0
	v_pk_mul_f32 v[6:7], v[6:7], v[12:13]
	s_nop 0
	v_pk_mul_f32 v[2:3], v[6:7], v[2:3]
	s_nop 0
	v_cvt_pk_bf16_f32 v12, v2, v3
	v_mul_f32_e32 v2, 0xbfb8aa3b, v8
	v_mul_f32_e32 v3, 0xbfb8aa3b, v9
	v_exp_f32_e32 v2, v2
	v_exp_f32_e32 v3, v3
	v_add_f32_e32 v2, 1.0, v2
	v_add_f32_e32 v3, 1.0, v3
	v_rcp_f32_e32 v2, v2
	v_rcp_f32_e32 v3, v3
	s_nop 0
	v_pk_mul_f32 v[2:3], v[8:9], v[2:3]
	s_nop 0
	v_pk_mul_f32 v[2:3], v[2:3], v[4:5]
	s_nop 0
	v_cvt_pk_bf16_f32 v13, v2, v3
	v_add_u32_e32 v2, 0xb0, v146
	v_mad_i64_i32 v[2:3], s[26:27], v2, s89, v[116:117]
	v_lshl_add_u64 v[2:3], v[2:3], 0, v[118:119]
	s_mov_b64 s[26:27], -1
	global_store_dwordx4 v[2:3], v[10:13], off
	s_cbranch_vccnz .LBB13_1404
	s_andn2_b64 vcc, exec, s[0:1]
	s_cbranch_vccnz .LBB13_1403
	s_branch .LBB13_1403

;     __device__ __forceinline__ size_t boff(const Unit& u) const { return (size_t)__builtin_amdgcn_readfirstlane(panel_e[u.pm]) * estride; }
; #define PG8_SETA(v, u) do { if constexpr (Sched::GATHER) { _Pragma("unroll") for (int h_ = 0; h_ < 2; ++h_) _Pragma("unroll") for (int i_ = 0; i_ < 2; ++i_) { \
;         int R_, C_; stage_rc(tid * 16 + i_ * 8192, R_, C_); int tok_ = S.arow[(u).pm * BM + h_ * HALF + R_]; tok_ = tok_ < 0 ? 0 : tok_; (v)[h_][i_] = (unsigned)(tok_ * K + C_) * 2u; } } } while (0)
; #define PG8_STAGE_A(bufoff, h, ptr, nsel) do { if constexpr (Sched::GATHER) { if (nsel) PG8_STAGE_X(bufoff, ptr, vAn[h], PG8_A_AUX); else PG8_STAGE_X(bufoff, ptr, vAc[h], PG8_A_AUX); } \
;         else PG8_STAGE_X(bufoff, (ptr) + (h) * hstep, voffA, PG8_A_AUX); } while (0)
; #define PG8_STAGE(bufoff, gbase, voff) PG8_STAGE_X(bufoff, gbase, voff, PG8_B_AUX)
; #define PG8_WAIT_V(n) asm volatile("s_waitcnt vmcnt(" #n ")" ::: "memory")
; #define PG8_BAR __builtin_amdgcn_s_barrier()
; template <class Epi, class Sched, bool ALIGN_EPI = false, bool SP2 = false>
; __device__ __forceinline__ void gemm_phase(PG8_LAS unsigned char* lds, const Gemm g, const Sched& S, const Epi& E) {
;     ...
;     const char* cA = Sched::GATHER ? (const char*)g.A : (const char*)g.A + (size_t)cur.pm * tstep; PG8_SETA(vAc, cur); const char* cB = (const char*)g.Bt + S.boff(cur) + (size_t)cur.pn * tstep;
;     S.a_ready(cur);
;     if constexpr (SP2) {
;         PG8_STAGE(PG8_SB(0, 0), cB, voffB); PG8_STAGE(PG8_SB(0, 1), cB + hstep, voffB); PG8_STAGE_A(PG8_SA(0, 0), 0, cA, false); PG8_STAGE_A(PG8_SA(0, 1), 1, cA, false);
;         if (wr == 1) PG8_BAR;
;         PG8_WAIT_V(2); PG8_BAR;
;         PG8_STAGE(PG8_SB(1, 0), cB + kstep, voffB); PG8_STAGE_A(PG8_SA(1, 0), 0, cA + kstep, false); PG8_STAGE(PG8_SB(1, 1), cB + hstep + kstep, voffB);
;         PG8_WAIT_V(6); PG8_BAR;
.LBB13_1427:
	s_andn2_b64 vcc, exec, s[6:7]
	s_cbranch_vccnz .LBB13_1465
	v_bfe_i32 v4, v2, 27, 1
	v_lshlrev_b32_e32 v1, 4, v2
	v_lshrrev_b32_e32 v4, 22, v4
	v_add_u32_e32 v4, v1, v4
	v_and_b32_e32 v4, 0xfffffc00, v4
	v_sub_u32_e32 v4, v1, v4
	v_ashrrev_i32_e32 v3, 31, v2
	v_lshrrev_b32_e32 v5, 4, v4
	v_lshrrev_b32_e32 v3, 26, v3
	v_bitop3_b32 v4, v5, v4, 32 bitop3:0x6c
	v_add_u32_e32 v3, v2, v3
	v_ashrrev_i32_e32 v6, 31, v4
	v_ashrrev_i32_e32 v3, 6, v3
	v_lshrrev_b32_e32 v6, 26, v6
	v_lshlrev_b32_e32 v5, 3, v3
	v_add_u32_e32 v6, v4, v6
	v_and_b32_e32 v5, -16, v5
	v_ashrrev_i32_e32 v7, 6, v6
	v_add_u32_e32 v99, v7, v5
	v_and_b32_e32 v5, 0xc0, v6
	v_sub_u32_e32 v4, v4, v5
	v_lshlrev_b32_e32 v3, 5, v3
	v_ashrrev_i16_sdwa v4, v238, sext(v4) dst_sel:DWORD dst_unused:UNUSED_PAD src0_sel:DWORD src1_sel:BYTE_0
	v_and_b32_e32 v3, 32, v3
	v_bfe_i32 v4, v4, 0, 16
	v_add_lshl_u32 v241, v3, v4, 1
	v_add_u32_e32 v3, 0x2000, v1
	v_ashrrev_i32_e32 v4, 31, v3
	v_lshlrev_b32_e32 v5, 1, v99
	v_lshrrev_b32_e32 v6, 2, v99
	v_and_b32_e32 v7, 3, v7
	s_mov_b32 s5, 0x1fffe0
	v_lshrrev_b32_e32 v4, 22, v4
	v_and_b32_e32 v5, 24, v5
	v_and_b32_e32 v6, 4, v6
	v_and_or_b32 v7, v99, s5, v7
	v_add_u32_e32 v4, v3, v4
	v_or3_b32 v5, v7, v6, v5
	v_ashrrev_i32_e32 v4, 10, v4
	v_lshl_add_u32 v208, v5, 11, v241
	v_mul_i32_i24_e32 v5, 0x400, v4
	v_sub_u32_e32 v3, v3, v5
	v_lshrrev_b32_e32 v5, 4, v3
	v_bitop3_b32 v3, v5, v3, 32 bitop3:0x6c
	v_ashrrev_i32_e32 v6, 31, v3
	v_lshrrev_b32_e32 v6, 26, v6
	v_lshlrev_b32_e32 v5, 3, v4
	v_add_u32_e32 v6, v3, v6
	v_and_b32_e32 v5, -16, v5
	v_ashrrev_i32_e32 v7, 6, v6
	v_add_u32_e32 v242, v7, v5
	v_and_b32_e32 v7, 3, v7
	s_ashr_i32 s6, s1, 6
	s_ashr_i32 s4, s1, 8
	v_and_or_b32 v7, v242, s5, v7
	s_lshl_b32 s5, s6, 10
	s_add_u32 s48, s10, 0x2f0000
	s_addc_u32 s49, s11, 0
	s_mul_i32 s38, s38, 0xa800000
	s_add_u32 s7, s10, s38
	s_addc_u32 s12, s11, 0
	v_and_b32_e32 v5, 0xc0, v6
	s_add_u32 s53, s7, 0x7500000
	v_sub_u32_e32 v3, v3, v5
	s_addc_u32 s58, s12, 0
	v_lshlrev_b32_e32 v4, 5, v4
	v_ashrrev_i16_sdwa v3, v238, sext(v3) dst_sel:DWORD dst_unused:UNUSED_PAD src0_sel:DWORD src1_sel:BYTE_0
	v_lshlrev_b32_e32 v5, 1, v242
	v_lshrrev_b32_e32 v6, 2, v242
	s_add_u32 s12, s10, 0x300000
	v_and_b32_e32 v4, 32, v4
	v_bfe_i32 v3, v3, 0, 16
	v_and_b32_e32 v5, 24, v5
	v_and_b32_e32 v6, 4, v6
	s_addc_u32 s13, s11, 0
	s_lshl_b32 s7, s30, 8
	v_or3_b32 v5, v7, v6, v5
	v_add_lshl_u32 v243, v4, v3, 1
	v_add_u32_e32 v4, s7, v99
	v_lshl_add_u32 v210, v5, 11, v243
	v_ashrrev_i32_e32 v5, 31, v4
	v_lshl_add_u64 v[4:5], v[4:5], 2, s[12:13]
	global_load_dword v3, v[4:5], off
	v_add_u32_e32 v4, s7, v242
	v_ashrrev_i32_e32 v5, 31, v4
	v_lshl_add_u64 v[4:5], v[4:5], 2, s[12:13]
	s_bitset1_b32 s7, 7
	s_ashr_i32 s31, s30, 31
	v_add_u32_e32 v6, s7, v242
	s_lshl_b64 s[18:19], s[30:31], 2
	v_ashrrev_i32_e32 v7, 31, v6
	s_add_u32 s18, s48, s18
	v_lshl_add_u64 v[6:7], v[6:7], 2, s[12:13]
	s_addc_u32 s19, s49, s19
	v_mov_b32_e32 v209, v98
	v_mov_b32_e32 v211, v98
	v_writelane_b32 v249, s42, 55
	s_waitcnt vmcnt(0)
	v_max_i32_e32 v3, 0, v3
	v_lshl_add_u32 v212, v3, 11, v241
	global_load_dword v3, v[4:5], off
	v_add_u32_e32 v4, s7, v99
	v_ashrrev_i32_e32 v5, 31, v4
	v_lshl_add_u64 v[4:5], v[4:5], 2, s[12:13]
	global_load_dword v4, v[4:5], off
	v_writelane_b32 v249, s43, 56
	global_load_dword v5, v[6:7], off
	s_waitcnt vmcnt(2)
	v_max_i32_e32 v3, 0, v3
	global_load_dword v6, v98, s[18:19]
	v_lshl_add_u32 v3, v3, 11, v243
	s_waitcnt vmcnt(2)
	v_max_i32_e32 v4, 0, v4
	v_lshl_add_u32 v4, v4, 11, v241
	s_waitcnt vmcnt(1)
	v_max_i32_e32 v5, 0, v5
	v_lshl_add_u32 v5, v5, 11, v243
	s_waitcnt vmcnt(0)
	v_readfirstlane_b32 s7, v6
	s_mul_hi_i32 s18, s7, 0xe00000
	s_mul_i32 s7, s7, 0xe00000
	s_add_u32 s7, s53, s7
	s_addc_u32 s20, s58, s18
	s_ashr_i32 s29, s28, 31
	s_lshl_b64 s[18:19], s[28:29], 19
	s_add_u32 s34, s7, s18
	s_addc_u32 s35, s20, s19
	s_add_i32 s31, s47, s5
	s_add_i32 s59, s31, 0x2000
	s_mov_b32 m0, s31
	s_add_u32 s18, s34, 0x40000
	global_load_lds_dwordx4 v208, s[34:35]
	s_mov_b32 m0, s59
	s_addc_u32 s19, s35, 0
	s_add_i32 s61, s50, s5
	global_load_lds_dwordx4 v210, s[34:35]
	s_mov_b32 m0, s61
	s_add_i32 s68, s61, 0x2000
	global_load_lds_dwordx4 v208, s[18:19]
	s_mov_b32 m0, s68
	s_add_i32 s69, s2, s5
	global_load_lds_dwordx4 v210, s[18:19]
	s_mov_b32 m0, s69
	s_add_i32 s76, s69, 0x2000
	global_load_lds_dwordx4 v212, s[14:15]
	s_mov_b32 m0, s76
	s_add_i32 s88, s69, 0x4000
	global_load_lds_dwordx4 v3, s[14:15]
	s_mov_b32 m0, s88
	s_add_i32 s89, s69, 0x6000
	global_load_lds_dwordx4 v4, s[14:15]
	s_mov_b32 m0, s89
	s_cmp_eq_u32 s4, 1
	global_load_lds_dwordx4 v5, s[14:15]
	v_lshl_add_u64 v[6:7], s[34:35], 0, v[208:209]
	v_lshl_add_u64 v[8:9], s[34:35], 0, v[210:211]
	s_cselect_b64 s[18:19], -1, 0
	s_cmp_lg_u32 s4, 1
	s_cbranch_scc1 .LBB13_1430
.LBB13_1430:
	v_lshrrev_b32_e32 v13, 1, v2
	v_and_b32_e32 v13, 24, v13
	v_and_b32_e32 v12, 15, v2
	v_lshlrev_b32_e32 v14, 1, v13
	v_lshlrev_b32_e32 v2, 2, v2
	v_lshl_or_b32 v244, s4, 6, v12
	v_lshl_or_b32 v12, v12, 6, v14
	s_lshl_b32 s4, s4, 13
	v_and_b32_e32 v2, 32, v2
	v_bitop3_b32 v14, v12, s4, v2 bitop3:0xde
	s_lshl_b32 s4, s6, 5
	s_and_b32 s22, s4, 0x60
	s_lshl_b32 s4, s22, 7
	s_add_u32 s6, s10, 0x20700080
	s_addc_u32 s7, s11, 0
	s_add_i32 s90, s51, s5
	v_lshl_add_u64 v[6:7], v[6:7], 0, s[54:55]
	s_mov_b32 m0, s90
	s_add_i32 s95, s90, 0x2000
	v_mov_b32_e32 v213, v98
	s_waitcnt vmcnt(2)
	s_barrier
	global_load_lds_dwordx4 v[6:7], off
	v_lshl_add_u64 v[6:7], v[8:9], 0, s[54:55]
	s_mov_b32 m0, s95
	s_add_i32 s64, s69, 0x8000
	v_mov_b32_e32 v10, v3
	v_mov_b32_e32 v11, v98
	s_add_i32 s94, s2, 0x20000
	global_load_lds_dwordx4 v[6:7], off
	v_lshl_add_u64 v[6:7], s[6:7], 0, v[212:213]
	s_mov_b32 m0, s64
	s_add_i32 s52, s69, 0xa000
	global_load_lds_dwordx4 v[6:7], off
	v_lshl_add_u64 v[6:7], s[6:7], 0, v[10:11]
	s_add_u32 s6, s34, 0x40080
	v_bitop3_b32 v245, v12, s4, v2 bitop3:0xde
	s_mov_b32 m0, s52
	s_addc_u32 s7, s35, 0
	s_add_i32 s4, s56, s5
	global_load_lds_dwordx4 v[6:7], off
	v_lshl_add_u64 v[6:7], s[6:7], 0, v[208:209]
	s_mov_b32 m0, s4
	s_add_i32 s5, s4, 0x2000
	global_load_lds_dwordx4 v[6:7], off
	v_lshl_add_u64 v[6:7], s[6:7], 0, v[210:211]
	s_mov_b32 m0, s5
	s_cmpk_lt_u32 s1, 0x100
	global_load_lds_dwordx4 v[6:7], off
	s_cselect_b64 s[20:21], -1, 0
	s_ashr_i32 s1, s0, 31
	s_lshr_b32 s6, s1, 29
	s_add_i32 s6, s0, s6
	s_ashr_i32 s86, s6, 3
	s_and_b32 s6, s6, -8
	s_waitcnt vmcnt(6)
	s_sub_i32 s87, s0, s6
	s_add_i32 s60, s86, 1
	v_readlane_b32 s6, v249, 33
	v_or_b32_e32 v246, s22, v13
	s_add_u32 s22, s6, s8
	v_readlane_b32 s6, v249, 34
	s_addc_u32 s23, s6, s9
	s_mov_b32 s72, 0
	v_add_u32_e32 v247, s2, v14
	s_barrier
	s_branch .LBB13_1433

; #define PG8_LAS __attribute__((address_space(3)))
;     __device__ __forceinline__ size_t boff(const Unit& u) const { return (size_t)__builtin_amdgcn_readfirstlane(panel_e[u.pm]) * estride; }
; #define PG8_SETA(v, u) do { if constexpr (Sched::GATHER) { _Pragma("unroll") for (int h_ = 0; h_ < 2; ++h_) _Pragma("unroll") for (int i_ = 0; i_ < 2; ++i_) { \
;         int R_, C_; stage_rc(tid * 16 + i_ * 8192, R_, C_); int tok_ = S.arow[(u).pm * BM + h_ * HALF + R_]; tok_ = tok_ < 0 ? 0 : tok_; (v)[h_][i_] = (unsigned)(tok_ * K + C_) * 2u; } } } while (0)
; #define PG8_BAR __builtin_amdgcn_s_barrier()
; template <class Epi, class Sched, bool ALIGN_EPI = false, bool SP2 = false>
; __device__ __forceinline__ void gemm_phase(PG8_LAS unsigned char* lds, const Gemm g, const Sched& S, const Epi& E) {
;     ...
;         const bool has_next = S.next(ui + 1, nxt);
;         const char* nA = Sched::GATHER ? (const char*)g.A : (has_next ? (const char*)g.A + (size_t)nxt.pm * tstep : cA);
;         if constexpr (Sched::GATHER) { if (has_next) PG8_SETA(vAn, nxt); else { _Pragma("unroll") for (int h_ = 0; h_ < 2; ++h_) { vAn[h_][0] = vAc[h_][0]; vAn[h_][1] = vAc[h_][1]; } }
;             *(PG8_LAS u32x4*)(lds + STAGE_BYTES + tid * 16) = (u32x4){vAn[0][0], vAn[0][1], vAn[1][0], vAn[1][1]}; }     const char* nB = has_next ? (const char*)g.Bt + S.boff(nxt) + (size_t)nxt.pn * tstep : cB;
;     ...
; #pragma unroll
;         for (int a = 0; a < 2; ++a)
; #pragma unroll
;             for (int b = 0; b < 2; ++b)
; #pragma unroll
;                 for (int m = 0; m < 4; ++m)
; #pragma unroll
;                     for (int n = 0; n < 2; ++n) acc[a][b][m][n] = (f32x4){0.f, 0.f, 0.f, 0.f};
;         cur = nxt; cA = nA; cB = nB; ++ui;
;         if constexpr (Sched::GATHER) { const u32x4 pv_ = *(const PG8_LAS u32x4*)(lds + STAGE_BYTES + tid * 16); vAc[0][0] = pv_.x; vAc[0][1] = pv_.y; vAc[1][0] = pv_.z; vAc[1][1] = pv_.w; }
;         if constexpr (ALIGN_EPI) { if (wr == 1) PG8_BAR; }
.LBB13_1439:
	s_nop 0
	v_cndmask_b32_e64 v2, 0, 1, s[8:9]
	v_cmp_ne_u32_e64 s[6:7], 1, v2
	s_andn2_b64 vcc, exec, s[8:9]
	v_mov_b32_e32 v100, v212
	v_mov_b32_e32 v101, v3
	v_mov_b32_e32 v102, v4
	v_mov_b32_e32 v103, v5
	s_cbranch_vccnz .LBB13_1441
	s_mov_b32 s98, s26
	s_ashr_i32 s99, s26, 31
	s_lshl_b64 s[98:99], s[98:99], 2
	s_add_u32 s98, s48, s98
	s_addc_u32 s99, s49, s99
	s_lshl_b32 s2, s26, 8
	v_add_u32_e32 v6, s2, v99
	v_ashrrev_i32_e32 v7, 31, v6
	v_add_u32_e32 v8, s2, v242
	v_lshl_add_u64 v[6:7], v[6:7], 2, s[12:13]
	v_ashrrev_i32_e32 v9, 31, v8
	s_bitset1_b32 s2, 7
	v_lshl_add_u64 v[8:9], v[8:9], 2, s[12:13]
	global_load_dword v2, v[6:7], off
	global_load_dword v10, v[8:9], off
	v_add_u32_e32 v6, s2, v99
	v_ashrrev_i32_e32 v7, 31, v6
	v_add_u32_e32 v8, s2, v242
	v_lshl_add_u64 v[6:7], v[6:7], 2, s[12:13]
	v_ashrrev_i32_e32 v9, 31, v8
	v_lshl_add_u64 v[8:9], v[8:9], 2, s[12:13]
	global_load_dword v6, v[6:7], off
	s_nop 0
	global_load_dword v7, v[8:9], off
	s_nop 0
	global_load_dword v11, v98, s[98:99]
	s_waitcnt vmcnt(0)
	v_max_i32_e32 v2, 0, v2
	v_max_i32_e32 v8, 0, v10
	v_lshl_add_u32 v100, v2, 11, v241
	v_lshl_add_u32 v101, v8, 11, v243
	v_max_i32_e32 v2, 0, v6
	v_max_i32_e32 v6, 0, v7
	v_lshl_add_u32 v102, v2, 11, v241
	v_lshl_add_u32 v103, v6, 11, v243
.LBB13_1441:
	v_add_u32_e32 v248, s94, v1
	s_and_b64 vcc, exec, s[6:7]
	s_mov_b64 s[8:9], s[34:35]
	ds_write_b128 v248, v[100:103]
	s_cbranch_vccnz .LBB13_1443
	v_readfirstlane_b32 s2, v11
	s_mul_hi_i32 s8, s2, 0xe00000
	s_mul_i32 s2, s2, 0xe00000
	s_add_u32 s2, s53, s2
	s_addc_u32 s27, s58, s8
	s_ashr_i32 s25, s24, 31
	s_lshl_b64 s[8:9], s[24:25], 19
	s_add_u32 s8, s2, s8
	s_addc_u32 s9, s27, s9
.LBB13_1443:
	v_mov_b32_e32 v6, v4
	v_mov_b32_e32 v7, v98
	v_mov_b32_e32 v4, v5
	v_mov_b32_e32 v5, v98
	v_mov_b32_e32 v213, v98
	v_mov_b32_e32 v214, v3
	v_mov_b32_e32 v215, v98
	s_add_u32 s2, s34, 0x100
	v_mov_b32_e32 v2, 0
	v_lshl_add_u64 v[216:217], s[22:23], 0, v[214:215]
	v_lshl_add_u64 v[218:219], s[22:23], 0, v[212:213]
	v_lshl_add_u64 v[220:221], s[10:11], 0, v[4:5]
	v_lshl_add_u64 v[222:223], s[10:11], 0, v[6:7]
	s_addc_u32 s25, s35, 0
	s_mov_b32 s27, -2
	s_mov_b64 s[34:35], 0
	v_mov_b32_e32 v3, v2
	v_mov_b64_e32 v[4:5], 0
	v_mov_b64_e32 v[10:11], 0
	v_mov_b64_e32 v[12:13], 0
	v_mov_b64_e32 v[18:19], 0
	v_mov_b64_e32 v[20:21], 0
	v_mov_b64_e32 v[26:27], 0
	v_mov_b64_e32 v[28:29], 0
	v_mov_b64_e32 v[34:35], 0
	v_mov_b64_e32 v[36:37], 0
	v_mov_b64_e32 v[42:43], 0
	v_mov_b64_e32 v[44:45], 0
	v_mov_b64_e32 v[50:51], 0
	v_mov_b64_e32 v[52:53], 0
	v_mov_b64_e32 v[58:59], 0
	v_mov_b64_e32 v[60:61], 0
	v_mov_b64_e32 v[6:7], 0
	v_mov_b64_e32 v[8:9], 0
	v_mov_b64_e32 v[14:15], 0
	v_mov_b64_e32 v[16:17], 0
	v_mov_b64_e32 v[22:23], 0
	v_mov_b64_e32 v[24:25], 0
	v_mov_b64_e32 v[30:31], 0
	v_mov_b64_e32 v[32:33], 0
	v_mov_b64_e32 v[38:39], 0
	v_mov_b64_e32 v[40:41], 0
	v_mov_b64_e32 v[46:47], 0
	v_mov_b64_e32 v[48:49], 0
	v_mov_b64_e32 v[54:55], 0
	v_mov_b64_e32 v[56:57], 0
	v_mov_b64_e32 v[62:63], 0
	v_mov_b64_e32 v[64:65], 0
	v_mov_b64_e32 v[66:67], 0
	v_mov_b64_e32 v[68:69], 0
	v_mov_b64_e32 v[74:75], 0
	v_mov_b64_e32 v[76:77], 0
	v_mov_b64_e32 v[82:83], 0
	v_mov_b64_e32 v[84:85], 0
	v_mov_b64_e32 v[90:91], 0
	v_mov_b64_e32 v[92:93], 0
	v_mov_b64_e32 v[104:105], 0
	v_mov_b64_e32 v[106:107], 0
	v_mov_b64_e32 v[112:113], 0
	v_mov_b64_e32 v[114:115], 0
	v_mov_b64_e32 v[120:121], 0
	v_mov_b64_e32 v[122:123], 0
	v_mov_b64_e32 v[128:129], 0
	v_mov_b64_e32 v[130:131], 0
	v_mov_b64_e32 v[70:71], 0
	v_mov_b64_e32 v[72:73], 0
	v_mov_b64_e32 v[78:79], 0
	v_mov_b64_e32 v[80:81], 0
	v_mov_b64_e32 v[86:87], 0
	v_mov_b64_e32 v[88:89], 0
	v_mov_b64_e32 v[94:95], 0
	v_mov_b64_e32 v[96:97], 0
	v_mov_b64_e32 v[108:109], 0
	v_mov_b64_e32 v[110:111], 0
	v_mov_b64_e32 v[116:117], 0
	v_mov_b64_e32 v[118:119], 0
	v_mov_b64_e32 v[124:125], 0
	v_mov_b64_e32 v[126:127], 0
	v_mov_b64_e32 v[132:133], 0
	v_mov_b64_e32 v[134:135], 0
	s_and_b64 s[98:99], exec, s[20:21]
	s_cbranch_scc1 .Lrb_1446
	s_barrier
.Lrb_1446:
	s_branch .LBB13_1446
.LBB13_1444:
	v_mov_b32_e32 v226, v100
	v_mov_b32_e32 v227, v98
	v_lshl_add_u64 v[226:227], s[38:39], 0, v[226:227]
	v_lshl_add_u64 v[226:227], v[226:227], 0, s[54:55]
	s_mov_b32 m0, s64
	s_nop 0
	global_load_lds_dwordx4 v[226:227], off

; __device__ __forceinline__ unsigned pk2(float lo, float hi) { f32x2 v = {lo, hi}; return __builtin_bit_cast(unsigned, __builtin_convertvector(v, bf2_t)); }
; template <int BIT = 0> __device__ __forceinline__ void st16w(void* p, u32x4 v) { if ((WT_STORES >> BIT) & 1) asm volatile("global_store_dwordx4 %0, %1, off sc1\n\ts_nop 1" :: "v"(p), "v"(v) : "memory"); else *(u32x4*)p = v; }
; __device__ __forceinline__ float fsigm(float x) { return __builtin_amdgcn_rcpf(1.f + __builtin_amdgcn_exp2f(-1.4426950408889634f * x)); }
; __device__ __forceinline__ float fsilu(float x) { return x * fsigm(x); }
;     __device__ __forceinline__ void operator()(const f32x4 (&acc)[2][2][4][2], const Unit& u, int wr, int wc, int fr, int fq) const {
;         const int row0 = u.pm * BM + wr * 64 + fr, col0 = u.pn * HALF + wc * 32 + 8 * fq;
; #pragma unroll
;         for (int ai = 0; ai < 2; ++ai)
; #pragma unroll
;             for (int m = 0; m < 4; ++m) {
;                 const f32x4 g0 = acc[ai][0][m][0], g1 = acc[ai][0][m][1], u0 = acc[ai][1][m][0], u1 = acc[ai][1][m][1];
;                 u32x4 w; w.x = pk2(fsilu(g0[0]) * u0[0], fsilu(g0[1]) * u0[1]); w.y = pk2(fsilu(g0[2]) * u0[2], fsilu(g0[3]) * u0[3]);
;                 w.z = pk2(fsilu(g1[0]) * u1[0], fsilu(g1[1]) * u1[1]); w.w = pk2(fsilu(g1[2]) * u1[2], fsilu(g1[3]) * u1[3]);
;                 bf16* dst = HID + (size_t)(row0 + ai * HALF + m * 16) * ldh + col0;
;                 if (wt) asm volatile("global_store_dwordx4 %0, %1, off sc1\n\ts_nop 1" :: "v"(dst), "v"(w) : "memory");
;                 else st16w(dst, w);
;             }
.LBB13_1461:
	v_mul_f32_e32 v100, 0xbfb8aa3b, v132
	v_mul_f32_e32 v101, 0xbfb8aa3b, v133
	v_exp_f32_e32 v100, v100
	v_exp_f32_e32 v101, v101
	v_lshl_or_b32 v102, s28, 7, v246
	v_lshl_add_u32 v136, s30, 8, v244
	v_add_f32_e32 v100, 1.0, v100
	v_add_f32_e32 v101, 1.0, v101
	v_rcp_f32_e32 v100, v100
	v_rcp_f32_e32 v101, v101
	v_ashrrev_i32_e32 v103, 31, v102
	s_movk_i32 s2, 0x1c00
	v_lshlrev_b64 v[102:103], 1, v[102:103]
	v_pk_mul_f32 v[100:101], v[132:133], v[100:101]
	s_and_b64 vcc, exec, s[6:7]
	v_pk_mul_f32 v[100:101], v[100:101], v[128:129]
	s_nop 0
	v_cvt_pk_bf16_f32 v128, v100, v101
	v_mul_f32_e32 v100, 0xbfb8aa3b, v134
	v_mul_f32_e32 v101, 0xbfb8aa3b, v135
	v_exp_f32_e32 v100, v100
	v_exp_f32_e32 v101, v101
	v_add_f32_e32 v100, 1.0, v100
	v_add_f32_e32 v101, 1.0, v101
	v_rcp_f32_e32 v100, v100
	v_rcp_f32_e32 v101, v101
	s_nop 0
	v_pk_mul_f32 v[100:101], v[134:135], v[100:101]
	s_nop 0
	v_pk_mul_f32 v[100:101], v[100:101], v[130:131]
	s_nop 0
	v_cvt_pk_bf16_f32 v129, v100, v101
	v_mul_f32_e32 v100, 0xbfb8aa3b, v124
	v_mul_f32_e32 v101, 0xbfb8aa3b, v125
	v_exp_f32_e32 v100, v100
	v_exp_f32_e32 v101, v101
	v_add_f32_e32 v100, 1.0, v100
	v_add_f32_e32 v101, 1.0, v101
	v_rcp_f32_e32 v100, v100
	v_rcp_f32_e32 v101, v101
	s_nop 0
	v_pk_mul_f32 v[100:101], v[124:125], v[100:101]
	s_nop 0
	v_pk_mul_f32 v[100:101], v[100:101], v[120:121]
	s_nop 0
	v_cvt_pk_bf16_f32 v130, v100, v101
	v_mul_f32_e32 v100, 0xbfb8aa3b, v126
	v_mul_f32_e32 v101, 0xbfb8aa3b, v127
	v_exp_f32_e32 v100, v100
	v_exp_f32_e32 v101, v101
	v_add_f32_e32 v100, 1.0, v100
	v_add_f32_e32 v101, 1.0, v101
	v_rcp_f32_e32 v100, v100
	v_rcp_f32_e32 v101, v101
	s_nop 0
	v_pk_mul_f32 v[100:101], v[126:127], v[100:101]
	s_nop 0
	v_pk_mul_f32 v[100:101], v[100:101], v[122:123]
	s_nop 0
	v_cvt_pk_bf16_f32 v131, v100, v101
	v_mov_b64_e32 v[100:101], s[16:17]
	v_mad_i64_i32 v[120:121], s[28:29], v136, s2, v[100:101]
	v_lshl_add_u64 v[120:121], v[120:121], 0, v[102:103]
	global_store_dwordx4 v[120:121], v[128:131], off
	v_mul_f32_e32 v120, 0xbfb8aa3b, v116
	v_mul_f32_e32 v121, 0xbfb8aa3b, v117
	v_exp_f32_e32 v120, v120
	v_exp_f32_e32 v121, v121
	v_add_f32_e32 v120, 1.0, v120
	v_add_f32_e32 v121, 1.0, v121
	v_rcp_f32_e32 v120, v120
	v_rcp_f32_e32 v121, v121
	s_nop 0
	v_pk_mul_f32 v[116:117], v[116:117], v[120:121]
	s_nop 0
	v_pk_mul_f32 v[112:113], v[116:117], v[112:113]
	s_nop 0
	v_cvt_pk_bf16_f32 v112, v112, v113
	v_mul_f32_e32 v113, 0xbfb8aa3b, v118
	v_exp_f32_e32 v113, v113
	s_nop 0
	v_add_f32_e32 v113, 1.0, v113
	v_rcp_f32_e32 v116, v113
	v_mul_f32_e32 v113, 0xbfb8aa3b, v119
	v_exp_f32_e32 v113, v113
	s_nop 0
	v_add_f32_e32 v113, 1.0, v113
	v_rcp_f32_e32 v117, v113
	s_nop 0
	v_pk_mul_f32 v[116:117], v[118:119], v[116:117]
	s_nop 0
	v_pk_mul_f32 v[114:115], v[116:117], v[114:115]
	s_nop 0
	v_cvt_pk_bf16_f32 v113, v114, v115
	v_mul_f32_e32 v114, 0xbfb8aa3b, v108
	v_mul_f32_e32 v115, 0xbfb8aa3b, v109
	v_exp_f32_e32 v114, v114
	v_exp_f32_e32 v115, v115
	v_add_f32_e32 v114, 1.0, v114
	v_add_f32_e32 v115, 1.0, v115
	v_rcp_f32_e32 v114, v114
	v_rcp_f32_e32 v115, v115
	s_nop 0
	v_pk_mul_f32 v[108:109], v[108:109], v[114:115]
	s_nop 0
	v_pk_mul_f32 v[104:105], v[108:109], v[104:105]
	s_nop 0
	v_cvt_pk_bf16_f32 v114, v104, v105
	v_mul_f32_e32 v104, 0xbfb8aa3b, v110
	v_mul_f32_e32 v105, 0xbfb8aa3b, v111
	v_exp_f32_e32 v104, v104
	v_exp_f32_e32 v105, v105
	v_add_f32_e32 v104, 1.0, v104
	v_add_f32_e32 v105, 1.0, v105
	v_rcp_f32_e32 v104, v104
	v_rcp_f32_e32 v105, v105
	s_nop 0
	v_pk_mul_f32 v[104:105], v[110:111], v[104:105]
	s_nop 0
	v_pk_mul_f32 v[104:105], v[104:105], v[106:107]
	s_nop 0
	v_cvt_pk_bf16_f32 v115, v104, v105
	v_or_b32_e32 v104, 16, v136
	v_mad_i64_i32 v[104:105], s[28:29], v104, s2, v[100:101]
	v_lshl_add_u64 v[104:105], v[104:105], 0, v[102:103]
	global_store_dwordx4 v[104:105], v[112:115], off
	v_mul_f32_e32 v104, 0xbfb8aa3b, v94
	v_mul_f32_e32 v105, 0xbfb8aa3b, v95
	v_exp_f32_e32 v104, v104
	v_exp_f32_e32 v105, v105
	v_add_f32_e32 v104, 1.0, v104
	v_add_f32_e32 v105, 1.0, v105
	v_rcp_f32_e32 v104, v104
	v_rcp_f32_e32 v105, v105
	s_nop 0
	v_pk_mul_f32 v[94:95], v[94:95], v[104:105]
	s_nop 0
	v_pk_mul_f32 v[90:91], v[94:95], v[90:91]
	s_nop 0
	v_cvt_pk_bf16_f32 v90, v90, v91
	v_mul_f32_e32 v91, 0xbfb8aa3b, v96
	v_exp_f32_e32 v91, v91
	s_nop 0
	v_add_f32_e32 v91, 1.0, v91
	v_rcp_f32_e32 v94, v91
	v_mul_f32_e32 v91, 0xbfb8aa3b, v97
	v_exp_f32_e32 v91, v91
	s_nop 0
	v_add_f32_e32 v91, 1.0, v91
	v_rcp_f32_e32 v95, v91
	s_nop 0
	v_pk_mul_f32 v[94:95], v[96:97], v[94:95]
	s_nop 0
	v_pk_mul_f32 v[92:93], v[94:95], v[92:93]
	s_nop 0
	v_cvt_pk_bf16_f32 v91, v92, v93
	v_mul_f32_e32 v92, 0xbfb8aa3b, v86
	v_mul_f32_e32 v93, 0xbfb8aa3b, v87
	v_exp_f32_e32 v92, v92
	v_exp_f32_e32 v93, v93
	v_add_f32_e32 v92, 1.0, v92
	v_add_f32_e32 v93, 1.0, v93
	v_rcp_f32_e32 v92, v92
	v_rcp_f32_e32 v93, v93
	s_nop 0
	v_pk_mul_f32 v[86:87], v[86:87], v[92:93]
	s_nop 0
	v_pk_mul_f32 v[82:83], v[86:87], v[82:83]
	s_nop 0
	v_cvt_pk_bf16_f32 v92, v82, v83
	v_mul_f32_e32 v82, 0xbfb8aa3b, v88
	v_mul_f32_e32 v83, 0xbfb8aa3b, v89
	v_exp_f32_e32 v82, v82
	v_exp_f32_e32 v83, v83
	v_add_f32_e32 v82, 1.0, v82
	v_add_f32_e32 v83, 1.0, v83
	v_rcp_f32_e32 v82, v82
	v_rcp_f32_e32 v83, v83
	s_nop 0
	v_pk_mul_f32 v[82:83], v[88:89], v[82:83]
	s_nop 0
	v_pk_mul_f32 v[82:83], v[82:83], v[84:85]
	s_nop 0
	v_cvt_pk_bf16_f32 v93, v82, v83
	v_or_b32_e32 v82, 32, v136
	v_mad_i64_i32 v[82:83], s[28:29], v82, s2, v[100:101]
	v_lshl_add_u64 v[82:83], v[82:83], 0, v[102:103]
	global_store_dwordx4 v[82:83], v[90:93], off
	v_mul_f32_e32 v82, 0xbfb8aa3b, v78
	v_mul_f32_e32 v83, 0xbfb8aa3b, v79
	v_exp_f32_e32 v82, v82
	v_exp_f32_e32 v83, v83
; __device__ __forceinline__ unsigned pk2(float lo, float hi) { f32x2 v = {lo, hi}; return __builtin_bit_cast(unsigned, __builtin_convertvector(v, bf2_t)); }
; template <int BIT = 0> __device__ __forceinline__ void st16w(void* p, u32x4 v) { if ((WT_STORES >> BIT) & 1) asm volatile("global_store_dwordx4 %0, %1, off sc1\n\ts_nop 1" :: "v"(p), "v"(v) : "memory"); else *(u32x4*)p = v; }
; __device__ __forceinline__ float fsilu(float x) { return x * fsigm(x); }
;     __device__ __forceinline__ void operator()(const f32x4 (&acc)[2][2][4][2], const Unit& u, int wr, int wc, int fr, int fq) const {
;         const int row0 = u.pm * BM + wr * 64 + fr, col0 = u.pn * HALF + wc * 32 + 8 * fq;
; #pragma unroll
;         for (int ai = 0; ai < 2; ++ai)
; #pragma unroll
;             for (int m = 0; m < 4; ++m) {
;                 const f32x4 g0 = acc[ai][0][m][0], g1 = acc[ai][0][m][1], u0 = acc[ai][1][m][0], u1 = acc[ai][1][m][1];
;                 u32x4 w; w.x = pk2(fsilu(g0[0]) * u0[0], fsilu(g0[1]) * u0[1]); w.y = pk2(fsilu(g0[2]) * u0[2], fsilu(g0[3]) * u0[3]);
;                 w.z = pk2(fsilu(g1[0]) * u1[0], fsilu(g1[1]) * u1[1]); w.w = pk2(fsilu(g1[2]) * u1[2], fsilu(g1[3]) * u1[3]);
;                 bf16* dst = HID + (size_t)(row0 + ai * HALF + m * 16) * ldh + col0;
;                 if (wt) asm volatile("global_store_dwordx4 %0, %1, off sc1\n\ts_nop 1" :: "v"(dst), "v"(w) : "memory");
;                 else st16w(dst, w);
;             }
	v_add_f32_e32 v82, 1.0, v82
	v_add_f32_e32 v83, 1.0, v83
	v_rcp_f32_e32 v82, v82
	v_rcp_f32_e32 v83, v83
	s_nop 0
	v_pk_mul_f32 v[78:79], v[78:79], v[82:83]
	s_nop 0
	v_pk_mul_f32 v[74:75], v[78:79], v[74:75]
	s_nop 0
	v_cvt_pk_bf16_f32 v74, v74, v75
	v_mul_f32_e32 v75, 0xbfb8aa3b, v80
	v_exp_f32_e32 v75, v75
	s_nop 0
	v_add_f32_e32 v75, 1.0, v75
	v_rcp_f32_e32 v78, v75
	v_mul_f32_e32 v75, 0xbfb8aa3b, v81
	v_exp_f32_e32 v75, v75
	s_nop 0
	v_add_f32_e32 v75, 1.0, v75
	v_rcp_f32_e32 v79, v75
	s_nop 0
	v_pk_mul_f32 v[78:79], v[80:81], v[78:79]
	s_nop 0
	v_pk_mul_f32 v[76:77], v[78:79], v[76:77]
	s_nop 0
	v_cvt_pk_bf16_f32 v75, v76, v77
	v_mul_f32_e32 v76, 0xbfb8aa3b, v70
	v_mul_f32_e32 v77, 0xbfb8aa3b, v71
	v_exp_f32_e32 v76, v76
	v_exp_f32_e32 v77, v77
	v_add_f32_e32 v76, 1.0, v76
	v_add_f32_e32 v77, 1.0, v77
	v_rcp_f32_e32 v76, v76
	v_rcp_f32_e32 v77, v77
	s_nop 0
	v_pk_mul_f32 v[70:71], v[70:71], v[76:77]
	s_nop 0
	v_pk_mul_f32 v[66:67], v[70:71], v[66:67]
	s_nop 0
	v_cvt_pk_bf16_f32 v76, v66, v67
	v_mul_f32_e32 v66, 0xbfb8aa3b, v72
	v_mul_f32_e32 v67, 0xbfb8aa3b, v73
	v_exp_f32_e32 v66, v66
	v_exp_f32_e32 v67, v67
	v_add_f32_e32 v66, 1.0, v66
	v_add_f32_e32 v67, 1.0, v67
	v_rcp_f32_e32 v66, v66
	v_rcp_f32_e32 v67, v67
	s_nop 0
	v_pk_mul_f32 v[66:67], v[72:73], v[66:67]
	s_nop 0
	v_pk_mul_f32 v[66:67], v[66:67], v[68:69]
	v_add_u32_e32 v68, 0x80, v136
	v_cvt_pk_bf16_f32 v77, v66, v67
	v_or_b32_e32 v66, 48, v136
	v_mad_i64_i32 v[66:67], s[28:29], v66, s2, v[100:101]
	v_lshl_add_u64 v[66:67], v[66:67], 0, v[102:103]
	global_store_dwordx4 v[66:67], v[74:77], off
	v_mul_f32_e32 v66, 0xbfb8aa3b, v62
	v_mul_f32_e32 v67, 0xbfb8aa3b, v63
	v_exp_f32_e32 v66, v66
	v_exp_f32_e32 v67, v67
	v_add_f32_e32 v66, 1.0, v66
	v_add_f32_e32 v67, 1.0, v67
	v_rcp_f32_e32 v66, v66
	v_rcp_f32_e32 v67, v67
	s_nop 0
	v_pk_mul_f32 v[62:63], v[62:63], v[66:67]
	s_nop 0
	v_pk_mul_f32 v[58:59], v[62:63], v[58:59]
	s_nop 0
	v_cvt_pk_bf16_f32 v58, v58, v59
	v_mul_f32_e32 v59, 0xbfb8aa3b, v64
	v_exp_f32_e32 v59, v59
	s_nop 0
	v_add_f32_e32 v59, 1.0, v59
	v_rcp_f32_e32 v62, v59
	v_mul_f32_e32 v59, 0xbfb8aa3b, v65
	v_exp_f32_e32 v59, v59
	s_nop 0
	v_add_f32_e32 v59, 1.0, v59
	v_rcp_f32_e32 v63, v59
	s_nop 0
	v_pk_mul_f32 v[62:63], v[64:65], v[62:63]
	s_nop 0
	v_pk_mul_f32 v[60:61], v[62:63], v[60:61]
	s_nop 0
	v_cvt_pk_bf16_f32 v59, v60, v61
	v_mul_f32_e32 v60, 0xbfb8aa3b, v54
	v_mul_f32_e32 v61, 0xbfb8aa3b, v55
	v_exp_f32_e32 v60, v60
	v_exp_f32_e32 v61, v61
	v_add_f32_e32 v60, 1.0, v60
	v_add_f32_e32 v61, 1.0, v61
	v_rcp_f32_e32 v60, v60
	v_rcp_f32_e32 v61, v61
	s_nop 0
	v_pk_mul_f32 v[54:55], v[54:55], v[60:61]
	s_nop 0
	v_pk_mul_f32 v[50:51], v[54:55], v[50:51]
	s_nop 0
	v_cvt_pk_bf16_f32 v60, v50, v51
	v_mul_f32_e32 v50, 0xbfb8aa3b, v56
	v_mul_f32_e32 v51, 0xbfb8aa3b, v57
	v_exp_f32_e32 v50, v50
	v_exp_f32_e32 v51, v51
	v_add_f32_e32 v50, 1.0, v50
	v_add_f32_e32 v51, 1.0, v51
	v_rcp_f32_e32 v50, v50
	v_rcp_f32_e32 v51, v51
	s_nop 0
	v_pk_mul_f32 v[50:51], v[56:57], v[50:51]
	s_nop 0
	v_pk_mul_f32 v[50:51], v[50:51], v[52:53]
	s_nop 0
	v_cvt_pk_bf16_f32 v61, v50, v51
	v_mad_i64_i32 v[50:51], s[28:29], v68, s2, v[100:101]
	v_lshl_add_u64 v[50:51], v[50:51], 0, v[102:103]
	global_store_dwordx4 v[50:51], v[58:61], off
	v_mul_f32_e32 v50, 0xbfb8aa3b, v46
	v_mul_f32_e32 v51, 0xbfb8aa3b, v47
	v_exp_f32_e32 v50, v50
	v_exp_f32_e32 v51, v51
	v_add_f32_e32 v50, 1.0, v50
	v_add_f32_e32 v51, 1.0, v51
	v_rcp_f32_e32 v50, v50
	v_rcp_f32_e32 v51, v51
	s_nop 0
	v_pk_mul_f32 v[46:47], v[46:47], v[50:51]
	s_nop 0
	v_pk_mul_f32 v[42:43], v[46:47], v[42:43]
	s_nop 0
	v_cvt_pk_bf16_f32 v42, v42, v43
	v_mul_f32_e32 v43, 0xbfb8aa3b, v48
	v_exp_f32_e32 v43, v43
	s_nop 0
	v_add_f32_e32 v43, 1.0, v43
	v_rcp_f32_e32 v46, v43
	v_mul_f32_e32 v43, 0xbfb8aa3b, v49
	v_exp_f32_e32 v43, v43
	s_nop 0
	v_add_f32_e32 v43, 1.0, v43
	v_rcp_f32_e32 v47, v43
	s_nop 0
	v_pk_mul_f32 v[46:47], v[48:49], v[46:47]
	s_nop 0
	v_pk_mul_f32 v[44:45], v[46:47], v[44:45]
	s_nop 0
	v_cvt_pk_bf16_f32 v43, v44, v45
	v_mul_f32_e32 v44, 0xbfb8aa3b, v38
	v_mul_f32_e32 v45, 0xbfb8aa3b, v39
	v_exp_f32_e32 v44, v44
	v_exp_f32_e32 v45, v45
	v_add_f32_e32 v44, 1.0, v44
	v_add_f32_e32 v45, 1.0, v45
	v_rcp_f32_e32 v44, v44
; __device__ __forceinline__ unsigned pk2(float lo, float hi) { f32x2 v = {lo, hi}; return __builtin_bit_cast(unsigned, __builtin_convertvector(v, bf2_t)); }
; template <int BIT = 0> __device__ __forceinline__ void st16w(void* p, u32x4 v) { if ((WT_STORES >> BIT) & 1) asm volatile("global_store_dwordx4 %0, %1, off sc1\n\ts_nop 1" :: "v"(p), "v"(v) : "memory"); else *(u32x4*)p = v; }
; __device__ __forceinline__ float fsilu(float x) { return x * fsigm(x); }
; #define PG8_LAS __attribute__((address_space(3)))
; #define PG8_BAR __builtin_amdgcn_s_barrier()
;     __device__ __forceinline__ void operator()(const f32x4 (&acc)[2][2][4][2], const Unit& u, int wr, int wc, int fr, int fq) const {
;     ...
;                 const f32x4 g0 = acc[ai][0][m][0], g1 = acc[ai][0][m][1], u0 = acc[ai][1][m][0], u1 = acc[ai][1][m][1];
;                 u32x4 w; w.x = pk2(fsilu(g0[0]) * u0[0], fsilu(g0[1]) * u0[1]); w.y = pk2(fsilu(g0[2]) * u0[2], fsilu(g0[3]) * u0[3]);
;                 w.z = pk2(fsilu(g1[0]) * u1[0], fsilu(g1[1]) * u1[1]); w.w = pk2(fsilu(g1[2]) * u1[2], fsilu(g1[3]) * u1[3]);
;                 bf16* dst = HID + (size_t)(row0 + ai * HALF + m * 16) * ldh + col0;
;                 if (wt) asm volatile("global_store_dwordx4 %0, %1, off sc1\n\ts_nop 1" :: "v"(dst), "v"(w) : "memory");
;                 else st16w(dst, w);
;             }
; template <class Epi, class Sched, bool ALIGN_EPI = false, bool SP2 = false>
; __device__ __forceinline__ void gemm_phase(PG8_LAS unsigned char* lds, const Gemm g, const Sched& S, const Epi& E) {
;     ...
;         cur = nxt; cA = nA; cB = nB; ++ui;
;         if constexpr (Sched::GATHER) { const u32x4 pv_ = *(const PG8_LAS u32x4*)(lds + STAGE_BYTES + tid * 16); vAc[0][0] = pv_.x; vAc[0][1] = pv_.y; vAc[1][0] = pv_.z; vAc[1][1] = pv_.w; }
;         if constexpr (ALIGN_EPI) { if (wr == 1) PG8_BAR; }
	v_rcp_f32_e32 v45, v45
	s_nop 0
	v_pk_mul_f32 v[38:39], v[38:39], v[44:45]
	s_nop 0
	v_pk_mul_f32 v[34:35], v[38:39], v[34:35]
	s_nop 0
	v_cvt_pk_bf16_f32 v44, v34, v35
	v_mul_f32_e32 v34, 0xbfb8aa3b, v40
	v_mul_f32_e32 v35, 0xbfb8aa3b, v41
	v_exp_f32_e32 v34, v34
	v_exp_f32_e32 v35, v35
	v_add_f32_e32 v34, 1.0, v34
	v_add_f32_e32 v35, 1.0, v35
	v_rcp_f32_e32 v34, v34
	v_rcp_f32_e32 v35, v35
	s_nop 0
	v_pk_mul_f32 v[34:35], v[40:41], v[34:35]
	s_nop 0
	v_pk_mul_f32 v[34:35], v[34:35], v[36:37]
	s_nop 0
	v_cvt_pk_bf16_f32 v45, v34, v35
	v_add_u32_e32 v34, 0x90, v136
	v_mad_i64_i32 v[34:35], s[28:29], v34, s2, v[100:101]
	v_lshl_add_u64 v[34:35], v[34:35], 0, v[102:103]
	global_store_dwordx4 v[34:35], v[42:45], off
	v_mul_f32_e32 v34, 0xbfb8aa3b, v30
	v_mul_f32_e32 v35, 0xbfb8aa3b, v31
	v_exp_f32_e32 v34, v34
	v_exp_f32_e32 v35, v35
	v_add_f32_e32 v34, 1.0, v34
	v_add_f32_e32 v35, 1.0, v35
	v_rcp_f32_e32 v34, v34
	v_rcp_f32_e32 v35, v35
	s_nop 0
	v_pk_mul_f32 v[30:31], v[30:31], v[34:35]
	s_nop 0
	v_pk_mul_f32 v[26:27], v[30:31], v[26:27]
	s_nop 0
	v_cvt_pk_bf16_f32 v26, v26, v27
	v_mul_f32_e32 v27, 0xbfb8aa3b, v32
	v_exp_f32_e32 v27, v27
	s_nop 0
	v_add_f32_e32 v27, 1.0, v27
	v_rcp_f32_e32 v30, v27
	v_mul_f32_e32 v27, 0xbfb8aa3b, v33
	v_exp_f32_e32 v27, v27
	s_nop 0
	v_add_f32_e32 v27, 1.0, v27
	v_rcp_f32_e32 v31, v27
	s_nop 0
	v_pk_mul_f32 v[30:31], v[32:33], v[30:31]
	s_nop 0
	v_pk_mul_f32 v[28:29], v[30:31], v[28:29]
	s_nop 0
	v_cvt_pk_bf16_f32 v27, v28, v29
	v_mul_f32_e32 v28, 0xbfb8aa3b, v22
	v_mul_f32_e32 v29, 0xbfb8aa3b, v23
	v_exp_f32_e32 v28, v28
	v_exp_f32_e32 v29, v29
	v_add_f32_e32 v28, 1.0, v28
	v_add_f32_e32 v29, 1.0, v29
	v_rcp_f32_e32 v28, v28
	v_rcp_f32_e32 v29, v29
	s_nop 0
	v_pk_mul_f32 v[22:23], v[22:23], v[28:29]
	s_nop 0
	v_pk_mul_f32 v[18:19], v[22:23], v[18:19]
	s_nop 0
	v_cvt_pk_bf16_f32 v28, v18, v19
	v_mul_f32_e32 v18, 0xbfb8aa3b, v24
	v_mul_f32_e32 v19, 0xbfb8aa3b, v25
	v_exp_f32_e32 v18, v18
	v_exp_f32_e32 v19, v19
	v_add_f32_e32 v18, 1.0, v18
	v_add_f32_e32 v19, 1.0, v19
	v_rcp_f32_e32 v18, v18
	v_rcp_f32_e32 v19, v19
	s_nop 0
	v_pk_mul_f32 v[18:19], v[24:25], v[18:19]
	s_nop 0
	v_pk_mul_f32 v[18:19], v[18:19], v[20:21]
	s_nop 0
	v_cvt_pk_bf16_f32 v29, v18, v19
	v_add_u32_e32 v18, 0xa0, v136
	v_mad_i64_i32 v[18:19], s[28:29], v18, s2, v[100:101]
	v_lshl_add_u64 v[18:19], v[18:19], 0, v[102:103]
	global_store_dwordx4 v[18:19], v[26:29], off
	v_mul_f32_e32 v18, 0xbfb8aa3b, v14
	v_mul_f32_e32 v19, 0xbfb8aa3b, v15
	v_exp_f32_e32 v18, v18
	v_exp_f32_e32 v19, v19
	v_add_f32_e32 v18, 1.0, v18
	v_add_f32_e32 v19, 1.0, v19
	v_rcp_f32_e32 v18, v18
	v_rcp_f32_e32 v19, v19
	s_nop 0
	v_pk_mul_f32 v[14:15], v[14:15], v[18:19]
	s_nop 0
	v_pk_mul_f32 v[10:11], v[14:15], v[10:11]
	s_nop 0
	v_cvt_pk_bf16_f32 v10, v10, v11
	v_mul_f32_e32 v11, 0xbfb8aa3b, v16
	v_exp_f32_e32 v11, v11
	s_nop 0
	v_add_f32_e32 v11, 1.0, v11
	v_rcp_f32_e32 v14, v11
	v_mul_f32_e32 v11, 0xbfb8aa3b, v17
	v_exp_f32_e32 v11, v11
	s_nop 0
	v_add_f32_e32 v11, 1.0, v11
	v_rcp_f32_e32 v15, v11
	s_nop 0
	v_pk_mul_f32 v[14:15], v[16:17], v[14:15]
	s_nop 0
	v_pk_mul_f32 v[12:13], v[14:15], v[12:13]
	s_nop 0
	v_cvt_pk_bf16_f32 v11, v12, v13
	v_mul_f32_e32 v12, 0xbfb8aa3b, v6
	v_mul_f32_e32 v13, 0xbfb8aa3b, v7
	v_exp_f32_e32 v12, v12
	v_exp_f32_e32 v13, v13
	v_add_f32_e32 v12, 1.0, v12
	v_add_f32_e32 v13, 1.0, v13
	v_rcp_f32_e32 v12, v12
	v_rcp_f32_e32 v13, v13
	s_nop 0
	v_pk_mul_f32 v[6:7], v[6:7], v[12:13]
	s_nop 0
	v_pk_mul_f32 v[2:3], v[6:7], v[2:3]
	s_nop 0
	v_cvt_pk_bf16_f32 v12, v2, v3
	v_mul_f32_e32 v2, 0xbfb8aa3b, v8
	v_mul_f32_e32 v3, 0xbfb8aa3b, v9
	v_exp_f32_e32 v2, v2
	v_exp_f32_e32 v3, v3
	v_add_f32_e32 v2, 1.0, v2
	v_add_f32_e32 v3, 1.0, v3
	v_rcp_f32_e32 v2, v2
	v_rcp_f32_e32 v3, v3
	s_nop 0
	v_pk_mul_f32 v[2:3], v[8:9], v[2:3]
	s_nop 0
	v_pk_mul_f32 v[2:3], v[2:3], v[4:5]
	s_nop 0
	v_cvt_pk_bf16_f32 v13, v2, v3
	v_add_u32_e32 v2, 0xb0, v136
	v_mad_i64_i32 v[2:3], s[28:29], v2, s2, v[100:101]
	v_lshl_add_u64 v[2:3], v[2:3], 0, v[102:103]
	s_mov_b64 s[28:29], -1
	global_store_dwordx4 v[2:3], v[10:13], off
	s_cbranch_vccnz .LBB13_1432
	ds_read_b128 v[2:5], v248
	s_andn2_b64 vcc, exec, s[18:19]
	s_cbranch_vccnz .LBB13_1431
	s_branch .LBB13_1431

; #define PG8_STAGE(bufoff, gbase, voff) PG8_STAGE_X(bufoff, gbase, voff, PG8_B_AUX)
; template <class Epi, class Sched, bool ALIGN_EPI = false, bool SP2 = false>
; __device__ __forceinline__ void gemm_phase(PG8_LAS unsigned char* lds, const Gemm g, const Sched& S, const Epi& E) {
;     ...
;     for (int i = 0; i < 2; ++i) { int R, C; stage_rc(tid * 16 + i * 8192, R, C); const int Rb = Epi::PERM ? ((R & ~31) + perm32(R & 31)) : R;
;         voffA[i] = (unsigned)(R * K + C) * 2u; voffB[i] = (unsigned)(Rb * K + C) * 2u; }
;     unsigned vAc[2][2] = {{0u, 0u}, {0u, 0u}}, vAn[2][2] = {{0u, 0u}, {0u, 0u}};
;     ...
;     const size_t kstep = (size_t)(BK * 2);
;     const size_t hstep = (size_t)HALF * K * 2;
;     const size_t tstep = 2 * hstep;
;     const unsigned ldsw = (unsigned)wid * 1024u;
;     const int aoff = lds_byte(wr * 64 + fr, fq * 8), boff = lds_byte(wc * 32 + fr, fq * 8);
;     ...
;     Unit cur, nxt; int ui = 0;
;     if (!S.next(0, cur)) return;
;     f32x4 acc[2][2][4][2];
; #pragma unroll
;     for (int a = 0; a < 2; ++a)
; #pragma unroll
;         for (int b = 0; b < 2; ++b)
; #pragma unroll
;             for (int m = 0; m < 4; ++m)
; #pragma unroll
;                 for (int n = 0; n < 2; ++n) acc[a][b][m][n] = (f32x4){0.f, 0.f, 0.f, 0.f};
;     bf16x8 At[4][2], B0[2][2], B1[2][2];
;     const char* cA = Sched::GATHER ? (const char*)g.A : (const char*)g.A + (size_t)cur.pm * tstep; PG8_SETA(vAc, cur); const char* cB = (const char*)g.Bt + S.boff(cur) + (size_t)cur.pn * tstep;
;     S.a_ready(cur);
;     if constexpr (SP2) {
;         PG8_STAGE(PG8_SB(0, 0), cB, voffB); PG8_STAGE(PG8_SB(0, 1), cB + hstep, voffB); PG8_STAGE_A(PG8_SA(0, 0), 0, cA, false); PG8_STAGE_A(PG8_SA(0, 1), 1, cA, false);
;         if (wr == 1) PG8_BAR;
;         PG8_WAIT_V(2); PG8_BAR;
;         PG8_STAGE(PG8_SB(1, 0), cB + kstep, voffB); PG8_STAGE_A(PG8_SA(1, 0), 0, cA + kstep, false); PG8_STAGE(PG8_SB(1, 1), cB + hstep + kstep, voffB);
;         PG8_WAIT_V(6); PG8_BAR;
;     } else {
;         PG8_STAGE(PG8_SB(0, 0), cB, voffB); PG8_STAGE_A(PG8_SA(0, 0), 0, cA, false); PG8_STAGE(PG8_SB(0, 1), cB + hstep, voffB); PG8_STAGE_A(PG8_SA(0, 1), 1, cA, false);
;         if (wr == 1) PG8_BAR;
;         PG8_WAIT_V(4); PG8_BAR;
;         PG8_STAGE(PG8_SB(1, 0), cB + kstep, voffB); PG8_STAGE_A(PG8_SA(1, 0), 0, cA + kstep, false); PG8_STAGE(PG8_SB(1, 1), cB + hstep + kstep, voffB);
.LBB13_1522:
	v_ashrrev_i32_e32 v3, 31, v18
	v_lshrrev_b32_e32 v3, 26, v3
	v_add_u32_e32 v3, v18, v3
	v_ashrrev_i32_e32 v10, 6, v3
	v_bfe_i32 v3, v18, 27, 1
	v_lshlrev_b32_e32 v2, 4, v18
	v_lshrrev_b32_e32 v3, 22, v3
	v_add_u32_e32 v3, v2, v3
	v_and_b32_e32 v3, 0xfffffc00, v3
	v_sub_u32_e32 v3, v2, v3
	v_lshrrev_b32_e32 v4, 4, v3
	v_bitop3_b32 v3, v4, v3, 32 bitop3:0x6c
	v_ashrrev_i32_e32 v5, 31, v3
	v_lshrrev_b32_e32 v5, 26, v5
	v_lshlrev_b32_e32 v4, 3, v10
	v_add_u32_e32 v5, v3, v5
	v_and_b32_e32 v4, -16, v4
	v_ashrrev_i32_e32 v12, 6, v5
	v_and_b32_e32 v5, 0xc0, v5
	v_add_u32_e32 v4, v12, v4
	v_lshlrev_b32_e32 v6, 5, v10
	v_sub_u32_e32 v3, v3, v5
	s_ashr_i32 s4, s7, 3
	v_and_b32_e32 v11, 32, v6
	v_ashrrev_i16_sdwa v3, v238, sext(v3) dst_sel:DWORD dst_unused:UNUSED_PAD src0_sel:DWORD src1_sel:BYTE_0
	v_lshlrev_b32_e32 v5, 1, v4
	v_lshrrev_b32_e32 v6, 2, v4
	v_and_b32_e32 v7, 3, v12
	s_mov_b32 s7, 0xffffe0
	s_lshr_b32 s5, s10, 31
	v_bfe_i32 v13, v3, 0, 16
	v_and_b32_e32 v5, 24, v5
	v_and_b32_e32 v6, 4, v6
	v_and_or_b32 v7, v4, s7, v7
	s_movk_i32 s10, 0xb00
	v_add_u32_e32 v3, v11, v13
	v_or3_b32 v5, v7, v6, v5
	v_mul_lo_u32 v4, v4, s10
	v_add_lshl_u32 v148, v3, v4, 1
	v_mul_u32_u24_e32 v4, 0xb00, v5
	v_add_u32_e32 v2, 0x2000, v2
	v_add_lshl_u32 v150, v4, v3, 1
	v_ashrrev_i32_e32 v3, 31, v2
	v_lshrrev_b32_e32 v3, 22, v3
	v_add_u32_e32 v3, v2, v3
	v_ashrrev_i32_e32 v14, 10, v3
	v_mul_i32_i24_e32 v3, 0x400, v14
	v_sub_u32_e32 v2, v2, v3
	v_lshrrev_b32_e32 v3, 4, v2
	v_bitop3_b32 v2, v3, v2, 32 bitop3:0x6c
	v_ashrrev_i32_e32 v4, 31, v2
	v_lshrrev_b32_e32 v4, 26, v4
	v_lshlrev_b32_e32 v3, 3, v14
	v_add_u32_e32 v4, v2, v4
	s_sub_i32 s4, s5, s4
	v_and_b32_e32 v3, -16, v3
	v_ashrrev_i32_e32 v16, 6, v4
	s_add_i32 s5, s4, s11
	v_add_u32_e32 v3, v16, v3
	v_lshlrev_b32_e32 v5, 5, v14
	v_and_b32_e32 v4, 0xc0, v4
	v_and_b32_e32 v6, 3, v16
	v_and_b32_e32 v15, 32, v5
	v_sub_u32_e32 v2, v2, v4
	v_lshlrev_b32_e32 v4, 1, v3
	v_lshrrev_b32_e32 v5, 2, v3
	v_and_or_b32 v6, v3, s7, v6
	v_mul_lo_u32 v3, v3, s10
	s_add_i32 s10, s5, 31
	s_ashr_i32 s5, s10, 31
	s_lshr_b32 s5, s5, 28
	s_add_i32 s11, s10, s5
	s_ashr_i32 s5, s11, 4
	s_lshl_b32 s12, s5, 2
	v_ashrrev_i16_sdwa v2, v238, sext(v2) dst_sel:DWORD dst_unused:UNUSED_PAD src0_sel:DWORD src1_sel:BYTE_0
	s_sub_i32 s5, 64, s12
	v_bfe_i32 v17, v2, 0, 16
	v_and_b32_e32 v4, 24, v4
	v_and_b32_e32 v5, 4, v5
	s_min_i32 s13, s5, 4
	v_add_u32_e32 v2, v15, v17
	v_or3_b32 v4, v6, v5, v4
	s_abs_i32 s14, s13
	v_add_lshl_u32 v152, v2, v3, 1
	v_mul_u32_u24_e32 v3, 0xb00, v4
	v_cvt_f32_u32_e32 v4, s14
	v_add_lshl_u32 v154, v3, v2, 1
	s_sub_i32 s16, 0, s14
	s_and_b32 s11, s11, -16
	v_rcp_iflag_f32_e32 v2, v4
	s_sub_i32 s10, s10, s11
	s_abs_i32 s15, s10
	s_ashr_i32 s4, s6, 6
	v_mul_f32_e32 v2, 0x4f7ffffe, v2
	v_cvt_u32_f32_e32 v2, v2
	s_xor_b32 s11, s10, s13
	s_ashr_i32 s7, s6, 8
	s_lshl_b32 s5, s4, 10
	v_readfirstlane_b32 s17, v2
	s_mul_i32 s16, s16, s17
	s_mul_hi_u32 s16, s17, s16
	s_add_i32 s17, s17, s16
	s_mul_hi_u32 s16, s15, s17
	s_mul_i32 s17, s16, s14
	s_sub_i32 s15, s15, s17
	s_ashr_i32 s11, s11, 31
	s_add_i32 s17, s16, 1
	s_sub_i32 s18, s15, s14
	s_cmp_ge_u32 s15, s14
	s_cselect_b32 s16, s17, s16
	s_cselect_b32 s15, s18, s15
	s_add_i32 s17, s16, 1
	s_cmp_ge_u32 s15, s14
	s_cselect_b32 s14, s17, s16
	s_xor_b32 s14, s14, s11
	s_sub_i32 s60, s14, s11
	s_mul_i32 s11, s60, s13
	s_sub_i32 s10, s10, s11
	s_add_i32 s52, s12, s10
	s_mul_i32 s11, s60, 0x160000
	s_mul_hi_i32 s10, s60, 0x160000
	s_add_u32 s18, s2, s11
	s_addc_u32 s19, s3, s10
	s_add_i32 s36, s31, 0x10000
	s_add_i32 s37, s36, s5
	s_add_i32 s38, s37, 0x2000
	s_add_u32 s10, s18, 0xb0000
	s_addc_u32 s11, s19, 0
	s_add_i32 s39, s31, 0x14000
	s_add_i32 s40, s39, s5
	s_mul_i32 s13, s52, 0x160000
	s_mov_b32 m0, s37
	s_add_i32 s41, s40, 0x2000
	s_mul_hi_i32 s12, s52, 0x160000
	global_load_lds_dwordx4 v150, s[18:19]
	s_mov_b32 m0, s38
	s_add_u32 s16, s25, s13
	global_load_lds_dwordx4 v154, s[18:19]
	s_mov_b32 m0, s40
	s_addc_u32 s17, s26, s12
	s_add_i32 s42, s31, s5
	global_load_lds_dwordx4 v150, s[10:11]
	s_mov_b32 m0, s41
	s_add_i32 s43, s42, 0x2000
	global_load_lds_dwordx4 v154, s[10:11]
	s_mov_b32 m0, s42
	s_add_u32 s10, s16, 0xb0000
	global_load_lds_dwordx4 v148, s[16:17]
	s_mov_b32 m0, s43
	s_addc_u32 s11, s17, 0
	s_add_i32 s44, s42, 0x4000
	global_load_lds_dwordx4 v152, s[16:17]
	s_mov_b32 m0, s44
	s_add_i32 s45, s42, 0x6000
	global_load_lds_dwordx4 v148, s[10:11]
	s_mov_b32 m0, s45
	v_mov_b32_e32 v151, v98
	global_load_lds_dwordx4 v152, s[10:11]
	v_mov_b32_e32 v155, v98
	v_mov_b32_e32 v149, v98
	v_mov_b32_e32 v153, v98
	s_cmp_eq_u32 s7, 1
	v_lshl_add_u64 v[8:9], s[18:19], 0, v[150:151]
	v_lshl_add_u64 v[6:7], s[18:19], 0, v[154:155]
	v_lshl_add_u64 v[2:3], s[16:17], 0, v[148:149]
	s_cselect_b64 s[10:11], -1, 0
	s_cmp_lg_u32 s7, 1
	v_lshl_add_u64 v[4:5], s[16:17], 0, v[152:153]
	s_cbranch_scc1 .LBB13_1524
.LBB13_1524:
	v_lshrrev_b32_e32 v20, 1, v18
	s_add_u32 s46, s27, 0x205000
	v_and_b32_e32 v20, 24, v20
	s_addc_u32 s47, s34, 0
	v_and_b32_e32 v19, 15, v18
	v_lshlrev_b32_e32 v21, 1, v20
	v_lshlrev_b32_e32 v18, 2, v18
	s_lshl_b32 s4, s4, 5
	s_add_i32 s48, s31, 0x18000
	v_lshl_or_b32 v166, s7, 6, v19
	v_lshl_or_b32 v19, v19, 6, v21
	s_lshl_b32 s7, s7, 13
	v_and_b32_e32 v18, 32, v18
	s_and_b32 s4, s4, 0x60
	s_add_i32 s49, s48, s5
	v_bitop3_b32 v21, v19, s7, v18 bitop3:0xde
	s_lshl_b32 s7, s4, 7
	v_lshl_add_u64 v[8:9], v[8:9], 0, s[54:55]
	s_mov_b32 m0, s49
	s_add_i32 s50, s49, 0x2000
	s_add_i32 s51, s42, 0x8000
	s_add_i32 s53, s42, 0xa000
	s_waitcnt vmcnt(2)
	s_barrier
	global_load_lds_dwordx4 v[8:9], off
	v_lshl_add_u64 v[6:7], v[6:7], 0, s[54:55]
	s_mov_b32 m0, s50
	s_add_u32 s12, s18, 0xb0080
	global_load_lds_dwordx4 v[6:7], off
	v_lshl_add_u64 v[2:3], v[2:3], 0, s[54:55]
	s_mov_b32 m0, s51
	s_addc_u32 s13, s19, 0
	s_add_i32 s56, s31, 0x1c000
	global_load_lds_dwordx4 v[2:3], off
	v_lshl_add_u64 v[2:3], v[4:5], 0, s[54:55]
	s_mov_b32 m0, s53
	s_add_i32 s57, s56, s5
	global_load_lds_dwordx4 v[2:3], off
	v_lshl_add_u64 v[2:3], s[12:13], 0, v[150:151]
	s_mov_b32 m0, s57
	s_add_i32 s58, s57, 0x2000
	global_load_lds_dwordx4 v[2:3], off
	v_lshl_add_u64 v[2:3], s[12:13], 0, v[154:155]
	s_mov_b32 m0, s58
	s_cmpk_lt_u32 s6, 0x100
	global_load_lds_dwordx4 v[2:3], off
	s_movk_i32 s6, 0xb00
	v_bitop3_b32 v167, v19, s7, v18 bitop3:0xde
	v_lshrrev_b32_e32 v3, 1, v10
	v_mul_lo_u32 v2, v12, s6
	s_mov_b32 s7, 0xb000
	v_or_b32_e32 v168, s4, v20
	v_mad_u64_u32 v[2:3], s[4:5], v3, s7, v[2:3]
	v_or_b32_e32 v2, v2, v11
	v_add_lshl_u32 v2, v2, v13, 1
	v_mov_b32_e32 v3, v98
	s_mov_b64 s[14:15], 0xb0080
	v_lshl_add_u64 v[156:157], v[2:3], 0, s[14:15]
	v_lshrrev_b32_e32 v3, 1, v14
	v_mul_lo_u32 v2, v16, s6
	v_mad_u64_u32 v[2:3], s[4:5], v3, s7, v[2:3]
	s_waitcnt vmcnt(6)
	v_or_b32_e32 v2, v2, v15
	v_add_lshl_u32 v2, v2, v17, 1
	v_mov_b32_e32 v3, v98
	s_cselect_b64 s[12:13], -1, 0
	s_ashr_i32 s59, s28, 31
	v_lshl_add_u64 v[158:159], v[2:3], 0, s[14:15]
	s_mov_b32 s61, 0
	v_add_u32_e32 v169, s31, v21
	s_barrier
	s_branch .LBB13_1527

; #define PG8_LAS __attribute__((address_space(3)))
; #define PG8_STAGE_A(bufoff, h, ptr, nsel) do { if constexpr (Sched::GATHER) { if (nsel) PG8_STAGE_X(bufoff, ptr, vAn[h], PG8_A_AUX); else PG8_STAGE_X(bufoff, ptr, vAc[h], PG8_A_AUX); } \
;         else PG8_STAGE_X(bufoff, (ptr) + (h) * hstep, voffA, PG8_A_AUX); } while (0)
; #define PG8_LDA(dst, b, h) do { _Pragma("unroll") for (int m = 0; m < 4; ++m) _Pragma("unroll") for (int k = 0; k < 2; ++k) dst[m][k] = *(const PG8_LAS bf16x8*)(lds + PG8_SA(b, h) + aoff + m * 2048 + k * 1024); } while (0)
; #define PG8_LDB(dst, b, h) do { _Pragma("unroll") for (int n = 0; n < 2; ++n) _Pragma("unroll") for (int k = 0; k < 2; ++k) dst[n][k] = *(const PG8_LAS bf16x8*)(lds + PG8_SB(b, h) + boff + n * 2048 + k * 1024); } while (0)
; #define PG8_MMA(ai, bj, At, Bt) do { __builtin_amdgcn_s_setprio(1); _Pragma("unroll") for (int m = 0; m < 4; ++m) _Pragma("unroll") for (int n = 0; n < 2; ++n) _Pragma("unroll") for (int k = 0; k < 2; ++k) \
;         acc[ai][bj][m][n] = __builtin_amdgcn_mfma_f32_16x16x32_bf16(Bt[n][k], At[m][k], acc[ai][bj][m][n], 0, 0, 0); __builtin_amdgcn_s_setprio(0); } while (0)
; template <class Epi, class Sched, bool ALIGN_EPI = false, bool SP2 = false>
; __device__ __forceinline__ void gemm_phase(PG8_LAS unsigned char* lds, const Gemm g, const Sched& S, const Epi& E) {
;     ...
;             const char* a2 = last ? nA : cA + (size_t)(t + 2) * kstep; const char* b2 = last ? nB : cB + (size_t)(t + 2) * kstep;
;             const char* a3 = a2 + kstep; const char* b3 = b2 + kstep;
;             if (last && has_next) S.a_ready(nxt);
;             if constexpr (Sched::GATHER) { if (last) { const u32x4 pv_ = *(const PG8_LAS u32x4*)(lds + STAGE_BYTES + tid * 16); vAn[0][0] = pv_.x; vAn[0][1] = pv_.y; vAn[1][0] = pv_.z; vAn[1][1] = pv_.w; } }
;             if constexpr (SP2) {
;             PG8_LDB(B0, 0, 0); PG8_LDB(B1, 0, 1); PG8_SCHED; PG8_LDA(At, 0, 0); PG8_STAGE_A(PG8_SA(1, 1), 1, a1, false);
;             PG8_WAIT_V(8); PG8_WAIT_L(0); PG8_BAR; PG8_MMA(0, 0, At, B0); PG8_MMA(0, 1, At, B1); PG8_BAR; PG8_SCHED;
;     ...
;         for (int a = 0; a < 2; ++a)
; #pragma unroll
;             for (int b = 0; b < 2; ++b)
; #pragma unroll
;                 for (int m = 0; m < 4; ++m)
; #pragma unroll
;                     for (int n = 0; n < 2; ++n) acc[a][b][m][n] = (f32x4){0.f, 0.f, 0.f, 0.f};
.LBB13_1537:
	s_add_u32 s64, s18, 0x100
	v_mov_b32_e32 v2, 0
	s_addc_u32 s72, s19, 0
	s_mov_b32 s73, -2
	v_mov_b32_e32 v3, v2
	v_mov_b64_e32 v[4:5], 0
	v_mov_b64_e32 v[6:7], 0
	v_mov_b64_e32 v[8:9], 0
	v_mov_b64_e32 v[18:19], 0
	v_mov_b64_e32 v[20:21], 0
	v_mov_b64_e32 v[22:23], 0
	v_mov_b64_e32 v[24:25], 0
	v_mov_b64_e32 v[34:35], 0
	v_mov_b64_e32 v[36:37], 0
	v_mov_b64_e32 v[38:39], 0
	v_mov_b64_e32 v[40:41], 0
	v_mov_b64_e32 v[66:67], 0
	v_mov_b64_e32 v[68:69], 0
	v_mov_b64_e32 v[70:71], 0
	v_mov_b64_e32 v[72:73], 0
	v_mov_b64_e32 v[10:11], 0
	v_mov_b64_e32 v[12:13], 0
	v_mov_b64_e32 v[14:15], 0
	v_mov_b64_e32 v[16:17], 0
	v_mov_b64_e32 v[26:27], 0
	v_mov_b64_e32 v[28:29], 0
	v_mov_b64_e32 v[30:31], 0
	v_mov_b64_e32 v[32:33], 0
	v_mov_b64_e32 v[46:47], 0
	v_mov_b64_e32 v[48:49], 0
	v_mov_b64_e32 v[54:55], 0
	v_mov_b64_e32 v[56:57], 0
	v_mov_b64_e32 v[74:75], 0
	v_mov_b64_e32 v[76:77], 0
	v_mov_b64_e32 v[78:79], 0
	v_mov_b64_e32 v[80:81], 0
	v_mov_b64_e32 v[82:83], 0
	v_mov_b64_e32 v[84:85], 0
	v_mov_b64_e32 v[86:87], 0
	v_mov_b64_e32 v[88:89], 0
	v_mov_b64_e32 v[100:101], 0
	v_mov_b64_e32 v[102:103], 0
	v_mov_b64_e32 v[104:105], 0
	v_mov_b64_e32 v[106:107], 0
	v_mov_b64_e32 v[116:117], 0
	v_mov_b64_e32 v[118:119], 0
	v_mov_b64_e32 v[120:121], 0
	v_mov_b64_e32 v[122:123], 0
	v_mov_b64_e32 v[132:133], 0
	v_mov_b64_e32 v[134:135], 0
	v_mov_b64_e32 v[136:137], 0
	v_mov_b64_e32 v[138:139], 0
	v_mov_b64_e32 v[90:91], 0
	v_mov_b64_e32 v[92:93], 0
	v_mov_b64_e32 v[94:95], 0
	v_mov_b64_e32 v[96:97], 0
	v_mov_b64_e32 v[108:109], 0
	v_mov_b64_e32 v[110:111], 0
	v_mov_b64_e32 v[112:113], 0
	v_mov_b64_e32 v[114:115], 0
	v_mov_b64_e32 v[124:125], 0
	v_mov_b64_e32 v[126:127], 0
	v_mov_b64_e32 v[128:129], 0
	v_mov_b64_e32 v[130:131], 0
	v_mov_b64_e32 v[140:141], 0
	v_mov_b64_e32 v[142:143], 0
	v_mov_b64_e32 v[144:145], 0
	v_mov_b64_e32 v[146:147], 0
	s_and_b64 s[98:99], exec, s[12:13]
	s_cbranch_scc1 .Lrb_1538
	s_barrier
.Lrb_1538:
.LBB13_1538:
	v_add_u32_e32 v62, s36, v167
	v_add_u32_e32 v164, s39, v167
	ds_read_b128 v[42:45], v62
	ds_read_b128 v[50:53], v62 offset:1024
	ds_read_b128 v[58:61], v62 offset:2048
	ds_read_b128 v[62:65], v62 offset:3072
	ds_read_b128 v[160:163], v164
	ds_read_b128 v[170:173], v164 offset:1024
	ds_read_b128 v[174:177], v164 offset:2048
	ds_read_b128 v[178:181], v164 offset:3072
	s_add_u32 s18, s16, 0x100
	s_addc_u32 s19, s17, 0
	s_cmp_eq_u32 s73, 40
	s_cselect_b32 s23, s7, s19
	s_cselect_b32 s22, s6, s18
	s_cselect_b32 s21, s15, s72
	s_cselect_b32 s20, s14, s64
	v_lshl_add_u64 v[164:165], s[16:17], 0, v[156:157]
	s_add_i32 m0, s42, 0xc000
	ds_read_b128 v[182:185], v169
	ds_read_b128 v[186:189], v169 offset:1024
	ds_read_b128 v[190:193], v169 offset:2048
	ds_read_b128 v[194:197], v169 offset:3072
	ds_read_b128 v[208:211], v169 offset:4096
	ds_read_b128 v[212:215], v169 offset:5120
	ds_read_b128 v[216:219], v169 offset:6144
	ds_read_b128 v[220:223], v169 offset:7168
	global_load_lds_dwordx4 v[164:165], off
	v_lshl_add_u64 v[164:165], s[16:17], 0, v[158:159]
	s_add_i32 m0, s42, 0xe000
	s_nop 0
	global_load_lds_dwordx4 v[164:165], off
	s_waitcnt vmcnt(8)
	s_waitcnt lgkmcnt(0)
	s_barrier
	s_setprio 1
	s_waitcnt lgkmcnt(0)
	v_mfma_f32_16x16x32_bf16 v[144:147], v[42:45], v[182:185], v[144:147]
	v_mfma_f32_16x16x32_bf16 v[140:143], v[58:61], v[182:185], v[140:143]
	v_mfma_f32_16x16x32_bf16 v[128:131], v[42:45], v[190:193], v[128:131]
	v_mfma_f32_16x16x32_bf16 v[124:127], v[58:61], v[190:193], v[124:127]
	v_mfma_f32_16x16x32_bf16 v[112:115], v[42:45], v[208:211], v[112:115]
	v_mfma_f32_16x16x32_bf16 v[108:111], v[58:61], v[208:211], v[108:111]
	v_mfma_f32_16x16x32_bf16 v[94:97], v[42:45], v[216:219], v[94:97]
	v_mfma_f32_16x16x32_bf16 v[90:93], v[58:61], v[216:219], v[90:93]
	v_mfma_f32_16x16x32_bf16 v[144:147], v[50:53], v[186:189], v[144:147]
	v_mfma_f32_16x16x32_bf16 v[140:143], v[62:65], v[186:189], v[140:143]
	v_mfma_f32_16x16x32_bf16 v[128:131], v[50:53], v[194:197], v[128:131]
	v_mfma_f32_16x16x32_bf16 v[124:127], v[62:65], v[194:197], v[124:127]
	v_mfma_f32_16x16x32_bf16 v[112:115], v[50:53], v[212:215], v[112:115]
	v_mfma_f32_16x16x32_bf16 v[108:111], v[62:65], v[212:215], v[108:111]
	v_mfma_f32_16x16x32_bf16 v[94:97], v[50:53], v[220:223], v[94:97]
	v_mfma_f32_16x16x32_bf16 v[90:93], v[62:65], v[220:223], v[90:93]
	s_setprio 0
	s_setprio 1
	v_mfma_f32_16x16x32_bf16 v[136:139], v[160:163], v[182:185], v[136:139]
	v_mfma_f32_16x16x32_bf16 v[132:135], v[174:177], v[182:185], v[132:135]
	v_mfma_f32_16x16x32_bf16 v[120:123], v[160:163], v[190:193], v[120:123]
	v_mfma_f32_16x16x32_bf16 v[116:119], v[174:177], v[190:193], v[116:119]
	v_mfma_f32_16x16x32_bf16 v[104:107], v[160:163], v[208:211], v[104:107]
	v_mfma_f32_16x16x32_bf16 v[100:103], v[174:177], v[208:211], v[100:103]
	v_mfma_f32_16x16x32_bf16 v[86:89], v[160:163], v[216:219], v[86:89]
	v_mfma_f32_16x16x32_bf16 v[82:85], v[174:177], v[216:219], v[82:85]
	v_mfma_f32_16x16x32_bf16 v[136:139], v[170:173], v[186:189], v[136:139]
	v_mfma_f32_16x16x32_bf16 v[132:135], v[178:181], v[186:189], v[132:135]
	v_mfma_f32_16x16x32_bf16 v[120:123], v[170:173], v[194:197], v[120:123]
	v_mfma_f32_16x16x32_bf16 v[116:119], v[178:181], v[194:197], v[116:119]
	v_mfma_f32_16x16x32_bf16 v[104:107], v[170:173], v[212:215], v[104:107]
	v_mfma_f32_16x16x32_bf16 v[100:103], v[178:181], v[212:215], v[100:103]
	v_mfma_f32_16x16x32_bf16 v[86:89], v[170:173], v[220:223], v[86:89]
	v_mfma_f32_16x16x32_bf16 v[82:85], v[178:181], v[220:223], v[82:85]
	s_setprio 0
	s_barrier
; #define PG8_STAGE_A(bufoff, h, ptr, nsel) do { if constexpr (Sched::GATHER) { if (nsel) PG8_STAGE_X(bufoff, ptr, vAn[h], PG8_A_AUX); else PG8_STAGE_X(bufoff, ptr, vAc[h], PG8_A_AUX); } \
;         else PG8_STAGE_X(bufoff, (ptr) + (h) * hstep, voffA, PG8_A_AUX); } while (0)
; #define PG8_STAGE(bufoff, gbase, voff) PG8_STAGE_X(bufoff, gbase, voff, PG8_B_AUX)
; #define PG8_LDA(dst, b, h) do { _Pragma("unroll") for (int m = 0; m < 4; ++m) _Pragma("unroll") for (int k = 0; k < 2; ++k) dst[m][k] = *(const PG8_LAS bf16x8*)(lds + PG8_SA(b, h) + aoff + m * 2048 + k * 1024); } while (0)
; #define PG8_LDB(dst, b, h) do { _Pragma("unroll") for (int n = 0; n < 2; ++n) _Pragma("unroll") for (int k = 0; k < 2; ++k) dst[n][k] = *(const PG8_LAS bf16x8*)(lds + PG8_SB(b, h) + boff + n * 2048 + k * 1024); } while (0)
; #define PG8_MMA(ai, bj, At, Bt) do { __builtin_amdgcn_s_setprio(1); _Pragma("unroll") for (int m = 0; m < 4; ++m) _Pragma("unroll") for (int n = 0; n < 2; ++n) _Pragma("unroll") for (int k = 0; k < 2; ++k) \
;         acc[ai][bj][m][n] = __builtin_amdgcn_mfma_f32_16x16x32_bf16(Bt[n][k], At[m][k], acc[ai][bj][m][n], 0, 0, 0); __builtin_amdgcn_s_setprio(0); } while (0)
; #define PG8_WAIT_V(n) asm volatile("s_waitcnt vmcnt(" #n ")" ::: "memory")
; #define PG8_WAIT_L(n) asm volatile("s_waitcnt lgkmcnt(" #n ")" ::: "memory")
; #define PG8_BAR __builtin_amdgcn_s_barrier()
; #define PG8_SCHED __builtin_amdgcn_sched_barrier(0)
; template <class Epi, class Sched, bool ALIGN_EPI = false, bool SP2 = false>
; __device__ __forceinline__ void gemm_phase(PG8_LAS unsigned char* lds, const Gemm g, const Sched& S, const Epi& E) {
;     ...
;             PG8_LDA(At, 0, 1); PG8_STAGE(PG8_SB(0, 0), b2, voffB); PG8_STAGE(PG8_SB(0, 1), b2 + hstep, voffB); PG8_STAGE_A(PG8_SA(0, 0), 0, a2, last);
;             PG8_WAIT_V(8); PG8_WAIT_L(0); PG8_BAR; PG8_MMA(1, 0, At, B0); PG8_MMA(1, 1, At, B1); PG8_BAR; PG8_SCHED;
;             PG8_LDB(B0, 1, 0); PG8_LDB(B1, 1, 1); PG8_SCHED; PG8_LDA(At, 1, 0); PG8_STAGE_A(PG8_SA(0, 1), 1, a2, last);
	s_mov_b32 m0, s37
	v_lshl_add_u64 v[164:165], s[20:21], 0, v[150:151]
	s_add_u32 s16, s20, 0xb0000
	ds_read_b128 v[182:185], v169 offset:16384
	ds_read_b128 v[186:189], v169 offset:17408
	ds_read_b128 v[190:193], v169 offset:18432
	ds_read_b128 v[194:197], v169 offset:19456
	ds_read_b128 v[208:211], v169 offset:20480
	ds_read_b128 v[212:215], v169 offset:21504
	ds_read_b128 v[216:219], v169 offset:22528
	ds_read_b128 v[220:223], v169 offset:23552
	global_load_lds_dwordx4 v[164:165], off
	v_lshl_add_u64 v[198:199], s[20:21], 0, v[154:155]
	s_mov_b32 m0, s38
	s_addc_u32 s17, s21, 0
	global_load_lds_dwordx4 v[198:199], off
	v_lshl_add_u64 v[224:225], s[16:17], 0, v[150:151]
	s_mov_b32 m0, s40
	v_lshl_add_u64 v[226:227], s[22:23], 0, v[152:153]
	global_load_lds_dwordx4 v[224:225], off
	v_lshl_add_u64 v[224:225], s[16:17], 0, v[154:155]
	s_mov_b32 m0, s41
	s_nop 0
	global_load_lds_dwordx4 v[224:225], off
	v_lshl_add_u64 v[224:225], s[22:23], 0, v[148:149]
	s_mov_b32 m0, s42
	s_nop 0
	global_load_lds_dwordx4 v[224:225], off
	s_mov_b32 m0, s43
	s_nop 0
	global_load_lds_dwordx4 v[226:227], off
	s_waitcnt vmcnt(8)
	s_waitcnt lgkmcnt(0)
	s_barrier
	s_setprio 1
	s_waitcnt lgkmcnt(0)
	v_mfma_f32_16x16x32_bf16 v[78:81], v[42:45], v[182:185], v[78:81]
	v_mfma_f32_16x16x32_bf16 v[74:77], v[58:61], v[182:185], v[74:77]
	v_mfma_f32_16x16x32_bf16 v[54:57], v[42:45], v[190:193], v[54:57]
	v_mfma_f32_16x16x32_bf16 v[46:49], v[58:61], v[190:193], v[46:49]
	v_mfma_f32_16x16x32_bf16 v[30:33], v[42:45], v[208:211], v[30:33]
	v_mfma_f32_16x16x32_bf16 v[26:29], v[58:61], v[208:211], v[26:29]
	v_mfma_f32_16x16x32_bf16 v[14:17], v[42:45], v[216:219], v[14:17]
	v_mfma_f32_16x16x32_bf16 v[10:13], v[58:61], v[216:219], v[10:13]
	v_mfma_f32_16x16x32_bf16 v[78:81], v[50:53], v[186:189], v[78:81]
	v_mfma_f32_16x16x32_bf16 v[74:77], v[62:65], v[186:189], v[74:77]
	v_mfma_f32_16x16x32_bf16 v[54:57], v[50:53], v[194:197], v[54:57]
	v_mfma_f32_16x16x32_bf16 v[46:49], v[62:65], v[194:197], v[46:49]
	v_mfma_f32_16x16x32_bf16 v[30:33], v[50:53], v[212:215], v[30:33]
	v_mfma_f32_16x16x32_bf16 v[26:29], v[62:65], v[212:215], v[26:29]
	v_mfma_f32_16x16x32_bf16 v[14:17], v[50:53], v[220:223], v[14:17]
	v_mfma_f32_16x16x32_bf16 v[10:13], v[62:65], v[220:223], v[10:13]
	s_setprio 0
	s_setprio 1
	v_mfma_f32_16x16x32_bf16 v[38:41], v[160:163], v[190:193], v[38:41]
	v_mfma_f32_16x16x32_bf16 v[34:37], v[174:177], v[190:193], v[34:37]
	v_mfma_f32_16x16x32_bf16 v[22:25], v[160:163], v[208:211], v[22:25]
	v_mfma_f32_16x16x32_bf16 v[18:21], v[174:177], v[208:211], v[18:21]
	v_mfma_f32_16x16x32_bf16 v[6:9], v[160:163], v[216:219], v[6:9]
	v_mfma_f32_16x16x32_bf16 v[2:5], v[174:177], v[216:219], v[2:5]
	v_mfma_f32_16x16x32_bf16 v[42:45], v[160:163], v[182:185], v[70:73]
	v_mfma_f32_16x16x32_bf16 v[50:53], v[174:177], v[182:185], v[66:69]
	v_mfma_f32_16x16x32_bf16 v[38:41], v[170:173], v[194:197], v[38:41]
	v_mfma_f32_16x16x32_bf16 v[34:37], v[178:181], v[194:197], v[34:37]
	v_mfma_f32_16x16x32_bf16 v[22:25], v[170:173], v[212:215], v[22:25]
	v_mfma_f32_16x16x32_bf16 v[18:21], v[178:181], v[212:215], v[18:21]
	v_mfma_f32_16x16x32_bf16 v[6:9], v[170:173], v[220:223], v[6:9]
	v_mfma_f32_16x16x32_bf16 v[2:5], v[178:181], v[220:223], v[2:5]
	v_mfma_f32_16x16x32_bf16 v[42:45], v[170:173], v[186:189], v[42:45]
	v_mfma_f32_16x16x32_bf16 v[50:53], v[178:181], v[186:189], v[50:53]
	s_setprio 0
	s_barrier
	v_add_u32_e32 v70, s48, v167
	v_add_u32_e32 v178, s56, v167
	ds_read_b128 v[58:61], v70
	ds_read_b128 v[62:65], v70 offset:1024
	ds_read_b128 v[66:69], v70 offset:2048
	ds_read_b128 v[70:73], v70 offset:3072
	ds_read_b128 v[160:163], v178
	ds_read_b128 v[170:173], v178 offset:1024
	ds_read_b128 v[174:177], v178 offset:2048
	ds_read_b128 v[178:181], v178 offset:3072
	s_add_u32 s16, s22, 0xb0000
	s_addc_u32 s17, s23, 0
	s_mov_b32 m0, s44
	v_lshl_add_u64 v[228:229], s[16:17], 0, v[148:149]
	ds_read_b128 v[182:185], v169 offset:32768
	ds_read_b128 v[186:189], v169 offset:33792
	ds_read_b128 v[190:193], v169 offset:34816
	ds_read_b128 v[194:197], v169 offset:35840
	ds_read_b128 v[208:211], v169 offset:36864
	ds_read_b128 v[212:215], v169 offset:37888
	ds_read_b128 v[216:219], v169 offset:38912
	ds_read_b128 v[220:223], v169 offset:39936
	global_load_lds_dwordx4 v[228:229], off
	v_lshl_add_u64 v[228:229], s[16:17], 0, v[152:153]
	s_mov_b32 m0, s45
	s_nop 0
	global_load_lds_dwordx4 v[228:229], off
	s_waitcnt vmcnt(8)
	s_waitcnt lgkmcnt(0)
	s_barrier
; #define PG8_STAGE_A(bufoff, h, ptr, nsel) do { if constexpr (Sched::GATHER) { if (nsel) PG8_STAGE_X(bufoff, ptr, vAn[h], PG8_A_AUX); else PG8_STAGE_X(bufoff, ptr, vAc[h], PG8_A_AUX); } \
;         else PG8_STAGE_X(bufoff, (ptr) + (h) * hstep, voffA, PG8_A_AUX); } while (0)
; #define PG8_STAGE(bufoff, gbase, voff) PG8_STAGE_X(bufoff, gbase, voff, PG8_B_AUX)
; #define PG8_LDA(dst, b, h) do { _Pragma("unroll") for (int m = 0; m < 4; ++m) _Pragma("unroll") for (int k = 0; k < 2; ++k) dst[m][k] = *(const PG8_LAS bf16x8*)(lds + PG8_SA(b, h) + aoff + m * 2048 + k * 1024); } while (0)
; #define PG8_MMA(ai, bj, At, Bt) do { __builtin_amdgcn_s_setprio(1); _Pragma("unroll") for (int m = 0; m < 4; ++m) _Pragma("unroll") for (int n = 0; n < 2; ++n) _Pragma("unroll") for (int k = 0; k < 2; ++k) \
;         acc[ai][bj][m][n] = __builtin_amdgcn_mfma_f32_16x16x32_bf16(Bt[n][k], At[m][k], acc[ai][bj][m][n], 0, 0, 0); __builtin_amdgcn_s_setprio(0); } while (0)
; #define PG8_WAIT_V(n) asm volatile("s_waitcnt vmcnt(" #n ")" ::: "memory")
; #define PG8_WAIT_L(n) asm volatile("s_waitcnt lgkmcnt(" #n ")" ::: "memory")
; #define PG8_BAR __builtin_amdgcn_s_barrier()
; #define PG8_SCHED __builtin_amdgcn_sched_barrier(0)
; template <class Epi, class Sched, bool ALIGN_EPI = false, bool SP2 = false>
; __device__ __forceinline__ void gemm_phase(PG8_LAS unsigned char* lds, const Gemm g, const Sched& S, const Epi& E) {
;     ...
;             PG8_WAIT_V(8); PG8_WAIT_L(0); PG8_BAR; PG8_MMA(0, 0, At, B0); PG8_MMA(0, 1, At, B1); PG8_BAR; PG8_SCHED;
;             PG8_LDA(At, 1, 1); PG8_STAGE(PG8_SB(1, 0), b3, voffB); PG8_STAGE(PG8_SB(1, 1), b3 + hstep, voffB); PG8_STAGE_A(PG8_SA(1, 0), 0, a3, last);
;             PG8_WAIT_V(8); PG8_WAIT_L(0); PG8_BAR; PG8_MMA(1, 0, At, B0); PG8_MMA(1, 1, At, B1); PG8_BAR; PG8_SCHED;
;     ...
;         }
;         if constexpr (ALIGN_EPI) { if (wr == 0) PG8_BAR; }
	s_setprio 1
	s_waitcnt lgkmcnt(0)
	v_mfma_f32_16x16x32_bf16 v[144:147], v[58:61], v[182:185], v[144:147]
	v_mfma_f32_16x16x32_bf16 v[140:143], v[66:69], v[182:185], v[140:143]
	v_mfma_f32_16x16x32_bf16 v[128:131], v[58:61], v[190:193], v[128:131]
	v_mfma_f32_16x16x32_bf16 v[124:127], v[66:69], v[190:193], v[124:127]
	v_mfma_f32_16x16x32_bf16 v[112:115], v[58:61], v[208:211], v[112:115]
	v_mfma_f32_16x16x32_bf16 v[108:111], v[66:69], v[208:211], v[108:111]
	v_mfma_f32_16x16x32_bf16 v[94:97], v[58:61], v[216:219], v[94:97]
	v_mfma_f32_16x16x32_bf16 v[90:93], v[66:69], v[216:219], v[90:93]
	v_mfma_f32_16x16x32_bf16 v[144:147], v[62:65], v[186:189], v[144:147]
	v_mfma_f32_16x16x32_bf16 v[140:143], v[70:73], v[186:189], v[140:143]
	v_mfma_f32_16x16x32_bf16 v[128:131], v[62:65], v[194:197], v[128:131]
	v_mfma_f32_16x16x32_bf16 v[124:127], v[70:73], v[194:197], v[124:127]
	v_mfma_f32_16x16x32_bf16 v[112:115], v[62:65], v[212:215], v[112:115]
	v_mfma_f32_16x16x32_bf16 v[108:111], v[70:73], v[212:215], v[108:111]
	v_mfma_f32_16x16x32_bf16 v[94:97], v[62:65], v[220:223], v[94:97]
	v_mfma_f32_16x16x32_bf16 v[90:93], v[70:73], v[220:223], v[90:93]
	s_setprio 0
	s_setprio 1
	v_mfma_f32_16x16x32_bf16 v[136:139], v[160:163], v[182:185], v[136:139]
	v_mfma_f32_16x16x32_bf16 v[132:135], v[174:177], v[182:185], v[132:135]
	v_mfma_f32_16x16x32_bf16 v[120:123], v[160:163], v[190:193], v[120:123]
	v_mfma_f32_16x16x32_bf16 v[116:119], v[174:177], v[190:193], v[116:119]
	v_mfma_f32_16x16x32_bf16 v[104:107], v[160:163], v[208:211], v[104:107]
	v_mfma_f32_16x16x32_bf16 v[100:103], v[174:177], v[208:211], v[100:103]
	v_mfma_f32_16x16x32_bf16 v[86:89], v[160:163], v[216:219], v[86:89]
	v_mfma_f32_16x16x32_bf16 v[82:85], v[174:177], v[216:219], v[82:85]
	v_mfma_f32_16x16x32_bf16 v[136:139], v[170:173], v[186:189], v[136:139]
	v_mfma_f32_16x16x32_bf16 v[132:135], v[178:181], v[186:189], v[132:135]
	v_mfma_f32_16x16x32_bf16 v[120:123], v[170:173], v[194:197], v[120:123]
	v_mfma_f32_16x16x32_bf16 v[116:119], v[178:181], v[194:197], v[116:119]
	v_mfma_f32_16x16x32_bf16 v[104:107], v[170:173], v[212:215], v[104:107]
	v_mfma_f32_16x16x32_bf16 v[100:103], v[178:181], v[212:215], v[100:103]
	v_mfma_f32_16x16x32_bf16 v[86:89], v[170:173], v[220:223], v[86:89]
	v_mfma_f32_16x16x32_bf16 v[82:85], v[178:181], v[220:223], v[82:85]
	s_setprio 0
	s_barrier
	s_mov_b32 m0, s49
	v_lshl_add_u64 v[164:165], v[164:165], 0, s[54:55]
	s_add_u32 s16, s20, 0xb0080
	ds_read_b128 v[182:185], v169 offset:49152
	ds_read_b128 v[186:189], v169 offset:50176
	ds_read_b128 v[190:193], v169 offset:51200
	ds_read_b128 v[194:197], v169 offset:52224
	ds_read_b128 v[208:211], v169 offset:53248
	ds_read_b128 v[212:215], v169 offset:54272
	ds_read_b128 v[216:219], v169 offset:55296
	ds_read_b128 v[220:223], v169 offset:56320
	global_load_lds_dwordx4 v[164:165], off
	v_lshl_add_u64 v[164:165], v[198:199], 0, s[54:55]
	s_mov_b32 m0, s50
	s_addc_u32 s17, s21, 0
	global_load_lds_dwordx4 v[164:165], off
	v_lshl_add_u64 v[164:165], s[16:17], 0, v[150:151]
	s_mov_b32 m0, s57
	s_nop 0
	global_load_lds_dwordx4 v[164:165], off
	v_lshl_add_u64 v[164:165], s[16:17], 0, v[154:155]
	s_mov_b32 m0, s58
	s_nop 0
	global_load_lds_dwordx4 v[164:165], off
	v_lshl_add_u64 v[164:165], v[224:225], 0, s[54:55]
	s_mov_b32 m0, s51
	s_nop 0
	global_load_lds_dwordx4 v[164:165], off
	v_lshl_add_u64 v[164:165], v[226:227], 0, s[54:55]
	s_mov_b32 m0, s53
	s_nop 0
	global_load_lds_dwordx4 v[164:165], off
	s_waitcnt vmcnt(8)
	s_waitcnt lgkmcnt(0)
	s_barrier
	s_setprio 1
	s_waitcnt lgkmcnt(0)
	v_mfma_f32_16x16x32_bf16 v[78:81], v[58:61], v[182:185], v[78:81]
	v_mfma_f32_16x16x32_bf16 v[74:77], v[66:69], v[182:185], v[74:77]
	v_mfma_f32_16x16x32_bf16 v[54:57], v[58:61], v[190:193], v[54:57]
	v_mfma_f32_16x16x32_bf16 v[46:49], v[66:69], v[190:193], v[46:49]
	v_mfma_f32_16x16x32_bf16 v[30:33], v[58:61], v[208:211], v[30:33]
	v_mfma_f32_16x16x32_bf16 v[26:29], v[66:69], v[208:211], v[26:29]
	v_mfma_f32_16x16x32_bf16 v[14:17], v[58:61], v[216:219], v[14:17]
	v_mfma_f32_16x16x32_bf16 v[10:13], v[66:69], v[216:219], v[10:13]
	v_mfma_f32_16x16x32_bf16 v[78:81], v[62:65], v[186:189], v[78:81]
	v_mfma_f32_16x16x32_bf16 v[74:77], v[70:73], v[186:189], v[74:77]
	v_mfma_f32_16x16x32_bf16 v[54:57], v[62:65], v[194:197], v[54:57]
	v_mfma_f32_16x16x32_bf16 v[46:49], v[70:73], v[194:197], v[46:49]
	v_mfma_f32_16x16x32_bf16 v[30:33], v[62:65], v[212:215], v[30:33]
	v_mfma_f32_16x16x32_bf16 v[26:29], v[70:73], v[212:215], v[26:29]
	v_mfma_f32_16x16x32_bf16 v[14:17], v[62:65], v[220:223], v[14:17]
	v_mfma_f32_16x16x32_bf16 v[10:13], v[70:73], v[220:223], v[10:13]
	s_setprio 0
	s_setprio 1
	v_mfma_f32_16x16x32_bf16 v[42:45], v[160:163], v[182:185], v[42:45]
	v_mfma_f32_16x16x32_bf16 v[70:73], v[170:173], v[186:189], v[42:45]
	v_mfma_f32_16x16x32_bf16 v[42:45], v[174:177], v[182:185], v[50:53]
	v_mfma_f32_16x16x32_bf16 v[38:41], v[160:163], v[190:193], v[38:41]
	v_mfma_f32_16x16x32_bf16 v[34:37], v[174:177], v[190:193], v[34:37]
	v_mfma_f32_16x16x32_bf16 v[22:25], v[160:163], v[208:211], v[22:25]
	v_mfma_f32_16x16x32_bf16 v[18:21], v[174:177], v[208:211], v[18:21]
	v_mfma_f32_16x16x32_bf16 v[6:9], v[160:163], v[216:219], v[6:9]
	v_mfma_f32_16x16x32_bf16 v[2:5], v[174:177], v[216:219], v[2:5]
	v_mfma_f32_16x16x32_bf16 v[66:69], v[178:181], v[186:189], v[42:45]
	v_mfma_f32_16x16x32_bf16 v[38:41], v[170:173], v[194:197], v[38:41]
	v_mfma_f32_16x16x32_bf16 v[34:37], v[178:181], v[194:197], v[34:37]
	v_mfma_f32_16x16x32_bf16 v[22:25], v[170:173], v[212:215], v[22:25]
	v_mfma_f32_16x16x32_bf16 v[18:21], v[178:181], v[212:215], v[18:21]
	v_mfma_f32_16x16x32_bf16 v[6:9], v[170:173], v[220:223], v[6:9]
	v_mfma_f32_16x16x32_bf16 v[2:5], v[178:181], v[220:223], v[2:5]
	s_setprio 0
	s_barrier
	s_add_i32 s73, s73, 2
	s_add_u32 s64, s64, 0x100
	s_addc_u32 s72, s72, 0
	s_cmp_gt_u32 s73, 41
	s_mov_b64 s[16:17], s[18:19]
	s_cbranch_scc0 .LBB13_1538
	s_and_b64 vcc, exec, s[12:13]
	s_cbranch_vccz .LBB13_1541
	s_barrier
; __device__ __forceinline__ unsigned pk2(float lo, float hi) { f32x2 v = {lo, hi}; return __builtin_bit_cast(unsigned, __builtin_convertvector(v, bf2_t)); }
; template <int BIT = 0> __device__ __forceinline__ void st16w(void* p, u32x4 v) { if ((WT_STORES >> BIT) & 1) asm volatile("global_store_dwordx4 %0, %1, off sc1\n\ts_nop 1" :: "v"(p), "v"(v) : "memory"); else *(u32x4*)p = v; }
; __device__ __forceinline__ float bflo(unsigned u) { return __uint_as_float(u << 16); }
; __device__ __forceinline__ float bfhi(unsigned u) { return __uint_as_float(u & 0xffff0000u); }
;     __device__ __forceinline__ void operator()(const f32x4 (&acc)[2][2][4][2], const Unit& u, int wr, int wc, int fr, int fq) const {
;         const int row0 = u.pm * BM + wr * 64 + fr, col0 = u.pn * BM + wc * 32 + 8 * fq;
;         const float* gv = gate + (size_t)(u.pm < 32 ? 0 : (u.pm < 64 ? 1 : 2)) * 6 * D;
;         f32x4 g4[2][2];
; #pragma unroll
;         for (int bj = 0; bj < 2; ++bj)
; #pragma unroll
;             for (int n = 0; n < 2; ++n) g4[bj][n] = *(const f32x4*)(gv + col0 + bj * HALF + 4 * n);
; #pragma unroll
;         for (int ai = 0; ai < 2; ++ai)
; #pragma unroll
;             for (int m = 0; m < 4; ++m) { const size_t ro = (size_t)(row0 + ai * HALF + m * 16) * D + col0;
; #pragma unroll
;                 for (int bj = 0; bj < 2; ++bj) { const size_t off = ro + bj * HALF;
;                     f32x4 b0, b1;
;                     if (base32) { b0 = *(const f32x4*)(base32 + off); b1 = *(const f32x4*)(base32 + off + 4); }
;                     else { const u32x4 hb = *(const u32x4*)(base + off); b0 = (f32x4){bflo(hb.x), bfhi(hb.x), bflo(hb.y), bfhi(hb.y)}; b1 = (f32x4){bflo(hb.z), bfhi(hb.z), bflo(hb.w), bfhi(hb.w)}; }
;                     const f32x4 o0 = b0 + g4[bj][0] * acc[ai][bj][m][0], o1 = b1 + g4[bj][1] * acc[ai][bj][m][1];
;                     u32x4 w; w.x = pk2(o0[0], o0[1]); w.y = pk2(o0[2], o0[3]); w.z = pk2(o1[0], o1[1]); w.w = pk2(o1[2], o1[3]);
;                     st16w(H + off, w); } }
.LBB13_1541:
	s_cmp_lt_i32 s52, 64
	s_movk_i32 s16, 0x1800
	s_cselect_b32 s16, s16, 0x3000
	s_cmp_gt_i32 s52, 31
	s_cselect_b32 s16, s16, 0
	s_lshl_b32 s16, s16, 2
	s_add_u32 s16, s46, s16
	s_addc_u32 s17, s47, 0
	v_lshl_add_u32 v52, s52, 8, v166
	v_lshl_or_b32 v53, s60, 8, v168
	v_lshlrev_b32_e32 v50, 2, v53
	global_load_dwordx4 v[62:65], v50, s[16:17] offset:16
	global_load_dwordx4 v[58:61], v50, s[16:17]
	global_load_dwordx4 v[170:173], v50, s[16:17] offset:528
	global_load_dwordx4 v[160:163], v50, s[16:17] offset:512
	v_lshlrev_b32_e32 v51, 11, v52
	v_lshl_add_u32 v51, v53, 1, v51
	global_load_dwordx4 v[174:177], v51, s[8:9]
	global_load_dwordx4 v[178:181], v51, s[8:9] offset:256
	v_add_u32_e32 v52, 0x8000, v51
	global_load_dwordx4 v[182:185], v52, s[8:9]
	v_add_u32_e32 v52, 0x8000, v51
	global_load_dwordx4 v[186:189], v52, s[8:9] offset:256
	v_add_u32_e32 v52, 0x10000, v51
	global_load_dwordx4 v[190:193], v52, s[8:9]
	v_add_u32_e32 v52, 0x10000, v51
	global_load_dwordx4 v[194:197], v52, s[8:9] offset:256
	v_add_u32_e32 v52, 0x18000, v51
	global_load_dwordx4 v[208:211], v52, s[8:9]
	v_add_u32_e32 v52, 0x18000, v51
	global_load_dwordx4 v[212:215], v52, s[8:9] offset:256
	v_add_u32_e32 v52, 0x40000, v51
	global_load_dwordx4 v[216:219], v52, s[8:9]
	v_add_u32_e32 v52, 0x40000, v51
	global_load_dwordx4 v[220:223], v52, s[8:9] offset:256
	s_waitcnt vmcnt(9)
	v_lshlrev_b32_e32 v42, 16, v174
	v_and_b32_e32 v43, 0xffff0000, v174
	v_pk_fma_f32 v[144:145], v[144:145], v[58:59], v[42:43]
	v_lshlrev_b32_e32 v44, 16, v175
	v_and_b32_e32 v45, 0xffff0000, v175
	v_pk_fma_f32 v[146:147], v[146:147], v[60:61], v[44:45]
	v_lshlrev_b32_e32 v42, 16, v176
	v_and_b32_e32 v43, 0xffff0000, v176
	v_pk_fma_f32 v[140:141], v[140:141], v[62:63], v[42:43]
	v_lshlrev_b32_e32 v44, 16, v177
	v_and_b32_e32 v45, 0xffff0000, v177
	v_pk_fma_f32 v[142:143], v[142:143], v[64:65], v[44:45]
	v_cvt_pk_bf16_f32 v144, v144, v145
	v_cvt_pk_bf16_f32 v145, v146, v147
	v_cvt_pk_bf16_f32 v146, v140, v141
	v_cvt_pk_bf16_f32 v147, v142, v143
	global_store_dwordx4 v51, v[144:147], s[8:9]
	v_add_u32_e32 v52, 0x48000, v51
	global_load_dwordx4 v[174:177], v52, s[8:9]
	v_add_u32_e32 v52, 0x48000, v51
	global_load_dwordx4 v[140:143], v52, s[8:9] offset:256
	s_waitcnt vmcnt(11)
	v_lshlrev_b32_e32 v42, 16, v178
	v_and_b32_e32 v43, 0xffff0000, v178
	v_pk_fma_f32 v[136:137], v[136:137], v[160:161], v[42:43]
	v_lshlrev_b32_e32 v44, 16, v179
	v_and_b32_e32 v45, 0xffff0000, v179
	v_pk_fma_f32 v[138:139], v[138:139], v[162:163], v[44:45]
	v_lshlrev_b32_e32 v42, 16, v180
	v_and_b32_e32 v43, 0xffff0000, v180
	v_pk_fma_f32 v[132:133], v[132:133], v[170:171], v[42:43]
	v_lshlrev_b32_e32 v44, 16, v181
	v_and_b32_e32 v45, 0xffff0000, v181
	v_pk_fma_f32 v[134:135], v[134:135], v[172:173], v[44:45]
	v_cvt_pk_bf16_f32 v136, v136, v137
	v_cvt_pk_bf16_f32 v137, v138, v139
	v_cvt_pk_bf16_f32 v138, v132, v133
	v_cvt_pk_bf16_f32 v139, v134, v135
	global_store_dwordx4 v51, v[136:139], s[8:9] offset:256
	v_add_u32_e32 v52, 0x50000, v51
	global_load_dwordx4 v[178:181], v52, s[8:9]
	v_add_u32_e32 v52, 0x50000, v51
	global_load_dwordx4 v[132:135], v52, s[8:9] offset:256
	s_waitcnt vmcnt(13)
	v_lshlrev_b32_e32 v42, 16, v182
	v_and_b32_e32 v43, 0xffff0000, v182
	v_pk_fma_f32 v[128:129], v[128:129], v[58:59], v[42:43]
	v_lshlrev_b32_e32 v44, 16, v183
	v_and_b32_e32 v45, 0xffff0000, v183
	v_pk_fma_f32 v[130:131], v[130:131], v[60:61], v[44:45]
	v_lshlrev_b32_e32 v42, 16, v184
	v_and_b32_e32 v43, 0xffff0000, v184
	v_pk_fma_f32 v[124:125], v[124:125], v[62:63], v[42:43]
	v_lshlrev_b32_e32 v44, 16, v185
	v_and_b32_e32 v45, 0xffff0000, v185
	v_pk_fma_f32 v[126:127], v[126:127], v[64:65], v[44:45]
	v_cvt_pk_bf16_f32 v128, v128, v129
	v_cvt_pk_bf16_f32 v129, v130, v131
	v_cvt_pk_bf16_f32 v130, v124, v125
	v_cvt_pk_bf16_f32 v131, v126, v127
	v_add_u32_e32 v53, 0x8000, v51
	global_store_dwordx4 v53, v[128:131], s[8:9]
	v_add_u32_e32 v52, 0x58000, v51
	global_load_dwordx4 v[182:185], v52, s[8:9]
	v_add_u32_e32 v52, 0x58000, v51
	global_load_dwordx4 v[124:127], v52, s[8:9] offset:256
	s_waitcnt vmcnt(15)
	v_lshlrev_b32_e32 v42, 16, v186
	v_and_b32_e32 v43, 0xffff0000, v186
	v_pk_fma_f32 v[120:121], v[120:121], v[160:161], v[42:43]
	v_lshlrev_b32_e32 v44, 16, v187
	v_and_b32_e32 v45, 0xffff0000, v187
	v_pk_fma_f32 v[122:123], v[122:123], v[162:163], v[44:45]
	v_lshlrev_b32_e32 v42, 16, v188
	v_and_b32_e32 v43, 0xffff0000, v188
	v_pk_fma_f32 v[116:117], v[116:117], v[170:171], v[42:43]
	v_lshlrev_b32_e32 v44, 16, v189
	v_and_b32_e32 v45, 0xffff0000, v189
	v_pk_fma_f32 v[118:119], v[118:119], v[172:173], v[44:45]
	v_cvt_pk_bf16_f32 v120, v120, v121
	v_cvt_pk_bf16_f32 v121, v122, v123
	v_cvt_pk_bf16_f32 v122, v116, v117
	v_cvt_pk_bf16_f32 v123, v118, v119
	v_add_u32_e32 v53, 0x8000, v51
	global_store_dwordx4 v53, v[120:123], s[8:9] offset:256
	s_waitcnt vmcnt(15)
	v_lshlrev_b32_e32 v42, 16, v190
	v_and_b32_e32 v43, 0xffff0000, v190
	v_pk_fma_f32 v[112:113], v[112:113], v[58:59], v[42:43]
	v_lshlrev_b32_e32 v44, 16, v191
	v_and_b32_e32 v45, 0xffff0000, v191
	v_pk_fma_f32 v[114:115], v[114:115], v[60:61], v[44:45]
	v_lshlrev_b32_e32 v42, 16, v192
	v_and_b32_e32 v43, 0xffff0000, v192
	v_pk_fma_f32 v[108:109], v[108:109], v[62:63], v[42:43]
	v_lshlrev_b32_e32 v44, 16, v193
	v_and_b32_e32 v45, 0xffff0000, v193
	v_pk_fma_f32 v[110:111], v[110:111], v[64:65], v[44:45]
	v_cvt_pk_bf16_f32 v112, v112, v113
	v_cvt_pk_bf16_f32 v113, v114, v115
	v_cvt_pk_bf16_f32 v114, v108, v109
	v_cvt_pk_bf16_f32 v115, v110, v111
	v_add_u32_e32 v53, 0x10000, v51
	global_store_dwordx4 v53, v[112:115], s[8:9]
	s_waitcnt vmcnt(15)
; __device__ __forceinline__ unsigned pk2(float lo, float hi) { f32x2 v = {lo, hi}; return __builtin_bit_cast(unsigned, __builtin_convertvector(v, bf2_t)); }
; template <int BIT = 0> __device__ __forceinline__ void st16w(void* p, u32x4 v) { if ((WT_STORES >> BIT) & 1) asm volatile("global_store_dwordx4 %0, %1, off sc1\n\ts_nop 1" :: "v"(p), "v"(v) : "memory"); else *(u32x4*)p = v; }
; __device__ __forceinline__ float bflo(unsigned u) { return __uint_as_float(u << 16); }
; __device__ __forceinline__ float bfhi(unsigned u) { return __uint_as_float(u & 0xffff0000u); }
;     __device__ __forceinline__ void operator()(const f32x4 (&acc)[2][2][4][2], const Unit& u, int wr, int wc, int fr, int fq) const {
;     ...
;             for (int m = 0; m < 4; ++m) { const size_t ro = (size_t)(row0 + ai * HALF + m * 16) * D + col0;
; #pragma unroll
;                 for (int bj = 0; bj < 2; ++bj) { const size_t off = ro + bj * HALF;
;                     f32x4 b0, b1;
;                     if (base32) { b0 = *(const f32x4*)(base32 + off); b1 = *(const f32x4*)(base32 + off + 4); }
;                     else { const u32x4 hb = *(const u32x4*)(base + off); b0 = (f32x4){bflo(hb.x), bfhi(hb.x), bflo(hb.y), bfhi(hb.y)}; b1 = (f32x4){bflo(hb.z), bfhi(hb.z), bflo(hb.w), bfhi(hb.w)}; }
;                     const f32x4 o0 = b0 + g4[bj][0] * acc[ai][bj][m][0], o1 = b1 + g4[bj][1] * acc[ai][bj][m][1];
;                     u32x4 w; w.x = pk2(o0[0], o0[1]); w.y = pk2(o0[2], o0[3]); w.z = pk2(o1[0], o1[1]); w.w = pk2(o1[2], o1[3]);
;                     st16w(H + off, w); } }
	v_lshlrev_b32_e32 v42, 16, v194
	v_and_b32_e32 v43, 0xffff0000, v194
	v_pk_fma_f32 v[104:105], v[104:105], v[160:161], v[42:43]
	v_lshlrev_b32_e32 v44, 16, v195
	v_and_b32_e32 v45, 0xffff0000, v195
	v_pk_fma_f32 v[106:107], v[106:107], v[162:163], v[44:45]
	v_lshlrev_b32_e32 v42, 16, v196
	v_and_b32_e32 v43, 0xffff0000, v196
	v_pk_fma_f32 v[100:101], v[100:101], v[170:171], v[42:43]
	v_lshlrev_b32_e32 v44, 16, v197
	v_and_b32_e32 v45, 0xffff0000, v197
	v_pk_fma_f32 v[102:103], v[102:103], v[172:173], v[44:45]
	v_cvt_pk_bf16_f32 v104, v104, v105
	v_cvt_pk_bf16_f32 v105, v106, v107
	v_cvt_pk_bf16_f32 v106, v100, v101
	v_cvt_pk_bf16_f32 v107, v102, v103
	v_add_u32_e32 v53, 0x10000, v51
	global_store_dwordx4 v53, v[104:107], s[8:9] offset:256
	s_waitcnt vmcnt(15)
	v_lshlrev_b32_e32 v42, 16, v208
	v_and_b32_e32 v43, 0xffff0000, v208
	v_pk_fma_f32 v[94:95], v[94:95], v[58:59], v[42:43]
	v_lshlrev_b32_e32 v44, 16, v209
	v_and_b32_e32 v45, 0xffff0000, v209
	v_pk_fma_f32 v[96:97], v[96:97], v[60:61], v[44:45]
	v_lshlrev_b32_e32 v42, 16, v210
	v_and_b32_e32 v43, 0xffff0000, v210
	v_pk_fma_f32 v[90:91], v[90:91], v[62:63], v[42:43]
	v_lshlrev_b32_e32 v44, 16, v211
	v_and_b32_e32 v45, 0xffff0000, v211
	v_pk_fma_f32 v[92:93], v[92:93], v[64:65], v[44:45]
	v_cvt_pk_bf16_f32 v94, v94, v95
	v_cvt_pk_bf16_f32 v95, v96, v97
	v_cvt_pk_bf16_f32 v96, v90, v91
	v_cvt_pk_bf16_f32 v97, v92, v93
	v_add_u32_e32 v53, 0x18000, v51
	global_store_dwordx4 v53, v[94:97], s[8:9]
	s_waitcnt vmcnt(15)
	v_lshlrev_b32_e32 v42, 16, v212
	v_and_b32_e32 v43, 0xffff0000, v212
	v_pk_fma_f32 v[86:87], v[86:87], v[160:161], v[42:43]
	v_lshlrev_b32_e32 v44, 16, v213
	v_and_b32_e32 v45, 0xffff0000, v213
	v_pk_fma_f32 v[88:89], v[88:89], v[162:163], v[44:45]
	v_lshlrev_b32_e32 v42, 16, v214
	v_and_b32_e32 v43, 0xffff0000, v214
	v_pk_fma_f32 v[82:83], v[82:83], v[170:171], v[42:43]
	v_lshlrev_b32_e32 v44, 16, v215
	v_and_b32_e32 v45, 0xffff0000, v215
	v_pk_fma_f32 v[84:85], v[84:85], v[172:173], v[44:45]
	v_cvt_pk_bf16_f32 v86, v86, v87
	v_cvt_pk_bf16_f32 v87, v88, v89
	v_cvt_pk_bf16_f32 v88, v82, v83
	v_cvt_pk_bf16_f32 v89, v84, v85
	v_add_u32_e32 v53, 0x18000, v51
	global_store_dwordx4 v53, v[86:89], s[8:9] offset:256
	s_waitcnt vmcnt(15)
	v_lshlrev_b32_e32 v42, 16, v216
	v_and_b32_e32 v43, 0xffff0000, v216
	v_pk_fma_f32 v[78:79], v[78:79], v[58:59], v[42:43]
	v_lshlrev_b32_e32 v44, 16, v217
	v_and_b32_e32 v45, 0xffff0000, v217
	v_pk_fma_f32 v[80:81], v[80:81], v[60:61], v[44:45]
	v_lshlrev_b32_e32 v42, 16, v218
	v_and_b32_e32 v43, 0xffff0000, v218
	v_pk_fma_f32 v[74:75], v[74:75], v[62:63], v[42:43]
	v_lshlrev_b32_e32 v44, 16, v219
	v_and_b32_e32 v45, 0xffff0000, v219
	v_pk_fma_f32 v[76:77], v[76:77], v[64:65], v[44:45]
	v_cvt_pk_bf16_f32 v78, v78, v79
	v_cvt_pk_bf16_f32 v79, v80, v81
	v_cvt_pk_bf16_f32 v80, v74, v75
	v_cvt_pk_bf16_f32 v81, v76, v77
	v_add_u32_e32 v53, 0x40000, v51
	global_store_dwordx4 v53, v[78:81], s[8:9]
	s_waitcnt vmcnt(15)
	v_lshlrev_b32_e32 v42, 16, v220
	v_and_b32_e32 v43, 0xffff0000, v220
	v_pk_fma_f32 v[70:71], v[70:71], v[160:161], v[42:43]
	v_lshlrev_b32_e32 v44, 16, v221
	v_and_b32_e32 v45, 0xffff0000, v221
	v_pk_fma_f32 v[72:73], v[72:73], v[162:163], v[44:45]
	v_lshlrev_b32_e32 v42, 16, v222
	v_and_b32_e32 v43, 0xffff0000, v222
	v_pk_fma_f32 v[66:67], v[66:67], v[170:171], v[42:43]
	v_lshlrev_b32_e32 v44, 16, v223
	v_and_b32_e32 v45, 0xffff0000, v223
	v_pk_fma_f32 v[68:69], v[68:69], v[172:173], v[44:45]
	v_cvt_pk_bf16_f32 v70, v70, v71
	v_cvt_pk_bf16_f32 v71, v72, v73
	v_cvt_pk_bf16_f32 v72, v66, v67
	v_cvt_pk_bf16_f32 v73, v68, v69
	v_add_u32_e32 v53, 0x40000, v51
	global_store_dwordx4 v53, v[70:73], s[8:9] offset:256
	s_waitcnt vmcnt(14)
	v_lshlrev_b32_e32 v42, 16, v174
	v_and_b32_e32 v43, 0xffff0000, v174
	v_pk_fma_f32 v[54:55], v[54:55], v[58:59], v[42:43]
	v_lshlrev_b32_e32 v44, 16, v175
	v_and_b32_e32 v45, 0xffff0000, v175
	v_pk_fma_f32 v[56:57], v[56:57], v[60:61], v[44:45]
	v_lshlrev_b32_e32 v42, 16, v176
	v_and_b32_e32 v43, 0xffff0000, v176
	v_pk_fma_f32 v[46:47], v[46:47], v[62:63], v[42:43]
	v_lshlrev_b32_e32 v44, 16, v177
	v_and_b32_e32 v45, 0xffff0000, v177
	v_pk_fma_f32 v[48:49], v[48:49], v[64:65], v[44:45]
	v_cvt_pk_bf16_f32 v54, v54, v55
	v_cvt_pk_bf16_f32 v55, v56, v57
	v_cvt_pk_bf16_f32 v56, v46, v47
	v_cvt_pk_bf16_f32 v57, v48, v49
	v_add_u32_e32 v53, 0x48000, v51
	global_store_dwordx4 v53, v[54:57], s[8:9]
	s_waitcnt vmcnt(14)
; __device__ __forceinline__ unsigned pk2(float lo, float hi) { f32x2 v = {lo, hi}; return __builtin_bit_cast(unsigned, __builtin_convertvector(v, bf2_t)); }
; template <int BIT = 0> __device__ __forceinline__ void st16w(void* p, u32x4 v) { if ((WT_STORES >> BIT) & 1) asm volatile("global_store_dwordx4 %0, %1, off sc1\n\ts_nop 1" :: "v"(p), "v"(v) : "memory"); else *(u32x4*)p = v; }
; __device__ __forceinline__ float bflo(unsigned u) { return __uint_as_float(u << 16); }
; __device__ __forceinline__ float bfhi(unsigned u) { return __uint_as_float(u & 0xffff0000u); }
; #define PG8_LAS __attribute__((address_space(3)))
; #define PG8_BAR __builtin_amdgcn_s_barrier()
;     __device__ __forceinline__ void operator()(const f32x4 (&acc)[2][2][4][2], const Unit& u, int wr, int wc, int fr, int fq) const {
;     ...
;             for (int m = 0; m < 4; ++m) { const size_t ro = (size_t)(row0 + ai * HALF + m * 16) * D + col0;
; #pragma unroll
;                 for (int bj = 0; bj < 2; ++bj) { const size_t off = ro + bj * HALF;
;                     f32x4 b0, b1;
;                     if (base32) { b0 = *(const f32x4*)(base32 + off); b1 = *(const f32x4*)(base32 + off + 4); }
;                     else { const u32x4 hb = *(const u32x4*)(base + off); b0 = (f32x4){bflo(hb.x), bfhi(hb.x), bflo(hb.y), bfhi(hb.y)}; b1 = (f32x4){bflo(hb.z), bfhi(hb.z), bflo(hb.w), bfhi(hb.w)}; }
;                     const f32x4 o0 = b0 + g4[bj][0] * acc[ai][bj][m][0], o1 = b1 + g4[bj][1] * acc[ai][bj][m][1];
;                     u32x4 w; w.x = pk2(o0[0], o0[1]); w.y = pk2(o0[2], o0[3]); w.z = pk2(o1[0], o1[1]); w.w = pk2(o1[2], o1[3]);
;                     st16w(H + off, w); } }
; template <class Epi, class Sched, bool ALIGN_EPI = false, bool SP2 = false>
; __device__ __forceinline__ void gemm_phase(PG8_LAS unsigned char* lds, const Gemm g, const Sched& S, const Epi& E) {
;     ...
;         cur = nxt; cA = nA; cB = nB; ++ui;
;         if constexpr (Sched::GATHER) { const u32x4 pv_ = *(const PG8_LAS u32x4*)(lds + STAGE_BYTES + tid * 16); vAc[0][0] = pv_.x; vAc[0][1] = pv_.y; vAc[1][0] = pv_.z; vAc[1][1] = pv_.w; }
;         if constexpr (ALIGN_EPI) { if (wr == 1) PG8_BAR; }
	v_lshlrev_b32_e32 v42, 16, v140
	v_and_b32_e32 v43, 0xffff0000, v140
	v_pk_fma_f32 v[38:39], v[38:39], v[160:161], v[42:43]
	v_lshlrev_b32_e32 v44, 16, v141
	v_and_b32_e32 v45, 0xffff0000, v141
	v_pk_fma_f32 v[40:41], v[40:41], v[162:163], v[44:45]
	v_lshlrev_b32_e32 v42, 16, v142
	v_and_b32_e32 v43, 0xffff0000, v142
	v_pk_fma_f32 v[34:35], v[34:35], v[170:171], v[42:43]
	v_lshlrev_b32_e32 v44, 16, v143
	v_and_b32_e32 v45, 0xffff0000, v143
	v_pk_fma_f32 v[36:37], v[36:37], v[172:173], v[44:45]
	v_cvt_pk_bf16_f32 v38, v38, v39
	v_cvt_pk_bf16_f32 v39, v40, v41
	v_cvt_pk_bf16_f32 v40, v34, v35
	v_cvt_pk_bf16_f32 v41, v36, v37
	v_add_u32_e32 v53, 0x48000, v51
	global_store_dwordx4 v53, v[38:41], s[8:9] offset:256
	s_waitcnt vmcnt(13)
	v_lshlrev_b32_e32 v42, 16, v178
	v_and_b32_e32 v43, 0xffff0000, v178
	v_pk_fma_f32 v[30:31], v[30:31], v[58:59], v[42:43]
	v_lshlrev_b32_e32 v44, 16, v179
	v_and_b32_e32 v45, 0xffff0000, v179
	v_pk_fma_f32 v[32:33], v[32:33], v[60:61], v[44:45]
	v_lshlrev_b32_e32 v42, 16, v180
	v_and_b32_e32 v43, 0xffff0000, v180
	v_pk_fma_f32 v[26:27], v[26:27], v[62:63], v[42:43]
	v_lshlrev_b32_e32 v44, 16, v181
	v_and_b32_e32 v45, 0xffff0000, v181
	v_pk_fma_f32 v[28:29], v[28:29], v[64:65], v[44:45]
	v_cvt_pk_bf16_f32 v30, v30, v31
	v_cvt_pk_bf16_f32 v31, v32, v33
	v_cvt_pk_bf16_f32 v32, v26, v27
	v_cvt_pk_bf16_f32 v33, v28, v29
	v_add_u32_e32 v53, 0x50000, v51
	global_store_dwordx4 v53, v[30:33], s[8:9]
	s_waitcnt vmcnt(13)
	v_lshlrev_b32_e32 v42, 16, v132
	v_and_b32_e32 v43, 0xffff0000, v132
	v_pk_fma_f32 v[22:23], v[22:23], v[160:161], v[42:43]
	v_lshlrev_b32_e32 v44, 16, v133
	v_and_b32_e32 v45, 0xffff0000, v133
	v_pk_fma_f32 v[24:25], v[24:25], v[162:163], v[44:45]
	v_lshlrev_b32_e32 v42, 16, v134
	v_and_b32_e32 v43, 0xffff0000, v134
	v_pk_fma_f32 v[18:19], v[18:19], v[170:171], v[42:43]
	v_lshlrev_b32_e32 v44, 16, v135
	v_and_b32_e32 v45, 0xffff0000, v135
	v_pk_fma_f32 v[20:21], v[20:21], v[172:173], v[44:45]
	v_cvt_pk_bf16_f32 v22, v22, v23
	v_cvt_pk_bf16_f32 v23, v24, v25
	v_cvt_pk_bf16_f32 v24, v18, v19
	v_cvt_pk_bf16_f32 v25, v20, v21
	v_add_u32_e32 v53, 0x50000, v51
	global_store_dwordx4 v53, v[22:25], s[8:9] offset:256
	s_waitcnt vmcnt(12)
	v_lshlrev_b32_e32 v42, 16, v182
	v_and_b32_e32 v43, 0xffff0000, v182
	v_pk_fma_f32 v[14:15], v[14:15], v[58:59], v[42:43]
	v_lshlrev_b32_e32 v44, 16, v183
	v_and_b32_e32 v45, 0xffff0000, v183
	v_pk_fma_f32 v[16:17], v[16:17], v[60:61], v[44:45]
	v_lshlrev_b32_e32 v42, 16, v184
	v_and_b32_e32 v43, 0xffff0000, v184
	v_pk_fma_f32 v[10:11], v[10:11], v[62:63], v[42:43]
	v_lshlrev_b32_e32 v44, 16, v185
	v_and_b32_e32 v45, 0xffff0000, v185
	v_pk_fma_f32 v[12:13], v[12:13], v[64:65], v[44:45]
	v_cvt_pk_bf16_f32 v14, v14, v15
	v_cvt_pk_bf16_f32 v15, v16, v17
	v_cvt_pk_bf16_f32 v16, v10, v11
	v_cvt_pk_bf16_f32 v17, v12, v13
	v_add_u32_e32 v53, 0x58000, v51
	global_store_dwordx4 v53, v[14:17], s[8:9]
	s_waitcnt vmcnt(12)
	v_lshlrev_b32_e32 v42, 16, v124
	v_and_b32_e32 v43, 0xffff0000, v124
	v_pk_fma_f32 v[6:7], v[6:7], v[160:161], v[42:43]
	v_lshlrev_b32_e32 v44, 16, v125
	v_and_b32_e32 v45, 0xffff0000, v125
	v_pk_fma_f32 v[8:9], v[8:9], v[162:163], v[44:45]
	v_lshlrev_b32_e32 v42, 16, v126
	v_and_b32_e32 v43, 0xffff0000, v126
	v_pk_fma_f32 v[2:3], v[2:3], v[170:171], v[42:43]
	v_lshlrev_b32_e32 v44, 16, v127
	v_and_b32_e32 v45, 0xffff0000, v127
	v_pk_fma_f32 v[4:5], v[4:5], v[172:173], v[44:45]
	v_cvt_pk_bf16_f32 v6, v6, v7
	v_cvt_pk_bf16_f32 v7, v8, v9
	v_cvt_pk_bf16_f32 v8, v2, v3
	v_cvt_pk_bf16_f32 v9, v4, v5
	v_add_u32_e32 v53, 0x58000, v51
	global_store_dwordx4 v53, v[6:9], s[8:9] offset:256
	s_nop 1
	s_mov_b32 s64, 0x18000
	s_mov_b64 s[16:17], -1
	s_and_b64 vcc, exec, s[4:5]
	s_cbranch_vccnz .LBB13_1526
	s_andn2_b64 vcc, exec, s[10:11]
	s_cbranch_vccnz .LBB13_1525
	s_branch .LBB13_1525

; #define PG8_STAGE(bufoff, gbase, voff) PG8_STAGE_X(bufoff, gbase, voff, PG8_B_AUX)
; template <class Epi, class Sched, bool ALIGN_EPI = false, bool SP2 = false>
; __device__ __forceinline__ void gemm_phase(PG8_LAS unsigned char* lds, const Gemm g, const Sched& S, const Epi& E) {
;     ...
;     for (int i = 0; i < 2; ++i) { int R, C; stage_rc(tid * 16 + i * 8192, R, C); const int Rb = Epi::PERM ? ((R & ~31) + perm32(R & 31)) : R;
;         voffA[i] = (unsigned)(R * K + C) * 2u; voffB[i] = (unsigned)(Rb * K + C) * 2u; }
;     unsigned vAc[2][2] = {{0u, 0u}, {0u, 0u}}, vAn[2][2] = {{0u, 0u}, {0u, 0u}};
;     ...
;     const size_t kstep = (size_t)(BK * 2);
;     const size_t hstep = (size_t)HALF * K * 2;
;     const size_t tstep = 2 * hstep;
;     const unsigned ldsw = (unsigned)wid * 1024u;
;     const int aoff = lds_byte(wr * 64 + fr, fq * 8), boff = lds_byte(wc * 32 + fr, fq * 8);
;     ...
;     Unit cur, nxt; int ui = 0;
;     if (!S.next(0, cur)) return;
;     f32x4 acc[2][2][4][2];
; #pragma unroll
;     for (int a = 0; a < 2; ++a)
; #pragma unroll
;         for (int b = 0; b < 2; ++b)
; #pragma unroll
;             for (int m = 0; m < 4; ++m)
; #pragma unroll
;                 for (int n = 0; n < 2; ++n) acc[a][b][m][n] = (f32x4){0.f, 0.f, 0.f, 0.f};
;     bf16x8 At[4][2], B0[2][2], B1[2][2];
;     const char* cA = Sched::GATHER ? (const char*)g.A : (const char*)g.A + (size_t)cur.pm * tstep; PG8_SETA(vAc, cur); const char* cB = (const char*)g.Bt + S.boff(cur) + (size_t)cur.pn * tstep;
;     S.a_ready(cur);
;     if constexpr (SP2) {
;         PG8_STAGE(PG8_SB(0, 0), cB, voffB); PG8_STAGE(PG8_SB(0, 1), cB + hstep, voffB); PG8_STAGE_A(PG8_SA(0, 0), 0, cA, false); PG8_STAGE_A(PG8_SA(0, 1), 1, cA, false);
;         if (wr == 1) PG8_BAR;
;         PG8_WAIT_V(2); PG8_BAR;
;         PG8_STAGE(PG8_SB(1, 0), cB + kstep, voffB); PG8_STAGE_A(PG8_SA(1, 0), 0, cA + kstep, false); PG8_STAGE(PG8_SB(1, 1), cB + hstep + kstep, voffB);
;         PG8_WAIT_V(6); PG8_BAR;
;     } else {
;         PG8_STAGE(PG8_SB(0, 0), cB, voffB); PG8_STAGE_A(PG8_SA(0, 0), 0, cA, false); PG8_STAGE(PG8_SB(0, 1), cB + hstep, voffB); PG8_STAGE_A(PG8_SA(0, 1), 1, cA, false);
;         if (wr == 1) PG8_BAR;
;         PG8_WAIT_V(4); PG8_BAR;
;         PG8_STAGE(PG8_SB(1, 0), cB + kstep, voffB); PG8_STAGE_A(PG8_SA(1, 0), 0, cA + kstep, false); PG8_STAGE(PG8_SB(1, 1), cB + hstep + kstep, voffB);
.LBB13_1557:
	v_cndmask_b32_e64 v2, 0, 1, s[4:5]
	s_not_b32 s4, s6
	s_add_i32 s4, s42, s4
	v_readfirstlane_b32 s5, v2
	s_add_i32 s4, s4, s5
	s_add_i32 s7, s4, s10
	s_ashr_i32 s4, s7, 31
	s_lshr_b32 s4, s4, 28
	s_add_i32 s10, s7, s4
	s_ashr_i32 s4, s10, 4
	s_lshl_b32 s11, s4, 2
	s_sub_i32 s4, s36, s11
	s_min_i32 s12, s4, 4
	s_abs_i32 s13, s12
	v_cvt_f32_u32_e32 v2, s13
	s_sub_i32 s16, 0, s13
	s_and_b32 s10, s10, -16
	s_sub_i32 s7, s7, s10
	v_rcp_iflag_f32_e32 v2, v2
	s_abs_i32 s15, s7
	s_ashr_i32 s5, s14, 6
	s_xor_b32 s10, s7, s12
	v_mul_f32_e32 v2, 0x4f7ffffe, v2
	v_cvt_u32_f32_e32 v2, v2
	s_ashr_i32 s6, s14, 8
	s_lshl_b32 s4, s5, 10
	s_ashr_i32 s10, s10, 31
	v_readfirstlane_b32 s17, v2
	s_mul_i32 s16, s16, s17
	s_mul_hi_u32 s16, s17, s16
	s_add_i32 s17, s17, s16
	s_mul_hi_u32 s16, s15, s17
	s_mul_i32 s17, s16, s13
	s_sub_i32 s15, s15, s17
	s_add_i32 s17, s16, 1
	s_sub_i32 s18, s15, s13
	s_cmp_ge_u32 s15, s13
	s_cselect_b32 s16, s17, s16
	s_cselect_b32 s15, s18, s15
	s_add_i32 s17, s16, 1
	s_cmp_ge_u32 s15, s13
	s_cselect_b32 s13, s17, s16
	s_xor_b32 s13, s13, s10
	s_sub_i32 s60, s13, s10
	s_mul_i32 s10, s60, s12
	s_sub_i32 s7, s7, s10
	s_add_i32 s12, s11, s7
	s_ashr_i32 s13, s12, 31
	s_mul_i32 s10, s12, 0x1c0000
	s_mul_hi_i32 s7, s12, 0x1c0000
	s_add_u32 s20, s37, s10
	s_addc_u32 s21, s38, s7
	s_lshl_b64 s[10:11], s[12:13], 2
	s_add_u32 s10, s2, s10
	s_addc_u32 s11, s3, s11
	global_load_dword v2, v98, s[10:11]
	v_lshlrev_b32_e32 v3, 4, v10
	v_ashrrev_i32_e32 v4, 31, v10
	v_bfe_i32 v5, v10, 27, 1
	v_lshrrev_b32_e32 v4, 26, v4
	v_lshrrev_b32_e32 v5, 22, v5
	v_add_u32_e32 v6, 0x2000, v3
	v_add_u32_e32 v4, v10, v4
	v_add_u32_e32 v5, v3, v5
	v_ashrrev_i32_e32 v7, 31, v6
	v_ashrrev_i32_e32 v12, 6, v4
	v_and_b32_e32 v4, 0xfffffc00, v5
	v_lshrrev_b32_e32 v5, 22, v7
	v_sub_u32_e32 v3, v3, v4
	v_add_u32_e32 v5, v6, v5
	v_lshrrev_b32_e32 v8, 4, v3
	v_ashrrev_i32_e32 v11, 10, v5
	v_lshlrev_b32_e32 v7, 5, v12
	v_bitop3_b32 v3, v8, v3, 32 bitop3:0x6c
	v_mul_i32_i24_e32 v5, 0x400, v11
	v_and_b32_e32 v14, 32, v7
	v_lshlrev_b32_e32 v7, 3, v11
	v_lshlrev_b32_e32 v8, 5, v11
	v_ashrrev_i32_e32 v9, 31, v3
	v_sub_u32_e32 v5, v6, v5
	v_and_b32_e32 v6, -16, v7
	v_and_b32_e32 v13, 32, v8
	v_lshrrev_b32_e32 v7, 26, v9
	v_lshrrev_b32_e32 v8, 4, v5
	v_lshlrev_b32_e32 v4, 3, v12
	v_add_u32_e32 v7, v3, v7
	v_bitop3_b32 v5, v8, v5, 32 bitop3:0x6c
	v_and_b32_e32 v4, -16, v4
	v_ashrrev_i32_e32 v15, 6, v7
	v_and_b32_e32 v7, 0xc0, v7
	v_ashrrev_i32_e32 v8, 31, v5
	v_add_u32_e32 v4, v15, v4
	v_sub_u32_e32 v3, v3, v7
	v_lshrrev_b32_e32 v8, 26, v8
	v_and_b32_e32 v7, 3, v15
	v_ashrrev_i16_sdwa v3, v238, sext(v3) dst_sel:DWORD dst_unused:UNUSED_PAD src0_sel:DWORD src1_sel:BYTE_0
	v_lshlrev_b32_e32 v9, 1, v4
	v_lshrrev_b32_e32 v16, 2, v4
	s_mov_b32 s7, 0x7fffe0
	v_add_u32_e32 v8, v5, v8
	v_and_or_b32 v7, v4, s7, v7
	v_bfe_i32 v17, v3, 0, 16
	v_and_b32_e32 v3, 24, v9
	v_and_b32_e32 v9, 4, v16
	v_ashrrev_i32_e32 v16, 6, v8
	s_movk_i32 s10, 0xe00
	v_and_b32_e32 v8, 0xc0, v8
	v_or3_b32 v3, v7, v9, v3
	v_add_u32_e32 v6, v16, v6
	v_and_b32_e32 v7, 3, v16
	v_mul_lo_u32 v4, v4, s10
	v_add_u32_e32 v18, v14, v17
	v_sub_u32_e32 v5, v5, v8
	v_and_or_b32 v7, v6, s7, v7
	v_add_lshl_u32 v132, v18, v4, 1
	v_ashrrev_i16_sdwa v4, v238, sext(v5) dst_sel:DWORD dst_unused:UNUSED_PAD src0_sel:DWORD src1_sel:BYTE_0
	v_lshlrev_b32_e32 v5, 1, v6
	v_lshrrev_b32_e32 v8, 2, v6
	v_mul_lo_u32 v6, v6, s10
	s_mul_i32 s13, s60, 0x1c0000
	s_mul_hi_i32 s11, s60, 0x1c0000
	v_mul_u32_u24_e32 v3, 0xe00, v3
	v_add_lshl_u32 v134, v3, v18, 1
	v_bfe_i32 v18, v4, 0, 16
	v_and_b32_e32 v3, 24, v5
	v_and_b32_e32 v4, 4, v8
	v_or3_b32 v3, v7, v4, v3
	v_add_u32_e32 v5, v13, v18
	v_mul_u32_u24_e32 v3, 0xe00, v3
	v_add_lshl_u32 v138, v3, v5, 1
	v_add_lshl_u32 v136, v5, v6, 1
	v_mov_b32_e32 v135, v98
	v_mov_b32_e32 v139, v98
	v_mov_b32_e32 v133, v98
	v_mov_b32_e32 v137, v98
	s_waitcnt vmcnt(0)
	v_readfirstlane_b32 s7, v2
	s_mul_hi_i32 s10, s7, 0x700000
	s_mul_i32 s7, s7, 0x700000
	s_add_u32 s7, s34, s7
	s_addc_u32 s10, s35, s10
	s_add_u32 s22, s7, s13
	s_addc_u32 s23, s10, s11
	s_add_i32 s13, s31, 0x10000
	s_add_i32 s47, s13, s4
	s_add_i32 s48, s47, 0x2000
	s_add_u32 s10, s22, 0xe0000
	s_mov_b32 m0, s47
	s_addc_u32 s11, s23, 0
	s_add_i32 s49, s31, 0x14000
	global_load_lds_dwordx4 v134, s[22:23]
	s_mov_b32 m0, s48
	s_add_i32 s50, s49, s4
	global_load_lds_dwordx4 v138, s[22:23]
	s_mov_b32 m0, s50
	s_add_i32 s51, s50, 0x2000
	s_add_i32 s52, s31, s4
	global_load_lds_dwordx4 v134, s[10:11]
	s_mov_b32 m0, s51
	s_add_i32 s53, s52, 0x2000
	global_load_lds_dwordx4 v138, s[10:11]
	s_mov_b32 m0, s52
	s_add_u32 s10, s20, 0xe0000
	global_load_lds_dwordx4 v132, s[20:21]
	s_mov_b32 m0, s53
	s_addc_u32 s11, s21, 0
	s_add_i32 s56, s52, 0x4000
	global_load_lds_dwordx4 v136, s[20:21]
	s_mov_b32 m0, s56
	s_add_i32 s57, s52, 0x6000
	global_load_lds_dwordx4 v132, s[10:11]
	s_mov_b32 m0, s57
	s_cmp_eq_u32 s6, 1
	global_load_lds_dwordx4 v136, s[10:11]
	v_lshl_add_u64 v[8:9], s[22:23], 0, v[134:135]
	v_lshl_add_u64 v[6:7], s[22:23], 0, v[138:139]
	v_lshl_add_u64 v[2:3], s[20:21], 0, v[132:133]
	s_cselect_b64 s[10:11], -1, 0
	s_cmp_lg_u32 s6, 1
	v_lshl_add_u64 v[4:5], s[20:21], 0, v[136:137]
	s_cbranch_scc1 .LBB13_1559
;     __device__ __forceinline__ size_t boff(const Unit& u) const { return (size_t)__builtin_amdgcn_readfirstlane(panel_e[u.pm]) * estride; }
; #define PG8_SETA(v, u) do { if constexpr (Sched::GATHER) { _Pragma("unroll") for (int h_ = 0; h_ < 2; ++h_) _Pragma("unroll") for (int i_ = 0; i_ < 2; ++i_) { \
;         int R_, C_; stage_rc(tid * 16 + i_ * 8192, R_, C_); int tok_ = S.arow[(u).pm * BM + h_ * HALF + R_]; tok_ = tok_ < 0 ? 0 : tok_; (v)[h_][i_] = (unsigned)(tok_ * K + C_) * 2u; } } } while (0)
; #define PG8_STAGE_A(bufoff, h, ptr, nsel) do { if constexpr (Sched::GATHER) { if (nsel) PG8_STAGE_X(bufoff, ptr, vAn[h], PG8_A_AUX); else PG8_STAGE_X(bufoff, ptr, vAc[h], PG8_A_AUX); } \
;         else PG8_STAGE_X(bufoff, (ptr) + (h) * hstep, voffA, PG8_A_AUX); } while (0)
; #define PG8_STAGE(bufoff, gbase, voff) PG8_STAGE_X(bufoff, gbase, voff, PG8_B_AUX)
; #define PG8_WAIT_V(n) asm volatile("s_waitcnt vmcnt(" #n ")" ::: "memory")
; #define PG8_BAR __builtin_amdgcn_s_barrier()
; template <class Epi, class Sched, bool ALIGN_EPI = false, bool SP2 = false>
; __device__ __forceinline__ void gemm_phase(PG8_LAS unsigned char* lds, const Gemm g, const Sched& S, const Epi& E) {
;     ...
;     const int aoff = lds_byte(wr * 64 + fr, fq * 8), boff = lds_byte(wc * 32 + fr, fq * 8);
;     ...
;     Unit cur, nxt; int ui = 0;
;     if (!S.next(0, cur)) return;
;     f32x4 acc[2][2][4][2];
; #pragma unroll
;     for (int a = 0; a < 2; ++a)
; #pragma unroll
;         for (int b = 0; b < 2; ++b)
; #pragma unroll
;             for (int m = 0; m < 4; ++m)
; #pragma unroll
;                 for (int n = 0; n < 2; ++n) acc[a][b][m][n] = (f32x4){0.f, 0.f, 0.f, 0.f};
;     bf16x8 At[4][2], B0[2][2], B1[2][2];
;     const char* cA = Sched::GATHER ? (const char*)g.A : (const char*)g.A + (size_t)cur.pm * tstep; PG8_SETA(vAc, cur); const char* cB = (const char*)g.Bt + S.boff(cur) + (size_t)cur.pn * tstep;
;     S.a_ready(cur);
;     if constexpr (SP2) {
;         PG8_STAGE(PG8_SB(0, 0), cB, voffB); PG8_STAGE(PG8_SB(0, 1), cB + hstep, voffB); PG8_STAGE_A(PG8_SA(0, 0), 0, cA, false); PG8_STAGE_A(PG8_SA(0, 1), 1, cA, false);
;         if (wr == 1) PG8_BAR;
;         PG8_WAIT_V(2); PG8_BAR;
;         PG8_STAGE(PG8_SB(1, 0), cB + kstep, voffB); PG8_STAGE_A(PG8_SA(1, 0), 0, cA + kstep, false); PG8_STAGE(PG8_SB(1, 1), cB + hstep + kstep, voffB);
;         PG8_WAIT_V(6); PG8_BAR;
.LBB13_1559:
	v_lshrrev_b32_e32 v20, 1, v10
	v_and_b32_e32 v20, 24, v20
	v_and_b32_e32 v19, 15, v10
	v_lshlrev_b32_e32 v21, 1, v20
	v_lshlrev_b32_e32 v10, 2, v10
	s_lshl_b32 s5, s5, 5
	s_add_i32 s58, s31, 0x18000
	v_lshl_or_b32 v144, s6, 6, v19
	v_lshl_or_b32 v19, v19, 6, v21
	s_lshl_b32 s6, s6, 13
	v_and_b32_e32 v10, 32, v10
	s_and_b32 s5, s5, 0x60
	s_add_i32 s59, s58, s4
	v_bitop3_b32 v21, v19, s6, v10 bitop3:0xde
	s_lshl_b32 s6, s5, 7
	v_lshl_add_u64 v[8:9], v[8:9], 0, s[54:55]
	s_mov_b32 m0, s59
	s_add_i32 s61, s59, 0x2000
	s_add_i32 s64, s52, 0x8000
	s_add_i32 s68, s52, 0xa000
	v_bitop3_b32 v145, v19, s6, v10 bitop3:0xde
	s_waitcnt vmcnt(2)
	s_barrier
	global_load_lds_dwordx4 v[8:9], off
	v_lshl_add_u64 v[6:7], v[6:7], 0, s[54:55]
	s_mov_b32 m0, s61
	s_add_u32 s6, s22, 0xe0080
	global_load_lds_dwordx4 v[6:7], off
	v_lshl_add_u64 v[2:3], v[2:3], 0, s[54:55]
	s_mov_b32 m0, s64
	s_addc_u32 s7, s23, 0
	s_add_i32 s69, s31, 0x1c000
	global_load_lds_dwordx4 v[2:3], off
	v_lshl_add_u64 v[2:3], v[4:5], 0, s[54:55]
	s_mov_b32 m0, s68
	s_add_i32 s72, s69, s4
	global_load_lds_dwordx4 v[2:3], off
	v_lshl_add_u64 v[2:3], s[6:7], 0, v[134:135]
	s_mov_b32 m0, s72
	s_add_i32 s73, s72, 0x2000
	global_load_lds_dwordx4 v[2:3], off
	v_lshl_add_u64 v[2:3], s[6:7], 0, v[138:139]
	s_mov_b32 m0, s73
	s_movk_i32 s7, 0xe00
	global_load_lds_dwordx4 v[2:3], off
	v_lshrrev_b32_e32 v3, 1, v12
	v_mul_lo_u32 v2, v15, s7
	s_mov_b32 s6, 0xe000
	v_or_b32_e32 v146, s5, v20
	v_mad_u64_u32 v[2:3], s[4:5], v3, s6, v[2:3]
	v_or_b32_e32 v2, v2, v14
	v_add_lshl_u32 v2, v2, v17, 1
	v_mov_b32_e32 v3, v98
	s_mov_b64 s[16:17], 0xe0080
	v_lshl_add_u64 v[140:141], v[2:3], 0, s[16:17]
	v_lshrrev_b32_e32 v3, 1, v11
	v_mul_lo_u32 v2, v16, s7
	v_mad_u64_u32 v[2:3], s[4:5], v3, s6, v[2:3]
	s_waitcnt vmcnt(6)
	v_or_b32_e32 v2, v2, v13
	s_cmpk_lt_u32 s14, 0x100
	v_add_lshl_u32 v2, v2, v18, 1
	v_mov_b32_e32 v3, v98
	s_cselect_b64 s[14:15], -1, 0
	v_lshl_add_u64 v[142:143], v[2:3], 0, s[16:17]
	s_mov_b32 s76, 0
	v_add_u32_e32 v147, s31, v21
	s_barrier
	s_branch .LBB13_1562

; #define PG8_LAS __attribute__((address_space(3)))
; #define PG8_STAGE_A(bufoff, h, ptr, nsel) do { if constexpr (Sched::GATHER) { if (nsel) PG8_STAGE_X(bufoff, ptr, vAn[h], PG8_A_AUX); else PG8_STAGE_X(bufoff, ptr, vAc[h], PG8_A_AUX); } \
;         else PG8_STAGE_X(bufoff, (ptr) + (h) * hstep, voffA, PG8_A_AUX); } while (0)
; #define PG8_LDA(dst, b, h) do { _Pragma("unroll") for (int m = 0; m < 4; ++m) _Pragma("unroll") for (int k = 0; k < 2; ++k) dst[m][k] = *(const PG8_LAS bf16x8*)(lds + PG8_SA(b, h) + aoff + m * 2048 + k * 1024); } while (0)
; #define PG8_LDB(dst, b, h) do { _Pragma("unroll") for (int n = 0; n < 2; ++n) _Pragma("unroll") for (int k = 0; k < 2; ++k) dst[n][k] = *(const PG8_LAS bf16x8*)(lds + PG8_SB(b, h) + boff + n * 2048 + k * 1024); } while (0)
; #define PG8_MMA(ai, bj, At, Bt) do { __builtin_amdgcn_s_setprio(1); _Pragma("unroll") for (int m = 0; m < 4; ++m) _Pragma("unroll") for (int n = 0; n < 2; ++n) _Pragma("unroll") for (int k = 0; k < 2; ++k) \
;         acc[ai][bj][m][n] = __builtin_amdgcn_mfma_f32_16x16x32_bf16(Bt[n][k], At[m][k], acc[ai][bj][m][n], 0, 0, 0); __builtin_amdgcn_s_setprio(0); } while (0)
; template <class Epi, class Sched, bool ALIGN_EPI = false, bool SP2 = false>
; __device__ __forceinline__ void gemm_phase(PG8_LAS unsigned char* lds, const Gemm g, const Sched& S, const Epi& E) {
;     ...
;             const char* a2 = last ? nA : cA + (size_t)(t + 2) * kstep; const char* b2 = last ? nB : cB + (size_t)(t + 2) * kstep;
;             const char* a3 = a2 + kstep; const char* b3 = b2 + kstep;
;             if (last && has_next) S.a_ready(nxt);
;             if constexpr (Sched::GATHER) { if (last) { const u32x4 pv_ = *(const PG8_LAS u32x4*)(lds + STAGE_BYTES + tid * 16); vAn[0][0] = pv_.x; vAn[0][1] = pv_.y; vAn[1][0] = pv_.z; vAn[1][1] = pv_.w; } }
;             if constexpr (SP2) {
;             PG8_LDB(B0, 0, 0); PG8_LDB(B1, 0, 1); PG8_SCHED; PG8_LDA(At, 0, 0); PG8_STAGE_A(PG8_SA(1, 1), 1, a1, false);
;             PG8_WAIT_V(8); PG8_WAIT_L(0); PG8_BAR; PG8_MMA(0, 0, At, B0); PG8_MMA(0, 1, At, B1); PG8_BAR; PG8_SCHED;
;     ...
;         for (int a = 0; a < 2; ++a)
; #pragma unroll
;             for (int b = 0; b < 2; ++b)
; #pragma unroll
;                 for (int m = 0; m < 4; ++m)
; #pragma unroll
;                     for (int n = 0; n < 2; ++n) acc[a][b][m][n] = (f32x4){0.f, 0.f, 0.f, 0.f};
.LBB13_1572:
	s_add_u32 s17, s22, 0x100
	v_mov_b32_e32 v2, 0
	s_addc_u32 s87, s23, 0
	s_mov_b32 s88, -2
	v_mov_b32_e32 v3, v2
	v_mov_b64_e32 v[4:5], 0
	v_mov_b64_e32 v[6:7], 0
	v_mov_b64_e32 v[8:9], 0
	v_mov_b64_e32 v[10:11], 0
	v_mov_b64_e32 v[12:13], 0
	v_mov_b64_e32 v[14:15], 0
	v_mov_b64_e32 v[16:17], 0
	v_mov_b64_e32 v[26:27], 0
	v_mov_b64_e32 v[28:29], 0
	v_mov_b64_e32 v[30:31], 0
	v_mov_b64_e32 v[32:33], 0
	v_mov_b64_e32 v[42:43], 0
	v_mov_b64_e32 v[44:45], 0
	v_mov_b64_e32 v[46:47], 0
	v_mov_b64_e32 v[48:49], 0
	v_mov_b64_e32 v[18:19], 0
	v_mov_b64_e32 v[20:21], 0
	v_mov_b64_e32 v[22:23], 0
	v_mov_b64_e32 v[24:25], 0
	v_mov_b64_e32 v[34:35], 0
	v_mov_b64_e32 v[36:37], 0
	v_mov_b64_e32 v[38:39], 0
	v_mov_b64_e32 v[40:41], 0
	v_mov_b64_e32 v[50:51], 0
	v_mov_b64_e32 v[52:53], 0
	v_mov_b64_e32 v[54:55], 0
	v_mov_b64_e32 v[56:57], 0
	v_mov_b64_e32 v[58:59], 0
	v_mov_b64_e32 v[60:61], 0
	v_mov_b64_e32 v[62:63], 0
	v_mov_b64_e32 v[64:65], 0
	v_mov_b64_e32 v[66:67], 0
	v_mov_b64_e32 v[68:69], 0
	v_mov_b64_e32 v[70:71], 0
	v_mov_b64_e32 v[72:73], 0
	v_mov_b64_e32 v[74:75], 0
	v_mov_b64_e32 v[76:77], 0
	v_mov_b64_e32 v[78:79], 0
	v_mov_b64_e32 v[80:81], 0
	v_mov_b64_e32 v[90:91], 0
	v_mov_b64_e32 v[92:93], 0
	v_mov_b64_e32 v[94:95], 0
	v_mov_b64_e32 v[96:97], 0
	v_mov_b64_e32 v[108:109], 0
	v_mov_b64_e32 v[110:111], 0
	v_mov_b64_e32 v[112:113], 0
	v_mov_b64_e32 v[114:115], 0
	v_mov_b64_e32 v[82:83], 0
	v_mov_b64_e32 v[84:85], 0
	v_mov_b64_e32 v[86:87], 0
	v_mov_b64_e32 v[88:89], 0
	v_mov_b64_e32 v[100:101], 0
	v_mov_b64_e32 v[102:103], 0
	v_mov_b64_e32 v[104:105], 0
	v_mov_b64_e32 v[106:107], 0
	v_mov_b64_e32 v[116:117], 0
	v_mov_b64_e32 v[118:119], 0
	v_mov_b64_e32 v[120:121], 0
	v_mov_b64_e32 v[122:123], 0
	v_mov_b64_e32 v[124:125], 0
	v_mov_b64_e32 v[126:127], 0
	v_mov_b64_e32 v[128:129], 0
	v_mov_b64_e32 v[130:131], 0
	s_and_b64 s[98:99], exec, s[14:15]
	s_cbranch_scc1 .Lrb_1573
	s_barrier
.Lrb_1573:
.LBB13_1573:
	v_add_u32_e32 v160, s13, v145
	v_add_u32_e32 v176, s49, v145
	ds_read_b128 v[148:151], v160
	ds_read_b128 v[152:155], v160 offset:1024
	ds_read_b128 v[156:159], v160 offset:2048
	ds_read_b128 v[160:163], v160 offset:3072
	ds_read_b128 v[164:167], v176
	ds_read_b128 v[168:171], v176 offset:1024
	ds_read_b128 v[172:175], v176 offset:2048
	ds_read_b128 v[176:179], v176 offset:3072
	s_add_u32 s22, s20, 0x100
	s_addc_u32 s23, s21, 0
	s_cmp_eq_u32 s88, 52
	s_cselect_b32 s27, s7, s23
	s_cselect_b32 s26, s6, s22
	s_cselect_b32 s25, s19, s87
	s_cselect_b32 s24, s18, s17
	v_lshl_add_u64 v[220:221], s[20:21], 0, v[140:141]
	s_add_i32 m0, s52, 0xc000
	ds_read_b128 v[180:183], v147
	ds_read_b128 v[184:187], v147 offset:1024
	ds_read_b128 v[188:191], v147 offset:2048
	ds_read_b128 v[192:195], v147 offset:3072
	ds_read_b128 v[196:199], v147 offset:4096
	ds_read_b128 v[208:211], v147 offset:5120
	ds_read_b128 v[212:215], v147 offset:6144
	ds_read_b128 v[216:219], v147 offset:7168
	global_load_lds_dwordx4 v[220:221], off
	v_lshl_add_u64 v[220:221], s[20:21], 0, v[142:143]
	s_add_i32 m0, s52, 0xe000
	s_nop 0
	global_load_lds_dwordx4 v[220:221], off
	s_waitcnt vmcnt(8)
	s_waitcnt lgkmcnt(0)
	s_barrier
	s_setprio 1
	s_waitcnt lgkmcnt(0)
	v_mfma_f32_16x16x32_bf16 v[128:131], v[148:151], v[180:183], v[128:131]
	v_mfma_f32_16x16x32_bf16 v[124:127], v[156:159], v[180:183], v[124:127]
	v_mfma_f32_16x16x32_bf16 v[120:123], v[148:151], v[188:191], v[120:123]
	v_mfma_f32_16x16x32_bf16 v[116:119], v[156:159], v[188:191], v[116:119]
	v_mfma_f32_16x16x32_bf16 v[104:107], v[148:151], v[196:199], v[104:107]
	v_mfma_f32_16x16x32_bf16 v[100:103], v[156:159], v[196:199], v[100:103]
	v_mfma_f32_16x16x32_bf16 v[86:89], v[148:151], v[212:215], v[86:89]
	v_mfma_f32_16x16x32_bf16 v[82:85], v[156:159], v[212:215], v[82:85]
	v_mfma_f32_16x16x32_bf16 v[128:131], v[152:155], v[184:187], v[128:131]
	v_mfma_f32_16x16x32_bf16 v[124:127], v[160:163], v[184:187], v[124:127]
	v_mfma_f32_16x16x32_bf16 v[120:123], v[152:155], v[192:195], v[120:123]
	v_mfma_f32_16x16x32_bf16 v[116:119], v[160:163], v[192:195], v[116:119]
	v_mfma_f32_16x16x32_bf16 v[104:107], v[152:155], v[208:211], v[104:107]
	v_mfma_f32_16x16x32_bf16 v[100:103], v[160:163], v[208:211], v[100:103]
	v_mfma_f32_16x16x32_bf16 v[86:89], v[152:155], v[216:219], v[86:89]
	v_mfma_f32_16x16x32_bf16 v[82:85], v[160:163], v[216:219], v[82:85]
	s_setprio 0
	s_setprio 1
	v_mfma_f32_16x16x32_bf16 v[112:115], v[164:167], v[180:183], v[112:115]
	v_mfma_f32_16x16x32_bf16 v[108:111], v[172:175], v[180:183], v[108:111]
	v_mfma_f32_16x16x32_bf16 v[94:97], v[164:167], v[188:191], v[94:97]
	v_mfma_f32_16x16x32_bf16 v[90:93], v[172:175], v[188:191], v[90:93]
	v_mfma_f32_16x16x32_bf16 v[78:81], v[164:167], v[196:199], v[78:81]
	v_mfma_f32_16x16x32_bf16 v[74:77], v[172:175], v[196:199], v[74:77]
	v_mfma_f32_16x16x32_bf16 v[70:73], v[164:167], v[212:215], v[70:73]
	v_mfma_f32_16x16x32_bf16 v[66:69], v[172:175], v[212:215], v[66:69]
	v_mfma_f32_16x16x32_bf16 v[112:115], v[168:171], v[184:187], v[112:115]
	v_mfma_f32_16x16x32_bf16 v[108:111], v[176:179], v[184:187], v[108:111]
	v_mfma_f32_16x16x32_bf16 v[94:97], v[168:171], v[192:195], v[94:97]
	v_mfma_f32_16x16x32_bf16 v[90:93], v[176:179], v[192:195], v[90:93]
	v_mfma_f32_16x16x32_bf16 v[78:81], v[168:171], v[208:211], v[78:81]
	v_mfma_f32_16x16x32_bf16 v[74:77], v[176:179], v[208:211], v[74:77]
	v_mfma_f32_16x16x32_bf16 v[70:73], v[168:171], v[216:219], v[70:73]
	v_mfma_f32_16x16x32_bf16 v[66:69], v[176:179], v[216:219], v[66:69]
	s_setprio 0
	s_barrier
; #define PG8_STAGE_A(bufoff, h, ptr, nsel) do { if constexpr (Sched::GATHER) { if (nsel) PG8_STAGE_X(bufoff, ptr, vAn[h], PG8_A_AUX); else PG8_STAGE_X(bufoff, ptr, vAc[h], PG8_A_AUX); } \
;         else PG8_STAGE_X(bufoff, (ptr) + (h) * hstep, voffA, PG8_A_AUX); } while (0)
; #define PG8_STAGE(bufoff, gbase, voff) PG8_STAGE_X(bufoff, gbase, voff, PG8_B_AUX)
; #define PG8_LDA(dst, b, h) do { _Pragma("unroll") for (int m = 0; m < 4; ++m) _Pragma("unroll") for (int k = 0; k < 2; ++k) dst[m][k] = *(const PG8_LAS bf16x8*)(lds + PG8_SA(b, h) + aoff + m * 2048 + k * 1024); } while (0)
; #define PG8_LDB(dst, b, h) do { _Pragma("unroll") for (int n = 0; n < 2; ++n) _Pragma("unroll") for (int k = 0; k < 2; ++k) dst[n][k] = *(const PG8_LAS bf16x8*)(lds + PG8_SB(b, h) + boff + n * 2048 + k * 1024); } while (0)
; #define PG8_MMA(ai, bj, At, Bt) do { __builtin_amdgcn_s_setprio(1); _Pragma("unroll") for (int m = 0; m < 4; ++m) _Pragma("unroll") for (int n = 0; n < 2; ++n) _Pragma("unroll") for (int k = 0; k < 2; ++k) \
;         acc[ai][bj][m][n] = __builtin_amdgcn_mfma_f32_16x16x32_bf16(Bt[n][k], At[m][k], acc[ai][bj][m][n], 0, 0, 0); __builtin_amdgcn_s_setprio(0); } while (0)
; #define PG8_WAIT_V(n) asm volatile("s_waitcnt vmcnt(" #n ")" ::: "memory")
; #define PG8_WAIT_L(n) asm volatile("s_waitcnt lgkmcnt(" #n ")" ::: "memory")
; #define PG8_BAR __builtin_amdgcn_s_barrier()
; #define PG8_SCHED __builtin_amdgcn_sched_barrier(0)
; template <class Epi, class Sched, bool ALIGN_EPI = false, bool SP2 = false>
; __device__ __forceinline__ void gemm_phase(PG8_LAS unsigned char* lds, const Gemm g, const Sched& S, const Epi& E) {
;     ...
;             PG8_LDA(At, 0, 1); PG8_STAGE(PG8_SB(0, 0), b2, voffB); PG8_STAGE(PG8_SB(0, 1), b2 + hstep, voffB); PG8_STAGE_A(PG8_SA(0, 0), 0, a2, last);
;             PG8_WAIT_V(8); PG8_WAIT_L(0); PG8_BAR; PG8_MMA(1, 0, At, B0); PG8_MMA(1, 1, At, B1); PG8_BAR; PG8_SCHED;
;             PG8_LDB(B0, 1, 0); PG8_LDB(B1, 1, 1); PG8_SCHED; PG8_LDA(At, 1, 0); PG8_STAGE_A(PG8_SA(0, 1), 1, a2, last);
	s_mov_b32 m0, s47
	v_lshl_add_u64 v[220:221], s[24:25], 0, v[134:135]
	s_add_u32 s20, s24, 0xe0000
	ds_read_b128 v[180:183], v147 offset:16384
	ds_read_b128 v[184:187], v147 offset:17408
	ds_read_b128 v[188:191], v147 offset:18432
	ds_read_b128 v[192:195], v147 offset:19456
	ds_read_b128 v[196:199], v147 offset:20480
	ds_read_b128 v[208:211], v147 offset:21504
	ds_read_b128 v[212:215], v147 offset:22528
	ds_read_b128 v[216:219], v147 offset:23552
	global_load_lds_dwordx4 v[220:221], off
	v_lshl_add_u64 v[222:223], s[24:25], 0, v[138:139]
	s_mov_b32 m0, s48
	s_addc_u32 s21, s25, 0
	global_load_lds_dwordx4 v[222:223], off
	v_lshl_add_u64 v[224:225], s[20:21], 0, v[134:135]
	s_mov_b32 m0, s50
	v_lshl_add_u64 v[226:227], s[26:27], 0, v[136:137]
	global_load_lds_dwordx4 v[224:225], off
	v_lshl_add_u64 v[224:225], s[20:21], 0, v[138:139]
	s_mov_b32 m0, s51
	s_nop 0
	global_load_lds_dwordx4 v[224:225], off
	v_lshl_add_u64 v[224:225], s[26:27], 0, v[132:133]
	s_mov_b32 m0, s52
	s_nop 0
	global_load_lds_dwordx4 v[224:225], off
	s_mov_b32 m0, s53
	s_nop 0
	global_load_lds_dwordx4 v[226:227], off
	s_waitcnt vmcnt(8)
	s_waitcnt lgkmcnt(0)
	s_barrier
	s_setprio 1
	s_waitcnt lgkmcnt(0)
	v_mfma_f32_16x16x32_bf16 v[62:65], v[148:151], v[180:183], v[62:65]
	v_mfma_f32_16x16x32_bf16 v[58:61], v[156:159], v[180:183], v[58:61]
	v_mfma_f32_16x16x32_bf16 v[54:57], v[148:151], v[188:191], v[54:57]
	v_mfma_f32_16x16x32_bf16 v[50:53], v[156:159], v[188:191], v[50:53]
	v_mfma_f32_16x16x32_bf16 v[38:41], v[148:151], v[196:199], v[38:41]
	v_mfma_f32_16x16x32_bf16 v[34:37], v[156:159], v[196:199], v[34:37]
	v_mfma_f32_16x16x32_bf16 v[22:25], v[148:151], v[212:215], v[22:25]
	v_mfma_f32_16x16x32_bf16 v[18:21], v[156:159], v[212:215], v[18:21]
	v_mfma_f32_16x16x32_bf16 v[62:65], v[152:155], v[184:187], v[62:65]
	v_mfma_f32_16x16x32_bf16 v[58:61], v[160:163], v[184:187], v[58:61]
	v_mfma_f32_16x16x32_bf16 v[54:57], v[152:155], v[192:195], v[54:57]
	v_mfma_f32_16x16x32_bf16 v[50:53], v[160:163], v[192:195], v[50:53]
	v_mfma_f32_16x16x32_bf16 v[38:41], v[152:155], v[208:211], v[38:41]
	v_mfma_f32_16x16x32_bf16 v[34:37], v[160:163], v[208:211], v[34:37]
	v_mfma_f32_16x16x32_bf16 v[22:25], v[152:155], v[216:219], v[22:25]
	v_mfma_f32_16x16x32_bf16 v[18:21], v[160:163], v[216:219], v[18:21]
	s_setprio 0
	s_setprio 1
	v_mfma_f32_16x16x32_bf16 v[46:49], v[164:167], v[180:183], v[46:49]
	v_mfma_f32_16x16x32_bf16 v[42:45], v[172:175], v[180:183], v[42:45]
	v_mfma_f32_16x16x32_bf16 v[30:33], v[164:167], v[188:191], v[30:33]
	v_mfma_f32_16x16x32_bf16 v[26:29], v[172:175], v[188:191], v[26:29]
	v_mfma_f32_16x16x32_bf16 v[14:17], v[164:167], v[196:199], v[14:17]
	v_mfma_f32_16x16x32_bf16 v[10:13], v[172:175], v[196:199], v[10:13]
	v_mfma_f32_16x16x32_bf16 v[6:9], v[164:167], v[212:215], v[6:9]
	v_mfma_f32_16x16x32_bf16 v[2:5], v[172:175], v[212:215], v[2:5]
	v_mfma_f32_16x16x32_bf16 v[46:49], v[168:171], v[184:187], v[46:49]
	v_mfma_f32_16x16x32_bf16 v[42:45], v[176:179], v[184:187], v[42:45]
	v_mfma_f32_16x16x32_bf16 v[30:33], v[168:171], v[192:195], v[30:33]
	v_mfma_f32_16x16x32_bf16 v[26:29], v[176:179], v[192:195], v[26:29]
	v_mfma_f32_16x16x32_bf16 v[14:17], v[168:171], v[208:211], v[14:17]
	v_mfma_f32_16x16x32_bf16 v[10:13], v[176:179], v[208:211], v[10:13]
	v_mfma_f32_16x16x32_bf16 v[6:9], v[168:171], v[216:219], v[6:9]
	v_mfma_f32_16x16x32_bf16 v[2:5], v[176:179], v[216:219], v[2:5]
	s_setprio 0
	s_barrier
	v_add_u32_e32 v160, s58, v145
	v_add_u32_e32 v176, s69, v145
	ds_read_b128 v[148:151], v160
	ds_read_b128 v[152:155], v160 offset:1024
	ds_read_b128 v[156:159], v160 offset:2048
	ds_read_b128 v[160:163], v160 offset:3072
	ds_read_b128 v[164:167], v176
	ds_read_b128 v[168:171], v176 offset:1024
	ds_read_b128 v[172:175], v176 offset:2048
	ds_read_b128 v[176:179], v176 offset:3072
	s_add_u32 s20, s26, 0xe0000
	s_addc_u32 s21, s27, 0
	s_mov_b32 m0, s56
	v_lshl_add_u64 v[228:229], s[20:21], 0, v[132:133]
	ds_read_b128 v[180:183], v147 offset:32768
	ds_read_b128 v[184:187], v147 offset:33792
	ds_read_b128 v[188:191], v147 offset:34816
	ds_read_b128 v[192:195], v147 offset:35840
	ds_read_b128 v[196:199], v147 offset:36864
	ds_read_b128 v[208:211], v147 offset:37888
	ds_read_b128 v[212:215], v147 offset:38912
	ds_read_b128 v[216:219], v147 offset:39936
	global_load_lds_dwordx4 v[228:229], off
	v_lshl_add_u64 v[228:229], s[20:21], 0, v[136:137]
	s_mov_b32 m0, s57
	s_nop 0
	global_load_lds_dwordx4 v[228:229], off
	s_waitcnt vmcnt(8)
	s_waitcnt lgkmcnt(0)
	s_barrier
; #define PG8_STAGE_A(bufoff, h, ptr, nsel) do { if constexpr (Sched::GATHER) { if (nsel) PG8_STAGE_X(bufoff, ptr, vAn[h], PG8_A_AUX); else PG8_STAGE_X(bufoff, ptr, vAc[h], PG8_A_AUX); } \
;         else PG8_STAGE_X(bufoff, (ptr) + (h) * hstep, voffA, PG8_A_AUX); } while (0)
; #define PG8_STAGE(bufoff, gbase, voff) PG8_STAGE_X(bufoff, gbase, voff, PG8_B_AUX)
; #define PG8_LDA(dst, b, h) do { _Pragma("unroll") for (int m = 0; m < 4; ++m) _Pragma("unroll") for (int k = 0; k < 2; ++k) dst[m][k] = *(const PG8_LAS bf16x8*)(lds + PG8_SA(b, h) + aoff + m * 2048 + k * 1024); } while (0)
; #define PG8_MMA(ai, bj, At, Bt) do { __builtin_amdgcn_s_setprio(1); _Pragma("unroll") for (int m = 0; m < 4; ++m) _Pragma("unroll") for (int n = 0; n < 2; ++n) _Pragma("unroll") for (int k = 0; k < 2; ++k) \
;         acc[ai][bj][m][n] = __builtin_amdgcn_mfma_f32_16x16x32_bf16(Bt[n][k], At[m][k], acc[ai][bj][m][n], 0, 0, 0); __builtin_amdgcn_s_setprio(0); } while (0)
; #define PG8_WAIT_V(n) asm volatile("s_waitcnt vmcnt(" #n ")" ::: "memory")
; #define PG8_WAIT_L(n) asm volatile("s_waitcnt lgkmcnt(" #n ")" ::: "memory")
; #define PG8_BAR __builtin_amdgcn_s_barrier()
; #define PG8_SCHED __builtin_amdgcn_sched_barrier(0)
; template <class Epi, class Sched, bool ALIGN_EPI = false, bool SP2 = false>
; __device__ __forceinline__ void gemm_phase(PG8_LAS unsigned char* lds, const Gemm g, const Sched& S, const Epi& E) {
;     ...
;             PG8_WAIT_V(8); PG8_WAIT_L(0); PG8_BAR; PG8_MMA(0, 0, At, B0); PG8_MMA(0, 1, At, B1); PG8_BAR; PG8_SCHED;
;             PG8_LDA(At, 1, 1); PG8_STAGE(PG8_SB(1, 0), b3, voffB); PG8_STAGE(PG8_SB(1, 1), b3 + hstep, voffB); PG8_STAGE_A(PG8_SA(1, 0), 0, a3, last);
;             PG8_WAIT_V(8); PG8_WAIT_L(0); PG8_BAR; PG8_MMA(1, 0, At, B0); PG8_MMA(1, 1, At, B1); PG8_BAR; PG8_SCHED;
;     ...
;         }
;         if constexpr (ALIGN_EPI) { if (wr == 0) PG8_BAR; }
	s_setprio 1
	s_waitcnt lgkmcnt(0)
	v_mfma_f32_16x16x32_bf16 v[128:131], v[148:151], v[180:183], v[128:131]
	v_mfma_f32_16x16x32_bf16 v[124:127], v[156:159], v[180:183], v[124:127]
	v_mfma_f32_16x16x32_bf16 v[120:123], v[148:151], v[188:191], v[120:123]
	v_mfma_f32_16x16x32_bf16 v[116:119], v[156:159], v[188:191], v[116:119]
	v_mfma_f32_16x16x32_bf16 v[104:107], v[148:151], v[196:199], v[104:107]
	v_mfma_f32_16x16x32_bf16 v[100:103], v[156:159], v[196:199], v[100:103]
	v_mfma_f32_16x16x32_bf16 v[86:89], v[148:151], v[212:215], v[86:89]
	v_mfma_f32_16x16x32_bf16 v[82:85], v[156:159], v[212:215], v[82:85]
	v_mfma_f32_16x16x32_bf16 v[128:131], v[152:155], v[184:187], v[128:131]
	v_mfma_f32_16x16x32_bf16 v[124:127], v[160:163], v[184:187], v[124:127]
	v_mfma_f32_16x16x32_bf16 v[120:123], v[152:155], v[192:195], v[120:123]
	v_mfma_f32_16x16x32_bf16 v[116:119], v[160:163], v[192:195], v[116:119]
	v_mfma_f32_16x16x32_bf16 v[104:107], v[152:155], v[208:211], v[104:107]
	v_mfma_f32_16x16x32_bf16 v[100:103], v[160:163], v[208:211], v[100:103]
	v_mfma_f32_16x16x32_bf16 v[86:89], v[152:155], v[216:219], v[86:89]
	v_mfma_f32_16x16x32_bf16 v[82:85], v[160:163], v[216:219], v[82:85]
	s_setprio 0
	s_setprio 1
	v_mfma_f32_16x16x32_bf16 v[112:115], v[164:167], v[180:183], v[112:115]
	v_mfma_f32_16x16x32_bf16 v[108:111], v[172:175], v[180:183], v[108:111]
	v_mfma_f32_16x16x32_bf16 v[94:97], v[164:167], v[188:191], v[94:97]
	v_mfma_f32_16x16x32_bf16 v[90:93], v[172:175], v[188:191], v[90:93]
	v_mfma_f32_16x16x32_bf16 v[78:81], v[164:167], v[196:199], v[78:81]
	v_mfma_f32_16x16x32_bf16 v[74:77], v[172:175], v[196:199], v[74:77]
	v_mfma_f32_16x16x32_bf16 v[70:73], v[164:167], v[212:215], v[70:73]
	v_mfma_f32_16x16x32_bf16 v[66:69], v[172:175], v[212:215], v[66:69]
	v_mfma_f32_16x16x32_bf16 v[112:115], v[168:171], v[184:187], v[112:115]
	v_mfma_f32_16x16x32_bf16 v[108:111], v[176:179], v[184:187], v[108:111]
	v_mfma_f32_16x16x32_bf16 v[94:97], v[168:171], v[192:195], v[94:97]
	v_mfma_f32_16x16x32_bf16 v[90:93], v[176:179], v[192:195], v[90:93]
	v_mfma_f32_16x16x32_bf16 v[78:81], v[168:171], v[208:211], v[78:81]
	v_mfma_f32_16x16x32_bf16 v[74:77], v[176:179], v[208:211], v[74:77]
	v_mfma_f32_16x16x32_bf16 v[70:73], v[168:171], v[216:219], v[70:73]
	v_mfma_f32_16x16x32_bf16 v[66:69], v[176:179], v[216:219], v[66:69]
	s_setprio 0
	s_barrier
	s_mov_b32 m0, s59
	v_lshl_add_u64 v[220:221], v[220:221], 0, s[54:55]
	s_add_u32 s20, s24, 0xe0080
	ds_read_b128 v[180:183], v147 offset:49152
	ds_read_b128 v[184:187], v147 offset:50176
	ds_read_b128 v[188:191], v147 offset:51200
	ds_read_b128 v[192:195], v147 offset:52224
	ds_read_b128 v[196:199], v147 offset:53248
	ds_read_b128 v[208:211], v147 offset:54272
	ds_read_b128 v[212:215], v147 offset:55296
	ds_read_b128 v[216:219], v147 offset:56320
	global_load_lds_dwordx4 v[220:221], off
	v_lshl_add_u64 v[220:221], v[222:223], 0, s[54:55]
	s_mov_b32 m0, s61
	s_addc_u32 s21, s25, 0
	global_load_lds_dwordx4 v[220:221], off
	v_lshl_add_u64 v[220:221], s[20:21], 0, v[134:135]
	s_mov_b32 m0, s72
	s_nop 0
	global_load_lds_dwordx4 v[220:221], off
	v_lshl_add_u64 v[220:221], s[20:21], 0, v[138:139]
	s_mov_b32 m0, s73
	s_nop 0
	global_load_lds_dwordx4 v[220:221], off
	v_lshl_add_u64 v[220:221], v[224:225], 0, s[54:55]
	s_mov_b32 m0, s64
	s_nop 0
	global_load_lds_dwordx4 v[220:221], off
	v_lshl_add_u64 v[220:221], v[226:227], 0, s[54:55]
	s_mov_b32 m0, s68
	s_nop 0
	global_load_lds_dwordx4 v[220:221], off
	s_waitcnt vmcnt(8)
	s_waitcnt lgkmcnt(0)
	s_barrier
	s_setprio 1
	s_waitcnt lgkmcnt(0)
	v_mfma_f32_16x16x32_bf16 v[62:65], v[148:151], v[180:183], v[62:65]
	v_mfma_f32_16x16x32_bf16 v[58:61], v[156:159], v[180:183], v[58:61]
	v_mfma_f32_16x16x32_bf16 v[54:57], v[148:151], v[188:191], v[54:57]
	v_mfma_f32_16x16x32_bf16 v[50:53], v[156:159], v[188:191], v[50:53]
	v_mfma_f32_16x16x32_bf16 v[38:41], v[148:151], v[196:199], v[38:41]
	v_mfma_f32_16x16x32_bf16 v[34:37], v[156:159], v[196:199], v[34:37]
	v_mfma_f32_16x16x32_bf16 v[22:25], v[148:151], v[212:215], v[22:25]
	v_mfma_f32_16x16x32_bf16 v[18:21], v[156:159], v[212:215], v[18:21]
	v_mfma_f32_16x16x32_bf16 v[62:65], v[152:155], v[184:187], v[62:65]
	v_mfma_f32_16x16x32_bf16 v[58:61], v[160:163], v[184:187], v[58:61]
	v_mfma_f32_16x16x32_bf16 v[54:57], v[152:155], v[192:195], v[54:57]
	v_mfma_f32_16x16x32_bf16 v[50:53], v[160:163], v[192:195], v[50:53]
	v_mfma_f32_16x16x32_bf16 v[38:41], v[152:155], v[208:211], v[38:41]
	v_mfma_f32_16x16x32_bf16 v[34:37], v[160:163], v[208:211], v[34:37]
	v_mfma_f32_16x16x32_bf16 v[22:25], v[152:155], v[216:219], v[22:25]
	v_mfma_f32_16x16x32_bf16 v[18:21], v[160:163], v[216:219], v[18:21]
	s_setprio 0
	s_setprio 1
	v_mfma_f32_16x16x32_bf16 v[46:49], v[164:167], v[180:183], v[46:49]
	v_mfma_f32_16x16x32_bf16 v[42:45], v[172:175], v[180:183], v[42:45]
	v_mfma_f32_16x16x32_bf16 v[30:33], v[164:167], v[188:191], v[30:33]
	v_mfma_f32_16x16x32_bf16 v[26:29], v[172:175], v[188:191], v[26:29]
	v_mfma_f32_16x16x32_bf16 v[14:17], v[164:167], v[196:199], v[14:17]
	v_mfma_f32_16x16x32_bf16 v[10:13], v[172:175], v[196:199], v[10:13]
	v_mfma_f32_16x16x32_bf16 v[6:9], v[164:167], v[212:215], v[6:9]
	v_mfma_f32_16x16x32_bf16 v[2:5], v[172:175], v[212:215], v[2:5]
	v_mfma_f32_16x16x32_bf16 v[46:49], v[168:171], v[184:187], v[46:49]
	v_mfma_f32_16x16x32_bf16 v[42:45], v[176:179], v[184:187], v[42:45]
	v_mfma_f32_16x16x32_bf16 v[30:33], v[168:171], v[192:195], v[30:33]
	v_mfma_f32_16x16x32_bf16 v[26:29], v[176:179], v[192:195], v[26:29]
	v_mfma_f32_16x16x32_bf16 v[14:17], v[168:171], v[208:211], v[14:17]
	v_mfma_f32_16x16x32_bf16 v[10:13], v[176:179], v[208:211], v[10:13]
	v_mfma_f32_16x16x32_bf16 v[6:9], v[168:171], v[216:219], v[6:9]
	v_mfma_f32_16x16x32_bf16 v[2:5], v[176:179], v[216:219], v[2:5]
	s_setprio 0
	s_barrier
	s_add_i32 s88, s88, 2
	s_add_u32 s17, s17, 0x100
	s_addc_u32 s87, s87, 0
	s_cmp_gt_u32 s88, 53
	s_mov_b64 s[20:21], s[22:23]
	s_cbranch_scc0 .LBB13_1573
	s_and_b64 vcc, exec, s[14:15]
	s_cbranch_vccz .LBB13_1576
	s_barrier
; __device__ __forceinline__ unsigned pk2(float lo, float hi) { f32x2 v = {lo, hi}; return __builtin_bit_cast(unsigned, __builtin_convertvector(v, bf2_t)); }
; template <int BIT = 0> __device__ __forceinline__ void st16w(void* p, u32x4 v) { if ((WT_STORES >> BIT) & 1) asm volatile("global_store_dwordx4 %0, %1, off sc1\n\ts_nop 1" :: "v"(p), "v"(v) : "memory"); else *(u32x4*)p = v; }
; #define PG8_LAS __attribute__((address_space(3)))
; #define PG8_BAR __builtin_amdgcn_s_barrier()
;     __device__ __forceinline__ void operator()(const f32x4 (&acc)[2][2][4][2], const Unit& u, int wr, int wc, int fr, int fq) const {
;         const int row0 = u.pm * BM + wr * 64 + fr, col0 = u.pn * BM + wc * 32 + 8 * fq;
; #pragma unroll
;         for (int ai = 0; ai < 2; ++ai)
; #pragma unroll
;             for (int m = 0; m < 4; ++m) { bf16* rowp = O + (size_t)(row0 + ai * HALF + m * 16) * ldc + col0;
; #pragma unroll
;                 for (int bj = 0; bj < 2; ++bj) { const f32x4 v0 = acc[ai][bj][m][0], v1 = acc[ai][bj][m][1];
;                     u32x4 w; w.x = pk2(v0[0], v0[1]); w.y = pk2(v0[2], v0[3]); w.z = pk2(v1[0], v1[1]); w.w = pk2(v1[2], v1[3]);
;                     st16w(rowp + bj * HALF, w); } }
;     }
; template <class Epi, class Sched, bool ALIGN_EPI = false, bool SP2 = false>
; __device__ __forceinline__ void gemm_phase(PG8_LAS unsigned char* lds, const Gemm g, const Sched& S, const Epi& E) {
;     ...
;         cur = nxt; cA = nA; cB = nB; ++ui;
;         if constexpr (Sched::GATHER) { const u32x4 pv_ = *(const PG8_LAS u32x4*)(lds + STAGE_BYTES + tid * 16); vAc[0][0] = pv_.x; vAc[0][1] = pv_.y; vAc[1][0] = pv_.z; vAc[1][1] = pv_.w; }
;         if constexpr (ALIGN_EPI) { if (wr == 1) PG8_BAR; }
.LBB13_1576:
	v_lshl_add_u32 v148, s12, 8, v144
	v_lshl_or_b32 v150, s60, 8, v146
	v_ashrrev_i32_e32 v149, 31, v148
	v_ashrrev_i32_e32 v151, 31, v150
	v_lshlrev_b64 v[152:153], 11, v[148:149]
	v_lshl_add_u64 v[152:153], s[0:1], 0, v[152:153]
	v_lshlrev_b64 v[150:151], 1, v[150:151]
	v_lshl_add_u64 v[152:153], v[152:153], 0, v[150:151]
	s_mov_b32 s12, 0x40000
	s_mov_b64 s[20:21], 0x40000
	v_cvt_pk_bf16_f32 v62, v62, v63
	v_cvt_pk_bf16_f32 v63, v64, v65
	v_cvt_pk_bf16_f32 v64, v58, v59
	v_add_co_u32_e32 v58, vcc, s12, v152
	v_cvt_pk_bf16_f32 v70, v70, v71
	v_cvt_pk_bf16_f32 v71, v72, v73
	v_cvt_pk_bf16_f32 v72, v66, v67
	v_lshl_add_u64 v[66:67], v[152:153], 0, s[20:21]
	v_addc_co_u32_e32 v59, vcc, 0, v153, vcc
	v_cvt_pk_bf16_f32 v46, v46, v47
	v_cvt_pk_bf16_f32 v47, v48, v49
	v_cvt_pk_bf16_f32 v48, v42, v43
	v_cvt_pk_bf16_f32 v49, v44, v45
	s_mov_b32 s12, 0x48000
	v_cvt_pk_bf16_f32 v112, v112, v113
	v_cvt_pk_bf16_f32 v113, v114, v115
	v_cvt_pk_bf16_f32 v114, v108, v109
	v_or_b32_e32 v108, 16, v148
	global_store_dwordx4 v[66:67], v[46:49], off offset:256
	s_mov_b64 s[20:21], 0x48000
	v_ashrrev_i32_e32 v109, 31, v108
	v_add_co_u32_e32 v48, vcc, s12, v152
	v_cvt_pk_bf16_f32 v94, v94, v95
	v_cvt_pk_bf16_f32 v95, v96, v97
	v_cvt_pk_bf16_f32 v96, v90, v91
	v_or_b32_e32 v90, 32, v148
	v_lshl_add_u64 v[46:47], v[152:153], 0, s[20:21]
	v_addc_co_u32_e32 v49, vcc, 0, v153, vcc
	v_cvt_pk_bf16_f32 v30, v30, v31
	v_cvt_pk_bf16_f32 v31, v32, v33
	v_cvt_pk_bf16_f32 v32, v26, v27
	v_cvt_pk_bf16_f32 v33, v28, v29
	s_mov_b32 s12, 0x50000
	v_lshlrev_b64 v[108:109], 11, v[108:109]
	v_ashrrev_i32_e32 v91, 31, v90
	v_cvt_pk_bf16_f32 v78, v78, v79
	v_cvt_pk_bf16_f32 v79, v80, v81
	v_cvt_pk_bf16_f32 v80, v74, v75
	v_or_b32_e32 v74, 48, v148
	global_store_dwordx4 v[46:47], v[30:33], off offset:256
	s_mov_b64 s[20:21], 0x50000
	v_cvt_pk_bf16_f32 v115, v110, v111
	v_add_co_u32_e32 v32, vcc, s12, v152
	v_lshl_add_u64 v[108:109], s[0:1], 0, v[108:109]
	v_lshlrev_b64 v[90:91], 11, v[90:91]
	v_ashrrev_i32_e32 v75, 31, v74
	v_lshl_add_u64 v[30:31], v[152:153], 0, s[20:21]
	v_addc_co_u32_e32 v33, vcc, 0, v153, vcc
	v_cvt_pk_bf16_f32 v14, v14, v15
	v_cvt_pk_bf16_f32 v15, v16, v17
	v_cvt_pk_bf16_f32 v16, v10, v11
	v_cvt_pk_bf16_f32 v17, v12, v13
	s_mov_b32 s12, 0x58000
	global_store_dwordx4 v[152:153], v[112:115], off offset:256
	v_cvt_pk_bf16_f32 v97, v92, v93
	v_lshl_add_u64 v[90:91], s[0:1], 0, v[90:91]
	v_lshl_add_u64 v[112:113], v[108:109], 0, v[150:151]
	v_lshlrev_b64 v[74:75], 11, v[74:75]
	global_store_dwordx4 v[30:31], v[14:17], off offset:256
	global_store_dwordx4 v[112:113], v[94:97], off offset:256
	v_cvt_pk_bf16_f32 v81, v76, v77
	v_add_co_u32_e32 v16, vcc, s12, v152
	v_lshl_add_u64 v[94:95], v[90:91], 0, v[150:151]
	v_lshl_add_u64 v[74:75], s[0:1], 0, v[74:75]
	s_mov_b64 s[20:21], 0x58000
	v_addc_co_u32_e32 v17, vcc, 0, v153, vcc
	v_cvt_pk_bf16_f32 v128, v128, v129
	v_cvt_pk_bf16_f32 v129, v130, v131
	v_cvt_pk_bf16_f32 v130, v124, v125
	v_cvt_pk_bf16_f32 v131, v126, v127
	v_cvt_pk_bf16_f32 v108, v120, v121
	v_cvt_pk_bf16_f32 v109, v122, v123
	v_cvt_pk_bf16_f32 v110, v116, v117
	v_cvt_pk_bf16_f32 v111, v118, v119
	v_cvt_pk_bf16_f32 v90, v104, v105
	v_cvt_pk_bf16_f32 v91, v106, v107
	v_cvt_pk_bf16_f32 v92, v100, v101
	v_cvt_pk_bf16_f32 v93, v102, v103
	global_store_dwordx4 v[94:95], v[78:81], off offset:256
	v_cvt_pk_bf16_f32 v76, v82, v83
	v_cvt_pk_bf16_f32 v77, v84, v85
	v_lshl_add_u64 v[78:79], v[74:75], 0, v[150:151]
	v_cvt_pk_bf16_f32 v74, v86, v87
	v_cvt_pk_bf16_f32 v75, v88, v89
	v_cvt_pk_bf16_f32 v73, v68, v69
	v_cvt_pk_bf16_f32 v65, v60, v61
	v_cvt_pk_bf16_f32 v42, v54, v55
	v_cvt_pk_bf16_f32 v43, v56, v57
	v_cvt_pk_bf16_f32 v44, v50, v51
	v_cvt_pk_bf16_f32 v45, v52, v53
	v_cvt_pk_bf16_f32 v26, v38, v39
	v_cvt_pk_bf16_f32 v27, v40, v41
	v_cvt_pk_bf16_f32 v28, v34, v35
	v_cvt_pk_bf16_f32 v29, v36, v37
	v_lshl_add_u64 v[14:15], v[152:153], 0, s[20:21]
	v_cvt_pk_bf16_f32 v10, v22, v23
	v_cvt_pk_bf16_f32 v11, v24, v25
	v_cvt_pk_bf16_f32 v12, v18, v19
	v_cvt_pk_bf16_f32 v13, v20, v21
	v_cvt_pk_bf16_f32 v6, v6, v7
	v_cvt_pk_bf16_f32 v7, v8, v9
	v_cvt_pk_bf16_f32 v8, v2, v3
	v_cvt_pk_bf16_f32 v9, v4, v5
	s_and_b64 vcc, exec, s[4:5]
	s_mov_b64 s[4:5], -1
	s_mov_b32 s87, 0x8000
	s_mov_b32 s88, 0x16000
	global_store_dwordx4 v[152:153], v[128:131], off
	global_store_dwordx4 v[112:113], v[108:111], off
	global_store_dwordx4 v[94:95], v[90:93], off
	global_store_dwordx4 v[78:79], v[74:77], off
	global_store_dwordx4 v[78:79], v[70:73], off offset:256
	global_store_dwordx4 v[58:59], v[62:65], off
	global_store_dwordx4 v[48:49], v[42:45], off
	global_store_dwordx4 v[32:33], v[26:29], off
	global_store_dwordx4 v[16:17], v[10:13], off
	global_store_dwordx4 v[14:15], v[6:9], off offset:256
	s_cbranch_vccnz .LBB13_1561
	s_andn2_b64 vcc, exec, s[10:11]
	s_cbranch_vccnz .LBB13_1560
	s_branch .LBB13_1560
